# full stack: adds RG-LRU gate epilogue load batching, fused top-2 pick reduction, LN2 gamma/beta preload, de-serialized expert gather loads on top of barrier rewrite + P1 steal quota 3 + LN1 preload +
# speedup vs baseline: 1.0487x; 1.0185x over previous
; __global__ void __launch_bounds__(NTHREADS, 2) hybrid_fwd(Args a) {
;     ...
;             for (int v = bid; v < 256; v += G) {
;                 u32x2 raw[2][8];
; #pragma unroll
;                 for (int q = 0; q < 2; ++q)
; #pragma unroll
;                     for (int j = 0; j < 8; ++j) raw[q][j] = __builtin_nontemporal_load((const u32x2*)(YB + (size_t)(v * 32 + wave + 8 * q) * DM + j * 256 + lane * 4));
;                 __syncthreads();
;                 if (tid < 16) hist[tid] = 0;
;                 __syncthreads();
;                 asm volatile("s_waitcnt vmcnt(0)" ::: "memory"); __syncthreads();
.LBB0_887:
	s_add_i32 s6, s22, s51
	s_ashr_i32 s7, s6, 31
	s_add_i32 s8, s6, 8
	s_lshl_b64 s[12:13], s[6:7], 12
	s_ashr_i32 s9, s8, 31
	v_lshl_add_u64 v[16:17], v[26:27], 0, s[12:13]
	s_lshl_b64 s[10:11], s[8:9], 12
	flat_load_dwordx2 v[58:59], v[16:17] nt
	flat_load_dwordx2 v[56:57], v[16:17] offset:512 nt
	flat_load_dwordx2 v[54:55], v[16:17] offset:1024 nt
	flat_load_dwordx2 v[52:53], v[16:17] offset:1536 nt
	flat_load_dwordx2 v[50:51], v[16:17] offset:2048 nt
	flat_load_dwordx2 v[48:49], v[16:17] offset:2560 nt
	flat_load_dwordx2 v[46:47], v[16:17] offset:3072 nt
	flat_load_dwordx2 v[44:45], v[16:17] offset:3584 nt
	v_lshl_add_u64 v[16:17], v[26:27], 0, s[10:11]
	flat_load_dwordx2 v[42:43], v[16:17] nt
	flat_load_dwordx2 v[40:41], v[16:17] offset:512 nt
	flat_load_dwordx2 v[38:39], v[16:17] offset:1024 nt
	flat_load_dwordx2 v[36:37], v[16:17] offset:1536 nt
	flat_load_dwordx2 v[22:23], v[16:17] offset:2048 nt
	flat_load_dwordx2 v[20:21], v[16:17] offset:2560 nt
	flat_load_dwordx2 v[18:19], v[16:17] offset:3072 nt
	s_nop 0
	flat_load_dwordx2 v[16:17], v[16:17] offset:3584 nt
	s_waitcnt vmcnt(0) lgkmcnt(0)
	s_barrier
	s_and_saveexec_b64 s[14:15], s[0:1]
	ds_write_b32 v156, v193
	s_or_b64 exec, exec, s[14:15]
	s_waitcnt lgkmcnt(0)
	s_barrier
	s_waitcnt vmcnt(0)
	s_add_i32 s38, s6, 16
	s_barrier
	s_mov_b64 s[14:15], s[34:35]
	v_lshlrev_b32_e32 v192, 2, v24
	s_mov_b64 s[16:17], s[36:37]
	v_lshl_add_u64 v[94:95], s[14:15], 0, v[192:193]
	v_lshlrev_b32_e32 v66, 16, v58
	v_lshl_add_u64 v[96:97], s[16:17], 0, v[192:193]
	s_nop 0
	v_and_b32_e32 v67, 0xffff0000, v58
	v_lshlrev_b32_e32 v64, 16, v59
	v_and_b32_e32 v65, 0xffff0000, v59
	v_add_f32_e32 v35, v66, v67
	v_add_f32_e32 v58, v64, v65
	v_lshlrev_b32_e32 v74, 16, v56
	v_and_b32_e32 v75, 0xffff0000, v56
	v_lshlrev_b32_e32 v72, 16, v57
	v_and_b32_e32 v73, 0xffff0000, v57
	v_add_f32_e32 v35, v35, v58
	v_add_f32_e32 v56, v74, v75
	v_add_f32_e32 v57, v72, v73
	v_lshlrev_b32_e32 v68, 16, v54
	v_and_b32_e32 v69, 0xffff0000, v54
	v_lshlrev_b32_e32 v70, 16, v55
	v_and_b32_e32 v71, 0xffff0000, v55
	v_add_f32_e32 v35, 0, v35
	v_add_f32_e32 v56, v56, v57
	v_add_f32_e32 v54, v68, v69
	v_add_f32_e32 v55, v70, v71
	v_lshlrev_b32_e32 v60, 16, v52
	v_and_b32_e32 v61, 0xffff0000, v52
	v_lshlrev_b32_e32 v62, 16, v53
	v_and_b32_e32 v63, 0xffff0000, v53
	v_add_f32_e32 v35, v35, v56
	v_add_f32_e32 v54, v54, v55
	v_add_f32_e32 v52, v60, v61
	v_add_f32_e32 v53, v62, v63
	v_add_f32_e32 v35, v35, v54
	v_add_f32_e32 v52, v52, v53
	v_lshlrev_b32_e32 v56, 16, v50
	v_and_b32_e32 v57, 0xffff0000, v50
	v_lshlrev_b32_e32 v58, 16, v51
	v_and_b32_e32 v59, 0xffff0000, v51
	v_add_f32_e32 v35, v35, v52
	v_add_f32_e32 v50, v56, v57
	v_add_f32_e32 v51, v58, v59
	v_lshlrev_b32_e32 v52, 16, v48
	v_and_b32_e32 v53, 0xffff0000, v48
	v_lshlrev_b32_e32 v54, 16, v49
	v_and_b32_e32 v55, 0xffff0000, v49
	v_add_f32_e32 v50, v50, v51
	v_add_f32_e32 v48, v52, v53
	v_add_f32_e32 v49, v54, v55
	v_add_f32_e32 v35, v35, v50
	v_add_f32_e32 v48, v48, v49
	v_add_f32_e32 v35, v35, v48
	v_lshlrev_b32_e32 v48, 16, v46
	v_and_b32_e32 v49, 0xffff0000, v46
	v_lshlrev_b32_e32 v50, 16, v47
	v_and_b32_e32 v51, 0xffff0000, v47
	v_add_f32_e32 v46, v48, v49
	v_add_f32_e32 v47, v50, v51
	v_add_f32_e32 v46, v46, v47
	v_add_f32_e32 v35, v35, v46
	v_lshlrev_b32_e32 v46, 16, v44
	v_and_b32_e32 v47, 0xffff0000, v44
	v_lshlrev_b32_e32 v44, 16, v45
	v_and_b32_e32 v45, 0xffff0000, v45
	v_add_f32_e32 v76, v46, v47
	v_add_f32_e32 v77, v44, v45
	v_add_f32_e32 v76, v76, v77
	v_add_f32_e32 v35, v35, v76
	s_lshl_b64 s[14:15], s[6:7], 11
	s_nop 0
	v_add_f32_dpp v35, v35, v35 quad_perm:[1,0,3,2] row_mask:0xf bank_mask:0xf bound_ctrl:1
	s_nop 1
	v_add_f32_dpp v35, v35, v35 quad_perm:[2,3,0,1] row_mask:0xf bank_mask:0xf bound_ctrl:1
	s_nop 1
	v_add_f32_dpp v35, v35, v35 row_ror:4 row_mask:0xf bank_mask:0xf bound_ctrl:1
	s_nop 1
	v_add_f32_dpp v35, v35, v35 row_ror:8 row_mask:0xf bank_mask:0xf bound_ctrl:1
	v_mov_b32_e32 v76, v35
	s_nop 1
	v_permlane16_swap_b32_e32 v35, v76
	v_add_f32_e32 v35, v35, v76
	v_mov_b32_e32 v76, v35
	s_nop 1
	v_permlane32_swap_b32_e32 v35, v76
	v_add_f32_e32 v35, v35, v76
	v_fmac_f32_e32 v65, 0xba000000, v35
	v_fmac_f32_e32 v67, 0xba000000, v35
	v_fmac_f32_e32 v64, 0xba000000, v35
	v_fmac_f32_e32 v66, 0xba000000, v35
	v_mul_f32_e32 v76, v67, v67
	v_mul_f32_e32 v77, v65, v65
	v_fmac_f32_e32 v76, v66, v66
	v_fmac_f32_e32 v77, v64, v64
	v_fmac_f32_e32 v73, 0xba000000, v35
	v_fmac_f32_e32 v75, 0xba000000, v35
	v_add_f32_e32 v76, v76, v77
	v_fmac_f32_e32 v72, 0xba000000, v35
	v_fmac_f32_e32 v74, 0xba000000, v35
	v_mul_f32_e32 v77, v75, v75
	v_mul_f32_e32 v78, v73, v73
	v_fmac_f32_e32 v77, v74, v74
	v_fmac_f32_e32 v78, v72, v72
	v_add_f32_e32 v77, v77, v78
	v_fmac_f32_e32 v71, 0xba000000, v35
	v_fmac_f32_e32 v69, 0xba000000, v35
	v_add_f32_e32 v76, v76, v77
	v_fmac_f32_e32 v70, 0xba000000, v35
	v_fmac_f32_e32 v68, 0xba000000, v35
	v_mul_f32_e32 v77, v69, v69
	v_mul_f32_e32 v78, v71, v71
	v_fmac_f32_e32 v77, v68, v68
	v_fmac_f32_e32 v78, v70, v70
	v_add_f32_e32 v77, v77, v78
	v_fmac_f32_e32 v63, 0xba000000, v35
	v_fmac_f32_e32 v61, 0xba000000, v35
	v_add_f32_e32 v76, v76, v77
	v_fmac_f32_e32 v62, 0xba000000, v35
	v_fmac_f32_e32 v60, 0xba000000, v35
	v_mul_f32_e32 v77, v61, v61
	v_mul_f32_e32 v78, v63, v63
	v_fmac_f32_e32 v77, v60, v60
	v_fmac_f32_e32 v78, v62, v62
	v_add_f32_e32 v77, v77, v78
	v_fmac_f32_e32 v59, 0xba000000, v35
	v_fmac_f32_e32 v57, 0xba000000, v35
	v_add_f32_e32 v76, v76, v77
	v_fmac_f32_e32 v58, 0xba000000, v35
	v_fmac_f32_e32 v56, 0xba000000, v35
	v_mul_f32_e32 v77, v57, v57
	v_mul_f32_e32 v78, v59, v59
	v_fmac_f32_e32 v77, v56, v56
	v_fmac_f32_e32 v78, v58, v58
	v_add_f32_e32 v77, v77, v78
	v_fmac_f32_e32 v55, 0xba000000, v35
	v_fmac_f32_e32 v53, 0xba000000, v35
	v_add_f32_e32 v76, v76, v77
	v_fmac_f32_e32 v54, 0xba000000, v35
	v_fmac_f32_e32 v52, 0xba000000, v35
	v_mul_f32_e32 v77, v53, v53
	v_mul_f32_e32 v78, v55, v55
	v_fmac_f32_e32 v77, v52, v52
	v_fmac_f32_e32 v78, v54, v54
	v_add_f32_e32 v77, v77, v78
	v_fmac_f32_e32 v51, 0xba000000, v35
	v_fmac_f32_e32 v49, 0xba000000, v35
	v_add_f32_e32 v76, v76, v77
	v_fmac_f32_e32 v50, 0xba000000, v35
	v_fmac_f32_e32 v48, 0xba000000, v35
	v_mul_f32_e32 v77, v49, v49
	v_mul_f32_e32 v78, v51, v51
	v_fmac_f32_e32 v77, v48, v48
	v_fmac_f32_e32 v78, v50, v50
	v_add_f32_e32 v77, v77, v78
	v_fmac_f32_e32 v45, 0xba000000, v35
	v_fmac_f32_e32 v47, 0xba000000, v35
	v_add_f32_e32 v76, v76, v77
	v_fmac_f32_e32 v44, 0xba000000, v35
	v_fmac_f32_e32 v46, 0xba000000, v35
	v_mul_f32_e32 v35, v47, v47
	v_mul_f32_e32 v77, v45, v45
	v_fmac_f32_e32 v35, v46, v46
	v_fmac_f32_e32 v77, v44, v44
	v_add_f32_e32 v35, v35, v77
	v_add_f32_e32 v35, v76, v35
	v_lshl_add_u64 v[78:79], v[30:31], 0, s[14:15]
	s_nop 0
	v_add_f32_dpp v35, v35, v35 quad_perm:[1,0,3,2] row_mask:0xf bank_mask:0xf bound_ctrl:1
	s_nop 1
	v_add_f32_dpp v35, v35, v35 quad_perm:[2,3,0,1] row_mask:0xf bank_mask:0xf bound_ctrl:1
	s_nop 1
	v_add_f32_dpp v35, v35, v35 row_ror:4 row_mask:0xf bank_mask:0xf bound_ctrl:1
	s_nop 1
	v_add_f32_dpp v35, v35, v35 row_ror:8 row_mask:0xf bank_mask:0xf bound_ctrl:1
	v_mov_b32_e32 v76, v35
	s_nop 1
	v_permlane16_swap_b32_e32 v35, v76
	v_add_f32_e32 v35, v35, v76
	v_mov_b32_e32 v76, v35
	s_nop 1
	v_permlane32_swap_b32_e32 v35, v76
	v_add_f32_e32 v35, v35, v76
	v_fmamk_f32 v35, v35, 0x3a000000, v207
	v_rsq_f32_e32 v84, v35
	v_lshl_add_u64 v[76:77], v[28:29], 0, s[12:13]
	v_pk_mul_f32 v[66:67], v[84:85], v[66:67] op_sel_hi:[0,1]
	v_pk_mul_f32 v[90:91], v[84:85], v[64:65] op_sel_hi:[0,1]
	s_waitcnt vmcnt(0) lgkmcnt(0)
	v_pk_fma_f32 v[64:65], v[158:159], v[66:67], v[198:199]
	v_mov_b32_e32 v85, 0
	v_med3_f32 v35, v64, s69, v208
	v_med3_f32 v66, v65, s69, v208
	v_cvt_pk_fp8_f32 v85, v35, v66
	v_pk_fma_f32 v[66:67], v[160:161], v[90:91], v[200:201]
	s_nop 0
	v_med3_f32 v35, v66, s69, v208
	v_med3_f32 v80, v67, s69, v208
	v_cvt_pk_fp8_f32 v85, v35, v80 op_sel:[0,0,1]
	v_cvt_pk_bf16_f32 v80, v64, v65
	v_cvt_pk_bf16_f32 v81, v66, v67
	global_store_dwordx2 v[76:77], v[80:81], off nt
	global_store_dword v[78:79], v85, off nt
	s_nop 0
	s_nop 0
	v_pk_mul_f32 v[74:75], v[84:85], v[74:75] op_sel_hi:[0,1]
	v_pk_mul_f32 v[90:91], v[84:85], v[72:73] op_sel_hi:[0,1]
	v_mov_b32_e32 v85, 0
	s_nop 0
	v_pk_fma_f32 v[72:73], v[162:163], v[74:75], v[202:203]
	s_nop 0
	v_med3_f32 v35, v72, s69, v208
	v_med3_f32 v74, v73, s69, v208
	v_cvt_pk_fp8_f32 v85, v35, v74
	v_pk_fma_f32 v[74:75], v[164:165], v[90:91], v[204:205]
	s_nop 0
	v_med3_f32 v35, v74, s69, v208
	v_med3_f32 v80, v75, s69, v208
	v_cvt_pk_fp8_f32 v85, v35, v80 op_sel:[0,0,1]
	v_cvt_pk_bf16_f32 v80, v72, v73
	v_cvt_pk_bf16_f32 v81, v74, v75
	global_store_dwordx2 v[76:77], v[80:81], off offset:512 nt
	global_store_dword v[78:79], v85, off offset:256 nt
	s_nop 0
	v_pk_mul_f32 v[68:69], v[84:85], v[68:69] op_sel_hi:[0,1]
	v_mov_b32_e32 v35, 0
	v_pk_mul_f32 v[70:71], v[84:85], v[70:71] op_sel_hi:[0,1]
	v_pk_mul_f32 v[60:61], v[84:85], v[60:61] op_sel_hi:[0,1]
	v_pk_mul_f32 v[62:63], v[84:85], v[62:63] op_sel_hi:[0,1]
	v_pk_mul_f32 v[56:57], v[84:85], v[56:57] op_sel_hi:[0,1]
	v_pk_mul_f32 v[58:59], v[84:85], v[58:59] op_sel_hi:[0,1]
	v_pk_mul_f32 v[52:53], v[84:85], v[52:53] op_sel_hi:[0,1]
	v_pk_mul_f32 v[54:55], v[84:85], v[54:55] op_sel_hi:[0,1]
	v_pk_mul_f32 v[48:49], v[84:85], v[48:49] op_sel_hi:[0,1]
	v_pk_mul_f32 v[50:51], v[84:85], v[50:51] op_sel_hi:[0,1]
	v_pk_mul_f32 v[46:47], v[84:85], v[46:47] op_sel_hi:[0,1]
	v_pk_mul_f32 v[44:45], v[84:85], v[44:45] op_sel_hi:[0,1]
	s_nop 0
	v_pk_fma_f32 v[82:83], v[166:167], v[68:69], v[216:217]
	s_nop 0
	v_med3_f32 v68, v82, s69, v208
	v_med3_f32 v69, v83, s69, v208
	v_cvt_pk_fp8_f32 v35, v68, v69
	v_pk_fma_f32 v[80:81], v[168:169], v[70:71], v[218:219]
	v_add_co_u32_e32 v90, vcc, s33, v94
	v_med3_f32 v68, v80, s69, v208
	v_med3_f32 v69, v81, s69, v208
	v_cvt_pk_fp8_f32 v35, v68, v69 op_sel:[0,0,1]
	v_cvt_pk_bf16_f32 v68, v82, v83
	v_cvt_pk_bf16_f32 v69, v80, v81
	global_store_dwordx2 v[76:77], v[68:69], off offset:1024 nt
	global_store_dword v[78:79], v35, off offset:512 nt
	s_nop 0
	s_nop 0
	v_addc_co_u32_e32 v91, vcc, 0, v95, vcc
	v_mov_b32_e32 v35, 0
	v_add_co_u32_e32 v96, vcc, s33, v96
	s_nop 0
	v_pk_fma_f32 v[94:95], v[170:171], v[60:61], v[220:221]
	s_nop 0
	v_med3_f32 v60, v94, s69, v208
	v_med3_f32 v61, v95, s69, v208
	v_cvt_pk_fp8_f32 v35, v60, v61
	v_pk_fma_f32 v[92:93], v[172:173], v[62:63], v[222:223]
	v_addc_co_u32_e32 v97, vcc, 0, v97, vcc
	v_med3_f32 v60, v92, s69, v208
	v_med3_f32 v61, v93, s69, v208
	v_cvt_pk_fp8_f32 v35, v60, v61 op_sel:[0,0,1]
	v_cvt_pk_bf16_f32 v60, v94, v95
	v_cvt_pk_bf16_f32 v61, v92, v93
	global_store_dwordx2 v[76:77], v[60:61], off offset:1536 nt
	global_store_dword v[78:79], v35, off offset:768 nt
	s_nop 0
	s_nop 0
	v_mov_b32_e32 v35, 0
	s_nop 0
	v_pk_fma_f32 v[114:115], v[174:175], v[56:57], v[224:225]
	s_nop 0
	v_med3_f32 v56, v114, s69, v208
	v_med3_f32 v57, v115, s69, v208
	v_cvt_pk_fp8_f32 v35, v56, v57
	v_pk_fma_f32 v[112:113], v[176:177], v[58:59], v[226:227]
	s_nop 0
	v_med3_f32 v56, v112, s69, v208
	v_med3_f32 v57, v113, s69, v208
	v_cvt_pk_fp8_f32 v35, v56, v57 op_sel:[0,0,1]
	v_cvt_pk_bf16_f32 v56, v114, v115
	v_cvt_pk_bf16_f32 v57, v112, v113
	global_store_dwordx2 v[76:77], v[56:57], off offset:2048 nt
	global_store_dword v[78:79], v35, off offset:1024 nt
	s_nop 0
	s_nop 0
	v_mov_b32_e32 v35, 0
	s_nop 0
	v_pk_fma_f32 v[118:119], v[178:179], v[52:53], v[228:229]
	s_nop 0
	v_med3_f32 v52, v118, s69, v208
	v_med3_f32 v53, v119, s69, v208
	v_cvt_pk_fp8_f32 v35, v52, v53
	v_pk_fma_f32 v[116:117], v[180:181], v[54:55], v[230:231]
	s_nop 0
	v_med3_f32 v52, v116, s69, v208
	v_med3_f32 v53, v117, s69, v208
	v_cvt_pk_fp8_f32 v35, v52, v53 op_sel:[0,0,1]
	v_cvt_pk_bf16_f32 v52, v118, v119
	v_cvt_pk_bf16_f32 v53, v116, v117
	global_store_dwordx2 v[76:77], v[52:53], off offset:2560 nt
	global_store_dword v[78:79], v35, off offset:1280 nt
	s_nop 0
	s_nop 0
	v_mov_b32_e32 v35, 0
	s_nop 0
	v_pk_fma_f32 v[122:123], v[182:183], v[48:49], v[232:233]
	s_nop 0
	v_med3_f32 v48, v122, s69, v208
	v_med3_f32 v49, v123, s69, v208
	v_cvt_pk_fp8_f32 v35, v48, v49
	v_pk_fma_f32 v[120:121], v[184:185], v[50:51], v[234:235]
	s_nop 0
	v_med3_f32 v48, v120, s69, v208
	v_med3_f32 v49, v121, s69, v208
	v_cvt_pk_fp8_f32 v35, v48, v49 op_sel:[0,0,1]
	v_cvt_pk_bf16_f32 v48, v122, v123
	v_cvt_pk_bf16_f32 v49, v120, v121
	global_store_dwordx2 v[76:77], v[48:49], off offset:3072 nt
	global_store_dword v[78:79], v35, off offset:1536 nt
	s_nop 0
	s_nop 0
	v_mov_b32_e32 v35, 0
	s_nop 0
	v_pk_fma_f32 v[124:125], v[186:187], v[46:47], v[246:247]
	s_nop 0
	v_med3_f32 v46, v124, s69, v208
	v_med3_f32 v47, v125, s69, v208
	v_mov_b32_e32 v48, 0
	v_cvt_pk_fp8_f32 v48, v46, v47
	v_pk_fma_f32 v[126:127], v[188:189], v[44:45], v[248:249]
	s_nop 0
	v_med3_f32 v44, v126, s69, v208
	v_med3_f32 v45, v127, s69, v208
	v_cvt_pk_fp8_f32 v48, v44, v45 op_sel:[0,0,1]
	v_cvt_pk_bf16_f32 v44, v124, v125
	v_cvt_pk_bf16_f32 v45, v126, v127
	global_store_dwordx2 v[76:77], v[44:45], off offset:3584 nt
	global_store_dword v[78:79], v48, off offset:1792 nt
	v_lshlrev_b32_e32 v84, 16, v42
	v_and_b32_e32 v85, 0xffff0000, v42
	v_lshlrev_b32_e32 v78, 16, v43
	v_and_b32_e32 v79, 0xffff0000, v43
	v_add_f32_e32 v42, v84, v85
	v_add_f32_e32 v43, v78, v79
	v_lshlrev_b32_e32 v76, 16, v40
	v_and_b32_e32 v77, 0xffff0000, v40
	v_lshlrev_b32_e32 v70, 16, v41
	v_and_b32_e32 v71, 0xffff0000, v41
	v_add_f32_e32 v42, v42, v43
	v_add_f32_e32 v40, v76, v77
	v_add_f32_e32 v41, v70, v71
	v_lshlrev_b32_e32 v62, 16, v38
	v_and_b32_e32 v63, 0xffff0000, v38
	v_lshlrev_b32_e32 v68, 16, v39
	v_and_b32_e32 v69, 0xffff0000, v39
	v_add_f32_e32 v42, 0, v42
	v_add_f32_e32 v40, v40, v41
	v_add_f32_e32 v38, v62, v63
	v_add_f32_e32 v39, v68, v69
	v_lshlrev_b32_e32 v58, 16, v36
	v_and_b32_e32 v59, 0xffff0000, v36
	v_lshlrev_b32_e32 v60, 16, v37
	v_and_b32_e32 v61, 0xffff0000, v37
	v_add_f32_e32 v40, v42, v40
	v_add_f32_e32 v38, v38, v39
	v_add_f32_e32 v36, v58, v59
	v_add_f32_e32 v37, v60, v61
	v_lshlrev_b32_e32 v50, 16, v22
	v_and_b32_e32 v51, 0xffff0000, v22
	v_lshlrev_b32_e32 v52, 16, v23
	v_and_b32_e32 v53, 0xffff0000, v23
	v_add_f32_e32 v38, v40, v38
	v_add_f32_e32 v36, v36, v37
	v_add_f32_e32 v22, v50, v51
	v_add_f32_e32 v23, v52, v53
	v_lshlrev_b32_e32 v46, 16, v20
	v_and_b32_e32 v47, 0xffff0000, v20
	v_lshlrev_b32_e32 v48, 16, v21
	v_and_b32_e32 v49, 0xffff0000, v21
	v_add_f32_e32 v36, v38, v36
	v_add_f32_e32 v22, v22, v23
	v_add_f32_e32 v20, v46, v47
	v_add_f32_e32 v21, v48, v49
	v_lshlrev_b32_e32 v40, 16, v18
	v_and_b32_e32 v41, 0xffff0000, v18
	v_lshlrev_b32_e32 v42, 16, v19
	v_and_b32_e32 v43, 0xffff0000, v19
	v_add_f32_e32 v22, v36, v22
	v_add_f32_e32 v20, v20, v21
	v_add_f32_e32 v18, v40, v41
	v_add_f32_e32 v19, v42, v43
	v_lshlrev_b32_e32 v38, 16, v16
	v_and_b32_e32 v39, 0xffff0000, v16
	v_lshlrev_b32_e32 v36, 16, v17
	v_and_b32_e32 v37, 0xffff0000, v17
	v_add_f32_e32 v20, v22, v20
	v_add_f32_e32 v18, v18, v19
	v_add_f32_e32 v16, v38, v39
	v_add_f32_e32 v17, v36, v37
	v_add_f32_e32 v18, v20, v18
	v_add_f32_e32 v16, v16, v17
	v_add_f32_e32 v16, v18, v16
	s_mov_b64 s[12:13], s[34:35]
	s_mov_b64 s[14:15], s[36:37]
	v_add_f32_dpp v16, v16, v16 quad_perm:[1,0,3,2] row_mask:0xf bank_mask:0xf bound_ctrl:1
	v_lshl_add_u64 v[100:101], s[12:13], 0, v[192:193]
	v_lshl_add_u64 v[56:57], v[28:29], 0, s[10:11]
	v_add_f32_dpp v16, v16, v16 quad_perm:[2,3,0,1] row_mask:0xf bank_mask:0xf bound_ctrl:1
	v_lshl_add_u64 v[86:87], s[14:15], 0, v[192:193]
	s_lshl_b64 s[8:9], s[8:9], 11
	v_add_f32_dpp v16, v16, v16 row_ror:4 row_mask:0xf bank_mask:0xf bound_ctrl:1
	v_lshl_add_u64 v[54:55], v[30:31], 0, s[8:9]
	s_nop 0
	v_add_f32_dpp v16, v16, v16 row_ror:8 row_mask:0xf bank_mask:0xf bound_ctrl:1
	v_mov_b32_e32 v17, v16
	s_nop 1
	v_permlane16_swap_b32_e32 v16, v17
	v_add_f32_e32 v16, v16, v17
	v_mov_b32_e32 v17, v16
	s_nop 1
	v_permlane32_swap_b32_e32 v16, v17
	v_add_f32_e32 v16, v16, v17
	v_fmac_f32_e32 v79, 0xba000000, v16
	v_fmac_f32_e32 v85, 0xba000000, v16
	v_fmac_f32_e32 v78, 0xba000000, v16
	v_fmac_f32_e32 v84, 0xba000000, v16
	v_mul_f32_e32 v17, v85, v85
	v_mul_f32_e32 v18, v79, v79
	v_fmac_f32_e32 v17, v84, v84
	v_fmac_f32_e32 v18, v78, v78
	v_fmac_f32_e32 v71, 0xba000000, v16
	v_fmac_f32_e32 v77, 0xba000000, v16
	v_add_f32_e32 v17, v17, v18
	v_fmac_f32_e32 v70, 0xba000000, v16
	v_fmac_f32_e32 v76, 0xba000000, v16
	v_mul_f32_e32 v18, v77, v77
	v_mul_f32_e32 v19, v71, v71
	v_fmac_f32_e32 v18, v76, v76
	v_fmac_f32_e32 v19, v70, v70
	v_add_f32_e32 v18, v18, v19
	v_fmac_f32_e32 v69, 0xba000000, v16
	v_fmac_f32_e32 v63, 0xba000000, v16
	v_add_f32_e32 v17, v17, v18
	v_fmac_f32_e32 v68, 0xba000000, v16
	v_fmac_f32_e32 v62, 0xba000000, v16
	v_mul_f32_e32 v18, v63, v63
	v_mul_f32_e32 v19, v69, v69
	v_fmac_f32_e32 v18, v62, v62
	v_fmac_f32_e32 v19, v68, v68
	v_add_f32_e32 v18, v18, v19
	v_fmac_f32_e32 v61, 0xba000000, v16
	v_fmac_f32_e32 v59, 0xba000000, v16
	v_add_f32_e32 v17, v17, v18
	v_fmac_f32_e32 v60, 0xba000000, v16
	v_fmac_f32_e32 v58, 0xba000000, v16
	v_mul_f32_e32 v18, v59, v59
	v_mul_f32_e32 v19, v61, v61
	v_fmac_f32_e32 v18, v58, v58
	v_fmac_f32_e32 v19, v60, v60
	v_add_f32_e32 v18, v18, v19
	v_fmac_f32_e32 v53, 0xba000000, v16
	v_fmac_f32_e32 v51, 0xba000000, v16
	v_add_f32_e32 v17, v17, v18
	v_fmac_f32_e32 v52, 0xba000000, v16
	v_fmac_f32_e32 v50, 0xba000000, v16
	v_mul_f32_e32 v18, v51, v51
	v_mul_f32_e32 v19, v53, v53
	v_fmac_f32_e32 v18, v50, v50
	v_fmac_f32_e32 v19, v52, v52
	v_add_f32_e32 v18, v18, v19
	v_fmac_f32_e32 v49, 0xba000000, v16
	v_fmac_f32_e32 v47, 0xba000000, v16
	v_add_f32_e32 v17, v17, v18
	v_fmac_f32_e32 v48, 0xba000000, v16
	v_fmac_f32_e32 v46, 0xba000000, v16
	v_mul_f32_e32 v18, v47, v47
	v_mul_f32_e32 v19, v49, v49
	v_fmac_f32_e32 v18, v46, v46
	v_fmac_f32_e32 v19, v48, v48
	v_add_f32_e32 v18, v18, v19
	v_fmac_f32_e32 v43, 0xba000000, v16
	v_fmac_f32_e32 v41, 0xba000000, v16
	v_add_f32_e32 v17, v17, v18
	v_fmac_f32_e32 v42, 0xba000000, v16
	v_fmac_f32_e32 v40, 0xba000000, v16
	v_mul_f32_e32 v18, v41, v41
	v_mul_f32_e32 v19, v43, v43
	v_fmac_f32_e32 v18, v40, v40
	v_fmac_f32_e32 v19, v42, v42
	v_add_f32_e32 v18, v18, v19
	v_fmac_f32_e32 v37, 0xba000000, v16
	v_fmac_f32_e32 v39, 0xba000000, v16
	v_add_f32_e32 v17, v17, v18
	v_fmac_f32_e32 v36, 0xba000000, v16
	v_fmac_f32_e32 v38, 0xba000000, v16
	v_mul_f32_e32 v16, v39, v39
	v_mul_f32_e32 v18, v37, v37
	v_fmac_f32_e32 v16, v38, v38
	v_fmac_f32_e32 v18, v36, v36
	v_add_f32_e32 v16, v16, v18
	v_add_f32_e32 v16, v17, v16
	s_nop 1
	v_add_f32_dpp v16, v16, v16 quad_perm:[1,0,3,2] row_mask:0xf bank_mask:0xf bound_ctrl:1
	s_nop 1
	v_add_f32_dpp v16, v16, v16 quad_perm:[2,3,0,1] row_mask:0xf bank_mask:0xf bound_ctrl:1
	s_nop 1
	v_add_f32_dpp v16, v16, v16 row_ror:4 row_mask:0xf bank_mask:0xf bound_ctrl:1
	s_nop 1
	v_add_f32_dpp v16, v16, v16 row_ror:8 row_mask:0xf bank_mask:0xf bound_ctrl:1
	v_mov_b32_e32 v17, v16
	s_nop 1
	v_permlane16_swap_b32_e32 v16, v17
	v_add_f32_e32 v16, v16, v17
	v_mov_b32_e32 v17, v16
	s_nop 1
	v_permlane32_swap_b32_e32 v16, v17
	v_add_f32_e32 v16, v16, v17
	v_fmamk_f32 v16, v16, 0x3a000000, v207
	v_rsq_f32_e32 v44, v16
	s_nop 0
	v_pk_mul_f32 v[84:85], v[44:45], v[84:85] op_sel_hi:[0,1]
	v_pk_mul_f32 v[78:79], v[44:45], v[78:79] op_sel_hi:[0,1]
	v_pk_mul_f32 v[76:77], v[44:45], v[76:77] op_sel_hi:[0,1]
	v_pk_mul_f32 v[70:71], v[44:45], v[70:71] op_sel_hi:[0,1]
	v_pk_mul_f32 v[62:63], v[44:45], v[62:63] op_sel_hi:[0,1]
	v_pk_mul_f32 v[68:69], v[44:45], v[68:69] op_sel_hi:[0,1]
	v_pk_mul_f32 v[58:59], v[44:45], v[58:59] op_sel_hi:[0,1]
	v_pk_mul_f32 v[60:61], v[44:45], v[60:61] op_sel_hi:[0,1]
	v_pk_mul_f32 v[50:51], v[44:45], v[50:51] op_sel_hi:[0,1]
	v_pk_mul_f32 v[52:53], v[44:45], v[52:53] op_sel_hi:[0,1]
	v_mov_b32_e32 v45, 0
	s_waitcnt vmcnt(0) lgkmcnt(0)
	v_pk_fma_f32 v[128:129], v[160:161], v[78:79], v[200:201]
	v_pk_fma_f32 v[130:131], v[158:159], v[84:85], v[198:199]
	v_mov_b32_e32 v20, 0
	v_cvt_pk_bf16_f32 v16, v130, v131
	v_cvt_pk_bf16_f32 v17, v128, v129
	global_store_dwordx2 v[56:57], v[16:17], off nt
	v_med3_f32 v16, v130, s69, v208
	v_med3_f32 v17, v131, s69, v208
	v_cvt_pk_fp8_f32 v20, v16, v17
	v_med3_f32 v18, v128, s69, v208
	v_med3_f32 v19, v129, s69, v208
	v_cvt_pk_fp8_f32 v20, v18, v19 op_sel:[0,0,1]
	global_store_dword v[54:55], v20, off nt
	s_nop 0
	s_nop 0
	s_nop 0
	v_pk_fma_f32 v[104:105], v[164:165], v[70:71], v[204:205]
	v_pk_fma_f32 v[106:107], v[162:163], v[76:77], v[202:203]
	v_mov_b32_e32 v20, 0
	v_cvt_pk_bf16_f32 v16, v106, v107
	v_cvt_pk_bf16_f32 v17, v104, v105
	global_store_dwordx2 v[56:57], v[16:17], off offset:512 nt
	v_med3_f32 v16, v106, s69, v208
	v_med3_f32 v17, v107, s69, v208
	v_cvt_pk_fp8_f32 v20, v16, v17
	v_med3_f32 v18, v104, s69, v208
	v_med3_f32 v19, v105, s69, v208
	v_cvt_pk_fp8_f32 v20, v18, v19 op_sel:[0,0,1]
	global_store_dword v[54:55], v20, off offset:256 nt
	s_nop 0
	s_nop 0
	s_nop 0
	v_pk_fma_f32 v[96:97], v[168:169], v[68:69], v[218:219]
	v_pk_fma_f32 v[98:99], v[166:167], v[62:63], v[216:217]
	v_mov_b32_e32 v20, 0
	v_cvt_pk_bf16_f32 v16, v98, v99
	v_cvt_pk_bf16_f32 v17, v96, v97
	global_store_dwordx2 v[56:57], v[16:17], off offset:1024 nt
	v_med3_f32 v16, v98, s69, v208
	v_med3_f32 v17, v99, s69, v208
	v_cvt_pk_fp8_f32 v20, v16, v17
	v_med3_f32 v18, v96, s69, v208
	v_med3_f32 v19, v97, s69, v208
	v_cvt_pk_fp8_f32 v20, v18, v19 op_sel:[0,0,1]
	global_store_dword v[54:55], v20, off offset:512 nt
	s_nop 0
	s_nop 0
	s_nop 0
	v_pk_fma_f32 v[88:89], v[172:173], v[60:61], v[222:223]
	v_pk_fma_f32 v[90:91], v[170:171], v[58:59], v[220:221]
	v_mov_b32_e32 v20, 0
	v_cvt_pk_bf16_f32 v16, v90, v91
	v_cvt_pk_bf16_f32 v17, v88, v89
	global_store_dwordx2 v[56:57], v[16:17], off offset:1536 nt
	v_med3_f32 v16, v90, s69, v208
	v_med3_f32 v17, v91, s69, v208
	v_cvt_pk_fp8_f32 v20, v16, v17
	v_med3_f32 v18, v88, s69, v208
	v_med3_f32 v19, v89, s69, v208
	v_add_co_u32_e32 v16, vcc, s33, v100
	v_cvt_pk_fp8_f32 v20, v18, v19 op_sel:[0,0,1]
	s_nop 0
	v_addc_co_u32_e32 v17, vcc, 0, v101, vcc
	v_add_co_u32_e32 v18, vcc, s33, v86
	global_store_dword v[54:55], v20, off offset:768 nt
	s_nop 0
	v_addc_co_u32_e32 v19, vcc, 0, v87, vcc
	s_nop 0
	s_nop 0
	v_pk_fma_f32 v[84:85], v[176:177], v[52:53], v[226:227]
	v_pk_fma_f32 v[86:87], v[174:175], v[50:51], v[224:225]
	v_med3_f32 v22, v84, s69, v208
	v_cvt_pk_bf16_f32 v20, v86, v87
	v_cvt_pk_bf16_f32 v21, v84, v85
	global_store_dwordx2 v[56:57], v[20:21], off offset:2048 nt
	v_med3_f32 v20, v86, s69, v208
	v_med3_f32 v21, v87, s69, v208
	v_cvt_pk_fp8_f32 v45, v20, v21
	v_med3_f32 v23, v85, s69, v208
; #define LAS __attribute__((address_space(3)))
; __global__ void __launch_bounds__(NTHREADS, 2) hybrid_fwd(Args a) {
;     ...
;                     if (qp == 0) {
; #pragma unroll
;                         for (int q = 0; q < 2; ++q)
; #pragma unroll
;                             for (int j = 0; j < 8; ++j) raw[q][j] = __builtin_nontemporal_load((const u32x2*)(YB + (size_t)(v * 32 + wave + 8 * (2 + q)) * DM + j * 256 + lane * 4));
;                         __builtin_amdgcn_sched_barrier(0);
;                     }
;                     f32x2 y2[8][4];
; #pragma unroll
;                     for (int j = 0; j < 8; ++j)
; #pragma unroll
;                         for (int c = 0; c < 4; ++c) y2[j][c] = (f32x2){ya[j][c], yb[j][c]};
;                     f32x2 acc2[16];
; #pragma unroll
;                     for (int e = 0; e < 16; ++e) acc2[e] = (f32x2){0.f, 0.f};
; #pragma unroll
;                     for (int j = 0; j < 8; ++j) {
; #pragma unroll
;                         for (int e = 0; e < 16; ++e) { const f32x4 w = *(const LAS f32x4*)(rwT + e * 2052 + j * 256 + lane * 4);
;                             acc2[e] += y2[j][0] * (f32x2){w[0], w[0]}; acc2[e] += y2[j][1] * (f32x2){w[1], w[1]};
;                             acc2[e] += y2[j][2] * (f32x2){w[2], w[2]}; acc2[e] += y2[j][3] * (f32x2){w[3], w[3]}; }
	v_cvt_pk_fp8_f32 v45, v22, v23 op_sel:[0,0,1]
	global_store_dword v[54:55], v45, off offset:1024 nt
	s_nop 0
	v_pk_mul_f32 v[46:47], v[44:45], v[46:47] op_sel_hi:[0,1]
	v_pk_mul_f32 v[48:49], v[44:45], v[48:49] op_sel_hi:[0,1]
	v_mov_b32_e32 v45, 0
	s_nop 0
	v_pk_fma_f32 v[76:77], v[180:181], v[48:49], v[230:231]
	v_pk_fma_f32 v[78:79], v[178:179], v[46:47], v[228:229]
	v_med3_f32 v22, v76, s69, v208
	v_cvt_pk_bf16_f32 v20, v78, v79
	v_cvt_pk_bf16_f32 v21, v76, v77
	global_store_dwordx2 v[56:57], v[20:21], off offset:2560 nt
	v_med3_f32 v20, v78, s69, v208
	v_med3_f32 v21, v79, s69, v208
	v_cvt_pk_fp8_f32 v45, v20, v21
	v_med3_f32 v23, v77, s69, v208
	v_cvt_pk_fp8_f32 v45, v22, v23 op_sel:[0,0,1]
	global_store_dword v[54:55], v45, off offset:1280 nt
	s_nop 0
	v_pk_mul_f32 v[40:41], v[44:45], v[40:41] op_sel_hi:[0,1]
	v_pk_mul_f32 v[42:43], v[44:45], v[42:43] op_sel_hi:[0,1]
	v_pk_mul_f32 v[38:39], v[44:45], v[38:39] op_sel_hi:[0,1]
	v_pk_mul_f32 v[36:37], v[44:45], v[36:37] op_sel_hi:[0,1]
	s_nop 0
	v_pk_fma_f32 v[68:69], v[184:185], v[42:43], v[234:235]
	v_pk_fma_f32 v[70:71], v[182:183], v[40:41], v[232:233]
	v_mov_b32_e32 v40, 0
	v_cvt_pk_bf16_f32 v20, v70, v71
	v_cvt_pk_bf16_f32 v21, v68, v69
	global_store_dwordx2 v[56:57], v[20:21], off offset:3072 nt
	v_med3_f32 v20, v70, s69, v208
	v_med3_f32 v21, v71, s69, v208
	v_cvt_pk_fp8_f32 v40, v20, v21
	v_med3_f32 v22, v68, s69, v208
	v_med3_f32 v23, v69, s69, v208
	v_cvt_pk_fp8_f32 v40, v22, v23 op_sel:[0,0,1]
	global_store_dword v[54:55], v40, off offset:1536 nt
	s_nop 0
	s_nop 0
	s_nop 0
	v_pk_fma_f32 v[60:61], v[188:189], v[36:37], v[248:249]
	v_pk_fma_f32 v[62:63], v[186:187], v[38:39], v[246:247]
	v_mov_b32_e32 v20, 0
	v_cvt_pk_bf16_f32 v16, v62, v63
	v_cvt_pk_bf16_f32 v17, v60, v61
	global_store_dwordx2 v[56:57], v[16:17], off offset:3584 nt
	v_med3_f32 v16, v62, s69, v208
	v_med3_f32 v17, v63, s69, v208
	v_cvt_pk_fp8_f32 v20, v16, v17
	v_med3_f32 v18, v60, s69, v208
	v_med3_f32 v19, v61, s69, v208
	v_cvt_pk_fp8_f32 v20, v18, v19 op_sel:[0,0,1]
	global_store_dword v[54:55], v20, off offset:1792 nt
	s_ashr_i32 s39, s38, 31
	s_add_i32 s40, s6, 24
	s_lshl_b64 s[44:45], s[38:39], 12
	s_ashr_i32 s41, s40, 31
	v_lshl_add_u64 v[16:17], v[26:27], 0, s[44:45]
	s_lshl_b64 s[42:43], s[40:41], 12
	flat_load_dwordx2 v[58:59], v[16:17] nt
	flat_load_dwordx2 v[56:57], v[16:17] offset:512 nt
	flat_load_dwordx2 v[54:55], v[16:17] offset:1024 nt
	flat_load_dwordx2 v[52:53], v[16:17] offset:1536 nt
	flat_load_dwordx2 v[50:51], v[16:17] offset:2048 nt
	flat_load_dwordx2 v[48:49], v[16:17] offset:2560 nt
	flat_load_dwordx2 v[46:47], v[16:17] offset:3072 nt
	flat_load_dwordx2 v[44:45], v[16:17] offset:3584 nt
	v_lshl_add_u64 v[16:17], v[26:27], 0, s[42:43]
	flat_load_dwordx2 v[42:43], v[16:17] nt
	flat_load_dwordx2 v[40:41], v[16:17] offset:512 nt
	flat_load_dwordx2 v[38:39], v[16:17] offset:1024 nt
	flat_load_dwordx2 v[36:37], v[16:17] offset:1536 nt
	flat_load_dwordx2 v[22:23], v[16:17] offset:2048 nt
	flat_load_dwordx2 v[20:21], v[16:17] offset:2560 nt
	flat_load_dwordx2 v[18:19], v[16:17] offset:3072 nt
	s_nop 0
	flat_load_dwordx2 v[16:17], v[16:17] offset:3584 nt
	v_add_u32_e32 v238, 0x10000, v25
	ds_read_b128 v[158:161], v25 offset:0
	ds_read_b128 v[162:165], v25 offset:8208
	ds_read_b128 v[166:169], v25 offset:16416
	ds_read_b128 v[170:173], v25 offset:24624
	ds_read_b128 v[174:177], v25 offset:32832
	ds_read_b128 v[178:181], v25 offset:41040
	ds_read_b128 v[182:185], v25 offset:49248
	ds_read_b128 v[186:189], v25 offset:57456
	v_mov_b32_e32 v100, v94
	v_mov_b32_e32 v101, v90
	v_mov_b32_e32 v90, v95
	v_mov_b32_e32 v102, v92
	v_mov_b32_e32 v103, v88
	v_mov_b32_e32 v88, v93
	v_mov_b32_e32 v92, v114
	v_mov_b32_e32 v93, v86
	v_mov_b32_e32 v86, v115
	v_mov_b32_e32 v94, v112
	v_mov_b32_e32 v95, v84
	v_mov_b32_e32 v84, v113
	ds_read_b128 v[198:201], v238 offset:128
	v_mov_b32_e32 v136, v64
	v_mov_b32_e32 v137, v130
	v_mov_b32_e32 v130, v65
	v_mov_b32_e32 v108, v82
	v_mov_b32_e32 v109, v98
	v_mov_b32_e32 v98, v83
	v_mov_b32_e32 v82, v116
	v_mov_b32_e32 v83, v76
	v_mov_b32_e32 v76, v117
	s_waitcnt lgkmcnt(8)
	v_pk_fma_f32 v[116:117], v[136:137], v[158:159], 0 op_sel_hi:[1,0,0]
	v_mov_b32_e32 v138, v66
	v_mov_b32_e32 v139, v128
	v_pk_fma_f32 v[112:113], v[158:159], v[130:131], v[116:117] op_sel:[1,0,0]
	v_mov_b32_e32 v128, v67
	v_pk_fma_f32 v[112:113], v[160:161], v[138:139], v[112:113] op_sel_hi:[0,1,1]
	v_mov_b32_e32 v114, v161
	v_pk_fma_f32 v[112:113], v[114:115], v[128:129], v[112:113] op_sel_hi:[0,1,1]
	ds_read_b128 v[202:205], v238 offset:8336
	v_mov_b32_e32 v110, v80
	v_mov_b32_e32 v111, v96
	v_mov_b32_e32 v96, v81
	v_mov_b32_e32 v80, v118
	v_mov_b32_e32 v81, v78
	v_mov_b32_e32 v78, v119
	s_waitcnt lgkmcnt(8)
	v_pk_fma_f32 v[118:119], v[136:137], v[162:163], 0 op_sel_hi:[1,0,0]
	v_mov_b32_e32 v134, v74
	v_pk_fma_f32 v[114:115], v[162:163], v[130:131], v[118:119] op_sel:[1,0,0]
	v_mov_b32_e32 v135, v104
	v_pk_fma_f32 v[114:115], v[164:165], v[138:139], v[114:115] op_sel_hi:[0,1,1]
	v_mov_b32_e32 v116, v165
	v_pk_fma_f32 v[152:153], v[116:117], v[128:129], v[114:115] op_sel_hi:[0,1,1]
	ds_read_b128 v[216:219], v238 offset:16544
	v_mov_b32_e32 v104, v75
	v_mov_b32_e32 v74, v120
	v_mov_b32_e32 v75, v68
	v_mov_b32_e32 v68, v121
	s_waitcnt lgkmcnt(8)
	v_pk_fma_f32 v[118:119], v[136:137], v[166:167], 0 op_sel_hi:[1,0,0]
	v_mov_b32_e32 v132, v72
	v_pk_fma_f32 v[114:115], v[166:167], v[130:131], v[118:119] op_sel:[1,0,0]
	v_mov_b32_e32 v133, v106
	v_pk_fma_f32 v[114:115], v[168:169], v[138:139], v[114:115] op_sel_hi:[0,1,1]
	v_mov_b32_e32 v116, v169
	v_pk_fma_f32 v[154:155], v[116:117], v[128:129], v[114:115] op_sel_hi:[0,1,1]
	ds_read_b128 v[220:223], v238 offset:24752
	v_mov_b32_e32 v106, v73
	v_mov_b32_e32 v72, v122
	v_mov_b32_e32 v73, v70
	v_mov_b32_e32 v70, v123
	s_waitcnt lgkmcnt(8)
; #define LAS __attribute__((address_space(3)))
; __global__ void __launch_bounds__(NTHREADS, 2) hybrid_fwd(Args a) {
;     ...
;                     f32x2 y2[8][4];
; #pragma unroll
;                     for (int j = 0; j < 8; ++j)
; #pragma unroll
;                         for (int c = 0; c < 4; ++c) y2[j][c] = (f32x2){ya[j][c], yb[j][c]};
;                     f32x2 acc2[16];
; #pragma unroll
;                     for (int e = 0; e < 16; ++e) acc2[e] = (f32x2){0.f, 0.f};
; #pragma unroll
;                     for (int j = 0; j < 8; ++j) {
; #pragma unroll
;                         for (int e = 0; e < 16; ++e) { const f32x4 w = *(const LAS f32x4*)(rwT + e * 2052 + j * 256 + lane * 4);
;                             acc2[e] += y2[j][0] * (f32x2){w[0], w[0]}; acc2[e] += y2[j][1] * (f32x2){w[1], w[1]};
;                             acc2[e] += y2[j][2] * (f32x2){w[2], w[2]}; acc2[e] += y2[j][3] * (f32x2){w[3], w[3]}; }
;                         __builtin_amdgcn_sched_barrier(0);
;                     }
	v_pk_fma_f32 v[118:119], v[136:137], v[170:171], 0 op_sel_hi:[1,0,0]
	v_mov_b32_e32 v66, v124
	v_pk_fma_f32 v[114:115], v[170:171], v[130:131], v[118:119] op_sel:[1,0,0]
	v_mov_b32_e32 v67, v62
	v_pk_fma_f32 v[114:115], v[172:173], v[138:139], v[114:115] op_sel_hi:[0,1,1]
	v_mov_b32_e32 v116, v173
	v_pk_fma_f32 v[114:115], v[116:117], v[128:129], v[114:115] op_sel_hi:[0,1,1]
	ds_read_b128 v[224:227], v238 offset:32960
	v_mov_b32_e32 v62, v125
	v_mov_b32_e32 v64, v126
	v_mov_b32_e32 v65, v60
	v_mov_b32_e32 v60, v127
	s_waitcnt lgkmcnt(8)
	v_pk_fma_f32 v[120:121], v[136:137], v[174:175], 0 op_sel_hi:[1,0,0]
	s_nop 0
	v_pk_fma_f32 v[116:117], v[174:175], v[130:131], v[120:121] op_sel:[1,0,0]
	s_nop 0
	v_pk_fma_f32 v[116:117], v[176:177], v[138:139], v[116:117] op_sel_hi:[0,1,1]
	v_mov_b32_e32 v118, v177
	v_pk_fma_f32 v[116:117], v[118:119], v[128:129], v[116:117] op_sel_hi:[0,1,1]
	ds_read_b128 v[228:231], v238 offset:41168
	s_waitcnt lgkmcnt(8)
	v_pk_fma_f32 v[122:123], v[136:137], v[178:179], 0 op_sel_hi:[1,0,0]
	s_nop 0
	v_pk_fma_f32 v[118:119], v[178:179], v[130:131], v[122:123] op_sel:[1,0,0]
	s_nop 0
	v_pk_fma_f32 v[118:119], v[180:181], v[138:139], v[118:119] op_sel_hi:[0,1,1]
	v_mov_b32_e32 v120, v181
	v_pk_fma_f32 v[118:119], v[120:121], v[128:129], v[118:119] op_sel_hi:[0,1,1]
	ds_read_b128 v[232:235], v238 offset:49376
	s_waitcnt lgkmcnt(8)
	v_pk_fma_f32 v[124:125], v[136:137], v[182:183], 0 op_sel_hi:[1,0,0]
	s_nop 0
	v_pk_fma_f32 v[120:121], v[182:183], v[130:131], v[124:125] op_sel:[1,0,0]
	s_nop 0
	v_pk_fma_f32 v[120:121], v[184:185], v[138:139], v[120:121] op_sel_hi:[0,1,1]
	v_mov_b32_e32 v122, v185
	v_pk_fma_f32 v[120:121], v[122:123], v[128:129], v[120:121] op_sel_hi:[0,1,1]
	ds_read_b128 v[242:245], v238 offset:57584
	s_waitcnt lgkmcnt(8)
	v_pk_fma_f32 v[126:127], v[136:137], v[186:187], 0 op_sel_hi:[1,0,0]
	s_nop 0
	v_pk_fma_f32 v[122:123], v[186:187], v[130:131], v[126:127] op_sel:[1,0,0]
	s_nop 0
	v_pk_fma_f32 v[122:123], v[188:189], v[138:139], v[122:123] op_sel_hi:[0,1,1]
	v_mov_b32_e32 v124, v189
	v_pk_fma_f32 v[122:123], v[124:125], v[128:129], v[122:123] op_sel_hi:[0,1,1]
	ds_read_b128 v[246:249], v25 offset:1024
	s_waitcnt lgkmcnt(8)
	v_pk_fma_f32 v[140:141], v[136:137], v[198:199], 0 op_sel_hi:[1,0,0]
	s_nop 0
	v_pk_fma_f32 v[124:125], v[198:199], v[130:131], v[140:141] op_sel:[1,0,0]
	ds_read_b128 v[250:253], v25 offset:9232
	v_pk_fma_f32 v[124:125], v[200:201], v[138:139], v[124:125] op_sel_hi:[0,1,1]
	v_mov_b32_e32 v126, v201
	v_pk_fma_f32 v[124:125], v[126:127], v[128:129], v[124:125] op_sel_hi:[0,1,1]
	s_waitcnt lgkmcnt(8)
	v_pk_fma_f32 v[126:127], v[136:137], v[202:203], 0 op_sel_hi:[1,0,0]
	s_nop 0
	v_pk_fma_f32 v[126:127], v[202:203], v[130:131], v[126:127] op_sel:[1,0,0]
	v_mov_b32_e32 v140, v205
	v_pk_fma_f32 v[126:127], v[204:205], v[138:139], v[126:127] op_sel_hi:[0,1,1]
	v_pk_fma_f32 v[126:127], v[140:141], v[128:129], v[126:127] op_sel_hi:[0,1,1]
	ds_read_b128 v[158:161], v25 offset:17440
	s_waitcnt lgkmcnt(8)
	v_pk_fma_f32 v[144:145], v[136:137], v[216:217], 0 op_sel_hi:[1,0,0]
	s_nop 0
	v_pk_fma_f32 v[140:141], v[216:217], v[130:131], v[144:145] op_sel:[1,0,0]
	s_nop 0
	v_pk_fma_f32 v[140:141], v[218:219], v[138:139], v[140:141] op_sel_hi:[0,1,1]
	v_mov_b32_e32 v142, v219
	v_pk_fma_f32 v[140:141], v[142:143], v[128:129], v[140:141] op_sel_hi:[0,1,1]
	ds_read_b128 v[162:165], v25 offset:25648
	s_waitcnt lgkmcnt(8)
	v_pk_fma_f32 v[146:147], v[136:137], v[220:221], 0 op_sel_hi:[1,0,0]
	s_nop 0
	v_pk_fma_f32 v[142:143], v[220:221], v[130:131], v[146:147] op_sel:[1,0,0]
	s_nop 0
	v_pk_fma_f32 v[142:143], v[222:223], v[138:139], v[142:143] op_sel_hi:[0,1,1]
	v_mov_b32_e32 v144, v223
	v_pk_fma_f32 v[142:143], v[144:145], v[128:129], v[142:143] op_sel_hi:[0,1,1]
	ds_read_b128 v[166:169], v25 offset:33856
	s_waitcnt lgkmcnt(8)
	v_pk_fma_f32 v[148:149], v[136:137], v[224:225], 0 op_sel_hi:[1,0,0]
	s_nop 0
	v_pk_fma_f32 v[144:145], v[224:225], v[130:131], v[148:149] op_sel:[1,0,0]
	s_nop 0
	v_pk_fma_f32 v[144:145], v[226:227], v[138:139], v[144:145] op_sel_hi:[0,1,1]
	v_mov_b32_e32 v146, v227
	v_pk_fma_f32 v[144:145], v[146:147], v[128:129], v[144:145] op_sel_hi:[0,1,1]
	ds_read_b128 v[170:173], v25 offset:42064
	s_waitcnt lgkmcnt(8)
	v_pk_fma_f32 v[150:151], v[136:137], v[228:229], 0 op_sel_hi:[1,0,0]
	s_nop 0
	v_pk_fma_f32 v[146:147], v[228:229], v[130:131], v[150:151] op_sel:[1,0,0]
	s_nop 0
	v_pk_fma_f32 v[146:147], v[230:231], v[138:139], v[146:147] op_sel_hi:[0,1,1]
	v_mov_b32_e32 v148, v231
	v_pk_fma_f32 v[146:147], v[148:149], v[128:129], v[146:147] op_sel_hi:[0,1,1]
	ds_read_b128 v[174:177], v25 offset:50272
	s_waitcnt lgkmcnt(8)
	v_pk_fma_f32 v[194:195], v[136:137], v[232:233], 0 op_sel_hi:[1,0,0]
	s_nop 0
	v_pk_fma_f32 v[148:149], v[232:233], v[130:131], v[194:195] op_sel:[1,0,0]
	ds_read_b128 v[178:181], v25 offset:58480
	v_pk_fma_f32 v[148:149], v[234:235], v[138:139], v[148:149] op_sel_hi:[0,1,1]
	v_mov_b32_e32 v150, v235
	v_pk_fma_f32 v[148:149], v[150:151], v[128:129], v[148:149] op_sel_hi:[0,1,1]
	s_waitcnt lgkmcnt(8)
	v_pk_fma_f32 v[136:137], v[136:137], v[242:243], 0 op_sel_hi:[1,0,0]
	s_nop 0
	v_pk_fma_f32 v[130:131], v[242:243], v[130:131], v[136:137] op_sel:[1,0,0]
	v_mov_b32_e32 v136, v245
	v_pk_fma_f32 v[130:131], v[244:245], v[138:139], v[130:131] op_sel_hi:[0,1,1]
	v_pk_fma_f32 v[150:151], v[136:137], v[128:129], v[130:131] op_sel_hi:[0,1,1]
	ds_read_b128 v[182:185], v238 offset:1152
	s_waitcnt lgkmcnt(8)
; #define LAS __attribute__((address_space(3)))
; __global__ void __launch_bounds__(NTHREADS, 2) hybrid_fwd(Args a) {
;     ...
;                     f32x2 y2[8][4];
; #pragma unroll
;                     for (int j = 0; j < 8; ++j)
; #pragma unroll
;                         for (int c = 0; c < 4; ++c) y2[j][c] = (f32x2){ya[j][c], yb[j][c]};
;                     f32x2 acc2[16];
; #pragma unroll
;                     for (int e = 0; e < 16; ++e) acc2[e] = (f32x2){0.f, 0.f};
; #pragma unroll
;                     for (int j = 0; j < 8; ++j) {
; #pragma unroll
;                         for (int e = 0; e < 16; ++e) { const f32x4 w = *(const LAS f32x4*)(rwT + e * 2052 + j * 256 + lane * 4);
;                             acc2[e] += y2[j][0] * (f32x2){w[0], w[0]}; acc2[e] += y2[j][1] * (f32x2){w[1], w[1]};
;                             acc2[e] += y2[j][2] * (f32x2){w[2], w[2]}; acc2[e] += y2[j][3] * (f32x2){w[3], w[3]}; }
;                         __builtin_amdgcn_sched_barrier(0);
;                     }
	v_pk_fma_f32 v[112:113], v[132:133], v[246:247], v[112:113] op_sel_hi:[1,0,1]
	s_nop 0
	v_pk_fma_f32 v[112:113], v[246:247], v[106:107], v[112:113] op_sel:[1,0,0]
	v_mov_b32_e32 v128, v249
	v_pk_fma_f32 v[112:113], v[248:249], v[134:135], v[112:113] op_sel_hi:[0,1,1]
	v_pk_fma_f32 v[112:113], v[128:129], v[104:105], v[112:113] op_sel_hi:[0,1,1]
	ds_read_b128 v[186:189], v238 offset:9360
	s_waitcnt lgkmcnt(8)
	v_pk_fma_f32 v[136:137], v[132:133], v[250:251], v[152:153] op_sel_hi:[1,0,1]
	s_nop 0
	v_pk_fma_f32 v[128:129], v[250:251], v[106:107], v[136:137] op_sel:[1,0,0]
	s_nop 0
	v_pk_fma_f32 v[128:129], v[252:253], v[134:135], v[128:129] op_sel_hi:[0,1,1]
	v_mov_b32_e32 v130, v253
	v_pk_fma_f32 v[152:153], v[130:131], v[104:105], v[128:129] op_sel_hi:[0,1,1]
	ds_read_b128 v[198:201], v238 offset:17568
	s_waitcnt lgkmcnt(8)
	v_pk_fma_f32 v[136:137], v[132:133], v[158:159], v[154:155] op_sel_hi:[1,0,1]
	s_nop 0
	v_pk_fma_f32 v[128:129], v[158:159], v[106:107], v[136:137] op_sel:[1,0,0]
	ds_read_b128 v[202:205], v238 offset:25776
	v_pk_fma_f32 v[128:129], v[160:161], v[134:135], v[128:129] op_sel_hi:[0,1,1]
	v_mov_b32_e32 v130, v161
	v_pk_fma_f32 v[128:129], v[130:131], v[104:105], v[128:129] op_sel_hi:[0,1,1]
	s_waitcnt lgkmcnt(8)
	v_pk_fma_f32 v[114:115], v[132:133], v[162:163], v[114:115] op_sel_hi:[1,0,1]
	s_nop 0
	v_pk_fma_f32 v[114:115], v[162:163], v[106:107], v[114:115] op_sel:[1,0,0]
	v_mov_b32_e32 v130, v165
	v_pk_fma_f32 v[114:115], v[164:165], v[134:135], v[114:115] op_sel_hi:[0,1,1]
	ds_read_b128 v[216:219], v238 offset:33984
	v_pk_fma_f32 v[114:115], v[130:131], v[104:105], v[114:115] op_sel_hi:[0,1,1]
	s_waitcnt lgkmcnt(8)
	v_pk_fma_f32 v[116:117], v[132:133], v[166:167], v[116:117] op_sel_hi:[1,0,1]
	s_nop 0
	v_pk_fma_f32 v[116:117], v[166:167], v[106:107], v[116:117] op_sel:[1,0,0]
	v_mov_b32_e32 v130, v169
	v_pk_fma_f32 v[116:117], v[168:169], v[134:135], v[116:117] op_sel_hi:[0,1,1]
	ds_read_b128 v[220:223], v238 offset:42192
	v_pk_fma_f32 v[116:117], v[130:131], v[104:105], v[116:117] op_sel_hi:[0,1,1]
	s_waitcnt lgkmcnt(8)
	v_pk_fma_f32 v[118:119], v[132:133], v[170:171], v[118:119] op_sel_hi:[1,0,1]
	s_nop 0
	v_pk_fma_f32 v[118:119], v[170:171], v[106:107], v[118:119] op_sel:[1,0,0]
	v_mov_b32_e32 v130, v173
	v_pk_fma_f32 v[118:119], v[172:173], v[134:135], v[118:119] op_sel_hi:[0,1,1]
	ds_read_b128 v[224:227], v238 offset:50400
	v_pk_fma_f32 v[118:119], v[130:131], v[104:105], v[118:119] op_sel_hi:[0,1,1]
	s_waitcnt lgkmcnt(8)
	v_pk_fma_f32 v[120:121], v[132:133], v[174:175], v[120:121] op_sel_hi:[1,0,1]
	s_nop 0
	v_pk_fma_f32 v[120:121], v[174:175], v[106:107], v[120:121] op_sel:[1,0,0]
	v_mov_b32_e32 v130, v177
	v_pk_fma_f32 v[120:121], v[176:177], v[134:135], v[120:121] op_sel_hi:[0,1,1]
	ds_read_b128 v[228:231], v238 offset:58608
	v_pk_fma_f32 v[120:121], v[130:131], v[104:105], v[120:121] op_sel_hi:[0,1,1]
	s_waitcnt lgkmcnt(8)
	v_pk_fma_f32 v[122:123], v[132:133], v[178:179], v[122:123] op_sel_hi:[1,0,1]
	s_nop 0
	v_pk_fma_f32 v[122:123], v[178:179], v[106:107], v[122:123] op_sel:[1,0,0]
	v_mov_b32_e32 v130, v181
	v_pk_fma_f32 v[122:123], v[180:181], v[134:135], v[122:123] op_sel_hi:[0,1,1]
	ds_read_b128 v[232:235], v25 offset:2048
	v_pk_fma_f32 v[122:123], v[130:131], v[104:105], v[122:123] op_sel_hi:[0,1,1]
	s_waitcnt lgkmcnt(8)
	v_pk_fma_f32 v[124:125], v[132:133], v[182:183], v[124:125] op_sel_hi:[1,0,1]
	s_nop 0
	v_pk_fma_f32 v[124:125], v[182:183], v[106:107], v[124:125] op_sel:[1,0,0]
	v_mov_b32_e32 v130, v185
	v_pk_fma_f32 v[124:125], v[184:185], v[134:135], v[124:125] op_sel_hi:[0,1,1]
	ds_read_b128 v[242:245], v25 offset:10256
	v_pk_fma_f32 v[124:125], v[130:131], v[104:105], v[124:125] op_sel_hi:[0,1,1]
	s_waitcnt lgkmcnt(8)
	v_pk_fma_f32 v[126:127], v[132:133], v[186:187], v[126:127] op_sel_hi:[1,0,1]
	s_nop 0
	v_pk_fma_f32 v[126:127], v[186:187], v[106:107], v[126:127] op_sel:[1,0,0]
	v_mov_b32_e32 v130, v189
	v_pk_fma_f32 v[126:127], v[188:189], v[134:135], v[126:127] op_sel_hi:[0,1,1]
	ds_read_b128 v[246:249], v25 offset:18464
	v_pk_fma_f32 v[126:127], v[130:131], v[104:105], v[126:127] op_sel_hi:[0,1,1]
	s_waitcnt lgkmcnt(8)
	v_pk_fma_f32 v[130:131], v[132:133], v[198:199], v[140:141] op_sel_hi:[1,0,1]
	s_nop 0
	v_pk_fma_f32 v[130:131], v[198:199], v[106:107], v[130:131] op_sel:[1,0,0]
	v_mov_b32_e32 v136, v201
	v_pk_fma_f32 v[130:131], v[200:201], v[134:135], v[130:131] op_sel_hi:[0,1,1]
	v_pk_fma_f32 v[130:131], v[136:137], v[104:105], v[130:131] op_sel_hi:[0,1,1]
	ds_read_b128 v[250:253], v25 offset:26672
	s_waitcnt lgkmcnt(8)
	v_pk_fma_f32 v[140:141], v[132:133], v[202:203], v[142:143] op_sel_hi:[1,0,1]
	s_nop 0
	v_pk_fma_f32 v[136:137], v[202:203], v[106:107], v[140:141] op_sel:[1,0,0]
	s_nop 0
	v_pk_fma_f32 v[136:137], v[204:205], v[134:135], v[136:137] op_sel_hi:[0,1,1]
	v_mov_b32_e32 v138, v205
	v_pk_fma_f32 v[136:137], v[138:139], v[104:105], v[136:137] op_sel_hi:[0,1,1]
	ds_read_b128 v[162:165], v25 offset:34880
	s_waitcnt lgkmcnt(8)
	v_pk_fma_f32 v[142:143], v[132:133], v[216:217], v[144:145] op_sel_hi:[1,0,1]
	s_nop 0
	v_pk_fma_f32 v[138:139], v[216:217], v[106:107], v[142:143] op_sel:[1,0,0]
	s_nop 0
	v_pk_fma_f32 v[138:139], v[218:219], v[134:135], v[138:139] op_sel_hi:[0,1,1]
	v_mov_b32_e32 v140, v219
	v_pk_fma_f32 v[138:139], v[140:141], v[104:105], v[138:139] op_sel_hi:[0,1,1]
	ds_read_b128 v[166:169], v25 offset:43088
	s_waitcnt lgkmcnt(8)
	v_pk_fma_f32 v[144:145], v[132:133], v[220:221], v[146:147] op_sel_hi:[1,0,1]
	s_nop 0
	v_pk_fma_f32 v[140:141], v[220:221], v[106:107], v[144:145] op_sel:[1,0,0]
	s_nop 0
	v_pk_fma_f32 v[140:141], v[222:223], v[134:135], v[140:141] op_sel_hi:[0,1,1]
	v_mov_b32_e32 v142, v223
	v_pk_fma_f32 v[140:141], v[142:143], v[104:105], v[140:141] op_sel_hi:[0,1,1]
	ds_read_b128 v[170:173], v25 offset:51296
	s_waitcnt lgkmcnt(8)
; #define LAS __attribute__((address_space(3)))
; __global__ void __launch_bounds__(NTHREADS, 2) hybrid_fwd(Args a) {
;     ...
;                     f32x2 y2[8][4];
; #pragma unroll
;                     for (int j = 0; j < 8; ++j)
; #pragma unroll
;                         for (int c = 0; c < 4; ++c) y2[j][c] = (f32x2){ya[j][c], yb[j][c]};
;                     f32x2 acc2[16];
; #pragma unroll
;                     for (int e = 0; e < 16; ++e) acc2[e] = (f32x2){0.f, 0.f};
; #pragma unroll
;                     for (int j = 0; j < 8; ++j) {
; #pragma unroll
;                         for (int e = 0; e < 16; ++e) { const f32x4 w = *(const LAS f32x4*)(rwT + e * 2052 + j * 256 + lane * 4);
;                             acc2[e] += y2[j][0] * (f32x2){w[0], w[0]}; acc2[e] += y2[j][1] * (f32x2){w[1], w[1]};
;                             acc2[e] += y2[j][2] * (f32x2){w[2], w[2]}; acc2[e] += y2[j][3] * (f32x2){w[3], w[3]}; }
;                         __builtin_amdgcn_sched_barrier(0);
;                     }
	v_pk_fma_f32 v[146:147], v[132:133], v[224:225], v[148:149] op_sel_hi:[1,0,1]
	s_nop 0
	v_pk_fma_f32 v[142:143], v[224:225], v[106:107], v[146:147] op_sel:[1,0,0]
	s_nop 0
	v_pk_fma_f32 v[142:143], v[226:227], v[134:135], v[142:143] op_sel_hi:[0,1,1]
	v_mov_b32_e32 v144, v227
	v_pk_fma_f32 v[142:143], v[144:145], v[104:105], v[142:143] op_sel_hi:[0,1,1]
	ds_read_b128 v[174:177], v25 offset:59504
	s_waitcnt lgkmcnt(8)
	v_pk_fma_f32 v[132:133], v[132:133], v[228:229], v[150:151] op_sel_hi:[1,0,1]
	s_nop 0
	v_pk_fma_f32 v[106:107], v[228:229], v[106:107], v[132:133] op_sel:[1,0,0]
	v_mov_b32_e32 v132, v231
	v_pk_fma_f32 v[106:107], v[230:231], v[134:135], v[106:107] op_sel_hi:[0,1,1]
	v_pk_fma_f32 v[144:145], v[132:133], v[104:105], v[106:107] op_sel_hi:[0,1,1]
	ds_read_b128 v[178:181], v238 offset:2176
	ds_read_b128 v[182:185], v238 offset:10384
	s_waitcnt lgkmcnt(8)
	v_pk_fma_f32 v[112:113], v[108:109], v[232:233], v[112:113] op_sel_hi:[1,0,1]
	s_nop 0
	v_pk_fma_f32 v[104:105], v[232:233], v[98:99], v[112:113] op_sel:[1,0,0]
	v_mov_b32_e32 v112, v245
	v_pk_fma_f32 v[104:105], v[234:235], v[110:111], v[104:105] op_sel_hi:[0,1,1]
	v_mov_b32_e32 v106, v235
	v_pk_fma_f32 v[104:105], v[106:107], v[96:97], v[104:105] op_sel_hi:[0,1,1]
	v_pk_fma_f32 v[106:107], v[108:109], v[242:243], v[152:153] op_sel_hi:[1,0,1]
	s_nop 0
	v_pk_fma_f32 v[106:107], v[242:243], v[98:99], v[106:107] op_sel:[1,0,0]
	s_nop 0
	v_pk_fma_f32 v[106:107], v[244:245], v[110:111], v[106:107] op_sel_hi:[0,1,1]
	ds_read_b128 v[186:189], v238 offset:18592
	v_pk_fma_f32 v[146:147], v[112:113], v[96:97], v[106:107] op_sel_hi:[0,1,1]
	s_waitcnt lgkmcnt(8)
	v_pk_fma_f32 v[106:107], v[108:109], v[246:247], v[128:129] op_sel_hi:[1,0,1]
	s_nop 0
	v_pk_fma_f32 v[106:107], v[246:247], v[98:99], v[106:107] op_sel:[1,0,0]
	v_mov_b32_e32 v112, v249
	v_pk_fma_f32 v[106:107], v[248:249], v[110:111], v[106:107] op_sel_hi:[0,1,1]
	ds_read_b128 v[158:161], v238 offset:26800
	v_pk_fma_f32 v[106:107], v[112:113], v[96:97], v[106:107] op_sel_hi:[0,1,1]
	s_waitcnt lgkmcnt(8)
	v_pk_fma_f32 v[112:113], v[108:109], v[250:251], v[114:115] op_sel_hi:[1,0,1]
	s_nop 0
	v_pk_fma_f32 v[112:113], v[250:251], v[98:99], v[112:113] op_sel:[1,0,0]
	v_mov_b32_e32 v114, v253
	v_pk_fma_f32 v[112:113], v[252:253], v[110:111], v[112:113] op_sel_hi:[0,1,1]
	ds_read_b128 v[198:201], v238 offset:35008
	v_pk_fma_f32 v[112:113], v[114:115], v[96:97], v[112:113] op_sel_hi:[0,1,1]
	s_waitcnt lgkmcnt(8)
	v_pk_fma_f32 v[114:115], v[108:109], v[162:163], v[116:117] op_sel_hi:[1,0,1]
	s_nop 0
	v_pk_fma_f32 v[114:115], v[162:163], v[98:99], v[114:115] op_sel:[1,0,0]
	v_mov_b32_e32 v116, v165
	v_pk_fma_f32 v[114:115], v[164:165], v[110:111], v[114:115] op_sel_hi:[0,1,1]
	ds_read_b128 v[202:205], v238 offset:43216
	v_pk_fma_f32 v[114:115], v[116:117], v[96:97], v[114:115] op_sel_hi:[0,1,1]
	s_waitcnt lgkmcnt(8)
	v_pk_fma_f32 v[116:117], v[108:109], v[166:167], v[118:119] op_sel_hi:[1,0,1]
	s_nop 0
	v_pk_fma_f32 v[116:117], v[166:167], v[98:99], v[116:117] op_sel:[1,0,0]
	v_mov_b32_e32 v118, v169
	v_pk_fma_f32 v[116:117], v[168:169], v[110:111], v[116:117] op_sel_hi:[0,1,1]
	ds_read_b128 v[216:219], v238 offset:51424
	v_pk_fma_f32 v[116:117], v[118:119], v[96:97], v[116:117] op_sel_hi:[0,1,1]
	s_waitcnt lgkmcnt(8)
	v_pk_fma_f32 v[118:119], v[108:109], v[170:171], v[120:121] op_sel_hi:[1,0,1]
	s_nop 0
	v_pk_fma_f32 v[118:119], v[170:171], v[98:99], v[118:119] op_sel:[1,0,0]
	v_mov_b32_e32 v120, v173
	v_pk_fma_f32 v[118:119], v[172:173], v[110:111], v[118:119] op_sel_hi:[0,1,1]
	ds_read_b128 v[220:223], v238 offset:59632
	v_pk_fma_f32 v[118:119], v[120:121], v[96:97], v[118:119] op_sel_hi:[0,1,1]
	s_waitcnt lgkmcnt(8)
	v_pk_fma_f32 v[120:121], v[108:109], v[174:175], v[122:123] op_sel_hi:[1,0,1]
	s_nop 0
	v_pk_fma_f32 v[120:121], v[174:175], v[98:99], v[120:121] op_sel:[1,0,0]
	v_mov_b32_e32 v122, v177
	v_pk_fma_f32 v[120:121], v[176:177], v[110:111], v[120:121] op_sel_hi:[0,1,1]
	ds_read_b128 v[224:227], v25 offset:3072
	v_pk_fma_f32 v[120:121], v[122:123], v[96:97], v[120:121] op_sel_hi:[0,1,1]
	s_waitcnt lgkmcnt(8)
	v_pk_fma_f32 v[122:123], v[108:109], v[178:179], v[124:125] op_sel_hi:[1,0,1]
	s_nop 0
	v_pk_fma_f32 v[122:123], v[178:179], v[98:99], v[122:123] op_sel:[1,0,0]
	v_mov_b32_e32 v124, v181
	v_pk_fma_f32 v[122:123], v[180:181], v[110:111], v[122:123] op_sel_hi:[0,1,1]
	ds_read_b128 v[228:231], v25 offset:11280
	v_pk_fma_f32 v[122:123], v[124:125], v[96:97], v[122:123] op_sel_hi:[0,1,1]
	s_waitcnt lgkmcnt(8)
	v_pk_fma_f32 v[124:125], v[108:109], v[182:183], v[126:127] op_sel_hi:[1,0,1]
	s_nop 0
	v_pk_fma_f32 v[124:125], v[182:183], v[98:99], v[124:125] op_sel:[1,0,0]
	v_mov_b32_e32 v126, v185
	v_pk_fma_f32 v[124:125], v[184:185], v[110:111], v[124:125] op_sel_hi:[0,1,1]
	v_pk_fma_f32 v[124:125], v[126:127], v[96:97], v[124:125] op_sel_hi:[0,1,1]
	ds_read_b128 v[232:235], v25 offset:19488
	s_waitcnt lgkmcnt(8)
	v_pk_fma_f32 v[130:131], v[108:109], v[186:187], v[130:131] op_sel_hi:[1,0,1]
	s_nop 0
	v_pk_fma_f32 v[126:127], v[186:187], v[98:99], v[130:131] op_sel:[1,0,0]
	s_nop 0
	v_pk_fma_f32 v[126:127], v[188:189], v[110:111], v[126:127] op_sel_hi:[0,1,1]
	v_mov_b32_e32 v128, v189
	v_pk_fma_f32 v[126:127], v[128:129], v[96:97], v[126:127] op_sel_hi:[0,1,1]
	ds_read_b128 v[242:245], v25 offset:27696
	s_waitcnt lgkmcnt(8)
	v_pk_fma_f32 v[132:133], v[108:109], v[158:159], v[136:137] op_sel_hi:[1,0,1]
	s_nop 0
	v_pk_fma_f32 v[128:129], v[158:159], v[98:99], v[132:133] op_sel:[1,0,0]
	s_nop 0
	v_pk_fma_f32 v[128:129], v[160:161], v[110:111], v[128:129] op_sel_hi:[0,1,1]
	v_mov_b32_e32 v130, v161
	v_pk_fma_f32 v[128:129], v[130:131], v[96:97], v[128:129] op_sel_hi:[0,1,1]
	ds_read_b128 v[246:249], v25 offset:35904
	s_waitcnt lgkmcnt(8)
; #define LAS __attribute__((address_space(3)))
; __global__ void __launch_bounds__(NTHREADS, 2) hybrid_fwd(Args a) {
;     ...
;                     f32x2 y2[8][4];
; #pragma unroll
;                     for (int j = 0; j < 8; ++j)
; #pragma unroll
;                         for (int c = 0; c < 4; ++c) y2[j][c] = (f32x2){ya[j][c], yb[j][c]};
;                     f32x2 acc2[16];
; #pragma unroll
;                     for (int e = 0; e < 16; ++e) acc2[e] = (f32x2){0.f, 0.f};
; #pragma unroll
;                     for (int j = 0; j < 8; ++j) {
; #pragma unroll
;                         for (int e = 0; e < 16; ++e) { const f32x4 w = *(const LAS f32x4*)(rwT + e * 2052 + j * 256 + lane * 4);
;                             acc2[e] += y2[j][0] * (f32x2){w[0], w[0]}; acc2[e] += y2[j][1] * (f32x2){w[1], w[1]};
;                             acc2[e] += y2[j][2] * (f32x2){w[2], w[2]}; acc2[e] += y2[j][3] * (f32x2){w[3], w[3]}; }
;                         __builtin_amdgcn_sched_barrier(0);
;                     }
	v_pk_fma_f32 v[134:135], v[108:109], v[198:199], v[138:139] op_sel_hi:[1,0,1]
	s_nop 0
	v_pk_fma_f32 v[130:131], v[198:199], v[98:99], v[134:135] op_sel:[1,0,0]
	s_nop 0
	v_pk_fma_f32 v[130:131], v[200:201], v[110:111], v[130:131] op_sel_hi:[0,1,1]
	v_mov_b32_e32 v132, v201
	v_pk_fma_f32 v[130:131], v[132:133], v[96:97], v[130:131] op_sel_hi:[0,1,1]
	ds_read_b128 v[250:253], v25 offset:44112
	s_waitcnt lgkmcnt(8)
	v_pk_fma_f32 v[136:137], v[108:109], v[202:203], v[140:141] op_sel_hi:[1,0,1]
	s_nop 0
	v_pk_fma_f32 v[132:133], v[202:203], v[98:99], v[136:137] op_sel:[1,0,0]
	s_nop 0
	v_pk_fma_f32 v[132:133], v[204:205], v[110:111], v[132:133] op_sel_hi:[0,1,1]
	v_mov_b32_e32 v134, v205
	v_pk_fma_f32 v[132:133], v[134:135], v[96:97], v[132:133] op_sel_hi:[0,1,1]
	ds_read_b128 v[162:165], v25 offset:52320
	s_waitcnt lgkmcnt(8)
	v_pk_fma_f32 v[138:139], v[108:109], v[216:217], v[142:143] op_sel_hi:[1,0,1]
	s_nop 0
	v_pk_fma_f32 v[134:135], v[216:217], v[98:99], v[138:139] op_sel:[1,0,0]
	s_nop 0
	v_pk_fma_f32 v[134:135], v[218:219], v[110:111], v[134:135] op_sel_hi:[0,1,1]
	v_mov_b32_e32 v136, v219
	v_pk_fma_f32 v[134:135], v[136:137], v[96:97], v[134:135] op_sel_hi:[0,1,1]
	ds_read_b128 v[166:169], v25 offset:60528
	s_waitcnt lgkmcnt(8)
	v_pk_fma_f32 v[108:109], v[108:109], v[220:221], v[144:145] op_sel_hi:[1,0,1]
	s_nop 0
	v_pk_fma_f32 v[98:99], v[220:221], v[98:99], v[108:109] op_sel:[1,0,0]
	v_mov_b32_e32 v108, v223
	v_pk_fma_f32 v[98:99], v[222:223], v[110:111], v[98:99] op_sel_hi:[0,1,1]
	v_pk_fma_f32 v[136:137], v[108:109], v[96:97], v[98:99] op_sel_hi:[0,1,1]
	ds_read_b128 v[170:173], v238 offset:3200
	ds_read_b128 v[174:177], v238 offset:11408
	s_waitcnt lgkmcnt(8)
	v_pk_fma_f32 v[104:105], v[100:101], v[224:225], v[104:105] op_sel_hi:[1,0,1]
	s_nop 0
	v_pk_fma_f32 v[96:97], v[224:225], v[90:91], v[104:105] op_sel:[1,0,0]
	v_mov_b32_e32 v104, v231
	v_pk_fma_f32 v[96:97], v[226:227], v[102:103], v[96:97] op_sel_hi:[0,1,1]
	v_mov_b32_e32 v98, v227
	v_pk_fma_f32 v[96:97], v[98:99], v[88:89], v[96:97] op_sel_hi:[0,1,1]
	v_pk_fma_f32 v[98:99], v[100:101], v[228:229], v[146:147] op_sel_hi:[1,0,1]
	s_nop 0
	v_pk_fma_f32 v[98:99], v[228:229], v[90:91], v[98:99] op_sel:[1,0,0]
	s_nop 0
	v_pk_fma_f32 v[98:99], v[230:231], v[102:103], v[98:99] op_sel_hi:[0,1,1]
	ds_read_b128 v[178:181], v238 offset:19616
	v_pk_fma_f32 v[138:139], v[104:105], v[88:89], v[98:99] op_sel_hi:[0,1,1]
	s_waitcnt lgkmcnt(8)
	v_pk_fma_f32 v[98:99], v[100:101], v[232:233], v[106:107] op_sel_hi:[1,0,1]
	s_nop 0
	v_pk_fma_f32 v[98:99], v[232:233], v[90:91], v[98:99] op_sel:[1,0,0]
	v_mov_b32_e32 v104, v235
	v_pk_fma_f32 v[98:99], v[234:235], v[102:103], v[98:99] op_sel_hi:[0,1,1]
	v_pk_fma_f32 v[98:99], v[104:105], v[88:89], v[98:99] op_sel_hi:[0,1,1]
	ds_read_b128 v[182:185], v238 offset:27824
	s_waitcnt lgkmcnt(8)
	v_pk_fma_f32 v[108:109], v[100:101], v[242:243], v[112:113] op_sel_hi:[1,0,1]
	s_nop 0
	v_pk_fma_f32 v[104:105], v[242:243], v[90:91], v[108:109] op_sel:[1,0,0]
	s_nop 0
	v_pk_fma_f32 v[104:105], v[244:245], v[102:103], v[104:105] op_sel_hi:[0,1,1]
	v_mov_b32_e32 v106, v245
	v_pk_fma_f32 v[104:105], v[106:107], v[88:89], v[104:105] op_sel_hi:[0,1,1]
	ds_read_b128 v[186:189], v238 offset:36032
	s_waitcnt lgkmcnt(8)
	v_pk_fma_f32 v[110:111], v[100:101], v[246:247], v[114:115] op_sel_hi:[1,0,1]
	s_nop 0
	v_pk_fma_f32 v[106:107], v[246:247], v[90:91], v[110:111] op_sel:[1,0,0]
	s_nop 0
	v_pk_fma_f32 v[106:107], v[248:249], v[102:103], v[106:107] op_sel_hi:[0,1,1]
	v_mov_b32_e32 v108, v249
	v_pk_fma_f32 v[106:107], v[108:109], v[88:89], v[106:107] op_sel_hi:[0,1,1]
	ds_read_b128 v[158:161], v238 offset:44240
	s_waitcnt lgkmcnt(8)
	v_pk_fma_f32 v[112:113], v[100:101], v[250:251], v[116:117] op_sel_hi:[1,0,1]
	s_nop 0
	v_pk_fma_f32 v[108:109], v[250:251], v[90:91], v[112:113] op_sel:[1,0,0]
	s_nop 0
	v_pk_fma_f32 v[108:109], v[252:253], v[102:103], v[108:109] op_sel_hi:[0,1,1]
	v_mov_b32_e32 v110, v253
	v_pk_fma_f32 v[108:109], v[110:111], v[88:89], v[108:109] op_sel_hi:[0,1,1]
	ds_read_b128 v[198:201], v238 offset:52448
	s_waitcnt lgkmcnt(8)
	v_pk_fma_f32 v[114:115], v[100:101], v[162:163], v[118:119] op_sel_hi:[1,0,1]
	s_nop 0
	v_pk_fma_f32 v[110:111], v[162:163], v[90:91], v[114:115] op_sel:[1,0,0]
	s_nop 0
	v_pk_fma_f32 v[110:111], v[164:165], v[102:103], v[110:111] op_sel_hi:[0,1,1]
	v_mov_b32_e32 v112, v165
	v_pk_fma_f32 v[110:111], v[112:113], v[88:89], v[110:111] op_sel_hi:[0,1,1]
	ds_read_b128 v[202:205], v238 offset:60656
	s_waitcnt lgkmcnt(8)
	v_pk_fma_f32 v[116:117], v[100:101], v[166:167], v[120:121] op_sel_hi:[1,0,1]
	s_nop 0
	v_pk_fma_f32 v[112:113], v[166:167], v[90:91], v[116:117] op_sel:[1,0,0]
	s_nop 0
	v_pk_fma_f32 v[112:113], v[168:169], v[102:103], v[112:113] op_sel_hi:[0,1,1]
	v_mov_b32_e32 v114, v169
	v_pk_fma_f32 v[112:113], v[114:115], v[88:89], v[112:113] op_sel_hi:[0,1,1]
	ds_read_b128 v[216:219], v25 offset:4096
	s_waitcnt lgkmcnt(8)
	v_pk_fma_f32 v[118:119], v[100:101], v[170:171], v[122:123] op_sel_hi:[1,0,1]
	s_nop 0
	v_pk_fma_f32 v[114:115], v[170:171], v[90:91], v[118:119] op_sel:[1,0,0]
	s_nop 0
	v_pk_fma_f32 v[114:115], v[172:173], v[102:103], v[114:115] op_sel_hi:[0,1,1]
	v_mov_b32_e32 v116, v173
	v_pk_fma_f32 v[114:115], v[116:117], v[88:89], v[114:115] op_sel_hi:[0,1,1]
	ds_read_b128 v[220:223], v25 offset:12304
	s_waitcnt lgkmcnt(8)
	v_pk_fma_f32 v[120:121], v[100:101], v[174:175], v[124:125] op_sel_hi:[1,0,1]
	s_nop 0
	v_pk_fma_f32 v[116:117], v[174:175], v[90:91], v[120:121] op_sel:[1,0,0]
	s_nop 0
	v_pk_fma_f32 v[116:117], v[176:177], v[102:103], v[116:117] op_sel_hi:[0,1,1]
	v_mov_b32_e32 v118, v177
	v_pk_fma_f32 v[116:117], v[118:119], v[88:89], v[116:117] op_sel_hi:[0,1,1]
	ds_read_b128 v[224:227], v25 offset:20512
	s_waitcnt lgkmcnt(8)
; #define LAS __attribute__((address_space(3)))
; __global__ void __launch_bounds__(NTHREADS, 2) hybrid_fwd(Args a) {
;     ...
;                     f32x2 y2[8][4];
; #pragma unroll
;                     for (int j = 0; j < 8; ++j)
; #pragma unroll
;                         for (int c = 0; c < 4; ++c) y2[j][c] = (f32x2){ya[j][c], yb[j][c]};
;                     f32x2 acc2[16];
; #pragma unroll
;                     for (int e = 0; e < 16; ++e) acc2[e] = (f32x2){0.f, 0.f};
; #pragma unroll
;                     for (int j = 0; j < 8; ++j) {
; #pragma unroll
;                         for (int e = 0; e < 16; ++e) { const f32x4 w = *(const LAS f32x4*)(rwT + e * 2052 + j * 256 + lane * 4);
;                             acc2[e] += y2[j][0] * (f32x2){w[0], w[0]}; acc2[e] += y2[j][1] * (f32x2){w[1], w[1]};
;                             acc2[e] += y2[j][2] * (f32x2){w[2], w[2]}; acc2[e] += y2[j][3] * (f32x2){w[3], w[3]}; }
;                         __builtin_amdgcn_sched_barrier(0);
;                     }
	v_pk_fma_f32 v[122:123], v[100:101], v[178:179], v[126:127] op_sel_hi:[1,0,1]
	s_nop 0
	v_pk_fma_f32 v[118:119], v[178:179], v[90:91], v[122:123] op_sel:[1,0,0]
	s_nop 0
	v_pk_fma_f32 v[118:119], v[180:181], v[102:103], v[118:119] op_sel_hi:[0,1,1]
	v_mov_b32_e32 v120, v181
	v_pk_fma_f32 v[118:119], v[120:121], v[88:89], v[118:119] op_sel_hi:[0,1,1]
	ds_read_b128 v[228:231], v25 offset:28720
	s_waitcnt lgkmcnt(8)
	v_pk_fma_f32 v[124:125], v[100:101], v[182:183], v[128:129] op_sel_hi:[1,0,1]
	s_nop 0
	v_pk_fma_f32 v[120:121], v[182:183], v[90:91], v[124:125] op_sel:[1,0,0]
	s_nop 0
	v_pk_fma_f32 v[120:121], v[184:185], v[102:103], v[120:121] op_sel_hi:[0,1,1]
	v_mov_b32_e32 v122, v185
	v_pk_fma_f32 v[120:121], v[122:123], v[88:89], v[120:121] op_sel_hi:[0,1,1]
	ds_read_b128 v[232:235], v25 offset:36928
	s_waitcnt lgkmcnt(8)
	v_pk_fma_f32 v[126:127], v[100:101], v[186:187], v[130:131] op_sel_hi:[1,0,1]
	s_nop 0
	v_pk_fma_f32 v[122:123], v[186:187], v[90:91], v[126:127] op_sel:[1,0,0]
	s_nop 0
	v_pk_fma_f32 v[122:123], v[188:189], v[102:103], v[122:123] op_sel_hi:[0,1,1]
	v_mov_b32_e32 v124, v189
	v_pk_fma_f32 v[122:123], v[124:125], v[88:89], v[122:123] op_sel_hi:[0,1,1]
	ds_read_b128 v[242:245], v25 offset:45136
	s_waitcnt lgkmcnt(8)
	v_pk_fma_f32 v[128:129], v[100:101], v[158:159], v[132:133] op_sel_hi:[1,0,1]
	s_nop 0
	v_pk_fma_f32 v[124:125], v[158:159], v[90:91], v[128:129] op_sel:[1,0,0]
	s_nop 0
	v_pk_fma_f32 v[124:125], v[160:161], v[102:103], v[124:125] op_sel_hi:[0,1,1]
	v_mov_b32_e32 v126, v161
	v_pk_fma_f32 v[124:125], v[126:127], v[88:89], v[124:125] op_sel_hi:[0,1,1]
	ds_read_b128 v[246:249], v25 offset:53344
	s_waitcnt lgkmcnt(8)
	v_pk_fma_f32 v[130:131], v[100:101], v[198:199], v[134:135] op_sel_hi:[1,0,1]
	s_nop 0
	v_pk_fma_f32 v[126:127], v[198:199], v[90:91], v[130:131] op_sel:[1,0,0]
	s_nop 0
	v_pk_fma_f32 v[126:127], v[200:201], v[102:103], v[126:127] op_sel_hi:[0,1,1]
	v_mov_b32_e32 v128, v201
	v_pk_fma_f32 v[126:127], v[128:129], v[88:89], v[126:127] op_sel_hi:[0,1,1]
	ds_read_b128 v[250:253], v25 offset:61552
	s_waitcnt lgkmcnt(8)
	v_pk_fma_f32 v[100:101], v[100:101], v[202:203], v[136:137] op_sel_hi:[1,0,1]
	s_nop 0
	v_pk_fma_f32 v[90:91], v[202:203], v[90:91], v[100:101] op_sel:[1,0,0]
	v_mov_b32_e32 v100, v205
	v_pk_fma_f32 v[90:91], v[204:205], v[102:103], v[90:91] op_sel_hi:[0,1,1]
	v_pk_fma_f32 v[128:129], v[100:101], v[88:89], v[90:91] op_sel_hi:[0,1,1]
	ds_read_b128 v[162:165], v238 offset:4224
	ds_read_b128 v[166:169], v238 offset:12432
	s_waitcnt lgkmcnt(8)
	v_pk_fma_f32 v[96:97], v[92:93], v[216:217], v[96:97] op_sel_hi:[1,0,1]
	s_nop 0
	v_pk_fma_f32 v[88:89], v[216:217], v[86:87], v[96:97] op_sel:[1,0,0]
	v_mov_b32_e32 v96, v223
	v_pk_fma_f32 v[88:89], v[218:219], v[94:95], v[88:89] op_sel_hi:[0,1,1]
	v_mov_b32_e32 v90, v219
	v_pk_fma_f32 v[88:89], v[90:91], v[84:85], v[88:89] op_sel_hi:[0,1,1]
	v_pk_fma_f32 v[90:91], v[92:93], v[220:221], v[138:139] op_sel_hi:[1,0,1]
	s_nop 0
	v_pk_fma_f32 v[90:91], v[220:221], v[86:87], v[90:91] op_sel:[1,0,0]
	s_nop 0
	v_pk_fma_f32 v[90:91], v[222:223], v[94:95], v[90:91] op_sel_hi:[0,1,1]
	ds_read_b128 v[170:173], v238 offset:20640
	v_pk_fma_f32 v[130:131], v[96:97], v[84:85], v[90:91] op_sel_hi:[0,1,1]
	s_waitcnt lgkmcnt(8)
	v_pk_fma_f32 v[90:91], v[92:93], v[224:225], v[98:99] op_sel_hi:[1,0,1]
	s_nop 0
	v_pk_fma_f32 v[90:91], v[224:225], v[86:87], v[90:91] op_sel:[1,0,0]
	v_mov_b32_e32 v96, v227
	v_pk_fma_f32 v[90:91], v[226:227], v[94:95], v[90:91] op_sel_hi:[0,1,1]
	v_pk_fma_f32 v[90:91], v[96:97], v[84:85], v[90:91] op_sel_hi:[0,1,1]
	ds_read_b128 v[174:177], v238 offset:28848
	s_waitcnt lgkmcnt(8)
	v_pk_fma_f32 v[100:101], v[92:93], v[228:229], v[104:105] op_sel_hi:[1,0,1]
	s_nop 0
	v_pk_fma_f32 v[96:97], v[228:229], v[86:87], v[100:101] op_sel:[1,0,0]
	s_nop 0
	v_pk_fma_f32 v[96:97], v[230:231], v[94:95], v[96:97] op_sel_hi:[0,1,1]
	v_mov_b32_e32 v98, v231
	v_pk_fma_f32 v[96:97], v[98:99], v[84:85], v[96:97] op_sel_hi:[0,1,1]
	ds_read_b128 v[178:181], v238 offset:37056
	s_waitcnt lgkmcnt(8)
	v_pk_fma_f32 v[102:103], v[92:93], v[232:233], v[106:107] op_sel_hi:[1,0,1]
	s_nop 0
	v_pk_fma_f32 v[98:99], v[232:233], v[86:87], v[102:103] op_sel:[1,0,0]
	s_nop 0
	v_pk_fma_f32 v[98:99], v[234:235], v[94:95], v[98:99] op_sel_hi:[0,1,1]
	v_mov_b32_e32 v100, v235
	v_pk_fma_f32 v[98:99], v[100:101], v[84:85], v[98:99] op_sel_hi:[0,1,1]
	ds_read_b128 v[182:185], v238 offset:45264
	s_waitcnt lgkmcnt(8)
	v_pk_fma_f32 v[104:105], v[92:93], v[242:243], v[108:109] op_sel_hi:[1,0,1]
	s_nop 0
	v_pk_fma_f32 v[100:101], v[242:243], v[86:87], v[104:105] op_sel:[1,0,0]
	s_nop 0
	v_pk_fma_f32 v[100:101], v[244:245], v[94:95], v[100:101] op_sel_hi:[0,1,1]
	v_mov_b32_e32 v102, v245
	v_pk_fma_f32 v[100:101], v[102:103], v[84:85], v[100:101] op_sel_hi:[0,1,1]
	ds_read_b128 v[186:189], v238 offset:53472
	s_waitcnt lgkmcnt(8)
	v_pk_fma_f32 v[106:107], v[92:93], v[246:247], v[110:111] op_sel_hi:[1,0,1]
	s_nop 0
	v_pk_fma_f32 v[102:103], v[246:247], v[86:87], v[106:107] op_sel:[1,0,0]
	s_nop 0
	v_pk_fma_f32 v[102:103], v[248:249], v[94:95], v[102:103] op_sel_hi:[0,1,1]
	v_mov_b32_e32 v104, v249
	v_pk_fma_f32 v[102:103], v[104:105], v[84:85], v[102:103] op_sel_hi:[0,1,1]
	ds_read_b128 v[158:161], v238 offset:61680
	s_waitcnt lgkmcnt(8)
	v_pk_fma_f32 v[108:109], v[92:93], v[250:251], v[112:113] op_sel_hi:[1,0,1]
	s_nop 0
	v_pk_fma_f32 v[104:105], v[250:251], v[86:87], v[108:109] op_sel:[1,0,0]
	s_nop 0
	v_pk_fma_f32 v[104:105], v[252:253], v[94:95], v[104:105] op_sel_hi:[0,1,1]
	v_mov_b32_e32 v106, v253
	v_pk_fma_f32 v[104:105], v[106:107], v[84:85], v[104:105] op_sel_hi:[0,1,1]
	ds_read_b128 v[198:201], v25 offset:5120
	s_waitcnt lgkmcnt(8)
; #define LAS __attribute__((address_space(3)))
; __global__ void __launch_bounds__(NTHREADS, 2) hybrid_fwd(Args a) {
;     ...
;                     f32x2 y2[8][4];
; #pragma unroll
;                     for (int j = 0; j < 8; ++j)
; #pragma unroll
;                         for (int c = 0; c < 4; ++c) y2[j][c] = (f32x2){ya[j][c], yb[j][c]};
;                     f32x2 acc2[16];
; #pragma unroll
;                     for (int e = 0; e < 16; ++e) acc2[e] = (f32x2){0.f, 0.f};
; #pragma unroll
;                     for (int j = 0; j < 8; ++j) {
; #pragma unroll
;                         for (int e = 0; e < 16; ++e) { const f32x4 w = *(const LAS f32x4*)(rwT + e * 2052 + j * 256 + lane * 4);
;                             acc2[e] += y2[j][0] * (f32x2){w[0], w[0]}; acc2[e] += y2[j][1] * (f32x2){w[1], w[1]};
;                             acc2[e] += y2[j][2] * (f32x2){w[2], w[2]}; acc2[e] += y2[j][3] * (f32x2){w[3], w[3]}; }
;                         __builtin_amdgcn_sched_barrier(0);
;                     }
	v_pk_fma_f32 v[110:111], v[92:93], v[162:163], v[114:115] op_sel_hi:[1,0,1]
	s_nop 0
	v_pk_fma_f32 v[106:107], v[162:163], v[86:87], v[110:111] op_sel:[1,0,0]
	s_nop 0
	v_pk_fma_f32 v[106:107], v[164:165], v[94:95], v[106:107] op_sel_hi:[0,1,1]
	v_mov_b32_e32 v108, v165
	v_pk_fma_f32 v[106:107], v[108:109], v[84:85], v[106:107] op_sel_hi:[0,1,1]
	ds_read_b128 v[202:205], v25 offset:13328
	s_waitcnt lgkmcnt(8)
	v_pk_fma_f32 v[112:113], v[92:93], v[166:167], v[116:117] op_sel_hi:[1,0,1]
	s_nop 0
	v_pk_fma_f32 v[108:109], v[166:167], v[86:87], v[112:113] op_sel:[1,0,0]
	s_nop 0
	v_pk_fma_f32 v[108:109], v[168:169], v[94:95], v[108:109] op_sel_hi:[0,1,1]
	v_mov_b32_e32 v110, v169
	v_pk_fma_f32 v[108:109], v[110:111], v[84:85], v[108:109] op_sel_hi:[0,1,1]
	ds_read_b128 v[216:219], v25 offset:21536
	s_waitcnt lgkmcnt(8)
	v_pk_fma_f32 v[114:115], v[92:93], v[170:171], v[118:119] op_sel_hi:[1,0,1]
	s_nop 0
	v_pk_fma_f32 v[110:111], v[170:171], v[86:87], v[114:115] op_sel:[1,0,0]
	s_nop 0
	v_pk_fma_f32 v[110:111], v[172:173], v[94:95], v[110:111] op_sel_hi:[0,1,1]
	v_mov_b32_e32 v112, v173
	v_pk_fma_f32 v[110:111], v[112:113], v[84:85], v[110:111] op_sel_hi:[0,1,1]
	ds_read_b128 v[220:223], v25 offset:29744
	s_waitcnt lgkmcnt(8)
	v_pk_fma_f32 v[116:117], v[92:93], v[174:175], v[120:121] op_sel_hi:[1,0,1]
	s_nop 0
	v_pk_fma_f32 v[112:113], v[174:175], v[86:87], v[116:117] op_sel:[1,0,0]
	s_nop 0
	v_pk_fma_f32 v[112:113], v[176:177], v[94:95], v[112:113] op_sel_hi:[0,1,1]
	v_mov_b32_e32 v114, v177
	v_pk_fma_f32 v[112:113], v[114:115], v[84:85], v[112:113] op_sel_hi:[0,1,1]
	ds_read_b128 v[224:227], v25 offset:37952
	s_waitcnt lgkmcnt(8)
	v_pk_fma_f32 v[118:119], v[92:93], v[178:179], v[122:123] op_sel_hi:[1,0,1]
	s_nop 0
	v_pk_fma_f32 v[114:115], v[178:179], v[86:87], v[118:119] op_sel:[1,0,0]
	s_nop 0
	v_pk_fma_f32 v[114:115], v[180:181], v[94:95], v[114:115] op_sel_hi:[0,1,1]
	v_mov_b32_e32 v116, v181
	v_pk_fma_f32 v[114:115], v[116:117], v[84:85], v[114:115] op_sel_hi:[0,1,1]
	ds_read_b128 v[228:231], v25 offset:46160
	s_waitcnt lgkmcnt(8)
	v_pk_fma_f32 v[120:121], v[92:93], v[182:183], v[124:125] op_sel_hi:[1,0,1]
	s_nop 0
	v_pk_fma_f32 v[116:117], v[182:183], v[86:87], v[120:121] op_sel:[1,0,0]
	s_nop 0
	v_pk_fma_f32 v[116:117], v[184:185], v[94:95], v[116:117] op_sel_hi:[0,1,1]
	v_mov_b32_e32 v118, v185
	v_pk_fma_f32 v[116:117], v[118:119], v[84:85], v[116:117] op_sel_hi:[0,1,1]
	ds_read_b128 v[232:235], v25 offset:54368
	s_waitcnt lgkmcnt(8)
	v_pk_fma_f32 v[122:123], v[92:93], v[186:187], v[126:127] op_sel_hi:[1,0,1]
	s_nop 0
	v_pk_fma_f32 v[118:119], v[186:187], v[86:87], v[122:123] op_sel:[1,0,0]
	s_nop 0
	v_pk_fma_f32 v[118:119], v[188:189], v[94:95], v[118:119] op_sel_hi:[0,1,1]
	v_mov_b32_e32 v120, v189
	v_pk_fma_f32 v[118:119], v[120:121], v[84:85], v[118:119] op_sel_hi:[0,1,1]
	ds_read_b128 v[242:245], v25 offset:62576
	s_waitcnt lgkmcnt(8)
	v_pk_fma_f32 v[92:93], v[92:93], v[158:159], v[128:129] op_sel_hi:[1,0,1]
	s_nop 0
	v_pk_fma_f32 v[86:87], v[158:159], v[86:87], v[92:93] op_sel:[1,0,0]
	v_mov_b32_e32 v92, v161
	v_pk_fma_f32 v[86:87], v[160:161], v[94:95], v[86:87] op_sel_hi:[0,1,1]
	v_pk_fma_f32 v[120:121], v[92:93], v[84:85], v[86:87] op_sel_hi:[0,1,1]
	ds_read_b128 v[246:249], v238 offset:5248
	s_waitcnt lgkmcnt(8)
	v_pk_fma_f32 v[88:89], v[80:81], v[198:199], v[88:89] op_sel_hi:[1,0,1]
	s_nop 0
	v_pk_fma_f32 v[84:85], v[198:199], v[78:79], v[88:89] op_sel:[1,0,0]
	s_nop 0
	v_pk_fma_f32 v[84:85], v[200:201], v[82:83], v[84:85] op_sel_hi:[0,1,1]
	v_mov_b32_e32 v86, v201
	v_pk_fma_f32 v[84:85], v[86:87], v[76:77], v[84:85] op_sel_hi:[0,1,1]
	ds_read_b128 v[250:253], v238 offset:13456
	s_waitcnt lgkmcnt(8)
	v_pk_fma_f32 v[92:93], v[80:81], v[202:203], v[130:131] op_sel_hi:[1,0,1]
	s_nop 0
	v_pk_fma_f32 v[86:87], v[202:203], v[78:79], v[92:93] op_sel:[1,0,0]
	s_nop 0
	v_pk_fma_f32 v[86:87], v[204:205], v[82:83], v[86:87] op_sel_hi:[0,1,1]
	v_mov_b32_e32 v88, v205
	v_pk_fma_f32 v[122:123], v[88:89], v[76:77], v[86:87] op_sel_hi:[0,1,1]
	ds_read_b128 v[162:165], v238 offset:21664
	s_waitcnt lgkmcnt(8)
	v_pk_fma_f32 v[90:91], v[80:81], v[216:217], v[90:91] op_sel_hi:[1,0,1]
	s_nop 0
	v_pk_fma_f32 v[86:87], v[216:217], v[78:79], v[90:91] op_sel:[1,0,0]
	s_nop 0
	v_pk_fma_f32 v[86:87], v[218:219], v[82:83], v[86:87] op_sel_hi:[0,1,1]
	v_mov_b32_e32 v88, v219
	v_pk_fma_f32 v[86:87], v[88:89], v[76:77], v[86:87] op_sel_hi:[0,1,1]
	ds_read_b128 v[166:169], v238 offset:29872
	s_waitcnt lgkmcnt(8)
	v_pk_fma_f32 v[92:93], v[80:81], v[220:221], v[96:97] op_sel_hi:[1,0,1]
	s_nop 0
	v_pk_fma_f32 v[88:89], v[220:221], v[78:79], v[92:93] op_sel:[1,0,0]
	s_nop 0
	v_pk_fma_f32 v[88:89], v[222:223], v[82:83], v[88:89] op_sel_hi:[0,1,1]
	v_mov_b32_e32 v90, v223
	v_pk_fma_f32 v[88:89], v[90:91], v[76:77], v[88:89] op_sel_hi:[0,1,1]
	ds_read_b128 v[170:173], v238 offset:38080
	s_waitcnt lgkmcnt(8)
	v_pk_fma_f32 v[94:95], v[80:81], v[224:225], v[98:99] op_sel_hi:[1,0,1]
	s_nop 0
	v_pk_fma_f32 v[90:91], v[224:225], v[78:79], v[94:95] op_sel:[1,0,0]
	s_nop 0
	v_pk_fma_f32 v[90:91], v[226:227], v[82:83], v[90:91] op_sel_hi:[0,1,1]
	v_mov_b32_e32 v92, v227
	v_pk_fma_f32 v[90:91], v[92:93], v[76:77], v[90:91] op_sel_hi:[0,1,1]
	ds_read_b128 v[174:177], v238 offset:46288
	s_waitcnt lgkmcnt(8)
	v_pk_fma_f32 v[96:97], v[80:81], v[228:229], v[100:101] op_sel_hi:[1,0,1]
	s_nop 0
	v_pk_fma_f32 v[92:93], v[228:229], v[78:79], v[96:97] op_sel:[1,0,0]
	s_nop 0
	v_pk_fma_f32 v[92:93], v[230:231], v[82:83], v[92:93] op_sel_hi:[0,1,1]
	v_mov_b32_e32 v94, v231
	v_pk_fma_f32 v[92:93], v[94:95], v[76:77], v[92:93] op_sel_hi:[0,1,1]
	ds_read_b128 v[178:181], v238 offset:54496
	s_waitcnt lgkmcnt(8)
; #define LAS __attribute__((address_space(3)))
; __global__ void __launch_bounds__(NTHREADS, 2) hybrid_fwd(Args a) {
;     ...
;                     for (int j = 0; j < 8; ++j) {
; #pragma unroll
;                         for (int e = 0; e < 16; ++e) { const f32x4 w = *(const LAS f32x4*)(rwT + e * 2052 + j * 256 + lane * 4);
;                             acc2[e] += y2[j][0] * (f32x2){w[0], w[0]}; acc2[e] += y2[j][1] * (f32x2){w[1], w[1]};
;                             acc2[e] += y2[j][2] * (f32x2){w[2], w[2]}; acc2[e] += y2[j][3] * (f32x2){w[3], w[3]}; }
;                         __builtin_amdgcn_sched_barrier(0);
;                     }
	v_pk_fma_f32 v[98:99], v[80:81], v[232:233], v[102:103] op_sel_hi:[1,0,1]
	s_nop 0
	v_pk_fma_f32 v[94:95], v[232:233], v[78:79], v[98:99] op_sel:[1,0,0]
	s_nop 0
	v_pk_fma_f32 v[94:95], v[234:235], v[82:83], v[94:95] op_sel_hi:[0,1,1]
	v_mov_b32_e32 v96, v235
	v_pk_fma_f32 v[94:95], v[96:97], v[76:77], v[94:95] op_sel_hi:[0,1,1]
	ds_read_b128 v[182:185], v238 offset:62704
	s_waitcnt lgkmcnt(8)
	v_pk_fma_f32 v[100:101], v[80:81], v[242:243], v[104:105] op_sel_hi:[1,0,1]
	s_nop 0
	v_pk_fma_f32 v[96:97], v[242:243], v[78:79], v[100:101] op_sel:[1,0,0]
	s_nop 0
	v_pk_fma_f32 v[96:97], v[244:245], v[82:83], v[96:97] op_sel_hi:[0,1,1]
	v_mov_b32_e32 v98, v245
	v_pk_fma_f32 v[96:97], v[98:99], v[76:77], v[96:97] op_sel_hi:[0,1,1]
	ds_read_b128 v[186:189], v25 offset:6144
	s_waitcnt lgkmcnt(8)
	v_pk_fma_f32 v[102:103], v[80:81], v[246:247], v[106:107] op_sel_hi:[1,0,1]
	s_nop 0
	v_pk_fma_f32 v[98:99], v[246:247], v[78:79], v[102:103] op_sel:[1,0,0]
	s_nop 0
	v_pk_fma_f32 v[98:99], v[248:249], v[82:83], v[98:99] op_sel_hi:[0,1,1]
	v_mov_b32_e32 v100, v249
	v_pk_fma_f32 v[98:99], v[100:101], v[76:77], v[98:99] op_sel_hi:[0,1,1]
	ds_read_b128 v[158:161], v25 offset:14352
	s_waitcnt lgkmcnt(8)
	v_pk_fma_f32 v[104:105], v[80:81], v[250:251], v[108:109] op_sel_hi:[1,0,1]
	s_nop 0
	v_pk_fma_f32 v[100:101], v[250:251], v[78:79], v[104:105] op_sel:[1,0,0]
	s_nop 0
	v_pk_fma_f32 v[100:101], v[252:253], v[82:83], v[100:101] op_sel_hi:[0,1,1]
	v_mov_b32_e32 v102, v253
	v_pk_fma_f32 v[100:101], v[102:103], v[76:77], v[100:101] op_sel_hi:[0,1,1]
	ds_read_b128 v[198:201], v25 offset:22560
	s_waitcnt lgkmcnt(8)
	v_pk_fma_f32 v[106:107], v[80:81], v[162:163], v[110:111] op_sel_hi:[1,0,1]
	s_nop 0
	v_pk_fma_f32 v[102:103], v[162:163], v[78:79], v[106:107] op_sel:[1,0,0]
	s_nop 0
	v_pk_fma_f32 v[102:103], v[164:165], v[82:83], v[102:103] op_sel_hi:[0,1,1]
	v_mov_b32_e32 v104, v165
	v_pk_fma_f32 v[102:103], v[104:105], v[76:77], v[102:103] op_sel_hi:[0,1,1]
	ds_read_b128 v[202:205], v25 offset:30768
	s_waitcnt lgkmcnt(8)
	v_pk_fma_f32 v[108:109], v[80:81], v[166:167], v[112:113] op_sel_hi:[1,0,1]
	s_nop 0
	v_pk_fma_f32 v[104:105], v[166:167], v[78:79], v[108:109] op_sel:[1,0,0]
	s_nop 0
	v_pk_fma_f32 v[104:105], v[168:169], v[82:83], v[104:105] op_sel_hi:[0,1,1]
	v_mov_b32_e32 v106, v169
	v_pk_fma_f32 v[104:105], v[106:107], v[76:77], v[104:105] op_sel_hi:[0,1,1]
	ds_read_b128 v[216:219], v25 offset:38976
	s_waitcnt lgkmcnt(8)
	v_pk_fma_f32 v[110:111], v[80:81], v[170:171], v[114:115] op_sel_hi:[1,0,1]
	s_nop 0
	v_pk_fma_f32 v[106:107], v[170:171], v[78:79], v[110:111] op_sel:[1,0,0]
	s_nop 0
	v_pk_fma_f32 v[106:107], v[172:173], v[82:83], v[106:107] op_sel_hi:[0,1,1]
	v_mov_b32_e32 v108, v173
	v_pk_fma_f32 v[106:107], v[108:109], v[76:77], v[106:107] op_sel_hi:[0,1,1]
	ds_read_b128 v[220:223], v25 offset:47184
	s_waitcnt lgkmcnt(8)
	v_pk_fma_f32 v[112:113], v[80:81], v[174:175], v[116:117] op_sel_hi:[1,0,1]
	s_nop 0
	v_pk_fma_f32 v[108:109], v[174:175], v[78:79], v[112:113] op_sel:[1,0,0]
	s_nop 0
	v_pk_fma_f32 v[108:109], v[176:177], v[82:83], v[108:109] op_sel_hi:[0,1,1]
	v_mov_b32_e32 v110, v177
	v_pk_fma_f32 v[108:109], v[110:111], v[76:77], v[108:109] op_sel_hi:[0,1,1]
	ds_read_b128 v[224:227], v25 offset:55392
	s_waitcnt lgkmcnt(8)
	v_pk_fma_f32 v[114:115], v[80:81], v[178:179], v[118:119] op_sel_hi:[1,0,1]
	s_nop 0
	v_pk_fma_f32 v[110:111], v[178:179], v[78:79], v[114:115] op_sel:[1,0,0]
	s_nop 0
	v_pk_fma_f32 v[110:111], v[180:181], v[82:83], v[110:111] op_sel_hi:[0,1,1]
	v_mov_b32_e32 v112, v181
	v_pk_fma_f32 v[110:111], v[112:113], v[76:77], v[110:111] op_sel_hi:[0,1,1]
	ds_read_b128 v[228:231], v25 offset:63600
	s_waitcnt lgkmcnt(8)
	v_pk_fma_f32 v[80:81], v[80:81], v[182:183], v[120:121] op_sel_hi:[1,0,1]
	s_nop 0
	v_pk_fma_f32 v[78:79], v[182:183], v[78:79], v[80:81] op_sel:[1,0,0]
	v_mov_b32_e32 v80, v185
	v_pk_fma_f32 v[78:79], v[184:185], v[82:83], v[78:79] op_sel_hi:[0,1,1]
	v_pk_fma_f32 v[112:113], v[80:81], v[76:77], v[78:79] op_sel_hi:[0,1,1]
	ds_read_b128 v[232:235], v238 offset:6272
	s_waitcnt lgkmcnt(8)
	v_pk_fma_f32 v[80:81], v[72:73], v[186:187], v[84:85] op_sel_hi:[1,0,1]
	s_nop 0
	v_pk_fma_f32 v[76:77], v[186:187], v[70:71], v[80:81] op_sel:[1,0,0]
	s_nop 0
	v_pk_fma_f32 v[76:77], v[188:189], v[74:75], v[76:77] op_sel_hi:[0,1,1]
	v_mov_b32_e32 v78, v189
	v_pk_fma_f32 v[76:77], v[78:79], v[68:69], v[76:77] op_sel_hi:[0,1,1]
	ds_read_b128 v[242:245], v238 offset:14480
	s_waitcnt lgkmcnt(8)
	v_pk_fma_f32 v[82:83], v[72:73], v[158:159], v[122:123] op_sel_hi:[1,0,1]
	s_nop 0
	v_pk_fma_f32 v[78:79], v[158:159], v[70:71], v[82:83] op_sel:[1,0,0]
	s_nop 0
	v_pk_fma_f32 v[78:79], v[160:161], v[74:75], v[78:79] op_sel_hi:[0,1,1]
	v_mov_b32_e32 v80, v161
	v_pk_fma_f32 v[114:115], v[80:81], v[68:69], v[78:79] op_sel_hi:[0,1,1]
	ds_read_b128 v[246:249], v238 offset:22688
	s_waitcnt lgkmcnt(8)
	v_pk_fma_f32 v[82:83], v[72:73], v[198:199], v[86:87] op_sel_hi:[1,0,1]
	s_nop 0
	v_pk_fma_f32 v[78:79], v[198:199], v[70:71], v[82:83] op_sel:[1,0,0]
	s_nop 0
	v_pk_fma_f32 v[78:79], v[200:201], v[74:75], v[78:79] op_sel_hi:[0,1,1]
	v_mov_b32_e32 v80, v201
	v_pk_fma_f32 v[78:79], v[80:81], v[68:69], v[78:79] op_sel_hi:[0,1,1]
	ds_read_b128 v[250:253], v238 offset:30896
	s_waitcnt lgkmcnt(8)
	v_pk_fma_f32 v[84:85], v[72:73], v[202:203], v[88:89] op_sel_hi:[1,0,1]
	s_nop 0
	v_pk_fma_f32 v[80:81], v[202:203], v[70:71], v[84:85] op_sel:[1,0,0]
	s_nop 0
	v_pk_fma_f32 v[80:81], v[204:205], v[74:75], v[80:81] op_sel_hi:[0,1,1]
	v_mov_b32_e32 v82, v205
	v_pk_fma_f32 v[80:81], v[82:83], v[68:69], v[80:81] op_sel_hi:[0,1,1]
	ds_read_b128 v[162:165], v238 offset:39104
	s_waitcnt lgkmcnt(8)
; #define LAS __attribute__((address_space(3)))
; __global__ void __launch_bounds__(NTHREADS, 2) hybrid_fwd(Args a) {
;     ...
;                     for (int j = 0; j < 8; ++j) {
; #pragma unroll
;                         for (int e = 0; e < 16; ++e) { const f32x4 w = *(const LAS f32x4*)(rwT + e * 2052 + j * 256 + lane * 4);
;                             acc2[e] += y2[j][0] * (f32x2){w[0], w[0]}; acc2[e] += y2[j][1] * (f32x2){w[1], w[1]};
;                             acc2[e] += y2[j][2] * (f32x2){w[2], w[2]}; acc2[e] += y2[j][3] * (f32x2){w[3], w[3]}; }
;                         __builtin_amdgcn_sched_barrier(0);
;                     }
	v_pk_fma_f32 v[86:87], v[72:73], v[216:217], v[90:91] op_sel_hi:[1,0,1]
	s_nop 0
	v_pk_fma_f32 v[82:83], v[216:217], v[70:71], v[86:87] op_sel:[1,0,0]
	s_nop 0
	v_pk_fma_f32 v[82:83], v[218:219], v[74:75], v[82:83] op_sel_hi:[0,1,1]
	v_mov_b32_e32 v84, v219
	v_pk_fma_f32 v[82:83], v[84:85], v[68:69], v[82:83] op_sel_hi:[0,1,1]
	ds_read_b128 v[166:169], v238 offset:47312
	s_waitcnt lgkmcnt(8)
	v_pk_fma_f32 v[88:89], v[72:73], v[220:221], v[92:93] op_sel_hi:[1,0,1]
	s_nop 0
	v_pk_fma_f32 v[84:85], v[220:221], v[70:71], v[88:89] op_sel:[1,0,0]
	s_nop 0
	v_pk_fma_f32 v[84:85], v[222:223], v[74:75], v[84:85] op_sel_hi:[0,1,1]
	v_mov_b32_e32 v86, v223
	v_pk_fma_f32 v[84:85], v[86:87], v[68:69], v[84:85] op_sel_hi:[0,1,1]
	ds_read_b128 v[170:173], v238 offset:55520
	s_waitcnt lgkmcnt(8)
	v_pk_fma_f32 v[90:91], v[72:73], v[224:225], v[94:95] op_sel_hi:[1,0,1]
	s_nop 0
	v_pk_fma_f32 v[86:87], v[224:225], v[70:71], v[90:91] op_sel:[1,0,0]
	s_nop 0
	v_pk_fma_f32 v[86:87], v[226:227], v[74:75], v[86:87] op_sel_hi:[0,1,1]
	v_mov_b32_e32 v88, v227
	v_pk_fma_f32 v[86:87], v[88:89], v[68:69], v[86:87] op_sel_hi:[0,1,1]
	ds_read_b128 v[174:177], v238 offset:63728
	s_waitcnt lgkmcnt(8)
	v_pk_fma_f32 v[92:93], v[72:73], v[228:229], v[96:97] op_sel_hi:[1,0,1]
	s_nop 0
	v_pk_fma_f32 v[88:89], v[228:229], v[70:71], v[92:93] op_sel:[1,0,0]
	s_nop 0
	v_pk_fma_f32 v[88:89], v[230:231], v[74:75], v[88:89] op_sel_hi:[0,1,1]
	v_mov_b32_e32 v90, v231
	v_pk_fma_f32 v[88:89], v[90:91], v[68:69], v[88:89] op_sel_hi:[0,1,1]
	ds_read_b128 v[178:181], v25 offset:7168
	s_waitcnt lgkmcnt(8)
	v_pk_fma_f32 v[94:95], v[72:73], v[232:233], v[98:99] op_sel_hi:[1,0,1]
	s_nop 0
	v_pk_fma_f32 v[90:91], v[232:233], v[70:71], v[94:95] op_sel:[1,0,0]
	s_nop 0
	v_pk_fma_f32 v[90:91], v[234:235], v[74:75], v[90:91] op_sel_hi:[0,1,1]
	v_mov_b32_e32 v92, v235
	v_pk_fma_f32 v[90:91], v[92:93], v[68:69], v[90:91] op_sel_hi:[0,1,1]
	ds_read_b128 v[182:185], v25 offset:15376
	s_waitcnt lgkmcnt(8)
	v_pk_fma_f32 v[96:97], v[72:73], v[242:243], v[100:101] op_sel_hi:[1,0,1]
	s_nop 0
	v_pk_fma_f32 v[92:93], v[242:243], v[70:71], v[96:97] op_sel:[1,0,0]
	s_nop 0
	v_pk_fma_f32 v[92:93], v[244:245], v[74:75], v[92:93] op_sel_hi:[0,1,1]
	v_mov_b32_e32 v94, v245
	v_pk_fma_f32 v[92:93], v[94:95], v[68:69], v[92:93] op_sel_hi:[0,1,1]
	ds_read_b128 v[186:189], v25 offset:23584
	s_waitcnt lgkmcnt(8)
	v_pk_fma_f32 v[98:99], v[72:73], v[246:247], v[102:103] op_sel_hi:[1,0,1]
	s_nop 0
	v_pk_fma_f32 v[94:95], v[246:247], v[70:71], v[98:99] op_sel:[1,0,0]
	s_nop 0
	v_pk_fma_f32 v[94:95], v[248:249], v[74:75], v[94:95] op_sel_hi:[0,1,1]
	v_mov_b32_e32 v96, v249
	v_pk_fma_f32 v[94:95], v[96:97], v[68:69], v[94:95] op_sel_hi:[0,1,1]
	ds_read_b128 v[158:161], v25 offset:31792
	s_waitcnt lgkmcnt(8)
	v_pk_fma_f32 v[100:101], v[72:73], v[250:251], v[104:105] op_sel_hi:[1,0,1]
	s_nop 0
	v_pk_fma_f32 v[96:97], v[250:251], v[70:71], v[100:101] op_sel:[1,0,0]
	s_nop 0
	v_pk_fma_f32 v[96:97], v[252:253], v[74:75], v[96:97] op_sel_hi:[0,1,1]
	v_mov_b32_e32 v98, v253
	v_pk_fma_f32 v[96:97], v[98:99], v[68:69], v[96:97] op_sel_hi:[0,1,1]
	ds_read_b128 v[198:201], v25 offset:40000
	s_waitcnt lgkmcnt(8)
	v_pk_fma_f32 v[102:103], v[72:73], v[162:163], v[106:107] op_sel_hi:[1,0,1]
	s_nop 0
	v_pk_fma_f32 v[98:99], v[162:163], v[70:71], v[102:103] op_sel:[1,0,0]
	s_nop 0
	v_pk_fma_f32 v[98:99], v[164:165], v[74:75], v[98:99] op_sel_hi:[0,1,1]
	v_mov_b32_e32 v100, v165
	v_pk_fma_f32 v[98:99], v[100:101], v[68:69], v[98:99] op_sel_hi:[0,1,1]
	ds_read_b128 v[202:205], v25 offset:48208
	s_waitcnt lgkmcnt(8)
	v_pk_fma_f32 v[104:105], v[72:73], v[166:167], v[108:109] op_sel_hi:[1,0,1]
	s_nop 0
	v_pk_fma_f32 v[100:101], v[166:167], v[70:71], v[104:105] op_sel:[1,0,0]
	s_nop 0
	v_pk_fma_f32 v[100:101], v[168:169], v[74:75], v[100:101] op_sel_hi:[0,1,1]
	v_mov_b32_e32 v102, v169
	v_pk_fma_f32 v[100:101], v[102:103], v[68:69], v[100:101] op_sel_hi:[0,1,1]
	ds_read_b128 v[216:219], v25 offset:56416
	s_waitcnt lgkmcnt(8)
	v_pk_fma_f32 v[106:107], v[72:73], v[170:171], v[110:111] op_sel_hi:[1,0,1]
	s_nop 0
	v_pk_fma_f32 v[102:103], v[170:171], v[70:71], v[106:107] op_sel:[1,0,0]
	s_nop 0
	v_pk_fma_f32 v[102:103], v[172:173], v[74:75], v[102:103] op_sel_hi:[0,1,1]
	v_mov_b32_e32 v104, v173
	v_pk_fma_f32 v[102:103], v[104:105], v[68:69], v[102:103] op_sel_hi:[0,1,1]
	ds_read_b128 v[220:223], v25 offset:64624
	s_waitcnt lgkmcnt(8)
	v_pk_fma_f32 v[72:73], v[72:73], v[174:175], v[112:113] op_sel_hi:[1,0,1]
	s_nop 0
	v_pk_fma_f32 v[70:71], v[174:175], v[70:71], v[72:73] op_sel:[1,0,0]
	v_mov_b32_e32 v72, v177
	v_pk_fma_f32 v[70:71], v[176:177], v[74:75], v[70:71] op_sel_hi:[0,1,1]
	v_pk_fma_f32 v[104:105], v[72:73], v[68:69], v[70:71] op_sel_hi:[0,1,1]
	ds_read_b128 v[224:227], v238 offset:7296
	s_waitcnt lgkmcnt(8)
	v_pk_fma_f32 v[72:73], v[66:67], v[178:179], v[76:77] op_sel_hi:[1,0,1]
	s_nop 0
	v_pk_fma_f32 v[68:69], v[178:179], v[62:63], v[72:73] op_sel:[1,0,0]
	s_nop 0
	v_pk_fma_f32 v[68:69], v[180:181], v[64:65], v[68:69] op_sel_hi:[0,1,1]
	v_mov_b32_e32 v70, v181
	v_pk_fma_f32 v[68:69], v[70:71], v[60:61], v[68:69] op_sel_hi:[0,1,1]
	ds_read_b128 v[228:231], v238 offset:15504
	s_waitcnt lgkmcnt(8)
	v_pk_fma_f32 v[74:75], v[66:67], v[182:183], v[114:115] op_sel_hi:[1,0,1]
	s_nop 0
	v_pk_fma_f32 v[70:71], v[182:183], v[62:63], v[74:75] op_sel:[1,0,0]
	s_nop 0
	v_pk_fma_f32 v[70:71], v[184:185], v[64:65], v[70:71] op_sel_hi:[0,1,1]
	v_mov_b32_e32 v72, v185
	v_pk_fma_f32 v[70:71], v[72:73], v[60:61], v[70:71] op_sel_hi:[0,1,1]
	ds_read_b128 v[232:235], v238 offset:23712
	s_waitcnt lgkmcnt(8)
; #define LAS __attribute__((address_space(3)))
; __global__ void __launch_bounds__(NTHREADS, 2) hybrid_fwd(Args a) {
;     ...
;                     for (int j = 0; j < 8; ++j) {
; #pragma unroll
;                         for (int e = 0; e < 16; ++e) { const f32x4 w = *(const LAS f32x4*)(rwT + e * 2052 + j * 256 + lane * 4);
;                             acc2[e] += y2[j][0] * (f32x2){w[0], w[0]}; acc2[e] += y2[j][1] * (f32x2){w[1], w[1]};
;                             acc2[e] += y2[j][2] * (f32x2){w[2], w[2]}; acc2[e] += y2[j][3] * (f32x2){w[3], w[3]}; }
;                         __builtin_amdgcn_sched_barrier(0);
;                     }
	v_pk_fma_f32 v[76:77], v[66:67], v[186:187], v[78:79] op_sel_hi:[1,0,1]
	s_nop 0
	v_pk_fma_f32 v[72:73], v[186:187], v[62:63], v[76:77] op_sel:[1,0,0]
	s_nop 0
	v_pk_fma_f32 v[72:73], v[188:189], v[64:65], v[72:73] op_sel_hi:[0,1,1]
	v_mov_b32_e32 v74, v189
	v_pk_fma_f32 v[72:73], v[74:75], v[60:61], v[72:73] op_sel_hi:[0,1,1]
	ds_read_b128 v[242:245], v238 offset:31920
	s_waitcnt lgkmcnt(8)
	v_pk_fma_f32 v[78:79], v[66:67], v[158:159], v[80:81] op_sel_hi:[1,0,1]
	s_nop 0
	v_pk_fma_f32 v[74:75], v[158:159], v[62:63], v[78:79] op_sel:[1,0,0]
	ds_read_b128 v[246:249], v238 offset:40128
	v_pk_fma_f32 v[74:75], v[160:161], v[64:65], v[74:75] op_sel_hi:[0,1,1]
	v_mov_b32_e32 v76, v161
	v_pk_fma_f32 v[76:77], v[76:77], v[60:61], v[74:75] op_sel_hi:[0,1,1]
	s_waitcnt lgkmcnt(8)
	v_pk_fma_f32 v[74:75], v[66:67], v[198:199], v[82:83] op_sel_hi:[1,0,1]
	s_nop 0
	v_pk_fma_f32 v[74:75], v[198:199], v[62:63], v[74:75] op_sel:[1,0,0]
	v_mov_b32_e32 v78, v201
	v_pk_fma_f32 v[74:75], v[200:201], v[64:65], v[74:75] op_sel_hi:[0,1,1]
	v_pk_fma_f32 v[74:75], v[78:79], v[60:61], v[74:75] op_sel_hi:[0,1,1]
	ds_read_b128 v[250:253], v238 offset:48336
	s_waitcnt lgkmcnt(8)
	v_pk_fma_f32 v[82:83], v[66:67], v[202:203], v[84:85] op_sel_hi:[1,0,1]
	s_nop 0
	v_pk_fma_f32 v[78:79], v[202:203], v[62:63], v[82:83] op_sel:[1,0,0]
	s_nop 0
	v_pk_fma_f32 v[78:79], v[204:205], v[64:65], v[78:79] op_sel_hi:[0,1,1]
	v_mov_b32_e32 v80, v205
	v_pk_fma_f32 v[78:79], v[80:81], v[60:61], v[78:79] op_sel_hi:[0,1,1]
	ds_read_b128 v[162:165], v238 offset:56544
	s_waitcnt lgkmcnt(8)
	v_pk_fma_f32 v[84:85], v[66:67], v[216:217], v[86:87] op_sel_hi:[1,0,1]
	s_nop 0
	v_pk_fma_f32 v[80:81], v[216:217], v[62:63], v[84:85] op_sel:[1,0,0]
	s_nop 0
	v_pk_fma_f32 v[80:81], v[218:219], v[64:65], v[80:81] op_sel_hi:[0,1,1]
	v_mov_b32_e32 v82, v219
	v_pk_fma_f32 v[80:81], v[82:83], v[60:61], v[80:81] op_sel_hi:[0,1,1]
	ds_read_b128 v[166:169], v238 offset:64752
	s_waitcnt lgkmcnt(8)
	v_pk_fma_f32 v[86:87], v[66:67], v[220:221], v[88:89] op_sel_hi:[1,0,1]
	s_nop 0
	v_pk_fma_f32 v[82:83], v[220:221], v[62:63], v[86:87] op_sel:[1,0,0]
	s_nop 0
	v_pk_fma_f32 v[82:83], v[222:223], v[64:65], v[82:83] op_sel_hi:[0,1,1]
	v_mov_b32_e32 v84, v223
	v_pk_fma_f32 v[82:83], v[84:85], v[60:61], v[82:83] op_sel_hi:[0,1,1]
	s_waitcnt lgkmcnt(7)
	v_pk_fma_f32 v[88:89], v[66:67], v[224:225], v[90:91] op_sel_hi:[1,0,1]
	s_nop 0
	v_pk_fma_f32 v[84:85], v[224:225], v[62:63], v[88:89] op_sel:[1,0,0]
	s_nop 0
	v_pk_fma_f32 v[84:85], v[226:227], v[64:65], v[84:85] op_sel_hi:[0,1,1]
	v_mov_b32_e32 v86, v227
	v_pk_fma_f32 v[84:85], v[86:87], v[60:61], v[84:85] op_sel_hi:[0,1,1]
	s_waitcnt lgkmcnt(6)
	v_pk_fma_f32 v[90:91], v[66:67], v[228:229], v[92:93] op_sel_hi:[1,0,1]
	s_nop 0
	v_pk_fma_f32 v[86:87], v[228:229], v[62:63], v[90:91] op_sel:[1,0,0]
	s_nop 0
	v_pk_fma_f32 v[86:87], v[230:231], v[64:65], v[86:87] op_sel_hi:[0,1,1]
	v_mov_b32_e32 v88, v231
	v_pk_fma_f32 v[86:87], v[88:89], v[60:61], v[86:87] op_sel_hi:[0,1,1]
	s_waitcnt lgkmcnt(5)
	v_pk_fma_f32 v[92:93], v[66:67], v[232:233], v[94:95] op_sel_hi:[1,0,1]
	s_nop 0
	v_pk_fma_f32 v[88:89], v[232:233], v[62:63], v[92:93] op_sel:[1,0,0]
	s_nop 0
	v_pk_fma_f32 v[88:89], v[234:235], v[64:65], v[88:89] op_sel_hi:[0,1,1]
	v_mov_b32_e32 v90, v235
	v_pk_fma_f32 v[88:89], v[90:91], v[60:61], v[88:89] op_sel_hi:[0,1,1]
	s_waitcnt lgkmcnt(4)
	v_pk_fma_f32 v[94:95], v[66:67], v[242:243], v[96:97] op_sel_hi:[1,0,1]
	s_nop 0
	v_pk_fma_f32 v[90:91], v[242:243], v[62:63], v[94:95] op_sel:[1,0,0]
	s_nop 0
	v_pk_fma_f32 v[90:91], v[244:245], v[64:65], v[90:91] op_sel_hi:[0,1,1]
	v_mov_b32_e32 v92, v245
	v_pk_fma_f32 v[90:91], v[92:93], v[60:61], v[90:91] op_sel_hi:[0,1,1]
	s_waitcnt lgkmcnt(3)
	v_pk_fma_f32 v[96:97], v[66:67], v[246:247], v[98:99] op_sel_hi:[1,0,1]
	s_nop 0
	v_pk_fma_f32 v[92:93], v[246:247], v[62:63], v[96:97] op_sel:[1,0,0]
	s_nop 0
	v_pk_fma_f32 v[92:93], v[248:249], v[64:65], v[92:93] op_sel_hi:[0,1,1]
	v_mov_b32_e32 v94, v249
	v_pk_fma_f32 v[92:93], v[94:95], v[60:61], v[92:93] op_sel_hi:[0,1,1]
	s_waitcnt lgkmcnt(2)
	v_pk_fma_f32 v[98:99], v[66:67], v[250:251], v[100:101] op_sel_hi:[1,0,1]
	s_nop 0
	v_pk_fma_f32 v[94:95], v[250:251], v[62:63], v[98:99] op_sel:[1,0,0]
	s_nop 0
	v_pk_fma_f32 v[94:95], v[252:253], v[64:65], v[94:95] op_sel_hi:[0,1,1]
	v_mov_b32_e32 v96, v253
	v_pk_fma_f32 v[94:95], v[96:97], v[60:61], v[94:95] op_sel_hi:[0,1,1]
	s_waitcnt lgkmcnt(1)
	v_pk_fma_f32 v[100:101], v[66:67], v[162:163], v[102:103] op_sel_hi:[1,0,1]
	s_nop 0
	v_pk_fma_f32 v[96:97], v[162:163], v[62:63], v[100:101] op_sel:[1,0,0]
	s_nop 0
	v_pk_fma_f32 v[96:97], v[164:165], v[64:65], v[96:97] op_sel_hi:[0,1,1]
	v_mov_b32_e32 v98, v165
	v_pk_fma_f32 v[96:97], v[98:99], v[60:61], v[96:97] op_sel_hi:[0,1,1]
	s_waitcnt lgkmcnt(0)
; #define LAS __attribute__((address_space(3)))
; __global__ void __launch_bounds__(NTHREADS, 2) hybrid_fwd(Args a) {
;     ...
;                     for (int j = 0; j < 8; ++j) {
; #pragma unroll
;                         for (int e = 0; e < 16; ++e) { const f32x4 w = *(const LAS f32x4*)(rwT + e * 2052 + j * 256 + lane * 4);
;                             acc2[e] += y2[j][0] * (f32x2){w[0], w[0]}; acc2[e] += y2[j][1] * (f32x2){w[1], w[1]};
;                             acc2[e] += y2[j][2] * (f32x2){w[2], w[2]}; acc2[e] += y2[j][3] * (f32x2){w[3], w[3]}; }
;                         __builtin_amdgcn_sched_barrier(0);
;                     }
;                     float acca[16], accb[16];
; #pragma unroll
;                     for (int e = 0; e < 16; ++e) { acca[e] = acc2[e][0]; accb[e] = acc2[e][1]; }
;                     P7_PICK(2 * qp, acca);
	v_pk_fma_f32 v[66:67], v[66:67], v[166:167], v[104:105] op_sel_hi:[1,0,1]
	s_nop 0
	v_pk_fma_f32 v[62:63], v[166:167], v[62:63], v[66:67] op_sel:[1,0,0]
	s_nop 0
	v_pk_fma_f32 v[62:63], v[168:169], v[64:65], v[62:63] op_sel_hi:[0,1,1]
	v_mov_b32_e32 v64, v169
	v_pk_fma_f32 v[60:61], v[64:65], v[60:61], v[62:63] op_sel_hi:[0,1,1]
	s_nop 1
	v_permlane32_swap_b32_e32 v60, v61
	v_permlane32_swap_b32_e32 v68, v69
	v_permlane32_swap_b32_e32 v70, v71
	v_permlane32_swap_b32_e32 v72, v73
	v_permlane32_swap_b32_e32 v74, v75
	v_permlane32_swap_b32_e32 v76, v77
	v_permlane32_swap_b32_e32 v78, v79
	v_permlane32_swap_b32_e32 v80, v81
	v_permlane32_swap_b32_e32 v82, v83
	v_permlane32_swap_b32_e32 v84, v85
	v_permlane32_swap_b32_e32 v86, v87
	v_permlane32_swap_b32_e32 v88, v89
	v_permlane32_swap_b32_e32 v90, v91
	v_permlane32_swap_b32_e32 v92, v93
	v_permlane32_swap_b32_e32 v94, v95
	v_permlane32_swap_b32_e32 v96, v97
	v_add_f32_e32 v60, v60, v61
	v_add_f32_e32 v68, v68, v69
	v_add_f32_e32 v70, v70, v71
	v_add_f32_e32 v72, v72, v73
	v_add_f32_e32 v74, v74, v75
	v_add_f32_e32 v76, v76, v77
	v_add_f32_e32 v78, v78, v79
	v_add_f32_e32 v80, v80, v81
	v_add_f32_e32 v82, v82, v83
	v_add_f32_e32 v84, v84, v85
	v_add_f32_e32 v86, v86, v87
	v_add_f32_e32 v88, v88, v89
	v_add_f32_e32 v90, v90, v91
	v_add_f32_e32 v92, v92, v93
	v_add_f32_e32 v94, v94, v95
	v_add_f32_e32 v96, v96, v97
	s_nop 1
	v_add_f32_dpp v62, v68, v68 quad_perm:[1,0,3,2] row_mask:0xf bank_mask:0xf bound_ctrl:1
	s_nop 0
	v_add_f32_dpp v60, v60, v60 quad_perm:[1,0,3,2] row_mask:0xf bank_mask:0xf bound_ctrl:1
	v_add_f32_dpp v68, v94, v94 quad_perm:[1,0,3,2] row_mask:0xf bank_mask:0xf bound_ctrl:1
	v_add_f32_dpp v62, v62, v62 quad_perm:[2,3,0,1] row_mask:0xf bank_mask:0xf bound_ctrl:1
	v_add_f32_dpp v60, v60, v60 quad_perm:[2,3,0,1] row_mask:0xf bank_mask:0xf bound_ctrl:1
	v_add_f32_dpp v68, v68, v68 quad_perm:[2,3,0,1] row_mask:0xf bank_mask:0xf bound_ctrl:1
	v_add_f32_dpp v62, v62, v62 row_ror:4 row_mask:0xf bank_mask:0xf bound_ctrl:1
	v_add_f32_dpp v60, v60, v60 row_ror:4 row_mask:0xf bank_mask:0xf bound_ctrl:1
	v_add_f32_dpp v68, v68, v68 row_ror:4 row_mask:0xf bank_mask:0xf bound_ctrl:1
	v_add_f32_dpp v62, v62, v62 row_ror:8 row_mask:0xf bank_mask:0xf bound_ctrl:1
	v_mov_b32_e32 v63, v62
	s_nop 1
	v_permlane16_swap_b32_e32 v62, v63
	v_add_f32_e32 v62, v62, v63
	v_mov_b32_e32 v63, v62
	s_nop 1
	s_nop 0
	v_mov_b32_e32 v62, v62
	s_nop 0
	v_add_f32_dpp v63, v70, v70 quad_perm:[1,0,3,2] row_mask:0xf bank_mask:0xf bound_ctrl:1
	v_mul_f32_e32 v62, 0xbfb8aa3b, v62
	v_exp_f32_e32 v62, v62
	v_add_f32_dpp v63, v63, v63 quad_perm:[2,3,0,1] row_mask:0xf bank_mask:0xf bound_ctrl:1
	v_add_f32_dpp v60, v60, v60 row_ror:8 row_mask:0xf bank_mask:0xf bound_ctrl:1
	v_add_f32_dpp v68, v68, v68 row_ror:8 row_mask:0xf bank_mask:0xf bound_ctrl:1
	v_add_f32_dpp v63, v63, v63 row_ror:4 row_mask:0xf bank_mask:0xf bound_ctrl:1
	v_add_f32_e32 v62, 1.0, v62
	v_rcp_f32_e32 v62, v62
	v_add_f32_dpp v63, v63, v63 row_ror:8 row_mask:0xf bank_mask:0xf bound_ctrl:1
	v_mov_b32_e32 v64, v63
	s_nop 1
	v_permlane16_swap_b32_e32 v63, v64
	v_add_f32_e32 v63, v63, v64
	v_mov_b32_e32 v64, v63
	s_nop 1
	s_nop 0
	v_mov_b32_e32 v63, v63
	s_nop 0
	v_add_f32_dpp v64, v72, v72 quad_perm:[1,0,3,2] row_mask:0xf bank_mask:0xf bound_ctrl:1
	v_mul_f32_e32 v63, 0xbfb8aa3b, v63
	v_exp_f32_e32 v63, v63
	v_add_f32_dpp v64, v64, v64 quad_perm:[2,3,0,1] row_mask:0xf bank_mask:0xf bound_ctrl:1
	v_add_f32_dpp v72, v96, v96 quad_perm:[1,0,3,2] row_mask:0xf bank_mask:0xf bound_ctrl:1
	v_mov_b32_e32 v70, v68
	v_add_f32_dpp v64, v64, v64 row_ror:4 row_mask:0xf bank_mask:0xf bound_ctrl:1
	v_add_f32_e32 v63, 1.0, v63
	v_rcp_f32_e32 v63, v63
	v_add_f32_dpp v64, v64, v64 row_ror:8 row_mask:0xf bank_mask:0xf bound_ctrl:1
	v_mov_b32_e32 v65, v64
	s_nop 1
	v_permlane16_swap_b32_e32 v64, v65
	v_add_f32_e32 v64, v64, v65
	v_mov_b32_e32 v65, v64
	s_nop 1
	s_nop 0
	v_mov_b32_e32 v64, v64
	s_nop 0
	v_add_f32_dpp v65, v76, v76 quad_perm:[1,0,3,2] row_mask:0xf bank_mask:0xf bound_ctrl:1
	v_mul_f32_e32 v64, 0xbfb8aa3b, v64
	v_exp_f32_e32 v64, v64
	v_add_f32_dpp v65, v65, v65 quad_perm:[2,3,0,1] row_mask:0xf bank_mask:0xf bound_ctrl:1
	v_mov_b32_e32 v76, v60
	s_nop 1
	v_permlane16_swap_b32_e32 v60, v76
	v_add_f32_dpp v65, v65, v65 row_ror:4 row_mask:0xf bank_mask:0xf bound_ctrl:1
	v_add_f32_e32 v64, 1.0, v64
	v_rcp_f32_e32 v102, v64
	v_add_f32_dpp v65, v65, v65 row_ror:8 row_mask:0xf bank_mask:0xf bound_ctrl:1
	v_mov_b32_e32 v66, v65
	s_nop 1
	v_permlane16_swap_b32_e32 v65, v66
	v_add_f32_e32 v65, v65, v66
	v_mov_b32_e32 v66, v65
	s_nop 1
	s_nop 0
	v_mov_b32_e32 v65, v65
	s_nop 0
	v_add_f32_dpp v66, v74, v74 quad_perm:[1,0,3,2] row_mask:0xf bank_mask:0xf bound_ctrl:1
	v_mul_f32_e32 v65, 0xbfb8aa3b, v65
	v_exp_f32_e32 v65, v65
	v_add_f32_dpp v66, v66, v66 quad_perm:[2,3,0,1] row_mask:0xf bank_mask:0xf bound_ctrl:1
	v_add_f32_e32 v111, v14, v102
	v_add_f32_e32 v76, v60, v76
	v_add_f32_dpp v66, v66, v66 row_ror:4 row_mask:0xf bank_mask:0xf bound_ctrl:1
	v_add_f32_e32 v64, 1.0, v65
	v_rcp_f32_e32 v104, v64
	v_add_f32_dpp v66, v66, v66 row_ror:8 row_mask:0xf bank_mask:0xf bound_ctrl:1
	v_mov_b32_e32 v67, v66
	s_nop 1
	v_permlane16_swap_b32_e32 v66, v67
	v_add_f32_e32 v101, v66, v67
	s_nop 0
	v_add_f32_dpp v66, v78, v78 quad_perm:[1,0,3,2] row_mask:0xf bank_mask:0xf bound_ctrl:1
	v_pk_add_f32 v[64:65], v[12:13], v[62:63]
	v_add_f32_e32 v112, v15, v104
	v_add_f32_dpp v66, v66, v66 quad_perm:[2,3,0,1] row_mask:0xf bank_mask:0xf bound_ctrl:1
	v_cmp_gt_f32_e32 vcc, v65, v64
	v_add_f32_dpp v72, v72, v72 quad_perm:[2,3,0,1] row_mask:0xf bank_mask:0xf bound_ctrl:1
	v_add_f32_dpp v66, v66, v66 row_ror:4 row_mask:0xf bank_mask:0xf bound_ctrl:1
	v_cndmask_b32_e32 v60, v64, v65, vcc
	v_cmp_gt_f32_e64 s[6:7], v111, v60
	v_add_f32_dpp v66, v66, v66 row_ror:8 row_mask:0xf bank_mask:0xf bound_ctrl:1
	v_mov_b32_e32 v67, v66
	s_nop 1
	v_permlane16_swap_b32_e32 v66, v67
	v_add_f32_e32 v105, v66, v67
	s_nop 0
	v_add_f32_dpp v66, v80, v80 quad_perm:[1,0,3,2] row_mask:0xf bank_mask:0xf bound_ctrl:1
	v_cndmask_b32_e64 v80, 0, 1, vcc
	v_cndmask_b32_e64 v60, v60, v111, s[6:7]
	v_add_f32_dpp v66, v66, v66 quad_perm:[2,3,0,1] row_mask:0xf bank_mask:0xf bound_ctrl:1
	v_cndmask_b32_e64 v80, v80, 2, s[6:7]
	v_cmp_ngt_f32_e64 s[8:9], v112, v60
	v_add_f32_dpp v66, v66, v66 row_ror:4 row_mask:0xf bank_mask:0xf bound_ctrl:1
	v_add_f32_dpp v72, v72, v72 row_ror:4 row_mask:0xf bank_mask:0xf bound_ctrl:1
	v_permlane16_swap_b32_e32 v68, v70
	v_add_f32_dpp v66, v66, v66 row_ror:8 row_mask:0xf bank_mask:0xf bound_ctrl:1
	v_mov_b32_e32 v67, v66
	s_nop 1
	v_permlane16_swap_b32_e32 v66, v67
	v_add_f32_e32 v107, v66, v67
	s_nop 0
	v_add_f32_dpp v66, v82, v82 quad_perm:[1,0,3,2] row_mask:0xf bank_mask:0xf bound_ctrl:1
	v_add_f32_dpp v72, v72, v72 row_ror:8 row_mask:0xf bank_mask:0xf bound_ctrl:1
	v_mov_b32_e32 v74, v72
	v_add_f32_dpp v66, v66, v66 quad_perm:[2,3,0,1] row_mask:0xf bank_mask:0xf bound_ctrl:1
	s_nop 0
	v_permlane16_swap_b32_e32 v72, v74
	v_add_f32_dpp v66, v66, v66 row_ror:4 row_mask:0xf bank_mask:0xf bound_ctrl:1
	v_add_f32_e32 v68, v68, v70
	v_add_f32_e32 v72, v72, v74
	v_add_f32_dpp v66, v66, v66 row_ror:8 row_mask:0xf bank_mask:0xf bound_ctrl:1
	v_mov_b32_e32 v67, v66
	s_nop 1
	v_permlane16_swap_b32_e32 v66, v67
	v_add_f32_e32 v109, v66, v67
	s_nop 0
	v_add_f32_dpp v66, v84, v84 quad_perm:[1,0,3,2] row_mask:0xf bank_mask:0xf bound_ctrl:1
	v_cndmask_b32_e64 v94, v112, v60, s[8:9]
	v_mov_b32_e32 v103, v101
	v_add_f32_dpp v66, v66, v66 quad_perm:[2,3,0,1] row_mask:0xf bank_mask:0xf bound_ctrl:1
	v_mov_b32_e32 v106, v105
	v_mov_b32_e32 v108, v107
	v_add_f32_dpp v66, v66, v66 row_ror:4 row_mask:0xf bank_mask:0xf bound_ctrl:1
	v_mov_b32_e32 v110, v109
	v_mov_b32_e32 v70, v68
	v_add_f32_dpp v66, v66, v66 row_ror:8 row_mask:0xf bank_mask:0xf bound_ctrl:1
	v_mov_b32_e32 v67, v66
	s_nop 1
	v_permlane16_swap_b32_e32 v66, v67
	v_add_f32_e32 v82, v66, v67
	s_nop 0
	v_add_f32_dpp v66, v86, v86 quad_perm:[1,0,3,2] row_mask:0xf bank_mask:0xf bound_ctrl:1
	v_mov_b32_e32 v84, v82
	v_mov_b32_e32 v74, v72
	v_add_f32_dpp v66, v66, v66 quad_perm:[2,3,0,1] row_mask:0xf bank_mask:0xf bound_ctrl:1
	v_mov_b32_e32 v78, v76
	s_nop 0
	v_add_f32_dpp v66, v66, v66 row_ror:4 row_mask:0xf bank_mask:0xf bound_ctrl:1
	s_nop 0
	s_nop 0
	v_add_f32_dpp v66, v66, v66 row_ror:8 row_mask:0xf bank_mask:0xf bound_ctrl:1
	v_mov_b32_e32 v67, v66
	s_nop 1
	v_permlane16_swap_b32_e32 v66, v67
	v_add_f32_e32 v86, v66, v67
	s_nop 0
	v_add_f32_dpp v66, v88, v88 quad_perm:[1,0,3,2] row_mask:0xf bank_mask:0xf bound_ctrl:1
	v_mov_b32_e32 v98, v86
	s_nop 0
	v_add_f32_dpp v66, v66, v66 quad_perm:[2,3,0,1] row_mask:0xf bank_mask:0xf bound_ctrl:1
	s_nop 0
	s_nop 0
	v_add_f32_dpp v66, v66, v66 row_ror:4 row_mask:0xf bank_mask:0xf bound_ctrl:1
	s_nop 0
	s_nop 0
	v_add_f32_dpp v66, v66, v66 row_ror:8 row_mask:0xf bank_mask:0xf bound_ctrl:1
	v_mov_b32_e32 v67, v66
	s_nop 1
	v_permlane16_swap_b32_e32 v66, v67
	v_add_f32_e32 v88, v66, v67
	s_nop 0
	v_add_f32_dpp v66, v90, v90 quad_perm:[1,0,3,2] row_mask:0xf bank_mask:0xf bound_ctrl:1
	v_mov_b32_e32 v99, v88
	s_nop 0
	v_add_f32_dpp v66, v66, v66 quad_perm:[2,3,0,1] row_mask:0xf bank_mask:0xf bound_ctrl:1
	s_nop 0
	s_nop 0
	v_add_f32_dpp v66, v66, v66 row_ror:4 row_mask:0xf bank_mask:0xf bound_ctrl:1
	s_nop 0
	s_nop 0
	v_add_f32_dpp v66, v66, v66 row_ror:8 row_mask:0xf bank_mask:0xf bound_ctrl:1
	v_mov_b32_e32 v67, v66
	s_nop 1
	v_permlane16_swap_b32_e32 v66, v67
	v_add_f32_e32 v90, v66, v67
	s_nop 0
	v_add_f32_dpp v66, v92, v92 quad_perm:[1,0,3,2] row_mask:0xf bank_mask:0xf bound_ctrl:1
	v_cndmask_b32_e64 v92, 3, v80, s[8:9]
	v_mov_b32_e32 v80, 0xff800000
	v_cmp_eq_u32_e64 s[10:11], 0, v92
	v_cmp_nlg_f32_e64 s[12:13], v64, v80
	s_or_b64 s[10:11], s[10:11], s[12:13]
	v_cndmask_b32_e64 v64, v64, v80, s[10:11]
	v_cmp_ne_u32_e64 s[12:13], 1, v92
	v_cmp_gt_f32_e64 s[14:15], v65, v64
	s_and_b64 s[12:13], s[12:13], s[14:15]
	v_cndmask_b32_e64 v64, v64, v65, s[12:13]
	v_add_f32_dpp v66, v66, v66 quad_perm:[2,3,0,1] row_mask:0xf bank_mask:0xf bound_ctrl:1
	v_cmp_ne_u32_e64 s[14:15], 2, v92
	v_cmp_gt_f32_e64 s[16:17], v111, v64
	v_add_f32_dpp v66, v66, v66 row_ror:4 row_mask:0xf bank_mask:0xf bound_ctrl:1
	s_and_b64 s[14:15], s[14:15], s[16:17]
	v_cndmask_b32_e64 v64, v64, v111, s[14:15]
	v_add_f32_dpp v66, v66, v66 row_ror:8 row_mask:0xf bank_mask:0xf bound_ctrl:1
	v_mov_b32_e32 v67, v66
	v_cmp_gt_f32_e64 s[16:17], v112, v64
	s_nop 0
	v_permlane16_swap_b32_e32 v66, v67
	s_and_b64 s[16:17], s[8:9], s[16:17]
	v_add_f32_e32 v66, v66, v67
	v_cndmask_b32_e64 v64, v64, v112, s[16:17]
	v_mov_b32_e32 v100, v90
	v_mov_b32_e32 v67, v66
	v_add_f32_e32 v94, v94, v64
	s_nop 0
	s_nop 0
	s_nop 0
	s_nop 0
	v_mov_b32_e32 v60, 1
	v_cmp_lg_f32_e64 s[18:19], v94, v80
	v_mov_b32_e32 v65, 0
	v_mov_b32_e32 v64, 0
	s_and_saveexec_b64 s[46:47], s[18:19]
	s_cbranch_execz .LBB0_891
	v_cndmask_b32_e64 v35, 0, 1, s[12:13]
	v_cndmask_b32_e64 v35, v35, 2, s[14:15]
	v_cndmask_b32_e64 v60, v35, 3, s[16:17]
	v_cndmask_b32_e64 v35, v62, 0, s[10:11]
	v_cndmask_b32_e64 v35, v35, v63, s[12:13]
	v_cndmask_b32_e32 v62, v62, v63, vcc
	v_cndmask_b32_e64 v35, v35, v102, s[14:15]
	v_cndmask_b32_e64 v62, v62, v102, s[6:7]
	v_cndmask_b32_e64 v35, v35, v104, s[16:17]
	v_cndmask_b32_e64 v65, v104, v62, s[8:9]
	v_mov_b32_e32 v64, v92
	v_mov_b32_e32 v80, v94

.LBB0_899:
	s_or_b64 exec, exec, s[6:7]
	v_mbcnt_lo_u32_b32 v242, -1, 0
	v_mbcnt_hi_u32_b32 v242, -1, v242
	v_lshlrev_b32_e32 v242, 4, v242
	v_mov_b32_e32 v243, 0
	v_lshl_add_u64 v[244:245], s[34:35], 0, v[242:243]
	global_load_dwordx4 v[158:161], v[244:245], off
	global_load_dwordx4 v[162:165], v[244:245], off offset:1024
	global_load_dwordx4 v[166:169], v[244:245], off offset:2048
	global_load_dwordx4 v[170:173], v[244:245], off offset:3072
	v_add_co_u32_e32 v244, vcc, 0x1000, v244
	s_nop 1
	v_addc_co_u32_e32 v245, vcc, 0, v245, vcc
	global_load_dwordx4 v[174:177], v[244:245], off
	global_load_dwordx4 v[178:181], v[244:245], off offset:1024
	global_load_dwordx4 v[182:185], v[244:245], off offset:2048
	global_load_dwordx4 v[186:189], v[244:245], off offset:3072
	v_lshl_add_u64 v[244:245], s[36:37], 0, v[242:243]
	global_load_dwordx4 v[198:201], v[244:245], off
	global_load_dwordx4 v[202:205], v[244:245], off offset:1024
	global_load_dwordx4 v[216:219], v[244:245], off offset:2048
	global_load_dwordx4 v[220:223], v[244:245], off offset:3072
	v_add_co_u32_e32 v244, vcc, 0x1000, v244
	s_nop 1
	v_addc_co_u32_e32 v245, vcc, 0, v245, vcc
	global_load_dwordx4 v[224:227], v[244:245], off
	global_load_dwordx4 v[228:231], v[244:245], off offset:1024
	global_load_dwordx4 v[232:235], v[244:245], off offset:2048
	global_load_dwordx4 v[246:249], v[244:245], off offset:3072
	s_waitcnt vmcnt(0)
	v_lshlrev_b32_e32 v80, 16, v58
	v_and_b32_e32 v81, 0xffff0000, v58
	v_lshlrev_b32_e32 v78, 16, v59
	v_and_b32_e32 v79, 0xffff0000, v59
	v_add_f32_e32 v35, v80, v81
	v_add_f32_e32 v58, v78, v79
	v_lshlrev_b32_e32 v62, 16, v56
	v_and_b32_e32 v63, 0xffff0000, v56
	v_lshlrev_b32_e32 v60, 16, v57
	v_and_b32_e32 v61, 0xffff0000, v57
	v_add_f32_e32 v35, v35, v58
	v_add_f32_e32 v56, v62, v63
	v_add_f32_e32 v57, v60, v61
	v_lshlrev_b32_e32 v68, 16, v54
	v_and_b32_e32 v69, 0xffff0000, v54
	v_lshlrev_b32_e32 v70, 16, v55
	v_and_b32_e32 v71, 0xffff0000, v55
	v_add_f32_e32 v35, 0, v35
	v_add_f32_e32 v56, v56, v57
	v_add_f32_e32 v54, v68, v69
	v_add_f32_e32 v55, v70, v71
	v_lshlrev_b32_e32 v72, 16, v52
	v_and_b32_e32 v73, 0xffff0000, v52
	v_lshlrev_b32_e32 v74, 16, v53
	v_and_b32_e32 v75, 0xffff0000, v53
	v_add_f32_e32 v35, v35, v56
	v_add_f32_e32 v54, v54, v55
	v_add_f32_e32 v52, v72, v73
	v_add_f32_e32 v53, v74, v75
	v_lshlrev_b32_e32 v64, 16, v50
	v_and_b32_e32 v65, 0xffff0000, v50
	v_lshlrev_b32_e32 v66, 16, v51
	v_and_b32_e32 v67, 0xffff0000, v51
	v_add_f32_e32 v35, v35, v54
	v_add_f32_e32 v52, v52, v53
	v_add_f32_e32 v50, v64, v65
	v_add_f32_e32 v51, v66, v67
	v_lshlrev_b32_e32 v56, 16, v48
	v_and_b32_e32 v57, 0xffff0000, v48
	v_lshlrev_b32_e32 v58, 16, v49
	v_and_b32_e32 v59, 0xffff0000, v49
	v_add_f32_e32 v35, v35, v52
	v_add_f32_e32 v50, v50, v51
	v_add_f32_e32 v48, v56, v57
	v_add_f32_e32 v49, v58, v59
	v_lshlrev_b32_e32 v52, 16, v46
	v_and_b32_e32 v53, 0xffff0000, v46
	v_lshlrev_b32_e32 v54, 16, v47
	v_and_b32_e32 v55, 0xffff0000, v47
	v_add_f32_e32 v35, v35, v50
	v_add_f32_e32 v48, v48, v49
	v_add_f32_e32 v46, v52, v53
	v_add_f32_e32 v47, v54, v55
	v_add_f32_e32 v35, v35, v48
	v_add_f32_e32 v46, v46, v47
	v_add_f32_e32 v35, v35, v46
	v_lshlrev_b32_e32 v46, 16, v44
	v_and_b32_e32 v47, 0xffff0000, v44
	v_lshlrev_b32_e32 v44, 16, v45
	v_and_b32_e32 v45, 0xffff0000, v45
	v_add_f32_e32 v48, v46, v47
	v_add_f32_e32 v49, v44, v45
	v_add_f32_e32 v48, v48, v49
	v_add_f32_e32 v35, v35, v48
	s_mov_b64 s[6:7], s[34:35]
	s_mov_b64 s[8:9], s[36:37]
	v_add_f32_dpp v35, v35, v35 quad_perm:[1,0,3,2] row_mask:0xf bank_mask:0xf bound_ctrl:1
	v_lshl_add_u64 v[92:93], s[6:7], 0, v[192:193]
	s_lshl_b64 s[6:7], s[38:39], 11
	v_add_f32_dpp v35, v35, v35 quad_perm:[2,3,0,1] row_mask:0xf bank_mask:0xf bound_ctrl:1
	v_lshl_add_u64 v[94:95], s[8:9], 0, v[192:193]
	v_add_co_u32_e32 v98, vcc, s33, v92
	v_add_f32_dpp v35, v35, v35 row_ror:4 row_mask:0xf bank_mask:0xf bound_ctrl:1
	s_nop 0
	v_addc_co_u32_e32 v99, vcc, 0, v93, vcc
	v_add_f32_dpp v35, v35, v35 row_ror:8 row_mask:0xf bank_mask:0xf bound_ctrl:1
	v_mov_b32_e32 v48, v35
	s_nop 1
	v_permlane16_swap_b32_e32 v35, v48
	v_add_f32_e32 v35, v35, v48
	v_mov_b32_e32 v48, v35
	s_nop 1
	v_permlane32_swap_b32_e32 v35, v48
	v_add_f32_e32 v35, v35, v48
	v_fmac_f32_e32 v79, 0xba000000, v35
	v_fmac_f32_e32 v81, 0xba000000, v35
	v_fmac_f32_e32 v78, 0xba000000, v35
	v_fmac_f32_e32 v80, 0xba000000, v35
	v_mul_f32_e32 v48, v81, v81
	v_mul_f32_e32 v49, v79, v79
	v_fmac_f32_e32 v48, v80, v80
	v_fmac_f32_e32 v49, v78, v78
	v_fmac_f32_e32 v61, 0xba000000, v35
	v_fmac_f32_e32 v63, 0xba000000, v35
	v_add_f32_e32 v48, v48, v49
	v_fmac_f32_e32 v60, 0xba000000, v35
	v_fmac_f32_e32 v62, 0xba000000, v35
	v_mul_f32_e32 v49, v63, v63
	v_mul_f32_e32 v50, v61, v61
	v_fmac_f32_e32 v49, v62, v62
	v_fmac_f32_e32 v50, v60, v60
	v_add_f32_e32 v49, v49, v50
	v_add_f32_e32 v76, v48, v49
	s_nop 0
	v_fmac_f32_e32 v71, 0xba000000, v35
	v_fmac_f32_e32 v69, 0xba000000, v35
	v_fmac_f32_e32 v70, 0xba000000, v35
	v_fmac_f32_e32 v68, 0xba000000, v35
	v_mul_f32_e32 v77, v69, v69
	v_mul_f32_e32 v82, v71, v71
	v_fmac_f32_e32 v77, v68, v68
	v_fmac_f32_e32 v82, v70, v70
	v_add_f32_e32 v77, v77, v82
	v_fmac_f32_e32 v75, 0xba000000, v35
	v_fmac_f32_e32 v73, 0xba000000, v35
	v_add_f32_e32 v76, v76, v77
	v_fmac_f32_e32 v74, 0xba000000, v35
	v_fmac_f32_e32 v72, 0xba000000, v35
	v_mul_f32_e32 v77, v73, v73
	v_mul_f32_e32 v82, v75, v75
	v_fmac_f32_e32 v77, v72, v72
	v_fmac_f32_e32 v82, v74, v74
	v_add_f32_e32 v77, v77, v82
	v_fmac_f32_e32 v67, 0xba000000, v35
	v_fmac_f32_e32 v65, 0xba000000, v35
	v_add_f32_e32 v76, v76, v77
	v_fmac_f32_e32 v66, 0xba000000, v35
	v_fmac_f32_e32 v64, 0xba000000, v35
	v_mul_f32_e32 v77, v65, v65
	v_mul_f32_e32 v82, v67, v67
	v_fmac_f32_e32 v77, v64, v64
	v_fmac_f32_e32 v82, v66, v66
	v_add_f32_e32 v77, v77, v82
	v_fmac_f32_e32 v59, 0xba000000, v35
	v_fmac_f32_e32 v57, 0xba000000, v35
	v_add_f32_e32 v76, v76, v77
	v_fmac_f32_e32 v58, 0xba000000, v35
	v_fmac_f32_e32 v56, 0xba000000, v35
	v_mul_f32_e32 v77, v57, v57
	v_mul_f32_e32 v82, v59, v59
	v_fmac_f32_e32 v77, v56, v56
	v_fmac_f32_e32 v82, v58, v58
	v_add_f32_e32 v77, v77, v82
	v_fmac_f32_e32 v55, 0xba000000, v35
	v_fmac_f32_e32 v53, 0xba000000, v35
	v_add_f32_e32 v76, v76, v77
	v_fmac_f32_e32 v54, 0xba000000, v35
	v_fmac_f32_e32 v52, 0xba000000, v35
	v_mul_f32_e32 v77, v53, v53
	v_mul_f32_e32 v82, v55, v55
	v_fmac_f32_e32 v77, v52, v52
	v_fmac_f32_e32 v82, v54, v54
	v_add_f32_e32 v77, v77, v82
	v_fmac_f32_e32 v45, 0xba000000, v35
	v_fmac_f32_e32 v47, 0xba000000, v35
	v_add_f32_e32 v76, v76, v77
	v_fmac_f32_e32 v44, 0xba000000, v35
	v_fmac_f32_e32 v46, 0xba000000, v35
	v_mul_f32_e32 v35, v47, v47
	v_mul_f32_e32 v77, v45, v45
	v_fmac_f32_e32 v35, v46, v46
	v_fmac_f32_e32 v77, v44, v44
	v_add_f32_e32 v35, v35, v77
	v_add_f32_e32 v35, v76, v35
	v_lshl_add_u64 v[82:83], v[30:31], 0, s[6:7]
	v_add_co_u32_e32 v100, vcc, s33, v94
	v_add_f32_dpp v35, v35, v35 quad_perm:[1,0,3,2] row_mask:0xf bank_mask:0xf bound_ctrl:1
	s_nop 0
	v_addc_co_u32_e32 v101, vcc, 0, v95, vcc
	v_add_f32_dpp v35, v35, v35 quad_perm:[2,3,0,1] row_mask:0xf bank_mask:0xf bound_ctrl:1
	s_nop 1
	v_add_f32_dpp v35, v35, v35 row_ror:4 row_mask:0xf bank_mask:0xf bound_ctrl:1
	s_nop 1
	v_add_f32_dpp v35, v35, v35 row_ror:8 row_mask:0xf bank_mask:0xf bound_ctrl:1
	v_mov_b32_e32 v76, v35
	s_nop 1
	v_permlane16_swap_b32_e32 v35, v76
	v_add_f32_e32 v35, v35, v76
	v_mov_b32_e32 v76, v35
	s_nop 1
	v_permlane32_swap_b32_e32 v35, v76
	v_add_f32_e32 v35, v35, v76
	v_fmamk_f32 v35, v35, 0x3a000000, v207
	v_rsq_f32_e32 v96, v35
	v_lshl_add_u64 v[76:77], v[28:29], 0, s[44:45]
	v_pk_mul_f32 v[80:81], v[96:97], v[80:81] op_sel_hi:[0,1]
	s_waitcnt vmcnt(0) lgkmcnt(0)
	v_pk_fma_f32 v[48:49], v[158:159], v[80:81], v[198:199]
	v_mov_b32_e32 v81, 0
	v_med3_f32 v35, v48, s69, v208
	v_med3_f32 v80, v49, s69, v208
	v_cvt_pk_fp8_f32 v81, v35, v80
	v_pk_mul_f32 v[78:79], v[96:97], v[78:79] op_sel_hi:[0,1]
	v_pk_fma_f32 v[50:51], v[160:161], v[78:79], v[200:201]
	v_pk_mul_f32 v[62:63], v[96:97], v[62:63] op_sel_hi:[0,1]
	v_med3_f32 v35, v50, s69, v208
	v_med3_f32 v78, v51, s69, v208
	v_cvt_pk_fp8_f32 v81, v35, v78 op_sel:[0,0,1]
	v_cvt_pk_bf16_f32 v78, v48, v49
	v_cvt_pk_bf16_f32 v79, v50, v51
	global_store_dwordx2 v[76:77], v[78:79], off nt
	global_store_dword v[82:83], v81, off nt
	s_nop 0
	s_nop 0
	v_pk_mul_f32 v[88:89], v[96:97], v[60:61] op_sel_hi:[0,1]
	v_pk_mul_f32 v[68:69], v[96:97], v[68:69] op_sel_hi:[0,1]
	v_pk_mul_f32 v[72:73], v[96:97], v[72:73] op_sel_hi:[0,1]
	v_pk_mul_f32 v[74:75], v[96:97], v[74:75] op_sel_hi:[0,1]
	v_pk_mul_f32 v[64:65], v[96:97], v[64:65] op_sel_hi:[0,1]
	v_pk_mul_f32 v[66:67], v[96:97], v[66:67] op_sel_hi:[0,1]
	v_pk_mul_f32 v[56:57], v[96:97], v[56:57] op_sel_hi:[0,1]
	v_pk_mul_f32 v[58:59], v[96:97], v[58:59] op_sel_hi:[0,1]
	v_pk_mul_f32 v[52:53], v[96:97], v[52:53] op_sel_hi:[0,1]
	v_pk_mul_f32 v[54:55], v[96:97], v[54:55] op_sel_hi:[0,1]
	v_pk_mul_f32 v[46:47], v[96:97], v[46:47] op_sel_hi:[0,1]
	v_pk_mul_f32 v[44:45], v[96:97], v[44:45] op_sel_hi:[0,1]
	s_nop 0
	v_pk_fma_f32 v[60:61], v[162:163], v[62:63], v[202:203]
	s_nop 0
	v_med3_f32 v35, v60, s69, v208
	v_med3_f32 v62, v61, s69, v208
	v_mov_b32_e32 v84, 0
	v_cvt_pk_fp8_f32 v84, v35, v62
	v_pk_fma_f32 v[62:63], v[164:165], v[88:89], v[204:205]
	v_pk_mul_f32 v[88:89], v[96:97], v[70:71] op_sel_hi:[0,1]
	v_med3_f32 v35, v62, s69, v208
	v_med3_f32 v78, v63, s69, v208
	v_cvt_pk_fp8_f32 v84, v35, v78 op_sel:[0,0,1]
	v_cvt_pk_bf16_f32 v78, v60, v61
	v_cvt_pk_bf16_f32 v79, v62, v63
	global_store_dwordx2 v[76:77], v[78:79], off offset:512 nt
	global_store_dword v[82:83], v84, off offset:256 nt
	s_nop 0
	s_nop 0
	v_mov_b32_e32 v35, 0
	s_nop 0
	v_pk_fma_f32 v[70:71], v[166:167], v[68:69], v[216:217]
	s_nop 0
	v_med3_f32 v68, v70, s69, v208
	v_med3_f32 v69, v71, s69, v208
	v_cvt_pk_fp8_f32 v35, v68, v69
	v_pk_fma_f32 v[68:69], v[168:169], v[88:89], v[218:219]
	s_nop 0
	v_med3_f32 v78, v68, s69, v208
	v_med3_f32 v79, v69, s69, v208
	v_cvt_pk_fp8_f32 v35, v78, v79 op_sel:[0,0,1]
	v_cvt_pk_bf16_f32 v78, v70, v71
	v_cvt_pk_bf16_f32 v79, v68, v69
	global_store_dwordx2 v[76:77], v[78:79], off offset:1024 nt
	global_store_dword v[82:83], v35, off offset:512 nt
	s_nop 0
	v_mov_b32_e32 v35, 0
	s_nop 0
	v_pk_fma_f32 v[80:81], v[170:171], v[72:73], v[220:221]
	s_nop 0
	v_med3_f32 v72, v80, s69, v208
	v_med3_f32 v73, v81, s69, v208
	v_cvt_pk_fp8_f32 v35, v72, v73
	v_pk_fma_f32 v[78:79], v[172:173], v[74:75], v[222:223]
	s_nop 0
	v_med3_f32 v72, v78, s69, v208
	v_med3_f32 v73, v79, s69, v208
	v_cvt_pk_fp8_f32 v35, v72, v73 op_sel:[0,0,1]
	v_cvt_pk_bf16_f32 v72, v80, v81
	v_cvt_pk_bf16_f32 v73, v78, v79
	global_store_dwordx2 v[76:77], v[72:73], off offset:1536 nt
	global_store_dword v[82:83], v35, off offset:768 nt
	s_nop 0
	s_nop 0
	v_mov_b32_e32 v35, 0
	s_nop 0
	v_pk_fma_f32 v[86:87], v[174:175], v[64:65], v[224:225]
	s_nop 0
	v_med3_f32 v64, v86, s69, v208
	v_med3_f32 v65, v87, s69, v208
	v_cvt_pk_fp8_f32 v35, v64, v65
	v_pk_fma_f32 v[84:85], v[176:177], v[66:67], v[226:227]
	s_nop 0
	v_med3_f32 v64, v84, s69, v208
	v_med3_f32 v65, v85, s69, v208
	v_cvt_pk_fp8_f32 v35, v64, v65 op_sel:[0,0,1]
	v_cvt_pk_bf16_f32 v64, v86, v87
	v_cvt_pk_bf16_f32 v65, v84, v85
	global_store_dwordx2 v[76:77], v[64:65], off offset:2048 nt
	global_store_dword v[82:83], v35, off offset:1024 nt
	s_nop 0
	s_nop 0
	v_mov_b32_e32 v35, 0
	s_nop 0
	v_pk_fma_f32 v[90:91], v[178:179], v[56:57], v[228:229]
	s_nop 0
	v_med3_f32 v56, v90, s69, v208
	v_med3_f32 v57, v91, s69, v208
	v_cvt_pk_fp8_f32 v35, v56, v57
	v_pk_fma_f32 v[88:89], v[180:181], v[58:59], v[230:231]
	s_nop 0
	v_med3_f32 v56, v88, s69, v208
	v_med3_f32 v57, v89, s69, v208
	v_cvt_pk_fp8_f32 v35, v56, v57 op_sel:[0,0,1]
	v_cvt_pk_bf16_f32 v56, v90, v91
	v_cvt_pk_bf16_f32 v57, v88, v89
	global_store_dwordx2 v[76:77], v[56:57], off offset:2560 nt
	global_store_dword v[82:83], v35, off offset:1280 nt
	s_nop 0
	s_nop 0
	v_mov_b32_e32 v35, 0
	s_nop 0
	v_pk_fma_f32 v[94:95], v[182:183], v[52:53], v[232:233]
	s_nop 0
	v_med3_f32 v52, v94, s69, v208
	v_med3_f32 v53, v95, s69, v208
	v_cvt_pk_fp8_f32 v35, v52, v53
	v_pk_fma_f32 v[92:93], v[184:185], v[54:55], v[234:235]
	s_nop 0
	v_med3_f32 v52, v92, s69, v208
	v_med3_f32 v53, v93, s69, v208
	v_cvt_pk_fp8_f32 v35, v52, v53 op_sel:[0,0,1]
	v_cvt_pk_bf16_f32 v52, v94, v95
	v_cvt_pk_bf16_f32 v53, v92, v93
	global_store_dwordx2 v[76:77], v[52:53], off offset:3072 nt
	global_store_dword v[82:83], v35, off offset:1536 nt
	s_nop 0
	s_nop 0
	v_mov_b32_e32 v35, 0
	s_nop 0
	v_pk_fma_f32 v[96:97], v[186:187], v[46:47], v[246:247]
	s_nop 0
	v_med3_f32 v46, v96, s69, v208
	v_med3_f32 v47, v97, s69, v208
	v_mov_b32_e32 v52, 0
	v_cvt_pk_fp8_f32 v52, v46, v47
	v_pk_fma_f32 v[98:99], v[188:189], v[44:45], v[248:249]
	s_nop 0
	v_med3_f32 v44, v98, s69, v208
	v_med3_f32 v45, v99, s69, v208
	v_cvt_pk_fp8_f32 v52, v44, v45 op_sel:[0,0,1]
	v_cvt_pk_bf16_f32 v44, v96, v97
	v_cvt_pk_bf16_f32 v45, v98, v99
	global_store_dwordx2 v[76:77], v[44:45], off offset:3584 nt
	global_store_dword v[82:83], v52, off offset:1792 nt
	v_lshlrev_b32_e32 v102, 16, v42
	v_and_b32_e32 v103, 0xffff0000, v42
	v_lshlrev_b32_e32 v100, 16, v43
	v_and_b32_e32 v101, 0xffff0000, v43
	v_add_f32_e32 v42, v102, v103
	v_add_f32_e32 v43, v100, v101
	v_lshlrev_b32_e32 v74, 16, v40
	v_and_b32_e32 v75, 0xffff0000, v40
	v_lshlrev_b32_e32 v72, 16, v41
	v_and_b32_e32 v73, 0xffff0000, v41
	v_add_f32_e32 v42, v42, v43
	v_add_f32_e32 v40, v74, v75
	v_add_f32_e32 v41, v72, v73
	v_lshlrev_b32_e32 v64, 16, v38
	v_and_b32_e32 v65, 0xffff0000, v38
	v_lshlrev_b32_e32 v66, 16, v39
	v_and_b32_e32 v67, 0xffff0000, v39
	v_add_f32_e32 v42, 0, v42
	v_add_f32_e32 v40, v40, v41
	v_add_f32_e32 v38, v64, v65
	v_add_f32_e32 v39, v66, v67
	v_lshlrev_b32_e32 v56, 16, v36
	v_and_b32_e32 v57, 0xffff0000, v36
	v_lshlrev_b32_e32 v58, 16, v37
	v_and_b32_e32 v59, 0xffff0000, v37
	v_add_f32_e32 v40, v42, v40
	v_add_f32_e32 v38, v38, v39
	v_add_f32_e32 v36, v56, v57
	v_add_f32_e32 v37, v58, v59
	v_lshlrev_b32_e32 v52, 16, v22
	v_and_b32_e32 v53, 0xffff0000, v22
	v_lshlrev_b32_e32 v54, 16, v23
	v_and_b32_e32 v55, 0xffff0000, v23
	v_add_f32_e32 v38, v40, v38
	v_add_f32_e32 v36, v36, v37
	v_add_f32_e32 v22, v52, v53
	v_add_f32_e32 v23, v54, v55
	v_add_f32_e32 v36, v38, v36
	v_add_f32_e32 v22, v22, v23
	v_lshlrev_b32_e32 v44, 16, v20
	v_and_b32_e32 v45, 0xffff0000, v20
	v_lshlrev_b32_e32 v46, 16, v21
	v_and_b32_e32 v47, 0xffff0000, v21
	v_add_f32_e32 v22, v36, v22
	v_add_f32_e32 v20, v44, v45
	v_add_f32_e32 v21, v46, v47
	v_lshlrev_b32_e32 v36, 16, v18
	v_and_b32_e32 v37, 0xffff0000, v18
	v_lshlrev_b32_e32 v38, 16, v19
	v_and_b32_e32 v39, 0xffff0000, v19
	v_add_f32_e32 v20, v20, v21
	v_add_f32_e32 v18, v36, v37
	v_add_f32_e32 v19, v38, v39
	v_lshlrev_b32_e32 v42, 16, v16
	v_and_b32_e32 v43, 0xffff0000, v16
	v_lshlrev_b32_e32 v40, 16, v17
	v_and_b32_e32 v41, 0xffff0000, v17
	v_add_f32_e32 v20, v22, v20
	v_add_f32_e32 v18, v18, v19
	v_add_f32_e32 v16, v42, v43
	v_add_f32_e32 v17, v40, v41
	v_add_f32_e32 v18, v20, v18
	v_add_f32_e32 v16, v16, v17
	v_add_f32_e32 v16, v18, v16
	s_mov_b64 s[6:7], s[34:35]
	s_mov_b64 s[8:9], s[36:37]
	v_add_f32_dpp v16, v16, v16 quad_perm:[1,0,3,2] row_mask:0xf bank_mask:0xf bound_ctrl:1
	v_lshl_add_u64 v[108:109], s[6:7], 0, v[192:193]
	v_lshl_add_u64 v[104:105], v[28:29], 0, s[42:43]
	v_add_f32_dpp v16, v16, v16 quad_perm:[2,3,0,1] row_mask:0xf bank_mask:0xf bound_ctrl:1
	v_lshl_add_u64 v[106:107], s[8:9], 0, v[192:193]
	s_lshl_b64 s[6:7], s[40:41], 11
	v_add_f32_dpp v16, v16, v16 row_ror:4 row_mask:0xf bank_mask:0xf bound_ctrl:1
	v_lshl_add_u64 v[82:83], v[30:31], 0, s[6:7]
	s_nop 0
	v_add_f32_dpp v16, v16, v16 row_ror:8 row_mask:0xf bank_mask:0xf bound_ctrl:1
	v_mov_b32_e32 v17, v16
	s_nop 1
	v_permlane16_swap_b32_e32 v16, v17
	v_add_f32_e32 v16, v16, v17
	v_mov_b32_e32 v17, v16
	s_nop 1
	v_permlane32_swap_b32_e32 v16, v17
	v_add_f32_e32 v16, v16, v17
	v_fmac_f32_e32 v101, 0xba000000, v16
	v_fmac_f32_e32 v103, 0xba000000, v16
	v_fmac_f32_e32 v100, 0xba000000, v16
	v_fmac_f32_e32 v102, 0xba000000, v16
	v_mul_f32_e32 v17, v103, v103
	v_mul_f32_e32 v18, v101, v101
	v_fmac_f32_e32 v17, v102, v102
	v_fmac_f32_e32 v18, v100, v100
	v_fmac_f32_e32 v73, 0xba000000, v16
	v_fmac_f32_e32 v75, 0xba000000, v16
	v_add_f32_e32 v17, v17, v18
	v_fmac_f32_e32 v72, 0xba000000, v16
	v_fmac_f32_e32 v74, 0xba000000, v16
	v_mul_f32_e32 v18, v75, v75
	v_mul_f32_e32 v19, v73, v73
	v_fmac_f32_e32 v18, v74, v74
	v_fmac_f32_e32 v19, v72, v72
	v_add_f32_e32 v18, v18, v19
	v_fmac_f32_e32 v67, 0xba000000, v16
	v_fmac_f32_e32 v65, 0xba000000, v16
	v_add_f32_e32 v17, v17, v18
	v_fmac_f32_e32 v66, 0xba000000, v16
	v_fmac_f32_e32 v64, 0xba000000, v16
	v_mul_f32_e32 v18, v65, v65
	v_mul_f32_e32 v19, v67, v67
	v_fmac_f32_e32 v18, v64, v64
	v_fmac_f32_e32 v19, v66, v66
	v_add_f32_e32 v18, v18, v19
	v_fmac_f32_e32 v59, 0xba000000, v16
	v_fmac_f32_e32 v57, 0xba000000, v16
	v_add_f32_e32 v17, v17, v18
	v_fmac_f32_e32 v58, 0xba000000, v16
	v_fmac_f32_e32 v56, 0xba000000, v16
	v_mul_f32_e32 v18, v57, v57
	v_mul_f32_e32 v19, v59, v59
	v_fmac_f32_e32 v18, v56, v56
	v_fmac_f32_e32 v19, v58, v58
	v_add_f32_e32 v18, v18, v19
	v_fmac_f32_e32 v55, 0xba000000, v16
	v_fmac_f32_e32 v53, 0xba000000, v16
	v_add_f32_e32 v17, v17, v18
	v_fmac_f32_e32 v54, 0xba000000, v16
	v_fmac_f32_e32 v52, 0xba000000, v16
	v_mul_f32_e32 v18, v53, v53
	v_mul_f32_e32 v19, v55, v55
	v_fmac_f32_e32 v18, v52, v52
	v_fmac_f32_e32 v19, v54, v54
	v_add_f32_e32 v18, v18, v19
	v_fmac_f32_e32 v47, 0xba000000, v16
	v_fmac_f32_e32 v45, 0xba000000, v16
	v_add_f32_e32 v17, v17, v18
	v_fmac_f32_e32 v46, 0xba000000, v16
	v_fmac_f32_e32 v44, 0xba000000, v16
	v_mul_f32_e32 v18, v45, v45
	v_mul_f32_e32 v19, v47, v47
	v_fmac_f32_e32 v18, v44, v44
	v_fmac_f32_e32 v19, v46, v46
	v_add_f32_e32 v18, v18, v19
	v_fmac_f32_e32 v39, 0xba000000, v16
	v_fmac_f32_e32 v37, 0xba000000, v16
	v_add_f32_e32 v17, v17, v18
	v_fmac_f32_e32 v38, 0xba000000, v16
	v_fmac_f32_e32 v36, 0xba000000, v16
	v_mul_f32_e32 v18, v37, v37
	v_mul_f32_e32 v19, v39, v39
	v_fmac_f32_e32 v18, v36, v36
	v_fmac_f32_e32 v19, v38, v38
	v_add_f32_e32 v18, v18, v19
	v_fmac_f32_e32 v41, 0xba000000, v16
	v_fmac_f32_e32 v43, 0xba000000, v16
	v_add_f32_e32 v17, v17, v18
	v_fmac_f32_e32 v40, 0xba000000, v16
	v_fmac_f32_e32 v42, 0xba000000, v16
	v_mul_f32_e32 v16, v43, v43
	v_mul_f32_e32 v18, v41, v41
	v_fmac_f32_e32 v16, v42, v42
	v_fmac_f32_e32 v18, v40, v40
	v_add_f32_e32 v16, v16, v18
	v_add_f32_e32 v16, v17, v16
	s_nop 1
	v_add_f32_dpp v16, v16, v16 quad_perm:[1,0,3,2] row_mask:0xf bank_mask:0xf bound_ctrl:1
	s_nop 1
	v_add_f32_dpp v16, v16, v16 quad_perm:[2,3,0,1] row_mask:0xf bank_mask:0xf bound_ctrl:1
	s_nop 1
	v_add_f32_dpp v16, v16, v16 row_ror:4 row_mask:0xf bank_mask:0xf bound_ctrl:1
	s_nop 1
	v_add_f32_dpp v16, v16, v16 row_ror:8 row_mask:0xf bank_mask:0xf bound_ctrl:1
	v_mov_b32_e32 v17, v16
	s_nop 1
	v_permlane16_swap_b32_e32 v16, v17
	v_add_f32_e32 v16, v16, v17
	v_mov_b32_e32 v17, v16
	s_nop 1
	v_permlane32_swap_b32_e32 v16, v17
	v_add_f32_e32 v16, v16, v17
	v_fmamk_f32 v16, v16, 0x3a000000, v207
	v_rsq_f32_e32 v76, v16
	s_nop 0
	v_pk_mul_f32 v[102:103], v[76:77], v[102:103] op_sel_hi:[0,1]
	v_pk_mul_f32 v[100:101], v[76:77], v[100:101] op_sel_hi:[0,1]
	v_pk_mul_f32 v[74:75], v[76:77], v[74:75] op_sel_hi:[0,1]
	v_pk_mul_f32 v[72:73], v[76:77], v[72:73] op_sel_hi:[0,1]
	v_pk_mul_f32 v[110:111], v[76:77], v[64:65] op_sel_hi:[0,1]
	v_pk_mul_f32 v[64:65], v[76:77], v[66:67] op_sel_hi:[0,1]
	s_waitcnt vmcnt(0) lgkmcnt(0)
	v_pk_fma_f32 v[100:101], v[160:161], v[100:101], v[200:201]
	v_pk_fma_f32 v[102:103], v[158:159], v[102:103], v[198:199]
	v_mov_b32_e32 v20, 0
	v_cvt_pk_bf16_f32 v16, v102, v103
	v_cvt_pk_bf16_f32 v17, v100, v101
	global_store_dwordx2 v[104:105], v[16:17], off nt
	v_med3_f32 v16, v102, s69, v208
	v_med3_f32 v17, v103, s69, v208
	v_cvt_pk_fp8_f32 v20, v16, v17
	v_med3_f32 v18, v100, s69, v208
	v_med3_f32 v19, v101, s69, v208
	v_cvt_pk_fp8_f32 v20, v18, v19 op_sel:[0,0,1]
	global_store_dword v[82:83], v20, off nt
	s_nop 0
	s_nop 0
	s_nop 0
	v_pk_fma_f32 v[72:73], v[164:165], v[72:73], v[204:205]
	v_pk_fma_f32 v[74:75], v[162:163], v[74:75], v[202:203]
	v_mov_b32_e32 v20, 0
	v_cvt_pk_bf16_f32 v16, v74, v75
	v_cvt_pk_bf16_f32 v17, v72, v73
	global_store_dwordx2 v[104:105], v[16:17], off offset:512 nt
	v_med3_f32 v16, v74, s69, v208
	v_med3_f32 v17, v75, s69, v208
	v_cvt_pk_fp8_f32 v20, v16, v17
	v_med3_f32 v18, v72, s69, v208
	v_med3_f32 v19, v73, s69, v208
	v_cvt_pk_fp8_f32 v20, v18, v19 op_sel:[0,0,1]
	global_store_dword v[82:83], v20, off offset:256 nt
	s_nop 0
	s_nop 0
	s_nop 0
	v_pk_fma_f32 v[64:65], v[168:169], v[64:65], v[218:219]
	v_pk_fma_f32 v[66:67], v[166:167], v[110:111], v[216:217]
	v_mov_b32_e32 v20, 0
	v_cvt_pk_bf16_f32 v16, v66, v67
	v_cvt_pk_bf16_f32 v17, v64, v65
	global_store_dwordx2 v[104:105], v[16:17], off offset:1024 nt
	v_med3_f32 v16, v66, s69, v208
	v_med3_f32 v17, v67, s69, v208
	v_cvt_pk_fp8_f32 v20, v16, v17
	v_med3_f32 v18, v64, s69, v208
	v_med3_f32 v19, v65, s69, v208
	v_pk_mul_f32 v[110:111], v[76:77], v[56:57] op_sel_hi:[0,1]
	v_cvt_pk_fp8_f32 v20, v18, v19 op_sel:[0,0,1]
	v_pk_mul_f32 v[56:57], v[76:77], v[58:59] op_sel_hi:[0,1]
	global_store_dword v[82:83], v20, off offset:512 nt
	s_nop 0
	s_nop 0
	s_nop 0
	v_pk_fma_f32 v[56:57], v[172:173], v[56:57], v[222:223]
	v_pk_fma_f32 v[58:59], v[170:171], v[110:111], v[220:221]
	v_mov_b32_e32 v20, 0
	v_cvt_pk_bf16_f32 v16, v58, v59
	v_cvt_pk_bf16_f32 v17, v56, v57
	global_store_dwordx2 v[104:105], v[16:17], off offset:1536 nt
	v_med3_f32 v16, v58, s69, v208
	v_med3_f32 v17, v59, s69, v208
	v_cvt_pk_fp8_f32 v20, v16, v17
	v_med3_f32 v18, v56, s69, v208
	v_med3_f32 v19, v57, s69, v208
	v_add_co_u32_e32 v16, vcc, s33, v108
	v_cvt_pk_fp8_f32 v20, v18, v19 op_sel:[0,0,1]
	s_nop 0
	v_addc_co_u32_e32 v17, vcc, 0, v109, vcc
	v_add_co_u32_e32 v18, vcc, s33, v106
	global_store_dword v[82:83], v20, off offset:768 nt
	s_nop 0
	v_addc_co_u32_e32 v19, vcc, 0, v107, vcc
	s_nop 0
	v_pk_mul_f32 v[110:111], v[76:77], v[52:53] op_sel_hi:[0,1]
	v_pk_mul_f32 v[52:53], v[76:77], v[54:55] op_sel_hi:[0,1]
	v_mov_b32_e32 v77, 0
	s_nop 0
	v_pk_fma_f32 v[52:53], v[176:177], v[52:53], v[226:227]
	v_pk_fma_f32 v[54:55], v[174:175], v[110:111], v[224:225]
	v_med3_f32 v22, v52, s69, v208
	v_cvt_pk_bf16_f32 v20, v54, v55
	v_cvt_pk_bf16_f32 v21, v52, v53
	global_store_dwordx2 v[104:105], v[20:21], off offset:2048 nt
	v_med3_f32 v20, v54, s69, v208
	v_med3_f32 v21, v55, s69, v208
	v_cvt_pk_fp8_f32 v77, v20, v21
	v_med3_f32 v23, v53, s69, v208
; #define LAS __attribute__((address_space(3)))
; __global__ void __launch_bounds__(NTHREADS, 2) hybrid_fwd(Args a) {
;     ...
;                     f32x2 y2[8][4];
; #pragma unroll
;                     for (int j = 0; j < 8; ++j)
; #pragma unroll
;                         for (int c = 0; c < 4; ++c) y2[j][c] = (f32x2){ya[j][c], yb[j][c]};
;                     f32x2 acc2[16];
; #pragma unroll
;                     for (int e = 0; e < 16; ++e) acc2[e] = (f32x2){0.f, 0.f};
; #pragma unroll
;                     for (int j = 0; j < 8; ++j) {
; #pragma unroll
;                         for (int e = 0; e < 16; ++e) { const f32x4 w = *(const LAS f32x4*)(rwT + e * 2052 + j * 256 + lane * 4);
;                             acc2[e] += y2[j][0] * (f32x2){w[0], w[0]}; acc2[e] += y2[j][1] * (f32x2){w[1], w[1]};
;                             acc2[e] += y2[j][2] * (f32x2){w[2], w[2]}; acc2[e] += y2[j][3] * (f32x2){w[3], w[3]}; }
;                         __builtin_amdgcn_sched_barrier(0);
;                     }
	v_cvt_pk_fp8_f32 v77, v22, v23 op_sel:[0,0,1]
	global_store_dword v[82:83], v77, off offset:1024 nt
	s_nop 0
	v_pk_mul_f32 v[110:111], v[76:77], v[44:45] op_sel_hi:[0,1]
	v_pk_mul_f32 v[44:45], v[76:77], v[46:47] op_sel_hi:[0,1]
	v_mov_b32_e32 v77, 0
	s_nop 0
	v_pk_fma_f32 v[44:45], v[180:181], v[44:45], v[230:231]
	v_pk_fma_f32 v[46:47], v[178:179], v[110:111], v[228:229]
	v_med3_f32 v22, v44, s69, v208
	v_cvt_pk_bf16_f32 v20, v46, v47
	v_cvt_pk_bf16_f32 v21, v44, v45
	global_store_dwordx2 v[104:105], v[20:21], off offset:2560 nt
	v_med3_f32 v20, v46, s69, v208
	v_med3_f32 v21, v47, s69, v208
	v_cvt_pk_fp8_f32 v77, v20, v21
	v_med3_f32 v23, v45, s69, v208
	v_cvt_pk_fp8_f32 v77, v22, v23 op_sel:[0,0,1]
	global_store_dword v[82:83], v77, off offset:1280 nt
	s_nop 0
	v_pk_mul_f32 v[110:111], v[76:77], v[36:37] op_sel_hi:[0,1]
	v_pk_mul_f32 v[36:37], v[76:77], v[38:39] op_sel_hi:[0,1]
	v_mov_b32_e32 v77, 0
	s_nop 0
	v_pk_fma_f32 v[36:37], v[184:185], v[36:37], v[234:235]
	v_pk_fma_f32 v[38:39], v[182:183], v[110:111], v[232:233]
	v_med3_f32 v22, v36, s69, v208
	v_cvt_pk_bf16_f32 v20, v38, v39
	v_cvt_pk_bf16_f32 v21, v36, v37
	global_store_dwordx2 v[104:105], v[20:21], off offset:3072 nt
	v_med3_f32 v20, v38, s69, v208
	v_med3_f32 v21, v39, s69, v208
	v_cvt_pk_fp8_f32 v77, v20, v21
	v_med3_f32 v23, v37, s69, v208
	v_cvt_pk_fp8_f32 v77, v22, v23 op_sel:[0,0,1]
	global_store_dword v[82:83], v77, off offset:1536 nt
	s_nop 0
	v_pk_mul_f32 v[18:19], v[76:77], v[42:43] op_sel_hi:[0,1]
	v_pk_mul_f32 v[16:17], v[76:77], v[40:41] op_sel_hi:[0,1]
	v_mov_b32_e32 v40, 0
	s_nop 0
	v_pk_fma_f32 v[16:17], v[188:189], v[16:17], v[248:249]
	v_pk_fma_f32 v[18:19], v[186:187], v[18:19], v[246:247]
	v_med3_f32 v22, v16, s69, v208
	v_cvt_pk_bf16_f32 v20, v18, v19
	v_cvt_pk_bf16_f32 v21, v16, v17
	global_store_dwordx2 v[104:105], v[20:21], off offset:3584 nt
	v_med3_f32 v20, v18, s69, v208
	v_med3_f32 v21, v19, s69, v208
	v_cvt_pk_fp8_f32 v40, v20, v21
	v_med3_f32 v23, v17, s69, v208
	v_cvt_pk_fp8_f32 v40, v22, v23 op_sel:[0,0,1]
	global_store_dword v[82:83], v40, off offset:1792 nt
	v_add_u32_e32 v238, 0x10000, v25
	ds_read_b128 v[158:161], v25 offset:0
	ds_read_b128 v[162:165], v25 offset:8208
	ds_read_b128 v[166:169], v25 offset:16416
	ds_read_b128 v[170:173], v25 offset:24624
	ds_read_b128 v[174:177], v25 offset:32832
	ds_read_b128 v[178:181], v25 offset:41040
	ds_read_b128 v[182:185], v25 offset:49248
	ds_read_b128 v[186:189], v25 offset:57456
	v_mov_b32_e32 v76, v70
	v_mov_b32_e32 v77, v66
	v_mov_b32_e32 v66, v71
	v_mov_b32_e32 v82, v68
	v_mov_b32_e32 v83, v64
	v_mov_b32_e32 v64, v69
	v_mov_b32_e32 v68, v80
	v_mov_b32_e32 v69, v58
	v_mov_b32_e32 v58, v81
	v_mov_b32_e32 v70, v78
	v_mov_b32_e32 v71, v56
	v_mov_b32_e32 v56, v79
	ds_read_b128 v[198:201], v238 offset:128
	v_mov_b32_e32 v108, v48
	v_mov_b32_e32 v109, v102
	v_mov_b32_e32 v102, v49
	v_mov_b32_e32 v106, v62
	v_mov_b32_e32 v107, v72
	v_mov_b32_e32 v72, v63
	v_mov_b32_e32 v62, v84
	v_mov_b32_e32 v63, v52
	v_mov_b32_e32 v52, v85
	s_waitcnt lgkmcnt(8)
	v_pk_fma_f32 v[84:85], v[108:109], v[158:159], 0 op_sel_hi:[1,0,0]
	v_mov_b32_e32 v104, v60
	v_mov_b32_e32 v105, v74
	v_mov_b32_e32 v74, v61
	v_mov_b32_e32 v60, v86
	v_mov_b32_e32 v61, v54
	v_mov_b32_e32 v54, v87
	v_pk_fma_f32 v[78:79], v[158:159], v[102:103], v[84:85] op_sel:[1,0,0]
	ds_read_b128 v[202:205], v238 offset:8336
	v_mov_b32_e32 v110, v50
	v_mov_b32_e32 v111, v100
	v_mov_b32_e32 v100, v51
	v_pk_fma_f32 v[78:79], v[160:161], v[110:111], v[78:79] op_sel_hi:[0,1,1]
	v_mov_b32_e32 v80, v161
	v_pk_fma_f32 v[78:79], v[80:81], v[100:101], v[78:79] op_sel_hi:[0,1,1]
	s_waitcnt lgkmcnt(8)
	v_pk_fma_f32 v[80:81], v[108:109], v[162:163], 0 op_sel_hi:[1,0,0]
	v_mov_b32_e32 v50, v88
	v_pk_fma_f32 v[80:81], v[162:163], v[102:103], v[80:81] op_sel:[1,0,0]
	v_mov_b32_e32 v84, v165
	v_pk_fma_f32 v[80:81], v[164:165], v[110:111], v[80:81] op_sel_hi:[0,1,1]
	v_pk_fma_f32 v[120:121], v[84:85], v[100:101], v[80:81] op_sel_hi:[0,1,1]
	ds_read_b128 v[216:219], v238 offset:16544
	v_mov_b32_e32 v51, v44
	v_mov_b32_e32 v44, v89
	v_mov_b32_e32 v48, v90
	v_mov_b32_e32 v49, v46
	s_waitcnt lgkmcnt(8)
	v_pk_fma_f32 v[80:81], v[108:109], v[166:167], 0 op_sel_hi:[1,0,0]
	v_mov_b32_e32 v46, v91
	v_pk_fma_f32 v[80:81], v[166:167], v[102:103], v[80:81] op_sel:[1,0,0]
	v_mov_b32_e32 v84, v169
	v_pk_fma_f32 v[80:81], v[168:169], v[110:111], v[80:81] op_sel_hi:[0,1,1]
	v_pk_fma_f32 v[122:123], v[84:85], v[100:101], v[80:81] op_sel_hi:[0,1,1]
	ds_read_b128 v[220:223], v238 offset:24752
	v_mov_b32_e32 v42, v92
	v_mov_b32_e32 v43, v36
	v_mov_b32_e32 v36, v93
	v_mov_b32_e32 v40, v94
	s_waitcnt lgkmcnt(8)
	v_pk_fma_f32 v[80:81], v[108:109], v[170:171], 0 op_sel_hi:[1,0,0]
	v_mov_b32_e32 v41, v38
	v_pk_fma_f32 v[80:81], v[170:171], v[102:103], v[80:81] op_sel:[1,0,0]
	v_mov_b32_e32 v84, v173
	v_pk_fma_f32 v[80:81], v[172:173], v[110:111], v[80:81] op_sel_hi:[0,1,1]
	v_pk_fma_f32 v[80:81], v[84:85], v[100:101], v[80:81] op_sel_hi:[0,1,1]
	ds_read_b128 v[224:227], v238 offset:32960
	v_mov_b32_e32 v38, v95
	v_mov_b32_e32 v22, v96
	v_mov_b32_e32 v23, v18
	v_mov_b32_e32 v18, v97
	s_waitcnt lgkmcnt(8)
	v_pk_fma_f32 v[88:89], v[108:109], v[174:175], 0 op_sel_hi:[1,0,0]
	v_mov_b32_e32 v20, v98
	v_pk_fma_f32 v[84:85], v[174:175], v[102:103], v[88:89] op_sel:[1,0,0]
	v_mov_b32_e32 v21, v16
	v_pk_fma_f32 v[84:85], v[176:177], v[110:111], v[84:85] op_sel_hi:[0,1,1]
	v_mov_b32_e32 v86, v177
	v_pk_fma_f32 v[84:85], v[86:87], v[100:101], v[84:85] op_sel_hi:[0,1,1]
	ds_read_b128 v[228:231], v238 offset:41168
	v_mov_b32_e32 v16, v99
	s_waitcnt lgkmcnt(8)
; #define LAS __attribute__((address_space(3)))
; __global__ void __launch_bounds__(NTHREADS, 2) hybrid_fwd(Args a) {
;     ...
;                     for (int j = 0; j < 8; ++j) {
; #pragma unroll
;                         for (int e = 0; e < 16; ++e) { const f32x4 w = *(const LAS f32x4*)(rwT + e * 2052 + j * 256 + lane * 4);
;                             acc2[e] += y2[j][0] * (f32x2){w[0], w[0]}; acc2[e] += y2[j][1] * (f32x2){w[1], w[1]};
;                             acc2[e] += y2[j][2] * (f32x2){w[2], w[2]}; acc2[e] += y2[j][3] * (f32x2){w[3], w[3]}; }
;                         __builtin_amdgcn_sched_barrier(0);
;                     }
	v_pk_fma_f32 v[90:91], v[108:109], v[178:179], 0 op_sel_hi:[1,0,0]
	s_nop 0
	v_pk_fma_f32 v[86:87], v[178:179], v[102:103], v[90:91] op_sel:[1,0,0]
	s_nop 0
	v_pk_fma_f32 v[86:87], v[180:181], v[110:111], v[86:87] op_sel_hi:[0,1,1]
	v_mov_b32_e32 v88, v181
	v_pk_fma_f32 v[86:87], v[88:89], v[100:101], v[86:87] op_sel_hi:[0,1,1]
	ds_read_b128 v[232:235], v238 offset:49376
	s_waitcnt lgkmcnt(8)
	v_pk_fma_f32 v[92:93], v[108:109], v[182:183], 0 op_sel_hi:[1,0,0]
	s_nop 0
	v_pk_fma_f32 v[88:89], v[182:183], v[102:103], v[92:93] op_sel:[1,0,0]
	s_nop 0
	v_pk_fma_f32 v[88:89], v[184:185], v[110:111], v[88:89] op_sel_hi:[0,1,1]
	v_mov_b32_e32 v90, v185
	v_pk_fma_f32 v[88:89], v[90:91], v[100:101], v[88:89] op_sel_hi:[0,1,1]
	ds_read_b128 v[242:245], v238 offset:57584
	s_waitcnt lgkmcnt(8)
	v_pk_fma_f32 v[94:95], v[108:109], v[186:187], 0 op_sel_hi:[1,0,0]
	s_nop 0
	v_pk_fma_f32 v[90:91], v[186:187], v[102:103], v[94:95] op_sel:[1,0,0]
	s_nop 0
	v_pk_fma_f32 v[90:91], v[188:189], v[110:111], v[90:91] op_sel_hi:[0,1,1]
	v_mov_b32_e32 v92, v189
	v_pk_fma_f32 v[90:91], v[92:93], v[100:101], v[90:91] op_sel_hi:[0,1,1]
	ds_read_b128 v[246:249], v25 offset:1024
	s_waitcnt lgkmcnt(8)
	v_pk_fma_f32 v[96:97], v[108:109], v[198:199], 0 op_sel_hi:[1,0,0]
	s_nop 0
	v_pk_fma_f32 v[92:93], v[198:199], v[102:103], v[96:97] op_sel:[1,0,0]
	s_nop 0
	v_pk_fma_f32 v[92:93], v[200:201], v[110:111], v[92:93] op_sel_hi:[0,1,1]
	v_mov_b32_e32 v94, v201
	v_pk_fma_f32 v[92:93], v[94:95], v[100:101], v[92:93] op_sel_hi:[0,1,1]
	ds_read_b128 v[250:253], v25 offset:9232
	s_waitcnt lgkmcnt(8)
	v_pk_fma_f32 v[98:99], v[108:109], v[202:203], 0 op_sel_hi:[1,0,0]
	s_nop 0
	v_pk_fma_f32 v[94:95], v[202:203], v[102:103], v[98:99] op_sel:[1,0,0]
	s_nop 0
	v_pk_fma_f32 v[94:95], v[204:205], v[110:111], v[94:95] op_sel_hi:[0,1,1]
	v_mov_b32_e32 v96, v205
	v_pk_fma_f32 v[94:95], v[96:97], v[100:101], v[94:95] op_sel_hi:[0,1,1]
	ds_read_b128 v[158:161], v25 offset:17440
	s_waitcnt lgkmcnt(8)
	v_pk_fma_f32 v[112:113], v[108:109], v[216:217], 0 op_sel_hi:[1,0,0]
	s_nop 0
	v_pk_fma_f32 v[96:97], v[216:217], v[102:103], v[112:113] op_sel:[1,0,0]
	ds_read_b128 v[162:165], v25 offset:25648
	v_pk_fma_f32 v[96:97], v[218:219], v[110:111], v[96:97] op_sel_hi:[0,1,1]
	v_mov_b32_e32 v98, v219
	v_pk_fma_f32 v[96:97], v[98:99], v[100:101], v[96:97] op_sel_hi:[0,1,1]
	s_waitcnt lgkmcnt(8)
	v_pk_fma_f32 v[98:99], v[108:109], v[220:221], 0 op_sel_hi:[1,0,0]
	s_nop 0
	v_pk_fma_f32 v[98:99], v[220:221], v[102:103], v[98:99] op_sel:[1,0,0]
	v_mov_b32_e32 v112, v223
	v_pk_fma_f32 v[98:99], v[222:223], v[110:111], v[98:99] op_sel_hi:[0,1,1]
	v_pk_fma_f32 v[98:99], v[112:113], v[100:101], v[98:99] op_sel_hi:[0,1,1]
	ds_read_b128 v[166:169], v25 offset:33856
	s_waitcnt lgkmcnt(8)
	v_pk_fma_f32 v[116:117], v[108:109], v[224:225], 0 op_sel_hi:[1,0,0]
	s_nop 0
	v_pk_fma_f32 v[112:113], v[224:225], v[102:103], v[116:117] op_sel:[1,0,0]
	s_nop 0
	v_pk_fma_f32 v[112:113], v[226:227], v[110:111], v[112:113] op_sel_hi:[0,1,1]
	v_mov_b32_e32 v114, v227
	v_pk_fma_f32 v[112:113], v[114:115], v[100:101], v[112:113] op_sel_hi:[0,1,1]
	ds_read_b128 v[170:173], v25 offset:42064
	s_waitcnt lgkmcnt(8)
	v_pk_fma_f32 v[118:119], v[108:109], v[228:229], 0 op_sel_hi:[1,0,0]
	s_nop 0
	v_pk_fma_f32 v[114:115], v[228:229], v[102:103], v[118:119] op_sel:[1,0,0]
	s_nop 0
	v_pk_fma_f32 v[114:115], v[230:231], v[110:111], v[114:115] op_sel_hi:[0,1,1]
	v_mov_b32_e32 v116, v231
	v_pk_fma_f32 v[114:115], v[116:117], v[100:101], v[114:115] op_sel_hi:[0,1,1]
	ds_read_b128 v[174:177], v25 offset:50272
	s_waitcnt lgkmcnt(8)
	v_pk_fma_f32 v[124:125], v[108:109], v[232:233], 0 op_sel_hi:[1,0,0]
	s_nop 0
	v_pk_fma_f32 v[116:117], v[232:233], v[102:103], v[124:125] op_sel:[1,0,0]
	ds_read_b128 v[178:181], v25 offset:58480
	v_pk_fma_f32 v[116:117], v[234:235], v[110:111], v[116:117] op_sel_hi:[0,1,1]
	v_mov_b32_e32 v118, v235
	v_pk_fma_f32 v[116:117], v[118:119], v[100:101], v[116:117] op_sel_hi:[0,1,1]
	s_waitcnt lgkmcnt(8)
	v_pk_fma_f32 v[108:109], v[108:109], v[242:243], 0 op_sel_hi:[1,0,0]
	s_nop 0
	v_pk_fma_f32 v[102:103], v[242:243], v[102:103], v[108:109] op_sel:[1,0,0]
	v_mov_b32_e32 v108, v245
	v_pk_fma_f32 v[102:103], v[244:245], v[110:111], v[102:103] op_sel_hi:[0,1,1]
	v_pk_fma_f32 v[118:119], v[108:109], v[100:101], v[102:103] op_sel_hi:[0,1,1]
	ds_read_b128 v[182:185], v238 offset:1152
	s_waitcnt lgkmcnt(8)
	v_pk_fma_f32 v[78:79], v[104:105], v[246:247], v[78:79] op_sel_hi:[1,0,1]
	s_nop 0
	v_pk_fma_f32 v[78:79], v[246:247], v[74:75], v[78:79] op_sel:[1,0,0]
	v_mov_b32_e32 v100, v249
	v_pk_fma_f32 v[78:79], v[248:249], v[106:107], v[78:79] op_sel_hi:[0,1,1]
	v_pk_fma_f32 v[78:79], v[100:101], v[72:73], v[78:79] op_sel_hi:[0,1,1]
	ds_read_b128 v[186:189], v238 offset:9360
	s_waitcnt lgkmcnt(8)
	v_pk_fma_f32 v[108:109], v[104:105], v[250:251], v[120:121] op_sel_hi:[1,0,1]
	s_nop 0
	v_pk_fma_f32 v[100:101], v[250:251], v[74:75], v[108:109] op_sel:[1,0,0]
	s_nop 0
	v_pk_fma_f32 v[100:101], v[252:253], v[106:107], v[100:101] op_sel_hi:[0,1,1]
	v_mov_b32_e32 v102, v253
	v_pk_fma_f32 v[120:121], v[102:103], v[72:73], v[100:101] op_sel_hi:[0,1,1]
	ds_read_b128 v[198:201], v238 offset:17568
	s_waitcnt lgkmcnt(8)
	v_pk_fma_f32 v[108:109], v[104:105], v[158:159], v[122:123] op_sel_hi:[1,0,1]
	s_nop 0
	v_pk_fma_f32 v[100:101], v[158:159], v[74:75], v[108:109] op_sel:[1,0,0]
	ds_read_b128 v[202:205], v238 offset:25776
	v_pk_fma_f32 v[100:101], v[160:161], v[106:107], v[100:101] op_sel_hi:[0,1,1]
	v_mov_b32_e32 v102, v161
	v_pk_fma_f32 v[100:101], v[102:103], v[72:73], v[100:101] op_sel_hi:[0,1,1]
	s_waitcnt lgkmcnt(8)
; #define LAS __attribute__((address_space(3)))
; __global__ void __launch_bounds__(NTHREADS, 2) hybrid_fwd(Args a) {
;     ...
;                     for (int j = 0; j < 8; ++j) {
; #pragma unroll
;                         for (int e = 0; e < 16; ++e) { const f32x4 w = *(const LAS f32x4*)(rwT + e * 2052 + j * 256 + lane * 4);
;                             acc2[e] += y2[j][0] * (f32x2){w[0], w[0]}; acc2[e] += y2[j][1] * (f32x2){w[1], w[1]};
;                             acc2[e] += y2[j][2] * (f32x2){w[2], w[2]}; acc2[e] += y2[j][3] * (f32x2){w[3], w[3]}; }
;                         __builtin_amdgcn_sched_barrier(0);
;                     }
	v_pk_fma_f32 v[80:81], v[104:105], v[162:163], v[80:81] op_sel_hi:[1,0,1]
	s_nop 0
	v_pk_fma_f32 v[80:81], v[162:163], v[74:75], v[80:81] op_sel:[1,0,0]
	v_mov_b32_e32 v102, v165
	v_pk_fma_f32 v[80:81], v[164:165], v[106:107], v[80:81] op_sel_hi:[0,1,1]
	ds_read_b128 v[216:219], v238 offset:33984
	v_pk_fma_f32 v[80:81], v[102:103], v[72:73], v[80:81] op_sel_hi:[0,1,1]
	s_waitcnt lgkmcnt(8)
	v_pk_fma_f32 v[84:85], v[104:105], v[166:167], v[84:85] op_sel_hi:[1,0,1]
	s_nop 0
	v_pk_fma_f32 v[84:85], v[166:167], v[74:75], v[84:85] op_sel:[1,0,0]
	v_mov_b32_e32 v102, v169
	v_pk_fma_f32 v[84:85], v[168:169], v[106:107], v[84:85] op_sel_hi:[0,1,1]
	ds_read_b128 v[220:223], v238 offset:42192
	v_pk_fma_f32 v[84:85], v[102:103], v[72:73], v[84:85] op_sel_hi:[0,1,1]
	s_waitcnt lgkmcnt(8)
	v_pk_fma_f32 v[86:87], v[104:105], v[170:171], v[86:87] op_sel_hi:[1,0,1]
	s_nop 0
	v_pk_fma_f32 v[86:87], v[170:171], v[74:75], v[86:87] op_sel:[1,0,0]
	v_mov_b32_e32 v102, v173
	v_pk_fma_f32 v[86:87], v[172:173], v[106:107], v[86:87] op_sel_hi:[0,1,1]
	ds_read_b128 v[224:227], v238 offset:50400
	v_pk_fma_f32 v[86:87], v[102:103], v[72:73], v[86:87] op_sel_hi:[0,1,1]
	s_waitcnt lgkmcnt(8)
	v_pk_fma_f32 v[88:89], v[104:105], v[174:175], v[88:89] op_sel_hi:[1,0,1]
	s_nop 0
	v_pk_fma_f32 v[88:89], v[174:175], v[74:75], v[88:89] op_sel:[1,0,0]
	v_mov_b32_e32 v102, v177
	v_pk_fma_f32 v[88:89], v[176:177], v[106:107], v[88:89] op_sel_hi:[0,1,1]
	ds_read_b128 v[228:231], v238 offset:58608
	v_pk_fma_f32 v[88:89], v[102:103], v[72:73], v[88:89] op_sel_hi:[0,1,1]
	s_waitcnt lgkmcnt(8)
	v_pk_fma_f32 v[90:91], v[104:105], v[178:179], v[90:91] op_sel_hi:[1,0,1]
	s_nop 0
	v_pk_fma_f32 v[90:91], v[178:179], v[74:75], v[90:91] op_sel:[1,0,0]
	v_mov_b32_e32 v102, v181
	v_pk_fma_f32 v[90:91], v[180:181], v[106:107], v[90:91] op_sel_hi:[0,1,1]
	ds_read_b128 v[232:235], v25 offset:2048
	v_pk_fma_f32 v[90:91], v[102:103], v[72:73], v[90:91] op_sel_hi:[0,1,1]
	s_waitcnt lgkmcnt(8)
	v_pk_fma_f32 v[92:93], v[104:105], v[182:183], v[92:93] op_sel_hi:[1,0,1]
	s_nop 0
	v_pk_fma_f32 v[92:93], v[182:183], v[74:75], v[92:93] op_sel:[1,0,0]
	v_mov_b32_e32 v102, v185
	v_pk_fma_f32 v[92:93], v[184:185], v[106:107], v[92:93] op_sel_hi:[0,1,1]
	ds_read_b128 v[242:245], v25 offset:10256
	v_pk_fma_f32 v[92:93], v[102:103], v[72:73], v[92:93] op_sel_hi:[0,1,1]
	s_waitcnt lgkmcnt(8)
	v_pk_fma_f32 v[94:95], v[104:105], v[186:187], v[94:95] op_sel_hi:[1,0,1]
	s_nop 0
	v_pk_fma_f32 v[94:95], v[186:187], v[74:75], v[94:95] op_sel:[1,0,0]
	v_mov_b32_e32 v102, v189
	v_pk_fma_f32 v[94:95], v[188:189], v[106:107], v[94:95] op_sel_hi:[0,1,1]
	ds_read_b128 v[246:249], v25 offset:18464
	v_pk_fma_f32 v[94:95], v[102:103], v[72:73], v[94:95] op_sel_hi:[0,1,1]
	s_waitcnt lgkmcnt(8)
	v_pk_fma_f32 v[96:97], v[104:105], v[198:199], v[96:97] op_sel_hi:[1,0,1]
	s_nop 0
	v_pk_fma_f32 v[96:97], v[198:199], v[74:75], v[96:97] op_sel:[1,0,0]
	v_mov_b32_e32 v102, v201
	v_pk_fma_f32 v[96:97], v[200:201], v[106:107], v[96:97] op_sel_hi:[0,1,1]
	ds_read_b128 v[250:253], v25 offset:26672
	v_pk_fma_f32 v[96:97], v[102:103], v[72:73], v[96:97] op_sel_hi:[0,1,1]
	s_waitcnt lgkmcnt(8)
	v_pk_fma_f32 v[98:99], v[104:105], v[202:203], v[98:99] op_sel_hi:[1,0,1]
	s_nop 0
	v_pk_fma_f32 v[98:99], v[202:203], v[74:75], v[98:99] op_sel:[1,0,0]
	v_mov_b32_e32 v102, v205
	v_pk_fma_f32 v[98:99], v[204:205], v[106:107], v[98:99] op_sel_hi:[0,1,1]
	ds_read_b128 v[162:165], v25 offset:34880
	v_pk_fma_f32 v[98:99], v[102:103], v[72:73], v[98:99] op_sel_hi:[0,1,1]
	s_waitcnt lgkmcnt(8)
	v_pk_fma_f32 v[102:103], v[104:105], v[216:217], v[112:113] op_sel_hi:[1,0,1]
	s_nop 0
	v_pk_fma_f32 v[102:103], v[216:217], v[74:75], v[102:103] op_sel:[1,0,0]
	v_mov_b32_e32 v108, v219
	v_pk_fma_f32 v[102:103], v[218:219], v[106:107], v[102:103] op_sel_hi:[0,1,1]
	v_pk_fma_f32 v[102:103], v[108:109], v[72:73], v[102:103] op_sel_hi:[0,1,1]
	ds_read_b128 v[166:169], v25 offset:43088
	s_waitcnt lgkmcnt(8)
	v_pk_fma_f32 v[112:113], v[104:105], v[220:221], v[114:115] op_sel_hi:[1,0,1]
	s_nop 0
	v_pk_fma_f32 v[108:109], v[220:221], v[74:75], v[112:113] op_sel:[1,0,0]
	s_nop 0
	v_pk_fma_f32 v[108:109], v[222:223], v[106:107], v[108:109] op_sel_hi:[0,1,1]
	v_mov_b32_e32 v110, v223
	v_pk_fma_f32 v[108:109], v[110:111], v[72:73], v[108:109] op_sel_hi:[0,1,1]
	ds_read_b128 v[170:173], v25 offset:51296
	s_waitcnt lgkmcnt(8)
	v_pk_fma_f32 v[114:115], v[104:105], v[224:225], v[116:117] op_sel_hi:[1,0,1]
	s_nop 0
	v_pk_fma_f32 v[110:111], v[224:225], v[74:75], v[114:115] op_sel:[1,0,0]
	s_nop 0
	v_pk_fma_f32 v[110:111], v[226:227], v[106:107], v[110:111] op_sel_hi:[0,1,1]
	v_mov_b32_e32 v112, v227
	v_pk_fma_f32 v[110:111], v[112:113], v[72:73], v[110:111] op_sel_hi:[0,1,1]
	ds_read_b128 v[174:177], v25 offset:59504
	s_waitcnt lgkmcnt(8)
	v_pk_fma_f32 v[104:105], v[104:105], v[228:229], v[118:119] op_sel_hi:[1,0,1]
	s_nop 0
	v_pk_fma_f32 v[74:75], v[228:229], v[74:75], v[104:105] op_sel:[1,0,0]
	v_mov_b32_e32 v104, v231
	v_pk_fma_f32 v[74:75], v[230:231], v[106:107], v[74:75] op_sel_hi:[0,1,1]
	v_pk_fma_f32 v[104:105], v[104:105], v[72:73], v[74:75] op_sel_hi:[0,1,1]
	ds_read_b128 v[178:181], v238 offset:2176
	ds_read_b128 v[182:185], v238 offset:10384
	s_waitcnt lgkmcnt(8)
	v_pk_fma_f32 v[78:79], v[76:77], v[232:233], v[78:79] op_sel_hi:[1,0,1]
	s_nop 0
	v_pk_fma_f32 v[72:73], v[232:233], v[66:67], v[78:79] op_sel:[1,0,0]
	v_mov_b32_e32 v78, v245
	v_pk_fma_f32 v[72:73], v[234:235], v[82:83], v[72:73] op_sel_hi:[0,1,1]
	v_mov_b32_e32 v74, v235
	v_pk_fma_f32 v[72:73], v[74:75], v[64:65], v[72:73] op_sel_hi:[0,1,1]
	v_pk_fma_f32 v[74:75], v[76:77], v[242:243], v[120:121] op_sel_hi:[1,0,1]
	s_nop 0
	v_pk_fma_f32 v[74:75], v[242:243], v[66:67], v[74:75] op_sel:[1,0,0]
	s_nop 0
	v_pk_fma_f32 v[74:75], v[244:245], v[82:83], v[74:75] op_sel_hi:[0,1,1]
	ds_read_b128 v[186:189], v238 offset:18592
	v_pk_fma_f32 v[106:107], v[78:79], v[64:65], v[74:75] op_sel_hi:[0,1,1]
	s_waitcnt lgkmcnt(8)
; #define LAS __attribute__((address_space(3)))
; __global__ void __launch_bounds__(NTHREADS, 2) hybrid_fwd(Args a) {
;     ...
;                     for (int j = 0; j < 8; ++j) {
; #pragma unroll
;                         for (int e = 0; e < 16; ++e) { const f32x4 w = *(const LAS f32x4*)(rwT + e * 2052 + j * 256 + lane * 4);
;                             acc2[e] += y2[j][0] * (f32x2){w[0], w[0]}; acc2[e] += y2[j][1] * (f32x2){w[1], w[1]};
;                             acc2[e] += y2[j][2] * (f32x2){w[2], w[2]}; acc2[e] += y2[j][3] * (f32x2){w[3], w[3]}; }
;                         __builtin_amdgcn_sched_barrier(0);
;                     }
	v_pk_fma_f32 v[74:75], v[76:77], v[246:247], v[100:101] op_sel_hi:[1,0,1]
	s_nop 0
	v_pk_fma_f32 v[74:75], v[246:247], v[66:67], v[74:75] op_sel:[1,0,0]
	v_mov_b32_e32 v78, v249
	v_pk_fma_f32 v[74:75], v[248:249], v[82:83], v[74:75] op_sel_hi:[0,1,1]
	ds_read_b128 v[198:201], v238 offset:26800
	v_pk_fma_f32 v[74:75], v[78:79], v[64:65], v[74:75] op_sel_hi:[0,1,1]
	s_waitcnt lgkmcnt(8)
	v_pk_fma_f32 v[78:79], v[76:77], v[250:251], v[80:81] op_sel_hi:[1,0,1]
	s_nop 0
	v_pk_fma_f32 v[78:79], v[250:251], v[66:67], v[78:79] op_sel:[1,0,0]
	v_mov_b32_e32 v80, v253
	v_pk_fma_f32 v[78:79], v[252:253], v[82:83], v[78:79] op_sel_hi:[0,1,1]
	ds_read_b128 v[202:205], v238 offset:35008
	v_pk_fma_f32 v[78:79], v[80:81], v[64:65], v[78:79] op_sel_hi:[0,1,1]
	s_waitcnt lgkmcnt(8)
	v_pk_fma_f32 v[80:81], v[76:77], v[162:163], v[84:85] op_sel_hi:[1,0,1]
	s_nop 0
	v_pk_fma_f32 v[80:81], v[162:163], v[66:67], v[80:81] op_sel:[1,0,0]
	v_mov_b32_e32 v84, v165
	v_pk_fma_f32 v[80:81], v[164:165], v[82:83], v[80:81] op_sel_hi:[0,1,1]
	ds_read_b128 v[158:161], v238 offset:51424
	v_pk_fma_f32 v[80:81], v[84:85], v[64:65], v[80:81] op_sel_hi:[0,1,1]
	s_waitcnt lgkmcnt(8)
	v_pk_fma_f32 v[84:85], v[76:77], v[166:167], v[86:87] op_sel_hi:[1,0,1]
	s_nop 0
	v_pk_fma_f32 v[84:85], v[166:167], v[66:67], v[84:85] op_sel:[1,0,0]
	v_mov_b32_e32 v86, v169
	v_pk_fma_f32 v[84:85], v[168:169], v[82:83], v[84:85] op_sel_hi:[0,1,1]
	ds_read_b128 v[216:219], v238 offset:43216
	v_pk_fma_f32 v[84:85], v[86:87], v[64:65], v[84:85] op_sel_hi:[0,1,1]
	s_waitcnt lgkmcnt(8)
	v_pk_fma_f32 v[86:87], v[76:77], v[170:171], v[88:89] op_sel_hi:[1,0,1]
	s_nop 0
	v_pk_fma_f32 v[86:87], v[170:171], v[66:67], v[86:87] op_sel:[1,0,0]
	v_mov_b32_e32 v88, v173
	v_pk_fma_f32 v[86:87], v[172:173], v[82:83], v[86:87] op_sel_hi:[0,1,1]
	ds_read_b128 v[220:223], v238 offset:59632
	v_pk_fma_f32 v[86:87], v[88:89], v[64:65], v[86:87] op_sel_hi:[0,1,1]
	s_waitcnt lgkmcnt(8)
	v_pk_fma_f32 v[88:89], v[76:77], v[174:175], v[90:91] op_sel_hi:[1,0,1]
	s_nop 0
	v_pk_fma_f32 v[88:89], v[174:175], v[66:67], v[88:89] op_sel:[1,0,0]
	v_mov_b32_e32 v90, v177
	v_pk_fma_f32 v[88:89], v[176:177], v[82:83], v[88:89] op_sel_hi:[0,1,1]
	ds_read_b128 v[224:227], v25 offset:3072
	v_pk_fma_f32 v[88:89], v[90:91], v[64:65], v[88:89] op_sel_hi:[0,1,1]
	s_waitcnt lgkmcnt(8)
	v_pk_fma_f32 v[90:91], v[76:77], v[178:179], v[92:93] op_sel_hi:[1,0,1]
	s_nop 0
	v_pk_fma_f32 v[90:91], v[178:179], v[66:67], v[90:91] op_sel:[1,0,0]
	v_mov_b32_e32 v92, v181
	v_pk_fma_f32 v[90:91], v[180:181], v[82:83], v[90:91] op_sel_hi:[0,1,1]
	ds_read_b128 v[228:231], v25 offset:11280
	v_pk_fma_f32 v[90:91], v[92:93], v[64:65], v[90:91] op_sel_hi:[0,1,1]
	s_waitcnt lgkmcnt(8)
	v_pk_fma_f32 v[92:93], v[76:77], v[182:183], v[94:95] op_sel_hi:[1,0,1]
	s_nop 0
	v_pk_fma_f32 v[92:93], v[182:183], v[66:67], v[92:93] op_sel:[1,0,0]
	v_mov_b32_e32 v94, v185
	v_pk_fma_f32 v[92:93], v[184:185], v[82:83], v[92:93] op_sel_hi:[0,1,1]
	ds_read_b128 v[232:235], v25 offset:19488
	v_pk_fma_f32 v[92:93], v[94:95], v[64:65], v[92:93] op_sel_hi:[0,1,1]
	s_waitcnt lgkmcnt(8)
	v_pk_fma_f32 v[94:95], v[76:77], v[186:187], v[96:97] op_sel_hi:[1,0,1]
	s_nop 0
	v_pk_fma_f32 v[94:95], v[186:187], v[66:67], v[94:95] op_sel:[1,0,0]
	v_mov_b32_e32 v96, v189
	v_pk_fma_f32 v[94:95], v[188:189], v[82:83], v[94:95] op_sel_hi:[0,1,1]
	ds_read_b128 v[242:245], v25 offset:27696
	v_pk_fma_f32 v[94:95], v[96:97], v[64:65], v[94:95] op_sel_hi:[0,1,1]
	s_waitcnt lgkmcnt(8)
	v_pk_fma_f32 v[96:97], v[76:77], v[198:199], v[98:99] op_sel_hi:[1,0,1]
	s_nop 0
	v_pk_fma_f32 v[96:97], v[198:199], v[66:67], v[96:97] op_sel:[1,0,0]
	v_mov_b32_e32 v98, v201
	v_pk_fma_f32 v[96:97], v[200:201], v[82:83], v[96:97] op_sel_hi:[0,1,1]
	v_pk_fma_f32 v[96:97], v[98:99], v[64:65], v[96:97] op_sel_hi:[0,1,1]
	ds_read_b128 v[246:249], v25 offset:35904
	ds_read_b128 v[250:253], v25 offset:44112
	s_waitcnt lgkmcnt(8)
	v_pk_fma_f32 v[102:103], v[76:77], v[202:203], v[102:103] op_sel_hi:[1,0,1]
	s_nop 0
	v_pk_fma_f32 v[98:99], v[202:203], v[66:67], v[102:103] op_sel:[1,0,0]
	s_nop 0
	v_pk_fma_f32 v[98:99], v[204:205], v[82:83], v[98:99] op_sel_hi:[0,1,1]
	v_mov_b32_e32 v100, v205
	v_pk_fma_f32 v[98:99], v[100:101], v[64:65], v[98:99] op_sel_hi:[0,1,1]
	ds_read_b128 v[162:165], v25 offset:52320
	s_waitcnt lgkmcnt(8)
	v_pk_fma_f32 v[108:109], v[76:77], v[216:217], v[108:109] op_sel_hi:[1,0,1]
	s_nop 0
	v_pk_fma_f32 v[100:101], v[216:217], v[66:67], v[108:109] op_sel:[1,0,0]
	v_mov_b32_e32 v108, v161
	v_pk_fma_f32 v[100:101], v[218:219], v[82:83], v[100:101] op_sel_hi:[0,1,1]
	v_mov_b32_e32 v102, v219
	v_pk_fma_f32 v[100:101], v[102:103], v[64:65], v[100:101] op_sel_hi:[0,1,1]
	v_pk_fma_f32 v[102:103], v[76:77], v[158:159], v[110:111] op_sel_hi:[1,0,1]
	s_nop 0
	v_pk_fma_f32 v[102:103], v[158:159], v[66:67], v[102:103] op_sel:[1,0,0]
	s_nop 0
	v_pk_fma_f32 v[102:103], v[160:161], v[82:83], v[102:103] op_sel_hi:[0,1,1]
	v_pk_fma_f32 v[102:103], v[108:109], v[64:65], v[102:103] op_sel_hi:[0,1,1]
	ds_read_b128 v[166:169], v25 offset:60528
	s_waitcnt lgkmcnt(8)
	v_pk_fma_f32 v[76:77], v[76:77], v[220:221], v[104:105] op_sel_hi:[1,0,1]
	s_nop 0
	v_pk_fma_f32 v[66:67], v[220:221], v[66:67], v[76:77] op_sel:[1,0,0]
	v_mov_b32_e32 v76, v223
	v_pk_fma_f32 v[66:67], v[222:223], v[82:83], v[66:67] op_sel_hi:[0,1,1]
	v_pk_fma_f32 v[104:105], v[76:77], v[64:65], v[66:67] op_sel_hi:[0,1,1]
	ds_read_b128 v[170:173], v238 offset:3200
	ds_read_b128 v[174:177], v238 offset:11408
	s_waitcnt lgkmcnt(8)
; #define LAS __attribute__((address_space(3)))
; __global__ void __launch_bounds__(NTHREADS, 2) hybrid_fwd(Args a) {
;     ...
;                     for (int j = 0; j < 8; ++j) {
; #pragma unroll
;                         for (int e = 0; e < 16; ++e) { const f32x4 w = *(const LAS f32x4*)(rwT + e * 2052 + j * 256 + lane * 4);
;                             acc2[e] += y2[j][0] * (f32x2){w[0], w[0]}; acc2[e] += y2[j][1] * (f32x2){w[1], w[1]};
;                             acc2[e] += y2[j][2] * (f32x2){w[2], w[2]}; acc2[e] += y2[j][3] * (f32x2){w[3], w[3]}; }
;                         __builtin_amdgcn_sched_barrier(0);
;                     }
	v_pk_fma_f32 v[72:73], v[68:69], v[224:225], v[72:73] op_sel_hi:[1,0,1]
	s_nop 0
	v_pk_fma_f32 v[64:65], v[224:225], v[58:59], v[72:73] op_sel:[1,0,0]
	v_mov_b32_e32 v72, v231
	v_pk_fma_f32 v[64:65], v[226:227], v[70:71], v[64:65] op_sel_hi:[0,1,1]
	v_mov_b32_e32 v66, v227
	v_pk_fma_f32 v[64:65], v[66:67], v[56:57], v[64:65] op_sel_hi:[0,1,1]
	v_pk_fma_f32 v[66:67], v[68:69], v[228:229], v[106:107] op_sel_hi:[1,0,1]
	s_nop 0
	v_pk_fma_f32 v[66:67], v[228:229], v[58:59], v[66:67] op_sel:[1,0,0]
	s_nop 0
	v_pk_fma_f32 v[66:67], v[230:231], v[70:71], v[66:67] op_sel_hi:[0,1,1]
	ds_read_b128 v[178:181], v238 offset:19616
	v_pk_fma_f32 v[106:107], v[72:73], v[56:57], v[66:67] op_sel_hi:[0,1,1]
	s_waitcnt lgkmcnt(8)
	v_pk_fma_f32 v[66:67], v[68:69], v[232:233], v[74:75] op_sel_hi:[1,0,1]
	s_nop 0
	v_pk_fma_f32 v[66:67], v[232:233], v[58:59], v[66:67] op_sel:[1,0,0]
	v_mov_b32_e32 v72, v235
	v_pk_fma_f32 v[66:67], v[234:235], v[70:71], v[66:67] op_sel_hi:[0,1,1]
	v_pk_fma_f32 v[66:67], v[72:73], v[56:57], v[66:67] op_sel_hi:[0,1,1]
	ds_read_b128 v[182:185], v238 offset:27824
	s_waitcnt lgkmcnt(8)
	v_pk_fma_f32 v[76:77], v[68:69], v[242:243], v[78:79] op_sel_hi:[1,0,1]
	s_nop 0
	v_pk_fma_f32 v[72:73], v[242:243], v[58:59], v[76:77] op_sel:[1,0,0]
	s_nop 0
	v_pk_fma_f32 v[72:73], v[244:245], v[70:71], v[72:73] op_sel_hi:[0,1,1]
	v_mov_b32_e32 v74, v245
	v_pk_fma_f32 v[72:73], v[74:75], v[56:57], v[72:73] op_sel_hi:[0,1,1]
	ds_read_b128 v[186:189], v238 offset:36032
	s_waitcnt lgkmcnt(8)
	v_pk_fma_f32 v[78:79], v[68:69], v[246:247], v[80:81] op_sel_hi:[1,0,1]
	s_nop 0
	v_pk_fma_f32 v[74:75], v[246:247], v[58:59], v[78:79] op_sel:[1,0,0]
	s_nop 0
	v_pk_fma_f32 v[74:75], v[248:249], v[70:71], v[74:75] op_sel_hi:[0,1,1]
	v_mov_b32_e32 v76, v249
	v_pk_fma_f32 v[74:75], v[76:77], v[56:57], v[74:75] op_sel_hi:[0,1,1]
	ds_read_b128 v[198:201], v238 offset:44240
	s_waitcnt lgkmcnt(8)
	v_pk_fma_f32 v[80:81], v[68:69], v[250:251], v[84:85] op_sel_hi:[1,0,1]
	s_nop 0
	v_pk_fma_f32 v[76:77], v[250:251], v[58:59], v[80:81] op_sel:[1,0,0]
	s_nop 0
	v_pk_fma_f32 v[76:77], v[252:253], v[70:71], v[76:77] op_sel_hi:[0,1,1]
	v_mov_b32_e32 v78, v253
	v_pk_fma_f32 v[76:77], v[78:79], v[56:57], v[76:77] op_sel_hi:[0,1,1]
	ds_read_b128 v[202:205], v238 offset:52448
	s_waitcnt lgkmcnt(8)
	v_pk_fma_f32 v[82:83], v[68:69], v[162:163], v[86:87] op_sel_hi:[1,0,1]
	s_nop 0
	v_pk_fma_f32 v[78:79], v[162:163], v[58:59], v[82:83] op_sel:[1,0,0]
	s_nop 0
	v_pk_fma_f32 v[78:79], v[164:165], v[70:71], v[78:79] op_sel_hi:[0,1,1]
	v_mov_b32_e32 v80, v165
	v_pk_fma_f32 v[78:79], v[80:81], v[56:57], v[78:79] op_sel_hi:[0,1,1]
	ds_read_b128 v[216:219], v238 offset:60656
	s_waitcnt lgkmcnt(8)
	v_pk_fma_f32 v[84:85], v[68:69], v[166:167], v[88:89] op_sel_hi:[1,0,1]
	s_nop 0
	v_pk_fma_f32 v[80:81], v[166:167], v[58:59], v[84:85] op_sel:[1,0,0]
	s_nop 0
	v_pk_fma_f32 v[80:81], v[168:169], v[70:71], v[80:81] op_sel_hi:[0,1,1]
	v_mov_b32_e32 v82, v169
	v_pk_fma_f32 v[80:81], v[82:83], v[56:57], v[80:81] op_sel_hi:[0,1,1]
	ds_read_b128 v[158:161], v25 offset:4096
	s_waitcnt lgkmcnt(8)
	v_pk_fma_f32 v[86:87], v[68:69], v[170:171], v[90:91] op_sel_hi:[1,0,1]
	s_nop 0
	v_pk_fma_f32 v[82:83], v[170:171], v[58:59], v[86:87] op_sel:[1,0,0]
	s_nop 0
	v_pk_fma_f32 v[82:83], v[172:173], v[70:71], v[82:83] op_sel_hi:[0,1,1]
	v_mov_b32_e32 v84, v173
	v_pk_fma_f32 v[82:83], v[84:85], v[56:57], v[82:83] op_sel_hi:[0,1,1]
	ds_read_b128 v[220:223], v25 offset:12304
	s_waitcnt lgkmcnt(8)
	v_pk_fma_f32 v[88:89], v[68:69], v[174:175], v[92:93] op_sel_hi:[1,0,1]
	s_nop 0
	v_pk_fma_f32 v[84:85], v[174:175], v[58:59], v[88:89] op_sel:[1,0,0]
	s_nop 0
	v_pk_fma_f32 v[84:85], v[176:177], v[70:71], v[84:85] op_sel_hi:[0,1,1]
	v_mov_b32_e32 v86, v177
	v_pk_fma_f32 v[84:85], v[86:87], v[56:57], v[84:85] op_sel_hi:[0,1,1]
	ds_read_b128 v[224:227], v25 offset:20512
	s_waitcnt lgkmcnt(8)
	v_pk_fma_f32 v[90:91], v[68:69], v[178:179], v[94:95] op_sel_hi:[1,0,1]
	s_nop 0
	v_pk_fma_f32 v[86:87], v[178:179], v[58:59], v[90:91] op_sel:[1,0,0]
	s_nop 0
	v_pk_fma_f32 v[86:87], v[180:181], v[70:71], v[86:87] op_sel_hi:[0,1,1]
	v_mov_b32_e32 v88, v181
	v_pk_fma_f32 v[86:87], v[88:89], v[56:57], v[86:87] op_sel_hi:[0,1,1]
	ds_read_b128 v[228:231], v25 offset:28720
	s_waitcnt lgkmcnt(8)
	v_pk_fma_f32 v[92:93], v[68:69], v[182:183], v[96:97] op_sel_hi:[1,0,1]
	s_nop 0
	v_pk_fma_f32 v[88:89], v[182:183], v[58:59], v[92:93] op_sel:[1,0,0]
	s_nop 0
	v_pk_fma_f32 v[88:89], v[184:185], v[70:71], v[88:89] op_sel_hi:[0,1,1]
	v_mov_b32_e32 v90, v185
	v_pk_fma_f32 v[88:89], v[90:91], v[56:57], v[88:89] op_sel_hi:[0,1,1]
	ds_read_b128 v[232:235], v25 offset:36928
	s_waitcnt lgkmcnt(8)
	v_pk_fma_f32 v[94:95], v[68:69], v[186:187], v[98:99] op_sel_hi:[1,0,1]
	s_nop 0
	v_pk_fma_f32 v[90:91], v[186:187], v[58:59], v[94:95] op_sel:[1,0,0]
	s_nop 0
	v_pk_fma_f32 v[90:91], v[188:189], v[70:71], v[90:91] op_sel_hi:[0,1,1]
	v_mov_b32_e32 v92, v189
	v_pk_fma_f32 v[90:91], v[92:93], v[56:57], v[90:91] op_sel_hi:[0,1,1]
	ds_read_b128 v[242:245], v25 offset:45136
	s_waitcnt lgkmcnt(8)
	v_pk_fma_f32 v[96:97], v[68:69], v[198:199], v[100:101] op_sel_hi:[1,0,1]
	s_nop 0
	v_pk_fma_f32 v[92:93], v[198:199], v[58:59], v[96:97] op_sel:[1,0,0]
	s_nop 0
	v_pk_fma_f32 v[92:93], v[200:201], v[70:71], v[92:93] op_sel_hi:[0,1,1]
	v_mov_b32_e32 v94, v201
	v_pk_fma_f32 v[92:93], v[94:95], v[56:57], v[92:93] op_sel_hi:[0,1,1]
	ds_read_b128 v[246:249], v25 offset:53344
	s_waitcnt lgkmcnt(8)
; #define LAS __attribute__((address_space(3)))
; __global__ void __launch_bounds__(NTHREADS, 2) hybrid_fwd(Args a) {
;     ...
;                     for (int j = 0; j < 8; ++j) {
; #pragma unroll
;                         for (int e = 0; e < 16; ++e) { const f32x4 w = *(const LAS f32x4*)(rwT + e * 2052 + j * 256 + lane * 4);
;                             acc2[e] += y2[j][0] * (f32x2){w[0], w[0]}; acc2[e] += y2[j][1] * (f32x2){w[1], w[1]};
;                             acc2[e] += y2[j][2] * (f32x2){w[2], w[2]}; acc2[e] += y2[j][3] * (f32x2){w[3], w[3]}; }
;                         __builtin_amdgcn_sched_barrier(0);
;                     }
	v_pk_fma_f32 v[98:99], v[68:69], v[202:203], v[102:103] op_sel_hi:[1,0,1]
	s_nop 0
	v_pk_fma_f32 v[94:95], v[202:203], v[58:59], v[98:99] op_sel:[1,0,0]
	s_nop 0
	v_pk_fma_f32 v[94:95], v[204:205], v[70:71], v[94:95] op_sel_hi:[0,1,1]
	v_mov_b32_e32 v96, v205
	v_pk_fma_f32 v[94:95], v[96:97], v[56:57], v[94:95] op_sel_hi:[0,1,1]
	ds_read_b128 v[250:253], v25 offset:61552
	s_waitcnt lgkmcnt(8)
	v_pk_fma_f32 v[68:69], v[68:69], v[216:217], v[104:105] op_sel_hi:[1,0,1]
	s_nop 0
	v_pk_fma_f32 v[58:59], v[216:217], v[58:59], v[68:69] op_sel:[1,0,0]
	v_mov_b32_e32 v68, v219
	v_pk_fma_f32 v[58:59], v[218:219], v[70:71], v[58:59] op_sel_hi:[0,1,1]
	v_pk_fma_f32 v[96:97], v[68:69], v[56:57], v[58:59] op_sel_hi:[0,1,1]
	ds_read_b128 v[162:165], v238 offset:4224
	ds_read_b128 v[166:169], v238 offset:12432
	s_waitcnt lgkmcnt(8)
	v_pk_fma_f32 v[64:65], v[60:61], v[158:159], v[64:65] op_sel_hi:[1,0,1]
	s_nop 0
	v_pk_fma_f32 v[56:57], v[158:159], v[54:55], v[64:65] op_sel:[1,0,0]
	v_mov_b32_e32 v64, v223
	v_pk_fma_f32 v[56:57], v[160:161], v[62:63], v[56:57] op_sel_hi:[0,1,1]
	v_mov_b32_e32 v58, v161
	v_pk_fma_f32 v[56:57], v[58:59], v[52:53], v[56:57] op_sel_hi:[0,1,1]
	v_pk_fma_f32 v[58:59], v[60:61], v[220:221], v[106:107] op_sel_hi:[1,0,1]
	s_nop 0
	v_pk_fma_f32 v[58:59], v[220:221], v[54:55], v[58:59] op_sel:[1,0,0]
	s_nop 0
	v_pk_fma_f32 v[58:59], v[222:223], v[62:63], v[58:59] op_sel_hi:[0,1,1]
	ds_read_b128 v[170:173], v238 offset:20640
	v_pk_fma_f32 v[98:99], v[64:65], v[52:53], v[58:59] op_sel_hi:[0,1,1]
	s_waitcnt lgkmcnt(8)
	v_pk_fma_f32 v[58:59], v[60:61], v[224:225], v[66:67] op_sel_hi:[1,0,1]
	s_nop 0
	v_pk_fma_f32 v[58:59], v[224:225], v[54:55], v[58:59] op_sel:[1,0,0]
	v_mov_b32_e32 v64, v227
	v_pk_fma_f32 v[58:59], v[226:227], v[62:63], v[58:59] op_sel_hi:[0,1,1]
	v_pk_fma_f32 v[58:59], v[64:65], v[52:53], v[58:59] op_sel_hi:[0,1,1]
	ds_read_b128 v[174:177], v238 offset:28848
	s_waitcnt lgkmcnt(8)
	v_pk_fma_f32 v[68:69], v[60:61], v[228:229], v[72:73] op_sel_hi:[1,0,1]
	s_nop 0
	v_pk_fma_f32 v[64:65], v[228:229], v[54:55], v[68:69] op_sel:[1,0,0]
	s_nop 0
	v_pk_fma_f32 v[64:65], v[230:231], v[62:63], v[64:65] op_sel_hi:[0,1,1]
	v_mov_b32_e32 v66, v231
	v_pk_fma_f32 v[64:65], v[66:67], v[52:53], v[64:65] op_sel_hi:[0,1,1]
	ds_read_b128 v[178:181], v238 offset:37056
	s_waitcnt lgkmcnt(8)
	v_pk_fma_f32 v[70:71], v[60:61], v[232:233], v[74:75] op_sel_hi:[1,0,1]
	s_nop 0
	v_pk_fma_f32 v[66:67], v[232:233], v[54:55], v[70:71] op_sel:[1,0,0]
	s_nop 0
	v_pk_fma_f32 v[66:67], v[234:235], v[62:63], v[66:67] op_sel_hi:[0,1,1]
	v_mov_b32_e32 v68, v235
	v_pk_fma_f32 v[66:67], v[68:69], v[52:53], v[66:67] op_sel_hi:[0,1,1]
	ds_read_b128 v[182:185], v238 offset:45264
	s_waitcnt lgkmcnt(8)
	v_pk_fma_f32 v[72:73], v[60:61], v[242:243], v[76:77] op_sel_hi:[1,0,1]
	s_nop 0
	v_pk_fma_f32 v[68:69], v[242:243], v[54:55], v[72:73] op_sel:[1,0,0]
	s_nop 0
	v_pk_fma_f32 v[68:69], v[244:245], v[62:63], v[68:69] op_sel_hi:[0,1,1]
	v_mov_b32_e32 v70, v245
	v_pk_fma_f32 v[68:69], v[70:71], v[52:53], v[68:69] op_sel_hi:[0,1,1]
	ds_read_b128 v[186:189], v238 offset:53472
	s_waitcnt lgkmcnt(8)
	v_pk_fma_f32 v[74:75], v[60:61], v[246:247], v[78:79] op_sel_hi:[1,0,1]
	s_nop 0
	v_pk_fma_f32 v[70:71], v[246:247], v[54:55], v[74:75] op_sel:[1,0,0]
	s_nop 0
	v_pk_fma_f32 v[70:71], v[248:249], v[62:63], v[70:71] op_sel_hi:[0,1,1]
	v_mov_b32_e32 v72, v249
	v_pk_fma_f32 v[70:71], v[72:73], v[52:53], v[70:71] op_sel_hi:[0,1,1]
	ds_read_b128 v[198:201], v238 offset:61680
	s_waitcnt lgkmcnt(8)
	v_pk_fma_f32 v[76:77], v[60:61], v[250:251], v[80:81] op_sel_hi:[1,0,1]
	s_nop 0
	v_pk_fma_f32 v[72:73], v[250:251], v[54:55], v[76:77] op_sel:[1,0,0]
	s_nop 0
	v_pk_fma_f32 v[72:73], v[252:253], v[62:63], v[72:73] op_sel_hi:[0,1,1]
	v_mov_b32_e32 v74, v253
	v_pk_fma_f32 v[72:73], v[74:75], v[52:53], v[72:73] op_sel_hi:[0,1,1]
	ds_read_b128 v[202:205], v25 offset:5120
	s_waitcnt lgkmcnt(8)
	v_pk_fma_f32 v[78:79], v[60:61], v[162:163], v[82:83] op_sel_hi:[1,0,1]
	s_nop 0
	v_pk_fma_f32 v[74:75], v[162:163], v[54:55], v[78:79] op_sel:[1,0,0]
	s_nop 0
	v_pk_fma_f32 v[74:75], v[164:165], v[62:63], v[74:75] op_sel_hi:[0,1,1]
	v_mov_b32_e32 v76, v165
	v_pk_fma_f32 v[74:75], v[76:77], v[52:53], v[74:75] op_sel_hi:[0,1,1]
	ds_read_b128 v[216:219], v25 offset:13328
	s_waitcnt lgkmcnt(8)
	v_pk_fma_f32 v[80:81], v[60:61], v[166:167], v[84:85] op_sel_hi:[1,0,1]
	s_nop 0
	v_pk_fma_f32 v[76:77], v[166:167], v[54:55], v[80:81] op_sel:[1,0,0]
	s_nop 0
	v_pk_fma_f32 v[76:77], v[168:169], v[62:63], v[76:77] op_sel_hi:[0,1,1]
	v_mov_b32_e32 v78, v169
	v_pk_fma_f32 v[76:77], v[78:79], v[52:53], v[76:77] op_sel_hi:[0,1,1]
	ds_read_b128 v[158:161], v25 offset:21536
	s_waitcnt lgkmcnt(8)
	v_pk_fma_f32 v[82:83], v[60:61], v[170:171], v[86:87] op_sel_hi:[1,0,1]
	s_nop 0
	v_pk_fma_f32 v[78:79], v[170:171], v[54:55], v[82:83] op_sel:[1,0,0]
	s_nop 0
	v_pk_fma_f32 v[78:79], v[172:173], v[62:63], v[78:79] op_sel_hi:[0,1,1]
	v_mov_b32_e32 v80, v173
	v_pk_fma_f32 v[78:79], v[80:81], v[52:53], v[78:79] op_sel_hi:[0,1,1]
	ds_read_b128 v[220:223], v25 offset:29744
	s_waitcnt lgkmcnt(8)
	v_pk_fma_f32 v[84:85], v[60:61], v[174:175], v[88:89] op_sel_hi:[1,0,1]
	s_nop 0
	v_pk_fma_f32 v[80:81], v[174:175], v[54:55], v[84:85] op_sel:[1,0,0]
	s_nop 0
	v_pk_fma_f32 v[80:81], v[176:177], v[62:63], v[80:81] op_sel_hi:[0,1,1]
	v_mov_b32_e32 v82, v177
	v_pk_fma_f32 v[80:81], v[82:83], v[52:53], v[80:81] op_sel_hi:[0,1,1]
	ds_read_b128 v[224:227], v25 offset:37952
	s_waitcnt lgkmcnt(8)
; #define LAS __attribute__((address_space(3)))
; __global__ void __launch_bounds__(NTHREADS, 2) hybrid_fwd(Args a) {
;     ...
;                     for (int j = 0; j < 8; ++j) {
; #pragma unroll
;                         for (int e = 0; e < 16; ++e) { const f32x4 w = *(const LAS f32x4*)(rwT + e * 2052 + j * 256 + lane * 4);
;                             acc2[e] += y2[j][0] * (f32x2){w[0], w[0]}; acc2[e] += y2[j][1] * (f32x2){w[1], w[1]};
;                             acc2[e] += y2[j][2] * (f32x2){w[2], w[2]}; acc2[e] += y2[j][3] * (f32x2){w[3], w[3]}; }
;                         __builtin_amdgcn_sched_barrier(0);
;                     }
	v_pk_fma_f32 v[86:87], v[60:61], v[178:179], v[90:91] op_sel_hi:[1,0,1]
	s_nop 0
	v_pk_fma_f32 v[82:83], v[178:179], v[54:55], v[86:87] op_sel:[1,0,0]
	s_nop 0
	v_pk_fma_f32 v[82:83], v[180:181], v[62:63], v[82:83] op_sel_hi:[0,1,1]
	v_mov_b32_e32 v84, v181
	v_pk_fma_f32 v[82:83], v[84:85], v[52:53], v[82:83] op_sel_hi:[0,1,1]
	ds_read_b128 v[228:231], v25 offset:46160
	s_waitcnt lgkmcnt(8)
	v_pk_fma_f32 v[88:89], v[60:61], v[182:183], v[92:93] op_sel_hi:[1,0,1]
	s_nop 0
	v_pk_fma_f32 v[84:85], v[182:183], v[54:55], v[88:89] op_sel:[1,0,0]
	s_nop 0
	v_pk_fma_f32 v[84:85], v[184:185], v[62:63], v[84:85] op_sel_hi:[0,1,1]
	v_mov_b32_e32 v86, v185
	v_pk_fma_f32 v[84:85], v[86:87], v[52:53], v[84:85] op_sel_hi:[0,1,1]
	ds_read_b128 v[232:235], v25 offset:54368
	s_waitcnt lgkmcnt(8)
	v_pk_fma_f32 v[90:91], v[60:61], v[186:187], v[94:95] op_sel_hi:[1,0,1]
	s_nop 0
	v_pk_fma_f32 v[86:87], v[186:187], v[54:55], v[90:91] op_sel:[1,0,0]
	s_nop 0
	v_pk_fma_f32 v[86:87], v[188:189], v[62:63], v[86:87] op_sel_hi:[0,1,1]
	v_mov_b32_e32 v88, v189
	v_pk_fma_f32 v[86:87], v[88:89], v[52:53], v[86:87] op_sel_hi:[0,1,1]
	ds_read_b128 v[242:245], v25 offset:62576
	s_waitcnt lgkmcnt(8)
	v_pk_fma_f32 v[60:61], v[60:61], v[198:199], v[96:97] op_sel_hi:[1,0,1]
	s_nop 0
	v_pk_fma_f32 v[54:55], v[198:199], v[54:55], v[60:61] op_sel:[1,0,0]
	v_mov_b32_e32 v60, v201
	v_pk_fma_f32 v[54:55], v[200:201], v[62:63], v[54:55] op_sel_hi:[0,1,1]
	v_pk_fma_f32 v[88:89], v[60:61], v[52:53], v[54:55] op_sel_hi:[0,1,1]
	ds_read_b128 v[246:249], v238 offset:5248
	s_waitcnt lgkmcnt(8)
	v_pk_fma_f32 v[56:57], v[48:49], v[202:203], v[56:57] op_sel_hi:[1,0,1]
	s_nop 0
	v_pk_fma_f32 v[52:53], v[202:203], v[46:47], v[56:57] op_sel:[1,0,0]
	s_nop 0
	v_pk_fma_f32 v[52:53], v[204:205], v[50:51], v[52:53] op_sel_hi:[0,1,1]
	v_mov_b32_e32 v54, v205
	v_pk_fma_f32 v[52:53], v[54:55], v[44:45], v[52:53] op_sel_hi:[0,1,1]
	ds_read_b128 v[250:253], v238 offset:13456
	s_waitcnt lgkmcnt(8)
	v_pk_fma_f32 v[60:61], v[48:49], v[216:217], v[98:99] op_sel_hi:[1,0,1]
	s_nop 0
	v_pk_fma_f32 v[54:55], v[216:217], v[46:47], v[60:61] op_sel:[1,0,0]
	s_nop 0
	v_pk_fma_f32 v[54:55], v[218:219], v[50:51], v[54:55] op_sel_hi:[0,1,1]
	v_mov_b32_e32 v56, v219
	v_pk_fma_f32 v[90:91], v[56:57], v[44:45], v[54:55] op_sel_hi:[0,1,1]
	ds_read_b128 v[162:165], v238 offset:21664
	s_waitcnt lgkmcnt(8)
	v_pk_fma_f32 v[58:59], v[48:49], v[158:159], v[58:59] op_sel_hi:[1,0,1]
	s_nop 0
	v_pk_fma_f32 v[54:55], v[158:159], v[46:47], v[58:59] op_sel:[1,0,0]
	s_nop 0
	v_pk_fma_f32 v[54:55], v[160:161], v[50:51], v[54:55] op_sel_hi:[0,1,1]
	v_mov_b32_e32 v56, v161
	v_pk_fma_f32 v[54:55], v[56:57], v[44:45], v[54:55] op_sel_hi:[0,1,1]
	ds_read_b128 v[166:169], v238 offset:29872
	s_waitcnt lgkmcnt(8)
	v_pk_fma_f32 v[60:61], v[48:49], v[220:221], v[64:65] op_sel_hi:[1,0,1]
	s_nop 0
	v_pk_fma_f32 v[56:57], v[220:221], v[46:47], v[60:61] op_sel:[1,0,0]
	s_nop 0
	v_pk_fma_f32 v[56:57], v[222:223], v[50:51], v[56:57] op_sel_hi:[0,1,1]
	v_mov_b32_e32 v58, v223
	v_pk_fma_f32 v[56:57], v[58:59], v[44:45], v[56:57] op_sel_hi:[0,1,1]
	ds_read_b128 v[170:173], v238 offset:38080
	s_waitcnt lgkmcnt(8)
	v_pk_fma_f32 v[62:63], v[48:49], v[224:225], v[66:67] op_sel_hi:[1,0,1]
	s_nop 0
	v_pk_fma_f32 v[58:59], v[224:225], v[46:47], v[62:63] op_sel:[1,0,0]
	s_nop 0
	v_pk_fma_f32 v[58:59], v[226:227], v[50:51], v[58:59] op_sel_hi:[0,1,1]
	v_mov_b32_e32 v60, v227
	v_pk_fma_f32 v[58:59], v[60:61], v[44:45], v[58:59] op_sel_hi:[0,1,1]
	ds_read_b128 v[174:177], v238 offset:46288
	s_waitcnt lgkmcnt(8)
	v_pk_fma_f32 v[64:65], v[48:49], v[228:229], v[68:69] op_sel_hi:[1,0,1]
	s_nop 0
	v_pk_fma_f32 v[60:61], v[228:229], v[46:47], v[64:65] op_sel:[1,0,0]
	s_nop 0
	v_pk_fma_f32 v[60:61], v[230:231], v[50:51], v[60:61] op_sel_hi:[0,1,1]
	v_mov_b32_e32 v62, v231
	v_pk_fma_f32 v[60:61], v[62:63], v[44:45], v[60:61] op_sel_hi:[0,1,1]
	ds_read_b128 v[178:181], v238 offset:54496
	s_waitcnt lgkmcnt(8)
	v_pk_fma_f32 v[66:67], v[48:49], v[232:233], v[70:71] op_sel_hi:[1,0,1]
	s_nop 0
	v_pk_fma_f32 v[62:63], v[232:233], v[46:47], v[66:67] op_sel:[1,0,0]
	s_nop 0
	v_pk_fma_f32 v[62:63], v[234:235], v[50:51], v[62:63] op_sel_hi:[0,1,1]
	v_mov_b32_e32 v64, v235
	v_pk_fma_f32 v[62:63], v[64:65], v[44:45], v[62:63] op_sel_hi:[0,1,1]
	ds_read_b128 v[182:185], v238 offset:62704
	s_waitcnt lgkmcnt(8)
	v_pk_fma_f32 v[68:69], v[48:49], v[242:243], v[72:73] op_sel_hi:[1,0,1]
	s_nop 0
	v_pk_fma_f32 v[64:65], v[242:243], v[46:47], v[68:69] op_sel:[1,0,0]
	s_nop 0
	v_pk_fma_f32 v[64:65], v[244:245], v[50:51], v[64:65] op_sel_hi:[0,1,1]
	v_mov_b32_e32 v66, v245
	v_pk_fma_f32 v[64:65], v[66:67], v[44:45], v[64:65] op_sel_hi:[0,1,1]
	ds_read_b128 v[186:189], v25 offset:6144
	s_waitcnt lgkmcnt(8)
	v_pk_fma_f32 v[70:71], v[48:49], v[246:247], v[74:75] op_sel_hi:[1,0,1]
	s_nop 0
	v_pk_fma_f32 v[66:67], v[246:247], v[46:47], v[70:71] op_sel:[1,0,0]
	s_nop 0
	v_pk_fma_f32 v[66:67], v[248:249], v[50:51], v[66:67] op_sel_hi:[0,1,1]
	v_mov_b32_e32 v68, v249
	v_pk_fma_f32 v[66:67], v[68:69], v[44:45], v[66:67] op_sel_hi:[0,1,1]
	ds_read_b128 v[198:201], v25 offset:14352
	s_waitcnt lgkmcnt(8)
	v_pk_fma_f32 v[72:73], v[48:49], v[250:251], v[76:77] op_sel_hi:[1,0,1]
	s_nop 0
	v_pk_fma_f32 v[68:69], v[250:251], v[46:47], v[72:73] op_sel:[1,0,0]
	s_nop 0
	v_pk_fma_f32 v[68:69], v[252:253], v[50:51], v[68:69] op_sel_hi:[0,1,1]
	v_mov_b32_e32 v70, v253
	v_pk_fma_f32 v[68:69], v[70:71], v[44:45], v[68:69] op_sel_hi:[0,1,1]
	ds_read_b128 v[202:205], v25 offset:22560
	s_waitcnt lgkmcnt(8)
; #define LAS __attribute__((address_space(3)))
; __global__ void __launch_bounds__(NTHREADS, 2) hybrid_fwd(Args a) {
;     ...
;                     for (int j = 0; j < 8; ++j) {
; #pragma unroll
;                         for (int e = 0; e < 16; ++e) { const f32x4 w = *(const LAS f32x4*)(rwT + e * 2052 + j * 256 + lane * 4);
;                             acc2[e] += y2[j][0] * (f32x2){w[0], w[0]}; acc2[e] += y2[j][1] * (f32x2){w[1], w[1]};
;                             acc2[e] += y2[j][2] * (f32x2){w[2], w[2]}; acc2[e] += y2[j][3] * (f32x2){w[3], w[3]}; }
;                         __builtin_amdgcn_sched_barrier(0);
;                     }
	v_pk_fma_f32 v[74:75], v[48:49], v[162:163], v[78:79] op_sel_hi:[1,0,1]
	s_nop 0
	v_pk_fma_f32 v[70:71], v[162:163], v[46:47], v[74:75] op_sel:[1,0,0]
	s_nop 0
	v_pk_fma_f32 v[70:71], v[164:165], v[50:51], v[70:71] op_sel_hi:[0,1,1]
	v_mov_b32_e32 v72, v165
	v_pk_fma_f32 v[70:71], v[72:73], v[44:45], v[70:71] op_sel_hi:[0,1,1]
	ds_read_b128 v[216:219], v25 offset:30768
	s_waitcnt lgkmcnt(8)
	v_pk_fma_f32 v[76:77], v[48:49], v[166:167], v[80:81] op_sel_hi:[1,0,1]
	s_nop 0
	v_pk_fma_f32 v[72:73], v[166:167], v[46:47], v[76:77] op_sel:[1,0,0]
	s_nop 0
	v_pk_fma_f32 v[72:73], v[168:169], v[50:51], v[72:73] op_sel_hi:[0,1,1]
	v_mov_b32_e32 v74, v169
	v_pk_fma_f32 v[72:73], v[74:75], v[44:45], v[72:73] op_sel_hi:[0,1,1]
	ds_read_b128 v[158:161], v25 offset:38976
	s_waitcnt lgkmcnt(8)
	v_pk_fma_f32 v[78:79], v[48:49], v[170:171], v[82:83] op_sel_hi:[1,0,1]
	s_nop 0
	v_pk_fma_f32 v[74:75], v[170:171], v[46:47], v[78:79] op_sel:[1,0,0]
	s_nop 0
	v_pk_fma_f32 v[74:75], v[172:173], v[50:51], v[74:75] op_sel_hi:[0,1,1]
	v_mov_b32_e32 v76, v173
	v_pk_fma_f32 v[74:75], v[76:77], v[44:45], v[74:75] op_sel_hi:[0,1,1]
	ds_read_b128 v[220:223], v25 offset:47184
	s_waitcnt lgkmcnt(8)
	v_pk_fma_f32 v[80:81], v[48:49], v[174:175], v[84:85] op_sel_hi:[1,0,1]
	s_nop 0
	v_pk_fma_f32 v[76:77], v[174:175], v[46:47], v[80:81] op_sel:[1,0,0]
	s_nop 0
	v_pk_fma_f32 v[76:77], v[176:177], v[50:51], v[76:77] op_sel_hi:[0,1,1]
	v_mov_b32_e32 v78, v177
	v_pk_fma_f32 v[76:77], v[78:79], v[44:45], v[76:77] op_sel_hi:[0,1,1]
	ds_read_b128 v[224:227], v25 offset:55392
	s_waitcnt lgkmcnt(8)
	v_pk_fma_f32 v[82:83], v[48:49], v[178:179], v[86:87] op_sel_hi:[1,0,1]
	s_nop 0
	v_pk_fma_f32 v[78:79], v[178:179], v[46:47], v[82:83] op_sel:[1,0,0]
	s_nop 0
	v_pk_fma_f32 v[78:79], v[180:181], v[50:51], v[78:79] op_sel_hi:[0,1,1]
	v_mov_b32_e32 v80, v181
	v_pk_fma_f32 v[78:79], v[80:81], v[44:45], v[78:79] op_sel_hi:[0,1,1]
	ds_read_b128 v[228:231], v25 offset:63600
	s_waitcnt lgkmcnt(8)
	v_pk_fma_f32 v[48:49], v[48:49], v[182:183], v[88:89] op_sel_hi:[1,0,1]
	s_nop 0
	v_pk_fma_f32 v[46:47], v[182:183], v[46:47], v[48:49] op_sel:[1,0,0]
	v_mov_b32_e32 v48, v185
	v_pk_fma_f32 v[46:47], v[184:185], v[50:51], v[46:47] op_sel_hi:[0,1,1]
	v_pk_fma_f32 v[80:81], v[48:49], v[44:45], v[46:47] op_sel_hi:[0,1,1]
	ds_read_b128 v[232:235], v238 offset:6272
	s_waitcnt lgkmcnt(8)
	v_pk_fma_f32 v[48:49], v[40:41], v[186:187], v[52:53] op_sel_hi:[1,0,1]
	s_nop 0
	v_pk_fma_f32 v[44:45], v[186:187], v[38:39], v[48:49] op_sel:[1,0,0]
	s_nop 0
	v_pk_fma_f32 v[44:45], v[188:189], v[42:43], v[44:45] op_sel_hi:[0,1,1]
	v_mov_b32_e32 v46, v189
	v_pk_fma_f32 v[44:45], v[46:47], v[36:37], v[44:45] op_sel_hi:[0,1,1]
	ds_read_b128 v[242:245], v238 offset:14480
	s_waitcnt lgkmcnt(8)
	v_pk_fma_f32 v[50:51], v[40:41], v[198:199], v[90:91] op_sel_hi:[1,0,1]
	s_nop 0
	v_pk_fma_f32 v[46:47], v[198:199], v[38:39], v[50:51] op_sel:[1,0,0]
	s_nop 0
	v_pk_fma_f32 v[46:47], v[200:201], v[42:43], v[46:47] op_sel_hi:[0,1,1]
	v_mov_b32_e32 v48, v201
	v_pk_fma_f32 v[82:83], v[48:49], v[36:37], v[46:47] op_sel_hi:[0,1,1]
	ds_read_b128 v[246:249], v238 offset:22688
	s_waitcnt lgkmcnt(8)
	v_pk_fma_f32 v[50:51], v[40:41], v[202:203], v[54:55] op_sel_hi:[1,0,1]
	s_nop 0
	v_pk_fma_f32 v[46:47], v[202:203], v[38:39], v[50:51] op_sel:[1,0,0]
	s_nop 0
	v_pk_fma_f32 v[46:47], v[204:205], v[42:43], v[46:47] op_sel_hi:[0,1,1]
	v_mov_b32_e32 v48, v205
	v_pk_fma_f32 v[46:47], v[48:49], v[36:37], v[46:47] op_sel_hi:[0,1,1]
	ds_read_b128 v[250:253], v238 offset:30896
	s_waitcnt lgkmcnt(8)
	v_pk_fma_f32 v[52:53], v[40:41], v[216:217], v[56:57] op_sel_hi:[1,0,1]
	s_nop 0
	v_pk_fma_f32 v[48:49], v[216:217], v[38:39], v[52:53] op_sel:[1,0,0]
	s_nop 0
	v_pk_fma_f32 v[48:49], v[218:219], v[42:43], v[48:49] op_sel_hi:[0,1,1]
	v_mov_b32_e32 v50, v219
	v_pk_fma_f32 v[48:49], v[50:51], v[36:37], v[48:49] op_sel_hi:[0,1,1]
	ds_read_b128 v[162:165], v238 offset:39104
	s_waitcnt lgkmcnt(8)
	v_pk_fma_f32 v[54:55], v[40:41], v[158:159], v[58:59] op_sel_hi:[1,0,1]
	s_nop 0
	v_pk_fma_f32 v[50:51], v[158:159], v[38:39], v[54:55] op_sel:[1,0,0]
	s_nop 0
	v_pk_fma_f32 v[50:51], v[160:161], v[42:43], v[50:51] op_sel_hi:[0,1,1]
	v_mov_b32_e32 v52, v161
	v_pk_fma_f32 v[50:51], v[52:53], v[36:37], v[50:51] op_sel_hi:[0,1,1]
	ds_read_b128 v[166:169], v238 offset:47312
	s_waitcnt lgkmcnt(8)
	v_pk_fma_f32 v[56:57], v[40:41], v[220:221], v[60:61] op_sel_hi:[1,0,1]
	s_nop 0
	v_pk_fma_f32 v[52:53], v[220:221], v[38:39], v[56:57] op_sel:[1,0,0]
	s_nop 0
	v_pk_fma_f32 v[52:53], v[222:223], v[42:43], v[52:53] op_sel_hi:[0,1,1]
	v_mov_b32_e32 v54, v223
	v_pk_fma_f32 v[52:53], v[54:55], v[36:37], v[52:53] op_sel_hi:[0,1,1]
	ds_read_b128 v[170:173], v238 offset:55520
	s_waitcnt lgkmcnt(8)
	v_pk_fma_f32 v[58:59], v[40:41], v[224:225], v[62:63] op_sel_hi:[1,0,1]
	s_nop 0
	v_pk_fma_f32 v[54:55], v[224:225], v[38:39], v[58:59] op_sel:[1,0,0]
	s_nop 0
	v_pk_fma_f32 v[54:55], v[226:227], v[42:43], v[54:55] op_sel_hi:[0,1,1]
	v_mov_b32_e32 v56, v227
	v_pk_fma_f32 v[54:55], v[56:57], v[36:37], v[54:55] op_sel_hi:[0,1,1]
	ds_read_b128 v[174:177], v238 offset:63728
	s_waitcnt lgkmcnt(8)
	v_pk_fma_f32 v[60:61], v[40:41], v[228:229], v[64:65] op_sel_hi:[1,0,1]
	s_nop 0
	v_pk_fma_f32 v[56:57], v[228:229], v[38:39], v[60:61] op_sel:[1,0,0]
	s_nop 0
	v_pk_fma_f32 v[56:57], v[230:231], v[42:43], v[56:57] op_sel_hi:[0,1,1]
	v_mov_b32_e32 v58, v231
	v_pk_fma_f32 v[56:57], v[58:59], v[36:37], v[56:57] op_sel_hi:[0,1,1]
	ds_read_b128 v[178:181], v25 offset:7168
	s_waitcnt lgkmcnt(8)
; #define LAS __attribute__((address_space(3)))
; __global__ void __launch_bounds__(NTHREADS, 2) hybrid_fwd(Args a) {
;     ...
;                     for (int j = 0; j < 8; ++j) {
; #pragma unroll
;                         for (int e = 0; e < 16; ++e) { const f32x4 w = *(const LAS f32x4*)(rwT + e * 2052 + j * 256 + lane * 4);
;                             acc2[e] += y2[j][0] * (f32x2){w[0], w[0]}; acc2[e] += y2[j][1] * (f32x2){w[1], w[1]};
;                             acc2[e] += y2[j][2] * (f32x2){w[2], w[2]}; acc2[e] += y2[j][3] * (f32x2){w[3], w[3]}; }
;                         __builtin_amdgcn_sched_barrier(0);
;                     }
	v_pk_fma_f32 v[62:63], v[40:41], v[232:233], v[66:67] op_sel_hi:[1,0,1]
	s_nop 0
	v_pk_fma_f32 v[58:59], v[232:233], v[38:39], v[62:63] op_sel:[1,0,0]
	s_nop 0
	v_pk_fma_f32 v[58:59], v[234:235], v[42:43], v[58:59] op_sel_hi:[0,1,1]
	v_mov_b32_e32 v60, v235
	v_pk_fma_f32 v[58:59], v[60:61], v[36:37], v[58:59] op_sel_hi:[0,1,1]
	ds_read_b128 v[182:185], v25 offset:15376
	s_waitcnt lgkmcnt(8)
	v_pk_fma_f32 v[64:65], v[40:41], v[242:243], v[68:69] op_sel_hi:[1,0,1]
	s_nop 0
	v_pk_fma_f32 v[60:61], v[242:243], v[38:39], v[64:65] op_sel:[1,0,0]
	s_nop 0
	v_pk_fma_f32 v[60:61], v[244:245], v[42:43], v[60:61] op_sel_hi:[0,1,1]
	v_mov_b32_e32 v62, v245
	v_pk_fma_f32 v[60:61], v[62:63], v[36:37], v[60:61] op_sel_hi:[0,1,1]
	ds_read_b128 v[186:189], v25 offset:23584
	s_waitcnt lgkmcnt(8)
	v_pk_fma_f32 v[66:67], v[40:41], v[246:247], v[70:71] op_sel_hi:[1,0,1]
	s_nop 0
	v_pk_fma_f32 v[62:63], v[246:247], v[38:39], v[66:67] op_sel:[1,0,0]
	s_nop 0
	v_pk_fma_f32 v[62:63], v[248:249], v[42:43], v[62:63] op_sel_hi:[0,1,1]
	v_mov_b32_e32 v64, v249
	v_pk_fma_f32 v[62:63], v[64:65], v[36:37], v[62:63] op_sel_hi:[0,1,1]
	ds_read_b128 v[198:201], v25 offset:31792
	s_waitcnt lgkmcnt(8)
	v_pk_fma_f32 v[68:69], v[40:41], v[250:251], v[72:73] op_sel_hi:[1,0,1]
	s_nop 0
	v_pk_fma_f32 v[64:65], v[250:251], v[38:39], v[68:69] op_sel:[1,0,0]
	s_nop 0
	v_pk_fma_f32 v[64:65], v[252:253], v[42:43], v[64:65] op_sel_hi:[0,1,1]
	v_mov_b32_e32 v66, v253
	v_pk_fma_f32 v[64:65], v[66:67], v[36:37], v[64:65] op_sel_hi:[0,1,1]
	ds_read_b128 v[202:205], v25 offset:40000
	s_waitcnt lgkmcnt(8)
	v_pk_fma_f32 v[70:71], v[40:41], v[162:163], v[74:75] op_sel_hi:[1,0,1]
	s_nop 0
	v_pk_fma_f32 v[66:67], v[162:163], v[38:39], v[70:71] op_sel:[1,0,0]
	s_nop 0
	v_pk_fma_f32 v[66:67], v[164:165], v[42:43], v[66:67] op_sel_hi:[0,1,1]
	v_mov_b32_e32 v68, v165
	v_pk_fma_f32 v[66:67], v[68:69], v[36:37], v[66:67] op_sel_hi:[0,1,1]
	ds_read_b128 v[216:219], v25 offset:48208
	s_waitcnt lgkmcnt(8)
	v_pk_fma_f32 v[72:73], v[40:41], v[166:167], v[76:77] op_sel_hi:[1,0,1]
	s_nop 0
	v_pk_fma_f32 v[68:69], v[166:167], v[38:39], v[72:73] op_sel:[1,0,0]
	s_nop 0
	v_pk_fma_f32 v[68:69], v[168:169], v[42:43], v[68:69] op_sel_hi:[0,1,1]
	v_mov_b32_e32 v70, v169
	v_pk_fma_f32 v[68:69], v[70:71], v[36:37], v[68:69] op_sel_hi:[0,1,1]
	ds_read_b128 v[158:161], v25 offset:56416
	s_waitcnt lgkmcnt(8)
	v_pk_fma_f32 v[74:75], v[40:41], v[170:171], v[78:79] op_sel_hi:[1,0,1]
	s_nop 0
	v_pk_fma_f32 v[70:71], v[170:171], v[38:39], v[74:75] op_sel:[1,0,0]
	s_nop 0
	v_pk_fma_f32 v[70:71], v[172:173], v[42:43], v[70:71] op_sel_hi:[0,1,1]
	v_mov_b32_e32 v72, v173
	v_pk_fma_f32 v[70:71], v[72:73], v[36:37], v[70:71] op_sel_hi:[0,1,1]
	ds_read_b128 v[220:223], v25 offset:64624
	s_waitcnt lgkmcnt(8)
	v_pk_fma_f32 v[40:41], v[40:41], v[174:175], v[80:81] op_sel_hi:[1,0,1]
	s_nop 0
	v_pk_fma_f32 v[38:39], v[174:175], v[38:39], v[40:41] op_sel:[1,0,0]
	v_mov_b32_e32 v40, v177
	v_pk_fma_f32 v[38:39], v[176:177], v[42:43], v[38:39] op_sel_hi:[0,1,1]
	v_pk_fma_f32 v[72:73], v[40:41], v[36:37], v[38:39] op_sel_hi:[0,1,1]
	ds_read_b128 v[224:227], v238 offset:7296
	s_waitcnt lgkmcnt(8)
	v_pk_fma_f32 v[40:41], v[22:23], v[178:179], v[44:45] op_sel_hi:[1,0,1]
	s_nop 0
	v_pk_fma_f32 v[36:37], v[178:179], v[18:19], v[40:41] op_sel:[1,0,0]
	s_nop 0
	v_pk_fma_f32 v[36:37], v[180:181], v[20:21], v[36:37] op_sel_hi:[0,1,1]
	v_mov_b32_e32 v38, v181
	v_pk_fma_f32 v[36:37], v[38:39], v[16:17], v[36:37] op_sel_hi:[0,1,1]
	ds_read_b128 v[228:231], v238 offset:15504
	s_waitcnt lgkmcnt(8)
	v_pk_fma_f32 v[42:43], v[22:23], v[182:183], v[82:83] op_sel_hi:[1,0,1]
	s_nop 0
	v_pk_fma_f32 v[38:39], v[182:183], v[18:19], v[42:43] op_sel:[1,0,0]
	s_nop 0
	v_pk_fma_f32 v[38:39], v[184:185], v[20:21], v[38:39] op_sel_hi:[0,1,1]
	v_mov_b32_e32 v40, v185
	v_pk_fma_f32 v[38:39], v[40:41], v[16:17], v[38:39] op_sel_hi:[0,1,1]
	ds_read_b128 v[232:235], v238 offset:23712
	s_waitcnt lgkmcnt(8)
	v_pk_fma_f32 v[44:45], v[22:23], v[186:187], v[46:47] op_sel_hi:[1,0,1]
	s_nop 0
	v_pk_fma_f32 v[40:41], v[186:187], v[18:19], v[44:45] op_sel:[1,0,0]
	s_nop 0
	v_pk_fma_f32 v[40:41], v[188:189], v[20:21], v[40:41] op_sel_hi:[0,1,1]
	v_mov_b32_e32 v42, v189
	v_pk_fma_f32 v[40:41], v[42:43], v[16:17], v[40:41] op_sel_hi:[0,1,1]
	ds_read_b128 v[242:245], v238 offset:31920
	s_waitcnt lgkmcnt(8)
	v_pk_fma_f32 v[46:47], v[22:23], v[198:199], v[48:49] op_sel_hi:[1,0,1]
	s_nop 0
	v_pk_fma_f32 v[42:43], v[198:199], v[18:19], v[46:47] op_sel:[1,0,0]
	ds_read_b128 v[246:249], v238 offset:40128
	v_pk_fma_f32 v[42:43], v[200:201], v[20:21], v[42:43] op_sel_hi:[0,1,1]
	v_mov_b32_e32 v44, v201
	v_pk_fma_f32 v[44:45], v[44:45], v[16:17], v[42:43] op_sel_hi:[0,1,1]
	s_waitcnt lgkmcnt(8)
	v_pk_fma_f32 v[42:43], v[22:23], v[202:203], v[50:51] op_sel_hi:[1,0,1]
	s_nop 0
	v_pk_fma_f32 v[42:43], v[202:203], v[18:19], v[42:43] op_sel:[1,0,0]
	v_mov_b32_e32 v46, v205
	v_pk_fma_f32 v[42:43], v[204:205], v[20:21], v[42:43] op_sel_hi:[0,1,1]
	v_pk_fma_f32 v[42:43], v[46:47], v[16:17], v[42:43] op_sel_hi:[0,1,1]
	ds_read_b128 v[250:253], v238 offset:48336
	s_waitcnt lgkmcnt(8)
	v_pk_fma_f32 v[50:51], v[22:23], v[216:217], v[52:53] op_sel_hi:[1,0,1]
	s_nop 0
	v_pk_fma_f32 v[46:47], v[216:217], v[18:19], v[50:51] op_sel:[1,0,0]
	s_nop 0
	v_pk_fma_f32 v[46:47], v[218:219], v[20:21], v[46:47] op_sel_hi:[0,1,1]
	v_mov_b32_e32 v48, v219
	v_pk_fma_f32 v[46:47], v[48:49], v[16:17], v[46:47] op_sel_hi:[0,1,1]
	ds_read_b128 v[162:165], v238 offset:56544
	s_waitcnt lgkmcnt(8)
; #define LAS __attribute__((address_space(3)))
; __global__ void __launch_bounds__(NTHREADS, 2) hybrid_fwd(Args a) {
;     ...
;                     for (int j = 0; j < 8; ++j) {
; #pragma unroll
;                         for (int e = 0; e < 16; ++e) { const f32x4 w = *(const LAS f32x4*)(rwT + e * 2052 + j * 256 + lane * 4);
;                             acc2[e] += y2[j][0] * (f32x2){w[0], w[0]}; acc2[e] += y2[j][1] * (f32x2){w[1], w[1]};
;                             acc2[e] += y2[j][2] * (f32x2){w[2], w[2]}; acc2[e] += y2[j][3] * (f32x2){w[3], w[3]}; }
;                         __builtin_amdgcn_sched_barrier(0);
;                     }
;                     float acca[16], accb[16];
; #pragma unroll
;                     for (int e = 0; e < 16; ++e) { acca[e] = acc2[e][0]; accb[e] = acc2[e][1]; }
;                     P7_PICK(2 * qp, acca);
	v_pk_fma_f32 v[52:53], v[22:23], v[158:159], v[54:55] op_sel_hi:[1,0,1]
	s_nop 0
	v_pk_fma_f32 v[48:49], v[158:159], v[18:19], v[52:53] op_sel:[1,0,0]
	s_nop 0
	v_pk_fma_f32 v[48:49], v[160:161], v[20:21], v[48:49] op_sel_hi:[0,1,1]
	v_mov_b32_e32 v50, v161
	v_pk_fma_f32 v[48:49], v[50:51], v[16:17], v[48:49] op_sel_hi:[0,1,1]
	ds_read_b128 v[166:169], v238 offset:64752
	s_waitcnt lgkmcnt(8)
	v_pk_fma_f32 v[54:55], v[22:23], v[220:221], v[56:57] op_sel_hi:[1,0,1]
	s_nop 0
	v_pk_fma_f32 v[50:51], v[220:221], v[18:19], v[54:55] op_sel:[1,0,0]
	s_nop 0
	v_pk_fma_f32 v[50:51], v[222:223], v[20:21], v[50:51] op_sel_hi:[0,1,1]
	v_mov_b32_e32 v52, v223
	v_pk_fma_f32 v[50:51], v[52:53], v[16:17], v[50:51] op_sel_hi:[0,1,1]
	s_waitcnt lgkmcnt(7)
	v_pk_fma_f32 v[56:57], v[22:23], v[224:225], v[58:59] op_sel_hi:[1,0,1]
	s_nop 0
	v_pk_fma_f32 v[52:53], v[224:225], v[18:19], v[56:57] op_sel:[1,0,0]
	s_nop 0
	v_pk_fma_f32 v[52:53], v[226:227], v[20:21], v[52:53] op_sel_hi:[0,1,1]
	v_mov_b32_e32 v54, v227
	v_pk_fma_f32 v[52:53], v[54:55], v[16:17], v[52:53] op_sel_hi:[0,1,1]
	s_waitcnt lgkmcnt(6)
	v_pk_fma_f32 v[58:59], v[22:23], v[228:229], v[60:61] op_sel_hi:[1,0,1]
	s_nop 0
	v_pk_fma_f32 v[54:55], v[228:229], v[18:19], v[58:59] op_sel:[1,0,0]
	s_nop 0
	v_pk_fma_f32 v[54:55], v[230:231], v[20:21], v[54:55] op_sel_hi:[0,1,1]
	v_mov_b32_e32 v56, v231
	v_pk_fma_f32 v[54:55], v[56:57], v[16:17], v[54:55] op_sel_hi:[0,1,1]
	s_waitcnt lgkmcnt(5)
	v_pk_fma_f32 v[60:61], v[22:23], v[232:233], v[62:63] op_sel_hi:[1,0,1]
	s_nop 0
	v_pk_fma_f32 v[56:57], v[232:233], v[18:19], v[60:61] op_sel:[1,0,0]
	s_nop 0
	v_pk_fma_f32 v[56:57], v[234:235], v[20:21], v[56:57] op_sel_hi:[0,1,1]
	v_mov_b32_e32 v58, v235
	v_pk_fma_f32 v[56:57], v[58:59], v[16:17], v[56:57] op_sel_hi:[0,1,1]
	s_waitcnt lgkmcnt(4)
	v_pk_fma_f32 v[62:63], v[22:23], v[242:243], v[64:65] op_sel_hi:[1,0,1]
	s_nop 0
	v_pk_fma_f32 v[58:59], v[242:243], v[18:19], v[62:63] op_sel:[1,0,0]
	s_nop 0
	v_pk_fma_f32 v[58:59], v[244:245], v[20:21], v[58:59] op_sel_hi:[0,1,1]
	v_mov_b32_e32 v60, v245
	v_pk_fma_f32 v[58:59], v[60:61], v[16:17], v[58:59] op_sel_hi:[0,1,1]
	s_waitcnt lgkmcnt(3)
	v_pk_fma_f32 v[64:65], v[22:23], v[246:247], v[66:67] op_sel_hi:[1,0,1]
	s_nop 0
	v_pk_fma_f32 v[60:61], v[246:247], v[18:19], v[64:65] op_sel:[1,0,0]
	s_nop 0
	v_pk_fma_f32 v[60:61], v[248:249], v[20:21], v[60:61] op_sel_hi:[0,1,1]
	v_mov_b32_e32 v62, v249
	v_pk_fma_f32 v[60:61], v[62:63], v[16:17], v[60:61] op_sel_hi:[0,1,1]
	s_waitcnt lgkmcnt(2)
	v_pk_fma_f32 v[66:67], v[22:23], v[250:251], v[68:69] op_sel_hi:[1,0,1]
	s_nop 0
	v_pk_fma_f32 v[62:63], v[250:251], v[18:19], v[66:67] op_sel:[1,0,0]
	s_nop 0
	v_pk_fma_f32 v[62:63], v[252:253], v[20:21], v[62:63] op_sel_hi:[0,1,1]
	v_mov_b32_e32 v64, v253
	v_pk_fma_f32 v[62:63], v[64:65], v[16:17], v[62:63] op_sel_hi:[0,1,1]
	s_waitcnt lgkmcnt(1)
	v_pk_fma_f32 v[68:69], v[22:23], v[162:163], v[70:71] op_sel_hi:[1,0,1]
	s_nop 0
	v_pk_fma_f32 v[64:65], v[162:163], v[18:19], v[68:69] op_sel:[1,0,0]
	s_nop 0
	v_pk_fma_f32 v[64:65], v[164:165], v[20:21], v[64:65] op_sel_hi:[0,1,1]
	v_mov_b32_e32 v66, v165
	v_pk_fma_f32 v[64:65], v[66:67], v[16:17], v[64:65] op_sel_hi:[0,1,1]
	s_waitcnt lgkmcnt(0)
	v_pk_fma_f32 v[22:23], v[22:23], v[166:167], v[72:73] op_sel_hi:[1,0,1]
	s_nop 0
	v_pk_fma_f32 v[18:19], v[166:167], v[18:19], v[22:23] op_sel:[1,0,0]
	s_nop 0
	v_pk_fma_f32 v[18:19], v[168:169], v[20:21], v[18:19] op_sel_hi:[0,1,1]
	v_mov_b32_e32 v20, v169
	v_pk_fma_f32 v[16:17], v[20:21], v[16:17], v[18:19] op_sel_hi:[0,1,1]
	s_nop 1
	v_permlane32_swap_b32_e32 v16, v17
	v_permlane32_swap_b32_e32 v36, v37
	v_permlane32_swap_b32_e32 v38, v39
	v_permlane32_swap_b32_e32 v40, v41
	v_permlane32_swap_b32_e32 v42, v43
	v_permlane32_swap_b32_e32 v44, v45
	v_permlane32_swap_b32_e32 v46, v47
	v_permlane32_swap_b32_e32 v48, v49
	v_permlane32_swap_b32_e32 v50, v51
	v_permlane32_swap_b32_e32 v52, v53
	v_permlane32_swap_b32_e32 v54, v55
	v_permlane32_swap_b32_e32 v56, v57
	v_permlane32_swap_b32_e32 v58, v59
	v_permlane32_swap_b32_e32 v60, v61
	v_permlane32_swap_b32_e32 v62, v63
	v_permlane32_swap_b32_e32 v64, v65
	v_add_f32_e32 v16, v16, v17
	v_add_f32_e32 v36, v36, v37
	v_add_f32_e32 v38, v38, v39
	v_add_f32_e32 v40, v40, v41
	v_add_f32_e32 v42, v42, v43
	v_add_f32_e32 v44, v44, v45
	v_add_f32_e32 v46, v46, v47
	v_add_f32_e32 v48, v48, v49
	v_add_f32_e32 v50, v50, v51
	v_add_f32_e32 v52, v52, v53
	v_add_f32_e32 v54, v54, v55
	v_add_f32_e32 v56, v56, v57
	v_add_f32_e32 v58, v58, v59
	v_add_f32_e32 v60, v60, v61
	v_add_f32_e32 v62, v62, v63
	v_add_f32_e32 v64, v64, v65
	s_nop 1
	v_add_f32_dpp v18, v36, v36 quad_perm:[1,0,3,2] row_mask:0xf bank_mask:0xf bound_ctrl:1
	s_nop 0
	v_add_f32_dpp v16, v16, v16 quad_perm:[1,0,3,2] row_mask:0xf bank_mask:0xf bound_ctrl:1
	v_add_f32_dpp v36, v62, v62 quad_perm:[1,0,3,2] row_mask:0xf bank_mask:0xf bound_ctrl:1
	v_add_f32_dpp v18, v18, v18 quad_perm:[2,3,0,1] row_mask:0xf bank_mask:0xf bound_ctrl:1
	v_add_f32_dpp v16, v16, v16 quad_perm:[2,3,0,1] row_mask:0xf bank_mask:0xf bound_ctrl:1
	v_add_f32_dpp v36, v36, v36 quad_perm:[2,3,0,1] row_mask:0xf bank_mask:0xf bound_ctrl:1
	v_add_f32_dpp v18, v18, v18 row_ror:4 row_mask:0xf bank_mask:0xf bound_ctrl:1
	v_add_f32_dpp v16, v16, v16 row_ror:4 row_mask:0xf bank_mask:0xf bound_ctrl:1
	v_add_f32_dpp v36, v36, v36 row_ror:4 row_mask:0xf bank_mask:0xf bound_ctrl:1
	v_add_f32_dpp v18, v18, v18 row_ror:8 row_mask:0xf bank_mask:0xf bound_ctrl:1
	v_mov_b32_e32 v19, v18
	s_nop 1
	v_permlane16_swap_b32_e32 v18, v19
	v_add_f32_e32 v18, v18, v19
	v_mov_b32_e32 v19, v18
	s_nop 1
	s_nop 0
	v_mov_b32_e32 v18, v18
	s_nop 0
	v_add_f32_dpp v19, v38, v38 quad_perm:[1,0,3,2] row_mask:0xf bank_mask:0xf bound_ctrl:1
	v_mul_f32_e32 v18, 0xbfb8aa3b, v18
	v_exp_f32_e32 v18, v18
	v_add_f32_dpp v19, v19, v19 quad_perm:[2,3,0,1] row_mask:0xf bank_mask:0xf bound_ctrl:1
	v_add_f32_dpp v16, v16, v16 row_ror:8 row_mask:0xf bank_mask:0xf bound_ctrl:1
	v_add_f32_dpp v36, v36, v36 row_ror:8 row_mask:0xf bank_mask:0xf bound_ctrl:1
	v_add_f32_dpp v19, v19, v19 row_ror:4 row_mask:0xf bank_mask:0xf bound_ctrl:1
	v_add_f32_e32 v18, 1.0, v18
	v_rcp_f32_e32 v18, v18
	v_add_f32_dpp v19, v19, v19 row_ror:8 row_mask:0xf bank_mask:0xf bound_ctrl:1
	v_mov_b32_e32 v20, v19
	s_nop 1
	v_permlane16_swap_b32_e32 v19, v20
	v_add_f32_e32 v19, v19, v20
	v_mov_b32_e32 v20, v19
	s_nop 1
	s_nop 0
	v_mov_b32_e32 v19, v19
	s_nop 0
	v_add_f32_dpp v20, v40, v40 quad_perm:[1,0,3,2] row_mask:0xf bank_mask:0xf bound_ctrl:1
	v_mul_f32_e32 v19, 0xbfb8aa3b, v19
	v_exp_f32_e32 v19, v19
	v_add_f32_dpp v20, v20, v20 quad_perm:[2,3,0,1] row_mask:0xf bank_mask:0xf bound_ctrl:1
	v_add_f32_dpp v40, v64, v64 quad_perm:[1,0,3,2] row_mask:0xf bank_mask:0xf bound_ctrl:1
	v_mov_b32_e32 v38, v36
	v_add_f32_dpp v20, v20, v20 row_ror:4 row_mask:0xf bank_mask:0xf bound_ctrl:1
	v_add_f32_e32 v19, 1.0, v19
	v_rcp_f32_e32 v19, v19
	v_add_f32_dpp v20, v20, v20 row_ror:8 row_mask:0xf bank_mask:0xf bound_ctrl:1
	v_mov_b32_e32 v21, v20
	s_nop 1
	v_permlane16_swap_b32_e32 v20, v21
	v_add_f32_e32 v20, v20, v21
	v_mov_b32_e32 v21, v20
	s_nop 1
	s_nop 0
	v_mov_b32_e32 v20, v20
	s_nop 0
	v_add_f32_dpp v21, v44, v44 quad_perm:[1,0,3,2] row_mask:0xf bank_mask:0xf bound_ctrl:1
	v_mul_f32_e32 v20, 0xbfb8aa3b, v20
	v_exp_f32_e32 v20, v20
	v_add_f32_dpp v21, v21, v21 quad_perm:[2,3,0,1] row_mask:0xf bank_mask:0xf bound_ctrl:1
	v_mov_b32_e32 v44, v16
	s_nop 1
	v_permlane16_swap_b32_e32 v16, v44
	v_add_f32_dpp v21, v21, v21 row_ror:4 row_mask:0xf bank_mask:0xf bound_ctrl:1
	v_add_f32_e32 v20, 1.0, v20
	v_rcp_f32_e32 v70, v20
	v_add_f32_dpp v21, v21, v21 row_ror:8 row_mask:0xf bank_mask:0xf bound_ctrl:1
	v_mov_b32_e32 v22, v21
	s_nop 1
	v_permlane16_swap_b32_e32 v21, v22
	v_add_f32_e32 v21, v21, v22
	v_mov_b32_e32 v22, v21
	s_nop 1
	s_nop 0
	v_mov_b32_e32 v21, v21
	s_nop 0
	v_add_f32_dpp v22, v42, v42 quad_perm:[1,0,3,2] row_mask:0xf bank_mask:0xf bound_ctrl:1
	v_mul_f32_e32 v21, 0xbfb8aa3b, v21
	v_exp_f32_e32 v21, v21
	v_add_f32_dpp v22, v22, v22 quad_perm:[2,3,0,1] row_mask:0xf bank_mask:0xf bound_ctrl:1
	v_add_f32_e32 v79, v14, v70
	v_add_f32_e32 v44, v16, v44
	v_add_f32_dpp v22, v22, v22 row_ror:4 row_mask:0xf bank_mask:0xf bound_ctrl:1
	v_add_f32_e32 v20, 1.0, v21
	v_rcp_f32_e32 v72, v20
	v_add_f32_dpp v22, v22, v22 row_ror:8 row_mask:0xf bank_mask:0xf bound_ctrl:1
	v_mov_b32_e32 v23, v22
	s_nop 1
	v_permlane16_swap_b32_e32 v22, v23
	v_add_f32_e32 v69, v22, v23
	s_nop 0
	v_add_f32_dpp v22, v46, v46 quad_perm:[1,0,3,2] row_mask:0xf bank_mask:0xf bound_ctrl:1
	v_pk_add_f32 v[20:21], v[12:13], v[18:19]
	v_add_f32_e32 v80, v15, v72
	v_add_f32_dpp v22, v22, v22 quad_perm:[2,3,0,1] row_mask:0xf bank_mask:0xf bound_ctrl:1
	v_cmp_gt_f32_e32 vcc, v21, v20
	v_add_f32_dpp v40, v40, v40 quad_perm:[2,3,0,1] row_mask:0xf bank_mask:0xf bound_ctrl:1
	v_add_f32_dpp v22, v22, v22 row_ror:4 row_mask:0xf bank_mask:0xf bound_ctrl:1
	v_cndmask_b32_e32 v16, v20, v21, vcc
	v_cmp_gt_f32_e64 s[6:7], v79, v16
	v_add_f32_dpp v22, v22, v22 row_ror:8 row_mask:0xf bank_mask:0xf bound_ctrl:1
	v_mov_b32_e32 v23, v22
	s_nop 1
	v_permlane16_swap_b32_e32 v22, v23
	v_add_f32_e32 v73, v22, v23
	s_nop 0
	v_add_f32_dpp v22, v48, v48 quad_perm:[1,0,3,2] row_mask:0xf bank_mask:0xf bound_ctrl:1
	v_cndmask_b32_e64 v48, 0, 1, vcc
	v_cndmask_b32_e64 v16, v16, v79, s[6:7]
	v_add_f32_dpp v22, v22, v22 quad_perm:[2,3,0,1] row_mask:0xf bank_mask:0xf bound_ctrl:1
	v_cndmask_b32_e64 v48, v48, 2, s[6:7]
	v_cmp_ngt_f32_e64 s[8:9], v80, v16
	v_add_f32_dpp v22, v22, v22 row_ror:4 row_mask:0xf bank_mask:0xf bound_ctrl:1
	v_add_f32_dpp v40, v40, v40 row_ror:4 row_mask:0xf bank_mask:0xf bound_ctrl:1
	v_permlane16_swap_b32_e32 v36, v38
	v_add_f32_dpp v22, v22, v22 row_ror:8 row_mask:0xf bank_mask:0xf bound_ctrl:1
	v_mov_b32_e32 v23, v22
	s_nop 1
	v_permlane16_swap_b32_e32 v22, v23
	v_add_f32_e32 v75, v22, v23
	s_nop 0
	v_add_f32_dpp v22, v50, v50 quad_perm:[1,0,3,2] row_mask:0xf bank_mask:0xf bound_ctrl:1
	v_add_f32_dpp v40, v40, v40 row_ror:8 row_mask:0xf bank_mask:0xf bound_ctrl:1
	v_mov_b32_e32 v42, v40
	v_add_f32_dpp v22, v22, v22 quad_perm:[2,3,0,1] row_mask:0xf bank_mask:0xf bound_ctrl:1
	s_nop 0
	v_permlane16_swap_b32_e32 v40, v42
	v_add_f32_dpp v22, v22, v22 row_ror:4 row_mask:0xf bank_mask:0xf bound_ctrl:1
	v_add_f32_e32 v36, v36, v38
	v_add_f32_e32 v40, v40, v42
	v_add_f32_dpp v22, v22, v22 row_ror:8 row_mask:0xf bank_mask:0xf bound_ctrl:1
	v_mov_b32_e32 v23, v22
	s_nop 1
	v_permlane16_swap_b32_e32 v22, v23
	v_add_f32_e32 v77, v22, v23
	s_nop 0
	v_add_f32_dpp v22, v52, v52 quad_perm:[1,0,3,2] row_mask:0xf bank_mask:0xf bound_ctrl:1
	v_cndmask_b32_e64 v62, v80, v16, s[8:9]
	v_mov_b32_e32 v71, v69
	v_add_f32_dpp v22, v22, v22 quad_perm:[2,3,0,1] row_mask:0xf bank_mask:0xf bound_ctrl:1
	v_mov_b32_e32 v74, v73
	v_mov_b32_e32 v76, v75
	v_add_f32_dpp v22, v22, v22 row_ror:4 row_mask:0xf bank_mask:0xf bound_ctrl:1
	v_mov_b32_e32 v78, v77
	v_mov_b32_e32 v38, v36
	v_add_f32_dpp v22, v22, v22 row_ror:8 row_mask:0xf bank_mask:0xf bound_ctrl:1
	v_mov_b32_e32 v23, v22
	s_nop 1
	v_permlane16_swap_b32_e32 v22, v23
	v_add_f32_e32 v50, v22, v23
	s_nop 0
	v_add_f32_dpp v22, v54, v54 quad_perm:[1,0,3,2] row_mask:0xf bank_mask:0xf bound_ctrl:1
	v_mov_b32_e32 v52, v50
	v_mov_b32_e32 v42, v40
	v_add_f32_dpp v22, v22, v22 quad_perm:[2,3,0,1] row_mask:0xf bank_mask:0xf bound_ctrl:1
	v_mov_b32_e32 v46, v44
	s_nop 0
	v_add_f32_dpp v22, v22, v22 row_ror:4 row_mask:0xf bank_mask:0xf bound_ctrl:1
	s_nop 0
	s_nop 0
	v_add_f32_dpp v22, v22, v22 row_ror:8 row_mask:0xf bank_mask:0xf bound_ctrl:1
	v_mov_b32_e32 v23, v22
	s_nop 1
	v_permlane16_swap_b32_e32 v22, v23
	v_add_f32_e32 v54, v22, v23
	s_nop 0
	v_add_f32_dpp v22, v56, v56 quad_perm:[1,0,3,2] row_mask:0xf bank_mask:0xf bound_ctrl:1
	v_mov_b32_e32 v66, v54
	s_nop 0
	v_add_f32_dpp v22, v22, v22 quad_perm:[2,3,0,1] row_mask:0xf bank_mask:0xf bound_ctrl:1
	s_nop 0
	s_nop 0
	v_add_f32_dpp v22, v22, v22 row_ror:4 row_mask:0xf bank_mask:0xf bound_ctrl:1
	s_nop 0
	s_nop 0
	v_add_f32_dpp v22, v22, v22 row_ror:8 row_mask:0xf bank_mask:0xf bound_ctrl:1
	v_mov_b32_e32 v23, v22
	s_nop 1
	v_permlane16_swap_b32_e32 v22, v23
	v_add_f32_e32 v56, v22, v23
	s_nop 0
	v_add_f32_dpp v22, v58, v58 quad_perm:[1,0,3,2] row_mask:0xf bank_mask:0xf bound_ctrl:1
	v_mov_b32_e32 v67, v56
	s_nop 0
	v_add_f32_dpp v22, v22, v22 quad_perm:[2,3,0,1] row_mask:0xf bank_mask:0xf bound_ctrl:1
	s_nop 0
	s_nop 0
	v_add_f32_dpp v22, v22, v22 row_ror:4 row_mask:0xf bank_mask:0xf bound_ctrl:1
	s_nop 0
	s_nop 0
	v_add_f32_dpp v22, v22, v22 row_ror:8 row_mask:0xf bank_mask:0xf bound_ctrl:1
	v_mov_b32_e32 v23, v22
	s_nop 1
	v_permlane16_swap_b32_e32 v22, v23
	v_add_f32_e32 v58, v22, v23
	s_nop 0
	v_add_f32_dpp v22, v60, v60 quad_perm:[1,0,3,2] row_mask:0xf bank_mask:0xf bound_ctrl:1
	v_cndmask_b32_e64 v60, 3, v48, s[8:9]
	v_mov_b32_e32 v48, 0xff800000
	v_cmp_eq_u32_e64 s[10:11], 0, v60
	v_cmp_nlg_f32_e64 s[12:13], v20, v48
	s_or_b64 s[10:11], s[10:11], s[12:13]
	v_cndmask_b32_e64 v20, v20, v48, s[10:11]
	v_cmp_ne_u32_e64 s[12:13], 1, v60
	v_cmp_gt_f32_e64 s[14:15], v21, v20
	s_and_b64 s[12:13], s[12:13], s[14:15]
	v_cndmask_b32_e64 v20, v20, v21, s[12:13]
	v_add_f32_dpp v22, v22, v22 quad_perm:[2,3,0,1] row_mask:0xf bank_mask:0xf bound_ctrl:1
	v_cmp_ne_u32_e64 s[14:15], 2, v60
	v_cmp_gt_f32_e64 s[16:17], v79, v20
	v_add_f32_dpp v22, v22, v22 row_ror:4 row_mask:0xf bank_mask:0xf bound_ctrl:1
	s_and_b64 s[14:15], s[14:15], s[16:17]
	v_cndmask_b32_e64 v20, v20, v79, s[14:15]
	v_add_f32_dpp v22, v22, v22 row_ror:8 row_mask:0xf bank_mask:0xf bound_ctrl:1
	v_mov_b32_e32 v23, v22
	v_cmp_gt_f32_e64 s[16:17], v80, v20
	s_nop 0
	v_permlane16_swap_b32_e32 v22, v23
	s_and_b64 s[16:17], s[8:9], s[16:17]
	v_add_f32_e32 v22, v22, v23
	v_cndmask_b32_e64 v20, v20, v80, s[16:17]
	v_mov_b32_e32 v68, v58
	v_mov_b32_e32 v23, v22
	v_add_f32_e32 v62, v62, v20
	s_nop 0
	s_nop 0
	s_nop 0
	s_nop 0
	v_mov_b32_e32 v16, 1
	v_cmp_lg_f32_e64 s[18:19], v62, v48
	v_mov_b32_e32 v21, 0
	v_mov_b32_e32 v20, 0
	s_and_saveexec_b64 s[38:39], s[18:19]
	s_cbranch_execz .LBB0_911
	v_cndmask_b32_e64 v20, v18, 0, s[10:11]
	v_cndmask_b32_e64 v16, 0, 1, s[12:13]
	v_cndmask_b32_e64 v20, v20, v19, s[12:13]
	v_cndmask_b32_e32 v18, v18, v19, vcc
	v_cndmask_b32_e64 v16, v16, 2, s[14:15]
	v_cndmask_b32_e64 v20, v20, v70, s[14:15]
	v_cndmask_b32_e64 v18, v18, v70, s[6:7]
	v_cndmask_b32_e64 v16, v16, 3, s[16:17]
	v_cndmask_b32_e64 v35, v20, v72, s[16:17]
	v_cndmask_b32_e64 v21, v72, v18, s[8:9]
	v_mov_b32_e32 v20, v60
	v_mov_b32_e32 v48, v62

; #define PG8_GATHER(d0, d1, U) do { _Pragma("unroll") for (int _i = 0; _i < 2; ++_i) { d0[_i] = S.arow(U, Rr[_i]) * (unsigned)(g.lda * 2) + (unsigned)Cc[_i]; d1[_i] = S.arow(U, Rr[_i] + HALF) * (unsigned)(g.lda * 2) + (unsigned)Cc[_i]; } } while (0)
; #define PG8_STAGE(bufoff, soff, voff) do { _Pragma("unroll") for (int _i = 0; _i < 2; ++_i) \
;         __builtin_amdgcn_raw_ptr_buffer_load_lds(rs, (LAS void*)(lds + (bufoff) + ldsw + _i * 8192), 16, (int)(voff)[_i], (int)(soff), 0, 0); } while (0)
; #define PG8_WAIT_V(n) asm volatile("s_waitcnt vmcnt(" #n ")" ::: "memory")
; #define PG8_BAR __builtin_amdgcn_s_barrier()
;     ...
;     for (int i = 0; i < 2; ++i) { int R, C; stage_rc(tid * 16 + i * 8192, R, C); const int Rb = Epi::PERM ? ((R & ~31) + perm32(R & 31)) : R;
;         Rr[i] = R; Cc[i] = C * 2; vA0[i] = (unsigned)(R * g.lda + C) * 2u; vA1[i] = vA0[i] + hsA_; voffB[i] = (unsigned)(Rb * g.ldb + C) * 2u; }
;     ...
;     const unsigned kstep = (unsigned)(BK * 2);
;     const unsigned hsB = (unsigned)HALF * g.ldb * 2;
;     const __amdgpu_buffer_rsrc_t rs = __builtin_amdgcn_make_buffer_rsrc((void*)g.base, (short)0, 0x7fffffff, 0x00020000);
;     const unsigned ldsw = (unsigned)wid * 1024u;
;     const int aoff = lds_byte(wr * 64 + fr, fq * 8), boff = lds_byte(wc * 32 + fr, fq * 8);
;     ...
;     if constexpr (Sched::GATHER) PG8_GATHER(vA0, vA1, cur);
;     PG8_STAGE(PG8_SB(0, 0), cB, voffB); PG8_STAGE(PG8_SB(0, 1), cB + hsB, voffB); PG8_STAGE(PG8_SA(0, 0), cA, vA0); PG8_STAGE(PG8_SA(0, 1), cA, vA1);
;     if (wr == 1) PG8_BAR;
;     PG8_WAIT_V(2); PG8_BAR;
;     PG8_STAGE(PG8_SB(1, 0), cB + kstep, voffB); PG8_STAGE(PG8_SA(1, 0), cA + kstep, vA0); PG8_STAGE(PG8_SB(1, 1), cB + hsB + kstep, voffB);
.LBB0_998:
	v_ashrrev_i32_e32 v2, 31, v1
	v_lshrrev_b32_e32 v2, 26, v2
	v_lshlrev_b32_e32 v6, 4, v1
	v_add_u32_e32 v2, v1, v2
	v_bfe_i32 v1, v1, 27, 1
	v_lshrrev_b32_e32 v1, 22, v1
	v_add_u32_e32 v1, v6, v1
	v_and_b32_e32 v1, 0xfffffc00, v1
	v_sub_u32_e32 v1, v6, v1
	v_ashrrev_i32_e32 v2, 6, v2
	v_lshrrev_b32_e32 v3, 4, v1
	v_bitop3_b32 v3, v3, v1, 32 bitop3:0x6c
	v_lshlrev_b32_e32 v1, 3, v2
	v_and_b32_e32 v4, -16, v1
	v_ashrrev_i32_e32 v1, 31, v3
	v_lshrrev_b32_e32 v1, 26, v1
	v_add_u32_e32 v1, v3, v1
	v_ashrrev_i32_e32 v1, 6, v1
	v_add_u32_e32 v172, v1, v4
	s_add_u32 s8, s56, 0x500000
	v_add_u32_e32 v7, s6, v172
	s_addc_u32 s9, s57, 0
	v_cmp_gt_i32_e32 vcc, s4, v7
	v_mov_b32_e32 v5, 0
	v_mov_b32_e32 v4, 0
	s_and_saveexec_b64 s[0:1], vcc
	s_cbranch_execz .LBB0_1000
	v_add_u32_e32 v8, s5, v7
	v_ashrrev_i32_e32 v9, 31, v8
	v_lshl_add_u64 v[8:9], v[8:9], 2, s[8:9]
	flat_load_dword v4, v[8:9]
.LBB0_1000:
	s_or_b64 exec, exec, s[0:1]
	s_add_i32 s7, s6, 0x80
	v_add_u32_e32 v7, s7, v172
	v_cmp_gt_i32_e32 vcc, s4, v7
	s_and_saveexec_b64 s[0:1], vcc
	s_cbranch_execz .LBB0_1002
	v_add_u32_e32 v8, s5, v7
	v_ashrrev_i32_e32 v9, 31, v8
	v_lshl_add_u64 v[8:9], v[8:9], 2, s[8:9]
	flat_load_dword v5, v[8:9]
.LBB0_1002:
	s_or_b64 exec, exec, s[0:1]
	v_add_u32_e32 v6, 0x2000, v6
	v_ashrrev_i32_e32 v7, 31, v6
	v_lshrrev_b32_e32 v7, 22, v7
	v_add_u32_e32 v7, v6, v7
	v_ashrrev_i32_e32 v8, 10, v7
	v_mul_i32_i24_e32 v7, 0x400, v8
	v_sub_u32_e32 v6, v6, v7
	v_lshrrev_b32_e32 v7, 4, v6
	v_bitop3_b32 v9, v7, v6, 32 bitop3:0x6c
	v_ashrrev_i32_e32 v7, 31, v9
	v_lshrrev_b32_e32 v7, 26, v7
	v_lshlrev_b32_e32 v6, 3, v8
	v_add_u32_e32 v7, v9, v7
	v_and_b32_e32 v6, -16, v6
	v_ashrrev_i32_e32 v7, 6, v7
	v_add_u32_e32 v173, v7, v6
	v_add_u32_e32 v11, s6, v173
	v_cmp_gt_i32_e32 vcc, s4, v11
	v_mov_b32_e32 v6, 0
	v_mov_b32_e32 v10, 0
	s_and_saveexec_b64 s[0:1], vcc
	s_cbranch_execz .LBB0_1004
	v_add_u32_e32 v10, s5, v11
	v_ashrrev_i32_e32 v11, 31, v10
	v_lshl_add_u64 v[10:11], v[10:11], 2, s[8:9]
	flat_load_dword v10, v[10:11]
.LBB0_1004:
	s_or_b64 exec, exec, s[0:1]
	v_add_u32_e32 v11, s7, v173
	v_cmp_gt_i32_e32 vcc, s4, v11
	s_and_saveexec_b64 s[0:1], vcc
	s_cbranch_execz .LBB0_1006
	v_add_u32_e32 v12, s5, v11
	v_ashrrev_i32_e32 v13, 31, v12
	v_lshl_add_u64 v[12:13], v[12:13], 2, s[8:9]
	flat_load_dword v6, v[12:13]
.LBB0_1006:
	s_or_b64 exec, exec, s[0:1]
	s_waitcnt vmcnt(0) lgkmcnt(0)
	v_lshlrev_b32_e32 v4, 11, v4
	v_lshlrev_b32_e32 v5, 11, v5
	v_lshlrev_b32_e32 v10, 11, v10
	v_lshlrev_b32_e32 v6, 11, v6
	v_lshlrev_b32_e32 v11, 6, v7
	v_sub_u32_e32 v9, v9, v11
	v_lshlrev_b32_e32 v8, 5, v8
	v_ashrrev_i16_sdwa v9, v206, sext(v9) dst_sel:DWORD dst_unused:UNUSED_PAD src0_sel:DWORD src1_sel:BYTE_0
	v_and_b32_e32 v8, 32, v8
	v_bfe_i32 v9, v9, 0, 16
	v_add_lshl_u32 v174, v8, v9, 1
	v_lshlrev_b32_e32 v8, 6, v1
	v_sub_u32_e32 v3, v3, v8
	v_lshlrev_b32_e32 v2, 5, v2
	v_ashrrev_i16_sdwa v3, v206, sext(v3) dst_sel:DWORD dst_unused:UNUSED_PAD src0_sel:DWORD src1_sel:BYTE_0
	v_and_b32_e32 v2, 32, v2
	v_bfe_i32 v3, v3, 0, 16
	v_add_lshl_u32 v175, v2, v3, 1
	v_lshlrev_b32_e32 v2, 1, v172
	v_lshrrev_b32_e32 v3, 2, v172
	v_and_b32_e32 v1, 3, v1
	s_mov_b32 s1, 0x1fffe0
	v_and_b32_e32 v2, 24, v2
	v_and_b32_e32 v3, 4, v3
	v_and_or_b32 v1, v172, s1, v1
	s_ashr_i32 s0, s15, 6
	v_or3_b32 v1, v1, v3, v2
	v_and_b32_e32 v3, 3, v7
	v_lshl_add_u32 v176, v1, 11, v175
	v_lshlrev_b32_e32 v1, 1, v173
	v_lshrrev_b32_e32 v2, 2, v173
	v_and_or_b32 v3, v173, s1, v3
	s_lshl_b32 s1, s0, 10
	s_lshl_b32 s23, s66, 26
	s_add_i32 s24, s16, 0x10000
	v_and_b32_e32 v1, 24, v1
	v_and_b32_e32 v2, 4, v2
	s_add_i32 s23, s23, 0x8000000
	s_add_i32 s25, s24, s1
	v_or3_b32 v1, v3, v2, v1
	s_and_b32 s5, s57, 0xffff
	s_mov_b32 s4, s56
	s_mov_b32 s6, s58
	s_mov_b32 s7, s59
	s_add_i32 s67, s10, s23
	s_mov_b32 m0, s25
	s_add_i32 s26, s25, 0x2000
	s_add_i32 s27, s16, 0x14000
	v_lshl_add_u32 v177, v1, 11, v174
	buffer_load_dwordx4 v176, s[4:7], s67 offen lds
	s_mov_b32 m0, s26
	s_add_i32 s28, s27, s1
	buffer_load_dwordx4 v177, s[4:7], s67 offen lds
	s_add_i32 s10, s67, 0x40000
	s_mov_b32 m0, s28
	s_add_i32 s29, s28, 0x2000
	buffer_load_dwordx4 v176, s[4:7], s10 offen lds
	s_mov_b32 m0, s29
	s_add_i32 s30, s16, s1
	v_add_u32_e32 v188, v4, v175
	buffer_load_dwordx4 v177, s[4:7], s10 offen lds
	s_mov_b32 m0, s30
	s_mov_b32 s10, 0x56000000
	s_add_i32 s31, s30, 0x2000
	v_add_u32_e32 v186, v10, v174
	buffer_load_dwordx4 v188, s[4:7], s10 offen lds
	s_mov_b32 m0, s31
	s_add_i32 s34, s30, 0x4000
	v_add_u32_e32 v187, v5, v175
	buffer_load_dwordx4 v186, s[4:7], s10 offen lds
	s_mov_b32 m0, s34
	s_add_i32 s35, s30, 0x6000
	v_add_u32_e32 v189, v6, v174
	buffer_load_dwordx4 v187, s[4:7], s10 offen lds
	s_mov_b32 m0, s35
	s_ashr_i32 s17, s15, 8
	buffer_load_dwordx4 v189, s[4:7], s10 offen lds
	s_cmp_eq_u32 s17, 1
	s_cselect_b64 s[10:11], -1, 0
	s_cmp_lg_u32 s17, 1
	s_cbranch_scc1 .LBB0_1008
	s_barrier

; #define PG8_GATHER(d0, d1, U) do { _Pragma("unroll") for (int _i = 0; _i < 2; ++_i) { d0[_i] = S.arow(U, Rr[_i]) * (unsigned)(g.lda * 2) + (unsigned)Cc[_i]; d1[_i] = S.arow(U, Rr[_i] + HALF) * (unsigned)(g.lda * 2) + (unsigned)Cc[_i]; } } while (0)
;     ...
;         const bool has_next = S.next(ui + 1, nxt);
;         const unsigned nA = has_next ? g.A + nxt.aoff : cA, nB = has_next ? g.Bt + nxt.boff : cB;
;         if (Sched::GATHER && has_next) PG8_GATHER(nA0, nA1, nxt);
;         else {
; #pragma unroll
;             for (int _i = 0; _i < 2; ++_i) { nA0[_i] = vA0[_i]; nA1[_i] = vA1[_i]; } }
;     __device__ __forceinline__ unsigned arow(const pg8::Unit& u, int r) const { const int p = u.pb + r; return (p < u.cnt) ? (unsigned)list[u.lb + p] : 0u; }
.LBB0_1013:
	v_cndmask_b32_e64 v0, 0, 1, s[16:17]
	v_cmp_ne_u32_e64 s[0:1], 1, v0
	s_andn2_b64 vcc, exec, s[16:17]
	v_mov_b32_e32 v182, v186
	v_mov_b32_e32 v183, v188
	v_mov_b32_e32 v184, v189
	v_mov_b32_e32 v185, v187
	s_cbranch_vccnz .LBB0_1023
	v_add_u32_e32 v2, s55, v172
	v_cmp_gt_i32_e32 vcc, s53, v2
	v_mov_b32_e32 v1, 0
	v_mov_b32_e32 v0, 0
	s_and_saveexec_b64 s[18:19], vcc
	s_cbranch_execz .LBB0_1016
	v_add_u32_e32 v2, s54, v2
	v_ashrrev_i32_e32 v3, 31, v2
	v_lshl_add_u64 v[2:3], v[2:3], 2, s[8:9]
	flat_load_dword v0, v[2:3]
.LBB0_1016:
	s_or_b64 exec, exec, s[18:19]
	s_add_i32 s57, s55, 0x80
	v_add_u32_e32 v2, s57, v172
	v_cmp_gt_i32_e32 vcc, s53, v2
	s_and_saveexec_b64 s[18:19], vcc
	s_cbranch_execz .LBB0_1018
	v_add_u32_e32 v2, s54, v2
	v_ashrrev_i32_e32 v3, 31, v2
	v_lshl_add_u64 v[2:3], v[2:3], 2, s[8:9]
	flat_load_dword v1, v[2:3]
.LBB0_1018:
	s_or_b64 exec, exec, s[18:19]
	v_add_u32_e32 v4, s55, v173
	v_cmp_gt_i32_e32 vcc, s53, v4
	v_mov_b32_e32 v2, 0
	v_mov_b32_e32 v3, 0
	s_and_saveexec_b64 s[18:19], vcc
	s_cbranch_execz .LBB0_1020
	v_add_u32_e32 v4, s54, v4
	v_ashrrev_i32_e32 v5, 31, v4
	v_lshl_add_u64 v[4:5], v[4:5], 2, s[8:9]
	flat_load_dword v3, v[4:5]
.LBB0_1020:
	s_or_b64 exec, exec, s[18:19]
	v_add_u32_e32 v4, s57, v173
	v_cmp_gt_i32_e32 vcc, s53, v4
	s_and_saveexec_b64 s[18:19], vcc
	s_cbranch_execz .LBB0_1022
	v_add_u32_e32 v4, s54, v4
	v_ashrrev_i32_e32 v5, 31, v4
	v_lshl_add_u64 v[4:5], v[4:5], 2, s[8:9]
	flat_load_dword v2, v[4:5]
.LBB0_1022:
	s_or_b64 exec, exec, s[18:19]
	s_waitcnt vmcnt(0) lgkmcnt(0)
	v_lshlrev_b32_e32 v0, 11, v0
	v_lshlrev_b32_e32 v1, 11, v1
	v_lshlrev_b32_e32 v3, 11, v3
	v_lshlrev_b32_e32 v2, 11, v2
	v_add_u32_e32 v182, v3, v174
	v_add_u32_e32 v185, v1, v175
	v_add_u32_e32 v183, v0, v175
	v_add_u32_e32 v184, v2, v174

; #define PG8_GATHER(d0, d1, U) do { _Pragma("unroll") for (int _i = 0; _i < 2; ++_i) { d0[_i] = S.arow(U, Rr[_i]) * (unsigned)(g.lda * 2) + (unsigned)Cc[_i]; d1[_i] = S.arow(U, Rr[_i] + HALF) * (unsigned)(g.lda * 2) + (unsigned)Cc[_i]; } } while (0)
; #define PG8_STAGE(bufoff, soff, voff) do { _Pragma("unroll") for (int _i = 0; _i < 2; ++_i) \
;         __builtin_amdgcn_raw_ptr_buffer_load_lds(rs, (LAS void*)(lds + (bufoff) + ldsw + _i * 8192), 16, (int)(voff)[_i], (int)(soff), 0, 0); } while (0)
; #define PG8_WAIT_V(n) asm volatile("s_waitcnt vmcnt(" #n ")" ::: "memory")
; #define PG8_BAR __builtin_amdgcn_s_barrier()
;     ...
;     for (int i = 0; i < 2; ++i) { int R, C; stage_rc(tid * 16 + i * 8192, R, C); const int Rb = Epi::PERM ? ((R & ~31) + perm32(R & 31)) : R;
;         Rr[i] = R; Cc[i] = C * 2; vA0[i] = (unsigned)(R * g.lda + C) * 2u; vA1[i] = vA0[i] + hsA_; voffB[i] = (unsigned)(Rb * g.ldb + C) * 2u; }
;     ...
;     const unsigned kstep = (unsigned)(BK * 2);
;     const unsigned hsB = (unsigned)HALF * g.ldb * 2;
;     const __amdgpu_buffer_rsrc_t rs = __builtin_amdgcn_make_buffer_rsrc((void*)g.base, (short)0, 0x7fffffff, 0x00020000);
;     const unsigned ldsw = (unsigned)wid * 1024u;
;     const int aoff = lds_byte(wr * 64 + fr, fq * 8), boff = lds_byte(wc * 32 + fr, fq * 8);
;     ...
;     unsigned cA = g.A + cur.aoff, cB = g.Bt + cur.boff;
;     S.a_ready(cur);
;     if constexpr (Sched::GATHER) PG8_GATHER(vA0, vA1, cur);
;     PG8_STAGE(PG8_SB(0, 0), cB, voffB); PG8_STAGE(PG8_SB(0, 1), cB + hsB, voffB); PG8_STAGE(PG8_SA(0, 0), cA, vA0); PG8_STAGE(PG8_SA(0, 1), cA, vA1);
;     if (wr == 1) PG8_BAR;
;     PG8_WAIT_V(2); PG8_BAR;
.LBB0_1109:
	s_and_b64 vcc, exec, s[0:1]
	s_cbranch_vccnz .LBB0_1145
	v_ashrrev_i32_e32 v2, 31, v1
	v_lshrrev_b32_e32 v2, 26, v2
	v_lshlrev_b32_e32 v6, 4, v1
	v_add_u32_e32 v2, v1, v2
	v_bfe_i32 v1, v1, 27, 1
	v_lshrrev_b32_e32 v1, 22, v1
	v_add_u32_e32 v1, v6, v1
	v_and_b32_e32 v1, 0xfffffc00, v1
	v_sub_u32_e32 v1, v6, v1
	v_ashrrev_i32_e32 v2, 6, v2
	v_lshrrev_b32_e32 v3, 4, v1
	v_bitop3_b32 v3, v3, v1, 32 bitop3:0x6c
	v_lshlrev_b32_e32 v1, 3, v2
	v_and_b32_e32 v4, -16, v1
	v_ashrrev_i32_e32 v1, 31, v3
	v_lshrrev_b32_e32 v1, 26, v1
	v_add_u32_e32 v1, v3, v1
	v_ashrrev_i32_e32 v1, 6, v1
	v_add_u32_e32 v172, v1, v4
	s_add_u32 s2, s56, 0x500000
	v_add_u32_e32 v7, s6, v172
	s_addc_u32 s3, s57, 0
	v_cmp_gt_i32_e32 vcc, s4, v7
	v_mov_b32_e32 v5, 0
	v_mov_b32_e32 v4, 0
	s_and_saveexec_b64 s[0:1], vcc
	s_cbranch_execz .LBB0_1112
	v_add_u32_e32 v8, s5, v7
	v_ashrrev_i32_e32 v9, 31, v8
	v_lshl_add_u64 v[8:9], v[8:9], 2, s[2:3]
	flat_load_dword v4, v[8:9]
.LBB0_1112:
	s_or_b64 exec, exec, s[0:1]
	s_add_i32 s7, s6, 0x80
	v_add_u32_e32 v7, s7, v172
	v_cmp_gt_i32_e32 vcc, s4, v7
	s_and_saveexec_b64 s[0:1], vcc
	s_cbranch_execz .LBB0_1114
	v_add_u32_e32 v8, s5, v7
	v_ashrrev_i32_e32 v9, 31, v8
	v_lshl_add_u64 v[8:9], v[8:9], 2, s[2:3]
	flat_load_dword v5, v[8:9]
.LBB0_1114:
	s_or_b64 exec, exec, s[0:1]
	v_add_u32_e32 v6, 0x2000, v6
	v_ashrrev_i32_e32 v7, 31, v6
	v_lshrrev_b32_e32 v7, 22, v7
	v_add_u32_e32 v7, v6, v7
	v_ashrrev_i32_e32 v8, 10, v7
	v_mul_i32_i24_e32 v7, 0x400, v8
	v_sub_u32_e32 v6, v6, v7
	v_lshrrev_b32_e32 v7, 4, v6
	v_bitop3_b32 v9, v7, v6, 32 bitop3:0x6c
	v_ashrrev_i32_e32 v7, 31, v9
	v_lshrrev_b32_e32 v7, 26, v7
	v_lshlrev_b32_e32 v6, 3, v8
	v_add_u32_e32 v7, v9, v7
	v_and_b32_e32 v6, -16, v6
	v_ashrrev_i32_e32 v7, 6, v7
	v_add_u32_e32 v173, v7, v6
	v_add_u32_e32 v11, s6, v173
	v_cmp_gt_i32_e32 vcc, s4, v11
	v_mov_b32_e32 v6, 0
	v_mov_b32_e32 v10, 0
	s_and_saveexec_b64 s[0:1], vcc
	s_cbranch_execz .LBB0_1116
	v_add_u32_e32 v10, s5, v11
	v_ashrrev_i32_e32 v11, 31, v10
	v_lshl_add_u64 v[10:11], v[10:11], 2, s[2:3]
	flat_load_dword v10, v[10:11]
.LBB0_1116:
	s_or_b64 exec, exec, s[0:1]
	v_add_u32_e32 v11, s7, v173
	v_cmp_gt_i32_e32 vcc, s4, v11
	s_and_saveexec_b64 s[0:1], vcc
	s_cbranch_execz .LBB0_1118
	v_add_u32_e32 v12, s5, v11
	v_ashrrev_i32_e32 v13, 31, v12
	v_lshl_add_u64 v[12:13], v[12:13], 2, s[2:3]
	flat_load_dword v6, v[12:13]
.LBB0_1118:
	s_or_b64 exec, exec, s[0:1]
	s_waitcnt vmcnt(0) lgkmcnt(0)
	v_lshlrev_b32_e32 v4, 11, v4
	v_lshlrev_b32_e32 v5, 11, v5
	v_lshlrev_b32_e32 v10, 11, v10
	v_lshlrev_b32_e32 v6, 11, v6
	v_lshlrev_b32_e32 v11, 6, v7
	v_sub_u32_e32 v9, v9, v11
	v_lshlrev_b32_e32 v8, 5, v8
	v_ashrrev_i16_sdwa v9, v206, sext(v9) dst_sel:DWORD dst_unused:UNUSED_PAD src0_sel:DWORD src1_sel:BYTE_0
	v_and_b32_e32 v8, 32, v8
	v_bfe_i32 v9, v9, 0, 16
	v_add_lshl_u32 v174, v8, v9, 1
	v_lshlrev_b32_e32 v8, 6, v1
	v_sub_u32_e32 v3, v3, v8
	v_lshlrev_b32_e32 v2, 5, v2
	v_ashrrev_i16_sdwa v3, v206, sext(v3) dst_sel:DWORD dst_unused:UNUSED_PAD src0_sel:DWORD src1_sel:BYTE_0
	v_and_b32_e32 v2, 32, v2
	v_bfe_i32 v3, v3, 0, 16
	v_add_lshl_u32 v175, v2, v3, 1
	v_lshlrev_b32_e32 v2, 1, v172
	v_lshrrev_b32_e32 v3, 2, v172
	v_and_b32_e32 v1, 3, v1
	s_mov_b32 s1, 0x1fffe0
	v_and_b32_e32 v2, 24, v2
	v_and_b32_e32 v3, 4, v3
	v_and_or_b32 v1, v172, s1, v1
	s_ashr_i32 s0, s13, 6
	v_or3_b32 v1, v1, v3, v2
	v_and_b32_e32 v3, 3, v7
	v_lshl_add_u32 v176, v1, 11, v175
	v_lshlrev_b32_e32 v1, 1, v173
	v_lshrrev_b32_e32 v2, 2, v173
	v_and_or_b32 v3, v173, s1, v3
	s_lshl_b32 s1, s0, 10
	s_lshl_b32 s18, s66, 26
	s_add_i32 s19, s23, 0x10000
	v_and_b32_e32 v1, 24, v1
	v_and_b32_e32 v2, 4, v2
	s_add_i32 s18, s18, 0x8000000
	s_add_i32 s24, s19, s1
	v_or3_b32 v1, v3, v2, v1
	s_and_b32 s5, s57, 0xffff
	s_mov_b32 s4, s56
	s_mov_b32 s6, s58
	s_mov_b32 s7, s59
	s_add_i32 s55, s8, s18
	s_mov_b32 m0, s24
	s_add_i32 s25, s24, 0x2000
	s_add_i32 s26, s23, 0x14000
	v_lshl_add_u32 v177, v1, 11, v174
	buffer_load_dwordx4 v176, s[4:7], s55 offen lds
	s_mov_b32 m0, s25
	s_add_i32 s27, s26, s1
	buffer_load_dwordx4 v177, s[4:7], s55 offen lds
	s_add_i32 s8, s55, 0x40000
	s_mov_b32 m0, s27
	s_add_i32 s28, s27, 0x2000
	buffer_load_dwordx4 v176, s[4:7], s8 offen lds
	s_mov_b32 m0, s28
	s_add_i32 s29, s23, s1
	v_add_u32_e32 v188, v4, v175
	buffer_load_dwordx4 v177, s[4:7], s8 offen lds
	s_mov_b32 m0, s29
	s_mov_b32 s8, 0x56000000
	s_add_i32 s30, s29, 0x2000
	v_add_u32_e32 v186, v10, v174
	buffer_load_dwordx4 v188, s[4:7], s8 offen lds
	s_mov_b32 m0, s30
	s_add_i32 s31, s29, 0x4000
	v_add_u32_e32 v187, v5, v175
	buffer_load_dwordx4 v186, s[4:7], s8 offen lds
	s_mov_b32 m0, s31
	s_add_i32 s34, s29, 0x6000
	v_add_u32_e32 v189, v6, v174
	buffer_load_dwordx4 v187, s[4:7], s8 offen lds
	s_mov_b32 m0, s34
	s_ashr_i32 s14, s13, 8
	buffer_load_dwordx4 v189, s[4:7], s8 offen lds
	s_cmp_eq_u32 s14, 1
	s_cselect_b64 s[8:9], -1, 0
	s_cmp_lg_u32 s14, 1
	s_cbranch_scc1 .LBB0_1120
	s_barrier

; #define PG8_GATHER(d0, d1, U) do { _Pragma("unroll") for (int _i = 0; _i < 2; ++_i) { d0[_i] = S.arow(U, Rr[_i]) * (unsigned)(g.lda * 2) + (unsigned)Cc[_i]; d1[_i] = S.arow(U, Rr[_i] + HALF) * (unsigned)(g.lda * 2) + (unsigned)Cc[_i]; } } while (0)
;     ...
;         const bool has_next = S.next(ui + 1, nxt);
;         const unsigned nA = has_next ? g.A + nxt.aoff : cA, nB = has_next ? g.Bt + nxt.boff : cB;
;         if (Sched::GATHER && has_next) PG8_GATHER(nA0, nA1, nxt);
;         else {
; #pragma unroll
;             for (int _i = 0; _i < 2; ++_i) { nA0[_i] = vA0[_i]; nA1[_i] = vA1[_i]; } }
;     __device__ __forceinline__ unsigned arow(const pg8::Unit& u, int r) const { const int p = u.pb + r; return (p < u.cnt) ? (unsigned)list[u.lb + p] : 0u; }
.LBB0_1125:
	v_cndmask_b32_e64 v0, 0, 1, s[14:15]
	v_cmp_ne_u32_e64 s[0:1], 1, v0
	s_andn2_b64 vcc, exec, s[14:15]
	v_mov_b32_e32 v182, v186
	v_mov_b32_e32 v183, v188
	v_mov_b32_e32 v184, v189
	v_mov_b32_e32 v185, v187
	s_cbranch_vccnz .LBB0_1135
	v_add_u32_e32 v2, s50, v172
	v_cmp_gt_i32_e32 vcc, s48, v2
	v_mov_b32_e32 v1, 0
	v_mov_b32_e32 v0, 0
	s_and_saveexec_b64 s[16:17], vcc
	s_cbranch_execz .LBB0_1128
	v_add_u32_e32 v2, s49, v2
	v_ashrrev_i32_e32 v3, 31, v2
	v_lshl_add_u64 v[2:3], v[2:3], 2, s[2:3]
	flat_load_dword v0, v[2:3]
.LBB0_1128:
	s_or_b64 exec, exec, s[16:17]
	s_add_i32 s57, s50, 0x80
	v_add_u32_e32 v2, s57, v172
	v_cmp_gt_i32_e32 vcc, s48, v2
	s_and_saveexec_b64 s[16:17], vcc
	s_cbranch_execz .LBB0_1130
	v_add_u32_e32 v2, s49, v2
	v_ashrrev_i32_e32 v3, 31, v2
	v_lshl_add_u64 v[2:3], v[2:3], 2, s[2:3]
	flat_load_dword v1, v[2:3]
.LBB0_1130:
	s_or_b64 exec, exec, s[16:17]
	v_add_u32_e32 v4, s50, v173
	v_cmp_gt_i32_e32 vcc, s48, v4
	v_mov_b32_e32 v2, 0
	v_mov_b32_e32 v3, 0
	s_and_saveexec_b64 s[16:17], vcc
	s_cbranch_execz .LBB0_1132
	v_add_u32_e32 v4, s49, v4
	v_ashrrev_i32_e32 v5, 31, v4
	v_lshl_add_u64 v[4:5], v[4:5], 2, s[2:3]
	flat_load_dword v3, v[4:5]
.LBB0_1132:
	s_or_b64 exec, exec, s[16:17]
	v_add_u32_e32 v4, s57, v173
	v_cmp_gt_i32_e32 vcc, s48, v4
	s_and_saveexec_b64 s[16:17], vcc
	s_cbranch_execz .LBB0_1134
	v_add_u32_e32 v4, s49, v4
	v_ashrrev_i32_e32 v5, 31, v4
	v_lshl_add_u64 v[4:5], v[4:5], 2, s[2:3]
	flat_load_dword v2, v[4:5]
.LBB0_1134:
	s_or_b64 exec, exec, s[16:17]
	s_waitcnt vmcnt(0) lgkmcnt(0)
	v_lshlrev_b32_e32 v0, 11, v0
	v_lshlrev_b32_e32 v1, 11, v1
	v_lshlrev_b32_e32 v3, 11, v3
	v_lshlrev_b32_e32 v2, 11, v2
	v_add_u32_e32 v182, v3, v174
	v_add_u32_e32 v185, v1, v175
	v_add_u32_e32 v183, v0, v175
	v_add_u32_e32 v184, v2, v174

; #define LAS __attribute__((address_space(3)))
; #define AIN(k) ldptr(lds, (k))
; __global__ void __launch_bounds__(NTHREADS, 2) hybrid_fwd(Args a) {
;     ...
;             const bool lastl = (l == NLAYER - 1); bf16_t* XA16 = (bf16_t*)(ws + WS_XA);
;             const bf16_t* X1B = (const bf16_t*)(ws + WS_X1B); const unsigned char* Y2 = ws + WS_Y2; const int* tokS = (const int*)(ws + WS_TOKS); const int* tokE = (const int*)(ws + WS_TOKE);
;     ...
;             moe_meta(a, lds, tid, l);
;     ...
;             volatile LAS int* meta = (volatile LAS int*)(lds + META_OFF);
;             unsigned char* XB = ws + WS_XB;
;             const float* lg = AIN(I_LN2G) + l * DM; const float* lb = AIN(I_LN2B) + l * DM;
;             int tk0 = F8_TILES_PER_LAYER;
;             if (l + 1 < NLAYER && tid == 0)
;                 tk0 = (int)__hip_atomic_fetch_add((unsigned*)(ws + WS_CTL) + CW_TICK + 64 * (l + 1), 1u, __ATOMIC_RELAXED, __HIP_MEMORY_SCOPE_AGENT);
;             for (int row0 = gw; row0 < MTOK; row0 += 2 * NGW) {
;                 int sl[2][2];
; #pragma unroll
;                 for (int rr = 0; rr < 2; ++rr) { const int row = row0 + rr * NGW; sl[rr][0] = meta[16 + tokE[row * 2]] + tokS[row * 2]; sl[rr][1] = meta[16 + tokE[row * 2 + 1]] + tokS[row * 2 + 1]; }
;                 u32x2 xw[2][8]; unsigned pw_[2][8], qw[2][8];
; #pragma unroll
;                 for (int rr = 0; rr < 2; ++rr) { const int row = row0 + rr * NGW;
; #pragma unroll
;                     for (int j = 0; j < 8; ++j) { xw[rr][j] = __builtin_nontemporal_load((const u32x2*)(X1B + (size_t)row * DM + j * 256 + lane * 4));
.LBB0_1333:
	s_or_b64 exec, exec, s[2:3]
	s_ashr_i32 s29, s12, 6
	s_lshl_b32 s2, s18, 3
	v_and_b32_e32 v129, 63, v145
	s_add_i32 s12, s29, s2
	s_cmpk_gt_i32 s12, 0x1fff
	v_lshlrev_b32_e32 v128, 2, v129
	v_lshlrev_b32_e32 v92, 3, v129
	s_cbranch_scc1 .LBB0_1432
	s_cmp_lg_u32 s66, 3
	s_cselect_b64 s[14:15], -1, 0
	s_lshl_b32 s20, s66, 11
	s_add_u32 s25, s4, 0x230000
	s_addc_u32 s26, s5, 0
	s_mov_b32 s21, s93
	s_add_u32 s27, s4, 0x210000
	s_addc_u32 s30, s5, 0
	s_add_i32 s31, s28, 0x20400
	s_lshl_b64 s[20:21], s[20:21], 2
	s_add_u32 s22, s16, s20
	s_addc_u32 s23, s13, s21
	s_add_u32 s16, s19, s20
	s_addc_u32 s17, s17, s21
	v_lshlrev_b32_e32 v192, 4, v129
	v_lshl_add_u64 v[10:11], s[22:23], 0, v[192:193]
	v_lshl_add_u64 v[12:13], s[16:17], 0, v[192:193]
	s_mov_b64 s[16:17], 0x1000
	v_lshl_add_u64 v[14:15], v[10:11], 0, s[16:17]
	v_lshl_add_u64 v[16:17], v[12:13], 0, s[16:17]
	s_mov_b64 s[16:17], 0x1400
	v_lshl_add_u64 v[18:19], v[10:11], 0, s[16:17]
	v_lshl_add_u64 v[20:21], v[12:13], 0, s[16:17]
	s_mov_b64 s[16:17], 0x1800
	v_lshl_add_u64 v[22:23], v[10:11], 0, s[16:17]
	v_lshl_add_u64 v[24:25], v[12:13], 0, s[16:17]
	s_mov_b64 s[16:17], 0x1c00
	s_ashr_i32 s13, s12, 31
	v_lshlrev_b32_e32 v0, 2, v129
	v_lshl_add_u64 v[26:27], v[10:11], 0, s[16:17]
	v_lshl_add_u64 v[28:29], v[12:13], 0, s[16:17]
	s_lshl_b64 s[16:17], s[12:13], 11
	v_or_b32_e32 v30, s16, v0
	v_mov_b32_e32 v31, s17
	s_lshl_b64 s[16:17], s[12:13], 13
	v_readlane_b32 s36, v255, 6
	v_readlane_b32 s37, v255, 7
	s_add_u32 s16, s36, s16
	s_addc_u32 s17, s37, s17
	s_lshl_b32 s3, s18, 4
	s_lshl_b32 s18, s29, 1
	v_mov_b32_e32 v1, v193
	s_add_i32 s18, s3, s18
	s_add_i32 s3, s79, s29
	v_lshl_add_u64 v[2:3], s[4:5], 0, v[0:1]
	s_mov_b64 s[20:21], 0x5d800000
	s_add_i32 s2, s3, s2
	v_lshl_add_u64 v[8:9], v[2:3], 0, s[20:21]
	s_lshl_b64 s[20:21], s[12:13], 12
	s_ashr_i32 s3, s2, 31
	v_or_b32_e32 v32, s20, v92
	v_mov_b32_e32 v33, s21
	s_lshl_b64 s[20:21], s[2:3], 11
	v_or_b32_e32 v34, s20, v0
	v_mov_b32_e32 v35, s21
	s_lshl_b64 s[20:21], s[2:3], 13
	s_add_u32 s20, s36, s20
	s_addc_u32 s21, s37, s21
	s_lshl_b64 s[2:3], s[2:3], 12
	v_readlane_b32 s36, v255, 35
	v_or_b32_e32 v36, s2, v92
	v_mov_b32_e32 v37, s3
	v_readlane_b32 s38, v255, 8
	v_readlane_b32 s39, v255, 9
	v_readlane_b32 s37, v255, 36
	global_load_dwordx4 v[152:155], v[10:11], off
	global_load_dwordx4 v[156:159], v[10:11], off offset:1024
	global_load_dwordx4 v[160:163], v[10:11], off offset:2048
	global_load_dwordx4 v[168:171], v[10:11], off offset:3072
	global_load_dwordx4 v[172:175], v[14:15], off
	global_load_dwordx4 v[176:179], v[18:19], off
	global_load_dwordx4 v[180:183], v[22:23], off
	global_load_dwordx4 v[184:187], v[26:27], off
	global_load_dwordx4 v[188:191], v[12:13], off
	global_load_dwordx4 v[194:197], v[12:13], off offset:1024
	global_load_dwordx4 v[198:201], v[12:13], off offset:2048
	global_load_dwordx4 v[202:205], v[12:13], off offset:3072
	global_load_dwordx4 v[216:219], v[16:17], off
	global_load_dwordx4 v[220:223], v[20:21], off
	global_load_dwordx4 v[224:227], v[24:25], off
	global_load_dwordx4 v[228:231], v[28:29], off
	s_branch .LBB0_1336

; __global__ void __launch_bounds__(NTHREADS, 2) hybrid_fwd(Args a) {
;     ...
;             for (int row0 = gw; row0 < MTOK; row0 += 2 * NGW) {
;                 int sl[2][2];
; #pragma unroll
;                 for (int rr = 0; rr < 2; ++rr) { const int row = row0 + rr * NGW; sl[rr][0] = meta[16 + tokE[row * 2]] + tokS[row * 2]; sl[rr][1] = meta[16 + tokE[row * 2 + 1]] + tokS[row * 2 + 1]; }
;                 u32x2 xw[2][8]; unsigned pw_[2][8], qw[2][8];
; #pragma unroll
;                 for (int rr = 0; rr < 2; ++rr) { const int row = row0 + rr * NGW;
; #pragma unroll
;                     for (int j = 0; j < 8; ++j) { xw[rr][j] = __builtin_nontemporal_load((const u32x2*)(X1B + (size_t)row * DM + j * 256 + lane * 4));
;                         pw_[rr][j] = __builtin_nontemporal_load((const unsigned*)(Y2 + (size_t)sl[rr][0] * DM + j * 256 + lane * 4)); qw[rr][j] = __builtin_nontemporal_load((const unsigned*)(Y2 + (size_t)sl[rr][1] * DM + j * 256 + lane * 4)); } }
.LBB0_1336:
	s_ashr_i32 s19, s18, 31
	s_lshl_b64 s[2:3], s[18:19], 2
	s_add_u32 s22, s27, s2
	s_addc_u32 s23, s30, s3
	v_mov_b64_e32 v[0:1], s[22:23]
	flat_load_dwordx2 v[0:1], v[0:1]
	s_add_u32 s2, s25, s2
	s_addc_u32 s3, s26, s3
	v_mov_b64_e32 v[2:3], s[2:3]
	s_add_i32 s2, s18, 1
	s_ashr_i32 s3, s2, 31
	s_lshl_b64 s[2:3], s[2:3], 2
	s_add_u32 s2, s25, s2
	s_addc_u32 s3, s26, s3
	v_lshl_add_u64 v[40:41], s[4:5], 0, v[32:33]
	s_waitcnt vmcnt(0) lgkmcnt(0)
	v_lshl_add_u32 v0, v0, 2, s31
	ds_read_b32 v0, v0 offset:64
	flat_load_dword v2, v[2:3]
	v_lshl_add_u32 v1, v1, 2, s31
	ds_read_b32 v1, v1 offset:64
	s_waitcnt vmcnt(0) lgkmcnt(0)
	v_add_u32_e32 v0, v2, v0
	v_mov_b64_e32 v[2:3], s[2:3]
	s_add_i32 s2, s36, s18
	s_ashr_i32 s3, s2, 31
	s_lshl_b64 s[22:23], s[2:3], 2
	s_add_u32 s34, s27, s22
	s_addc_u32 s35, s30, s23
	v_mov_b64_e32 v[4:5], s[34:35]
	flat_load_dword v2, v[2:3]
	s_add_u32 s22, s25, s22
	flat_load_dwordx2 v[4:5], v[4:5]
	s_addc_u32 s23, s26, s23
	v_mov_b64_e32 v[6:7], s[22:23]
	s_add_i32 s2, s2, 1
	s_ashr_i32 s3, s2, 31
	s_lshl_b64 s[2:3], s[2:3], 2
	s_add_u32 s2, s25, s2
	s_addc_u32 s3, s26, s3
	s_waitcnt vmcnt(0) lgkmcnt(0)
	v_add_u32_e32 v2, v2, v1
	v_lshl_add_u32 v1, v4, 2, s31
	ds_read_b32 v1, v1 offset:64
	flat_load_dword v3, v[6:7]
	s_waitcnt vmcnt(0) lgkmcnt(0)
	v_add_u32_e32 v42, v3, v1
	v_lshl_add_u32 v1, v5, 2, s31
	v_mov_b64_e32 v[4:5], s[2:3]
	ds_read_b32 v1, v1 offset:64
	flat_load_dword v3, v[4:5]
	s_mov_b32 s2, 0x42000000
	v_ashrrev_i32_e32 v43, 31, v42
	v_lshlrev_b64 v[42:43], 11, v[42:43]
	v_lshl_add_u64 v[70:71], v[8:9], 0, v[42:43]
	s_waitcnt vmcnt(0) lgkmcnt(0)
	v_add_u32_e32 v44, v3, v1
	v_ashrrev_i32_e32 v1, 31, v0
	v_lshlrev_b64 v[0:1], 11, v[0:1]
	v_ashrrev_i32_e32 v3, 31, v2
	v_lshl_add_u64 v[38:39], v[8:9], 0, v[0:1]
	v_lshlrev_b64 v[0:1], 11, v[2:3]
	v_lshl_add_u64 v[46:47], v[8:9], 0, v[0:1]
	v_add_co_u32_e32 v0, vcc, s2, v40
	v_ashrrev_i32_e32 v45, 31, v44
	s_nop 0
	v_addc_co_u32_e32 v1, vcc, 0, v41, vcc
	flat_load_dwordx2 v[64:65], v[0:1] nt
	flat_load_dword v74, v[38:39] nt
	flat_load_dword v76, v[46:47] nt
	flat_load_dwordx2 v[62:63], v[0:1] offset:512 nt
	flat_load_dword v80, v[38:39] offset:256 nt
	flat_load_dword v81, v[46:47] offset:256 nt
	flat_load_dwordx2 v[60:61], v[0:1] offset:1024 nt
	flat_load_dword v90, v[38:39] offset:512 nt
	flat_load_dword v91, v[46:47] offset:512 nt
	flat_load_dwordx2 v[58:59], v[0:1] offset:1536 nt
	flat_load_dword v110, v[38:39] offset:768 nt
	flat_load_dword v111, v[46:47] offset:768 nt
	flat_load_dwordx2 v[6:7], v[0:1] offset:2048 nt
	flat_load_dword v69, v[38:39] offset:1024 nt
	flat_load_dword v68, v[46:47] offset:1024 nt
	flat_load_dwordx2 v[4:5], v[0:1] offset:2560 nt
	flat_load_dword v67, v[38:39] offset:1280 nt
	flat_load_dword v66, v[46:47] offset:1280 nt
	flat_load_dwordx2 v[2:3], v[0:1] offset:3072 nt
	flat_load_dword v89, v[38:39] offset:1536 nt
	flat_load_dword v88, v[46:47] offset:1536 nt
	s_nop 0
	flat_load_dwordx2 v[0:1], v[0:1] offset:3584 nt
	s_nop 0
	flat_load_dword v87, v[38:39] offset:1792 nt
	flat_load_dword v86, v[46:47] offset:1792 nt
	v_lshl_add_u64 v[38:39], s[4:5], 0, v[36:37]
	v_lshlrev_b64 v[42:43], 11, v[44:45]
	v_lshl_add_u64 v[72:73], v[8:9], 0, v[42:43]
	v_add_co_u32_e32 v42, vcc, s2, v38
	s_mov_b64 s[2:3], -1
	s_nop 0
	v_addc_co_u32_e32 v43, vcc, 0, v39, vcc
	flat_load_dwordx2 v[56:57], v[42:43] nt
	flat_load_dword v109, v[70:71] nt
	flat_load_dword v108, v[72:73] nt
	flat_load_dwordx2 v[52:53], v[42:43] offset:512 nt
	flat_load_dword v106, v[70:71] offset:256 nt
	flat_load_dword v104, v[72:73] offset:256 nt
	flat_load_dwordx2 v[48:49], v[42:43] offset:1024 nt
	flat_load_dword v101, v[70:71] offset:512 nt
	flat_load_dword v100, v[72:73] offset:512 nt
	flat_load_dwordx2 v[54:55], v[42:43] offset:1536 nt
	flat_load_dword v107, v[70:71] offset:768 nt
	flat_load_dword v105, v[72:73] offset:768 nt
	flat_load_dwordx2 v[50:51], v[42:43] offset:2048 nt
	flat_load_dword v103, v[70:71] offset:1024 nt
	flat_load_dword v102, v[72:73] offset:1024 nt
	flat_load_dwordx2 v[46:47], v[42:43] offset:2560 nt
	flat_load_dword v99, v[70:71] offset:1280 nt
	flat_load_dword v98, v[72:73] offset:1280 nt
	flat_load_dwordx2 v[44:45], v[42:43] offset:3072 nt
	flat_load_dword v97, v[70:71] offset:1536 nt
	flat_load_dword v96, v[72:73] offset:1536 nt
	s_nop 0
	flat_load_dwordx2 v[42:43], v[42:43] offset:3584 nt
	s_nop 0
	flat_load_dword v95, v[70:71] offset:1792 nt
	flat_load_dword v94, v[72:73] offset:1792 nt
	s_and_b64 vcc, exec, s[14:15]
	s_waitcnt vmcnt(0) lgkmcnt(0)
; __device__ __forceinline__ float bflo(unsigned w) { return __uint_as_float(w << 16); }
; __device__ __forceinline__ float bfhi(unsigned w) { return __uint_as_float(w & 0xffff0000u); }
; __global__ void __launch_bounds__(NTHREADS, 2) hybrid_fwd(Args a) {
;     ...
;                 for (int rr = 0; rr < 2; ++rr) { const int row = row0 + rr * NGW;
;                     f32x4 y[8]; float s = 0.f;
; #pragma unroll
;                     for (int j = 0; j < 8; ++j) { const u32x2 x = xw[rr][j]; const int p = (int)pw_[rr][j], q = (int)qw[rr][j];
;                         const f32x2 p0 = __builtin_amdgcn_cvt_pk_f32_fp8(p, false), p1 = __builtin_amdgcn_cvt_pk_f32_fp8(p, true), q0 = __builtin_amdgcn_cvt_pk_f32_fp8(q, false), q1 = __builtin_amdgcn_cvt_pk_f32_fp8(q, true);
;                         y[j][0] = bflo(x.x) * ALPHA + (p0.x + q0.x) * (1.f / Y2_SCALE); y[j][1] = bfhi(x.x) * ALPHA + (p0.y + q0.y) * (1.f / Y2_SCALE);
;                         y[j][2] = bflo(x.y) * ALPHA + (p1.x + q1.x) * (1.f / Y2_SCALE); y[j][3] = bfhi(x.y) * ALPHA + (p1.y + q1.y) * (1.f / Y2_SCALE);
;                         s += (y[j][0] + y[j][1]) + (y[j][2] + y[j][3]); }
	v_lshlrev_b32_e32 v78, 16, v64
	v_cvt_pk_f32_fp8_e32 v[70:71], v74
	v_cvt_pk_f32_fp8_sdwa v[72:73], v74 src0_sel:WORD_1
	v_cvt_pk_f32_fp8_e32 v[74:75], v76
	v_cvt_pk_f32_fp8_sdwa v[76:77], v76 src0_sel:WORD_1
	v_and_b32_e32 v79, 0xffff0000, v64
	v_lshlrev_b32_e32 v64, 16, v65
	v_pk_add_f32 v[70:71], v[70:71], v[74:75]
	v_and_b32_e32 v65, 0xffff0000, v65
	v_pk_mul_f32 v[70:71], v[70:71], s[72:73] op_sel_hi:[1,0]
	v_cvt_pk_f32_fp8_sdwa v[74:75], v81 src0_sel:WORD_1
	v_pk_fma_f32 v[82:83], v[78:79], s[90:91], v[70:71] op_sel_hi:[1,0,1]
	v_pk_add_f32 v[70:71], v[72:73], v[76:77]
	v_cvt_pk_f32_fp8_e32 v[72:73], v81
	v_pk_mul_f32 v[70:71], v[70:71], s[72:73] op_sel_hi:[1,0]
	v_lshlrev_b32_e32 v76, 16, v62
	v_pk_fma_f32 v[84:85], v[64:65], s[90:91], v[70:71] op_sel_hi:[1,0,1]
	v_add_f32_e32 v65, v82, v83
	v_add_f32_e32 v64, v85, v84
	v_add_f32_e32 v64, v65, v64
	v_add_f32_e32 v78, 0, v64
	v_cvt_pk_f32_fp8_e32 v[64:65], v80
	v_cvt_pk_f32_fp8_sdwa v[70:71], v80 src0_sel:WORD_1
	v_and_b32_e32 v77, 0xffff0000, v62
	v_lshlrev_b32_e32 v62, 16, v63
	v_pk_add_f32 v[64:65], v[64:65], v[72:73]
	v_pk_add_f32 v[70:71], v[70:71], v[74:75]
	v_pk_mul_f32 v[64:65], v[64:65], s[72:73] op_sel_hi:[1,0]
	v_and_b32_e32 v63, 0xffff0000, v63
	v_pk_mul_f32 v[70:71], v[70:71], s[72:73] op_sel_hi:[1,0]
	v_pk_fma_f32 v[64:65], v[76:77], s[90:91], v[64:65] op_sel_hi:[1,0,1]
	v_pk_fma_f32 v[80:81], v[62:63], s[90:91], v[70:71] op_sel_hi:[1,0,1]
	v_add_f32_e32 v63, v64, v65
	v_add_f32_e32 v62, v81, v80
	v_add_f32_e32 v62, v63, v62
	v_add_f32_e32 v112, v78, v62
	v_cvt_pk_f32_fp8_e32 v[62:63], v90
	v_cvt_pk_f32_fp8_e32 v[72:73], v91
	v_cvt_pk_f32_fp8_sdwa v[70:71], v90 src0_sel:WORD_1
	v_cvt_pk_f32_fp8_sdwa v[74:75], v91 src0_sel:WORD_1
	v_lshlrev_b32_e32 v76, 16, v60
	v_pk_add_f32 v[62:63], v[62:63], v[72:73]
	v_and_b32_e32 v77, 0xffff0000, v60
	v_pk_mul_f32 v[62:63], v[62:63], s[72:73] op_sel_hi:[1,0]
	v_lshlrev_b32_e32 v60, 16, v61
	v_pk_fma_f32 v[72:73], v[76:77], s[90:91], v[62:63] op_sel_hi:[1,0,1]
	v_pk_add_f32 v[62:63], v[70:71], v[74:75]
	v_and_b32_e32 v61, 0xffff0000, v61
	v_pk_mul_f32 v[62:63], v[62:63], s[72:73] op_sel_hi:[1,0]
	v_cvt_pk_f32_fp8_e32 v[70:71], v111
	v_pk_fma_f32 v[78:79], v[60:61], s[90:91], v[62:63] op_sel_hi:[1,0,1]
	v_add_f32_e32 v61, v72, v73
	v_add_f32_e32 v60, v79, v78
	v_add_f32_e32 v60, v61, v60
	v_add_f32_e32 v90, v112, v60
	v_cvt_pk_f32_fp8_e32 v[60:61], v110
	v_cvt_pk_f32_fp8_sdwa v[62:63], v110 src0_sel:WORD_1
	v_cvt_pk_f32_fp8_sdwa v[74:75], v111 src0_sel:WORD_1
	v_lshlrev_b32_e32 v76, 16, v58
	v_pk_add_f32 v[60:61], v[60:61], v[70:71]
	v_and_b32_e32 v77, 0xffff0000, v58
	v_pk_mul_f32 v[60:61], v[60:61], s[72:73] op_sel_hi:[1,0]
	v_lshlrev_b32_e32 v58, 16, v59
	v_pk_fma_f32 v[70:71], v[76:77], s[90:91], v[60:61] op_sel_hi:[1,0,1]
	v_pk_add_f32 v[60:61], v[62:63], v[74:75]
	v_and_b32_e32 v59, 0xffff0000, v59
	v_pk_mul_f32 v[60:61], v[60:61], s[72:73] op_sel_hi:[1,0]
	v_cvt_pk_f32_fp8_e32 v[62:63], v68
	v_pk_fma_f32 v[76:77], v[58:59], s[90:91], v[60:61] op_sel_hi:[1,0,1]
	v_add_f32_e32 v59, v70, v71
	v_add_f32_e32 v58, v77, v76
	v_add_f32_e32 v58, v59, v58
	v_add_f32_e32 v90, v90, v58
	v_cvt_pk_f32_fp8_e32 v[58:59], v69
	v_cvt_pk_f32_fp8_sdwa v[60:61], v69 src0_sel:WORD_1
	v_cvt_pk_f32_fp8_sdwa v[74:75], v68 src0_sel:WORD_1
	v_lshlrev_b32_e32 v68, 16, v6
	v_pk_add_f32 v[58:59], v[58:59], v[62:63]
	v_and_b32_e32 v69, 0xffff0000, v6
	v_pk_mul_f32 v[58:59], v[58:59], s[72:73] op_sel_hi:[1,0]
	v_lshlrev_b32_e32 v6, 16, v7
	v_pk_fma_f32 v[68:69], v[68:69], s[90:91], v[58:59] op_sel_hi:[1,0,1]
	v_pk_add_f32 v[58:59], v[60:61], v[74:75]
	v_and_b32_e32 v7, 0xffff0000, v7
	v_pk_mul_f32 v[58:59], v[58:59], s[72:73] op_sel_hi:[1,0]
	v_cvt_pk_f32_fp8_e32 v[60:61], v66
	v_pk_fma_f32 v[74:75], v[6:7], s[90:91], v[58:59] op_sel_hi:[1,0,1]
	v_add_f32_e32 v7, v68, v69
	v_add_f32_e32 v6, v75, v74
	v_add_f32_e32 v6, v7, v6
	v_add_f32_e32 v90, v90, v6
	v_cvt_pk_f32_fp8_e32 v[6:7], v67
	v_cvt_pk_f32_fp8_sdwa v[58:59], v67 src0_sel:WORD_1
	v_cvt_pk_f32_fp8_sdwa v[66:67], v66 src0_sel:WORD_1
	v_lshlrev_b32_e32 v62, 16, v4
	v_pk_add_f32 v[6:7], v[6:7], v[60:61]
	v_and_b32_e32 v63, 0xffff0000, v4
	v_pk_mul_f32 v[6:7], v[6:7], s[72:73] op_sel_hi:[1,0]
	v_lshlrev_b32_e32 v4, 16, v5
	v_pk_fma_f32 v[62:63], v[62:63], s[90:91], v[6:7] op_sel_hi:[1,0,1]
	v_pk_add_f32 v[6:7], v[58:59], v[66:67]
	v_and_b32_e32 v5, 0xffff0000, v5
	v_pk_mul_f32 v[6:7], v[6:7], s[72:73] op_sel_hi:[1,0]
	v_cvt_pk_f32_fp8_e32 v[58:59], v88
	v_pk_fma_f32 v[66:67], v[4:5], s[90:91], v[6:7] op_sel_hi:[1,0,1]
	v_add_f32_e32 v5, v62, v63
	v_add_f32_e32 v4, v67, v66
	v_add_f32_e32 v4, v5, v4
	v_add_f32_e32 v90, v90, v4
	v_cvt_pk_f32_fp8_e32 v[4:5], v89
	v_cvt_pk_f32_fp8_sdwa v[6:7], v89 src0_sel:WORD_1
	v_cvt_pk_f32_fp8_sdwa v[60:61], v88 src0_sel:WORD_1
	v_lshlrev_b32_e32 v88, 16, v2
	v_pk_add_f32 v[4:5], v[4:5], v[58:59]
	v_and_b32_e32 v89, 0xffff0000, v2
	v_pk_mul_f32 v[4:5], v[4:5], s[72:73] op_sel_hi:[1,0]
	v_lshlrev_b32_e32 v2, 16, v3
	v_pk_fma_f32 v[58:59], v[88:89], s[90:91], v[4:5] op_sel_hi:[1,0,1]
	v_pk_add_f32 v[4:5], v[6:7], v[60:61]
; __device__ __forceinline__ unsigned cvt_pk_bf16(float lo, float hi) { unsigned r; asm volatile("v_cvt_pk_bf16_f32 %0, %1, %2" : "=v"(r) : "v"(lo), "v"(hi)); return r; }
; __global__ void __launch_bounds__(NTHREADS, 2) hybrid_fwd(Args a) {
;     ...
;                     const float mean = wave_sum(s) * (1.f / DM); float s2 = 0.f;
; #pragma unroll
;                     for (int j = 0; j < 8; ++j) { y[j] = y[j] - mean; s2 += (y[j][0] * y[j][0] + y[j][1] * y[j][1]) + (y[j][2] * y[j][2] + y[j][3] * y[j][3]); }
;                     const float rstd = __builtin_amdgcn_rsqf(wave_sum(s2) * (1.f / DM) + LN_EPS);
; #pragma unroll
;                     for (int j = 0; j < 8; ++j) { const f32x4 gg = *(const f32x4*)(lg + j * 256 + lane * 4), bb = *(const f32x4*)(lb + j * 256 + lane * 4);
;                         y[j] = y[j] * rstd * gg + bb;
;                         if (lastl) __builtin_nontemporal_store(y[j], (f32x4*)(a.out + (size_t)row * DM + j * 256 + lane * 4));
;                         else { u32x2 w; w.x = cvt_pk_bf16(y[j][0], y[j][1]); w.y = cvt_pk_bf16(y[j][2], y[j][3]); __builtin_nontemporal_store(w, (u32x2*)(XA16 + (size_t)row * DM + j * 256 + lane * 4)); }
;                         if (!lastl) __builtin_nontemporal_store(cvt4_fp8(y[j][0], y[j][1], y[j][2], y[j][3]), (unsigned*)(XB + (size_t)row * DM + j * 256 + lane * 4)); }
	v_and_b32_e32 v3, 0xffff0000, v3
	v_pk_mul_f32 v[4:5], v[4:5], s[72:73] op_sel_hi:[1,0]
	v_cvt_pk_f32_fp8_e32 v[88:89], v86
	v_pk_fma_f32 v[60:61], v[2:3], s[90:91], v[4:5] op_sel_hi:[1,0,1]
	v_add_f32_e32 v3, v58, v59
	v_add_f32_e32 v2, v61, v60
	v_cvt_pk_f32_fp8_e32 v[4:5], v87
	v_add_f32_e32 v2, v3, v2
	v_add_f32_e32 v2, v90, v2
	v_cvt_pk_f32_fp8_sdwa v[6:7], v87 src0_sel:WORD_1
	v_cvt_pk_f32_fp8_sdwa v[90:91], v86 src0_sel:WORD_1
	v_pk_add_f32 v[4:5], v[4:5], v[88:89]
	v_lshlrev_b32_e32 v86, 16, v0
	v_and_b32_e32 v87, 0xffff0000, v0
	v_pk_mul_f32 v[4:5], v[4:5], s[72:73] op_sel_hi:[1,0]
	v_lshlrev_b32_e32 v0, 16, v1
	v_pk_fma_f32 v[86:87], v[86:87], s[90:91], v[4:5] op_sel_hi:[1,0,1]
	v_pk_add_f32 v[4:5], v[6:7], v[90:91]
	v_and_b32_e32 v1, 0xffff0000, v1
	v_pk_mul_f32 v[4:5], v[4:5], s[72:73] op_sel_hi:[1,0]
	s_nop 0
	v_pk_fma_f32 v[88:89], v[0:1], s[90:91], v[4:5] op_sel_hi:[1,0,1]
	v_add_f32_e32 v1, v86, v87
	v_add_f32_e32 v0, v89, v88
	v_add_f32_e32 v0, v1, v0
	v_add_f32_e32 v0, v2, v0
	s_nop 1
	v_add_f32_dpp v0, v0, v0 quad_perm:[1,0,3,2] row_mask:0xf bank_mask:0xf bound_ctrl:1
	s_nop 1
	v_add_f32_dpp v0, v0, v0 quad_perm:[2,3,0,1] row_mask:0xf bank_mask:0xf bound_ctrl:1
	s_nop 1
	v_add_f32_dpp v0, v0, v0 row_ror:4 row_mask:0xf bank_mask:0xf bound_ctrl:1
	s_nop 1
	v_add_f32_dpp v0, v0, v0 row_ror:8 row_mask:0xf bank_mask:0xf bound_ctrl:1
	v_mov_b32_e32 v1, v0
	s_nop 1
	v_permlane16_swap_b32_e32 v0, v1
	v_add_f32_e32 v0, v0, v1
	v_mov_b32_e32 v1, v0
	s_nop 1
	v_permlane32_swap_b32_e32 v0, v1
	v_add_f32_e32 v0, v0, v1
	v_fmac_f32_e32 v85, 0xba000000, v0
	v_fmac_f32_e32 v83, 0xba000000, v0
	v_fmamk_f32 v84, v0, 0xba000000, v84
	v_fmamk_f32 v82, v0, 0xba000000, v82
	v_mul_f32_e32 v1, v83, v83
	v_mul_f32_e32 v2, v85, v85
	v_fmac_f32_e32 v1, v82, v82
	v_fmac_f32_e32 v2, v84, v84
	v_fmamk_f32 v81, v0, 0xba000000, v81
	v_fmamk_f32 v65, v0, 0xba000000, v65
	v_add_f32_e32 v1, v1, v2
	v_fmac_f32_e32 v80, 0xba000000, v0
	v_fmac_f32_e32 v64, 0xba000000, v0
	v_mul_f32_e32 v2, v65, v65
	v_mul_f32_e32 v3, v81, v81
	v_fmac_f32_e32 v2, v64, v64
	v_fmac_f32_e32 v3, v80, v80
	v_add_f32_e32 v2, v2, v3
	v_fmamk_f32 v79, v0, 0xba000000, v79
	v_fmamk_f32 v73, v0, 0xba000000, v73
	v_add_f32_e32 v1, v1, v2
	v_fmac_f32_e32 v78, 0xba000000, v0
	v_fmac_f32_e32 v72, 0xba000000, v0
	v_mul_f32_e32 v2, v73, v73
	v_mul_f32_e32 v3, v79, v79
	v_fmac_f32_e32 v2, v72, v72
	v_fmac_f32_e32 v3, v78, v78
	v_add_f32_e32 v2, v2, v3
	v_fmamk_f32 v77, v0, 0xba000000, v77
	v_fmamk_f32 v71, v0, 0xba000000, v71
	v_add_f32_e32 v1, v1, v2
	v_fmac_f32_e32 v76, 0xba000000, v0
	v_fmac_f32_e32 v70, 0xba000000, v0
	v_mul_f32_e32 v2, v71, v71
	v_mul_f32_e32 v3, v77, v77
	v_fmac_f32_e32 v2, v70, v70
	v_fmac_f32_e32 v3, v76, v76
	v_add_f32_e32 v2, v2, v3
	v_fmamk_f32 v75, v0, 0xba000000, v75
	v_fmamk_f32 v69, v0, 0xba000000, v69
	v_add_f32_e32 v1, v1, v2
	v_fmac_f32_e32 v74, 0xba000000, v0
	v_fmac_f32_e32 v68, 0xba000000, v0
	v_mul_f32_e32 v2, v69, v69
	v_mul_f32_e32 v3, v75, v75
	v_fmac_f32_e32 v2, v68, v68
	v_fmac_f32_e32 v3, v74, v74
	v_add_f32_e32 v2, v2, v3
	v_fmamk_f32 v67, v0, 0xba000000, v67
	v_fmamk_f32 v63, v0, 0xba000000, v63
	v_add_f32_e32 v1, v1, v2
	v_fmac_f32_e32 v66, 0xba000000, v0
	v_fmac_f32_e32 v62, 0xba000000, v0
	v_mul_f32_e32 v2, v63, v63
	v_mul_f32_e32 v3, v67, v67
	v_fmac_f32_e32 v2, v62, v62
	v_fmac_f32_e32 v3, v66, v66
	v_add_f32_e32 v2, v2, v3
	v_fmamk_f32 v61, v0, 0xba000000, v61
	v_fmamk_f32 v59, v0, 0xba000000, v59
	v_add_f32_e32 v1, v1, v2
	v_fmac_f32_e32 v60, 0xba000000, v0
	v_fmac_f32_e32 v58, 0xba000000, v0
	v_mul_f32_e32 v2, v59, v59
	v_mul_f32_e32 v3, v61, v61
	v_fmac_f32_e32 v2, v58, v58
	v_fmac_f32_e32 v3, v60, v60
	v_add_f32_e32 v2, v2, v3
	v_fmamk_f32 v89, v0, 0xba000000, v89
	v_fmamk_f32 v87, v0, 0xba000000, v87
	v_add_f32_e32 v1, v1, v2
	v_fmac_f32_e32 v88, 0xba000000, v0
	v_fmac_f32_e32 v86, 0xba000000, v0
	v_mul_f32_e32 v0, v87, v87
	v_mul_f32_e32 v2, v89, v89
	v_fmac_f32_e32 v0, v86, v86
	v_fmac_f32_e32 v2, v88, v88
	v_add_f32_e32 v0, v0, v2
	v_add_f32_e32 v0, v1, v0
	s_nop 1
	v_add_f32_dpp v0, v0, v0 quad_perm:[1,0,3,2] row_mask:0xf bank_mask:0xf bound_ctrl:1
	s_nop 1
	v_add_f32_dpp v0, v0, v0 quad_perm:[2,3,0,1] row_mask:0xf bank_mask:0xf bound_ctrl:1
	s_nop 1
	v_add_f32_dpp v0, v0, v0 row_ror:4 row_mask:0xf bank_mask:0xf bound_ctrl:1
	s_nop 1
	v_add_f32_dpp v0, v0, v0 row_ror:8 row_mask:0xf bank_mask:0xf bound_ctrl:1
	v_mov_b32_e32 v1, v0
	s_nop 1
	v_permlane16_swap_b32_e32 v0, v1
	v_add_f32_e32 v0, v0, v1
	v_mov_b32_e32 v1, v0
	s_nop 1
	v_permlane32_swap_b32_e32 v0, v1
	v_add_f32_e32 v0, v0, v1
	v_fmamk_f32 v0, v0, 0x3a000000, v207
	v_rsq_f32_e32 v90, v0
	s_nop 0
	v_pk_mul_f32 v[82:83], v[90:91], v[82:83] op_sel_hi:[0,1]
	v_pk_mul_f32 v[84:85], v[90:91], v[84:85] op_sel_hi:[0,1]
	v_pk_fma_f32 v[2:3], v[84:85], v[154:155], v[190:191]
	v_pk_fma_f32 v[0:1], v[82:83], v[152:153], v[188:189]
	s_cbranch_vccz .LBB0_1338
	v_add_co_u32_e32 v6, vcc, 0x38000000, v40
	v_cvt_pk_bf16_f32 v4, v0, v1
	v_cvt_pk_bf16_f32 v5, v2, v3
	s_mov_b64 s[2:3], 0
	s_nop 0
	v_addc_co_u32_e32 v7, vcc, 0, v41, vcc
	flat_store_dwordx2 v[6:7], v[4:5] nt

; __device__ __forceinline__ unsigned cvt_pk_bf16(float lo, float hi) { unsigned r; asm volatile("v_cvt_pk_bf16_f32 %0, %1, %2" : "=v"(r) : "v"(lo), "v"(hi)); return r; }
; __global__ void __launch_bounds__(NTHREADS, 2) hybrid_fwd(Args a) {
;     ...
; #pragma unroll
;                     for (int j = 0; j < 8; ++j) { const f32x4 gg = *(const f32x4*)(lg + j * 256 + lane * 4), bb = *(const f32x4*)(lb + j * 256 + lane * 4);
;                         y[j] = y[j] * rstd * gg + bb;
;                         if (lastl) __builtin_nontemporal_store(y[j], (f32x4*)(a.out + (size_t)row * DM + j * 256 + lane * 4));
;                         else { u32x2 w; w.x = cvt_pk_bf16(y[j][0], y[j][1]); w.y = cvt_pk_bf16(y[j][2], y[j][3]); __builtin_nontemporal_store(w, (u32x2*)(XA16 + (size_t)row * DM + j * 256 + lane * 4)); }
;                         if (!lastl) __builtin_nontemporal_store(cvt4_fp8(y[j][0], y[j][1], y[j][2], y[j][3]), (unsigned*)(XB + (size_t)row * DM + j * 256 + lane * 4)); }
.LBB0_1342:
	s_nop 0
	v_mov_b32_e32 v91, v90
	v_mov_b32_e32 v110, v90
	v_mov_b32_e32 v111, v90
	v_pk_mul_f32 v[80:81], v[110:111], v[80:81]
	v_pk_mul_f32 v[64:65], v[90:91], v[64:65]
	s_and_b64 vcc, exec, s[2:3]
	s_mov_b64 s[22:23], -1
	v_pk_fma_f32 v[2:3], v[80:81], v[158:159], v[196:197]
	v_pk_fma_f32 v[0:1], v[64:65], v[156:157], v[194:195]
	s_cbranch_vccnz .LBB0_1401
	v_add_co_u32_e32 v80, vcc, 0x38000000, v40
	s_nop 1
	v_addc_co_u32_e32 v81, vcc, 0, v41, vcc
	v_cvt_pk_bf16_f32 v64, v0, v1
	v_cvt_pk_bf16_f32 v65, v2, v3
	flat_store_dwordx2 v[80:81], v[64:65] offset:512 nt
	s_cbranch_execz .LBB0_1402

; __device__ __forceinline__ unsigned cvt_pk_bf16(float lo, float hi) { unsigned r; asm volatile("v_cvt_pk_bf16_f32 %0, %1, %2" : "=v"(r) : "v"(lo), "v"(hi)); return r; }
; __global__ void __launch_bounds__(NTHREADS, 2) hybrid_fwd(Args a) {
;     ...
; #pragma unroll
;                     for (int j = 0; j < 8; ++j) { const f32x4 gg = *(const f32x4*)(lg + j * 256 + lane * 4), bb = *(const f32x4*)(lb + j * 256 + lane * 4);
;                         y[j] = y[j] * rstd * gg + bb;
;                         if (lastl) __builtin_nontemporal_store(y[j], (f32x4*)(a.out + (size_t)row * DM + j * 256 + lane * 4));
;                         else { u32x2 w; w.x = cvt_pk_bf16(y[j][0], y[j][1]); w.y = cvt_pk_bf16(y[j][2], y[j][3]); __builtin_nontemporal_store(w, (u32x2*)(XA16 + (size_t)row * DM + j * 256 + lane * 4)); }
;                         if (!lastl) __builtin_nontemporal_store(cvt4_fp8(y[j][0], y[j][1], y[j][2], y[j][3]), (unsigned*)(XB + (size_t)row * DM + j * 256 + lane * 4)); }
.LBB0_1346:
	s_nop 0
	v_mov_b32_e32 v64, v90
	v_mov_b32_e32 v65, v90
	v_pk_mul_f32 v[72:73], v[90:91], v[72:73]
	v_pk_mul_f32 v[64:65], v[64:65], v[78:79]
	s_and_b64 vcc, exec, s[2:3]
	s_mov_b64 s[22:23], -1
	v_pk_fma_f32 v[2:3], v[64:65], v[162:163], v[200:201]
	v_pk_fma_f32 v[0:1], v[72:73], v[160:161], v[198:199]
	s_cbranch_vccnz .LBB0_1403
	v_add_co_u32_e32 v72, vcc, 0x38000000, v40
	s_nop 1
	v_addc_co_u32_e32 v73, vcc, 0, v41, vcc
	v_cvt_pk_bf16_f32 v64, v0, v1
	v_cvt_pk_bf16_f32 v65, v2, v3
	flat_store_dwordx2 v[72:73], v[64:65] offset:1024 nt
	s_cbranch_execz .LBB0_1404

; __device__ __forceinline__ unsigned cvt_pk_bf16(float lo, float hi) { unsigned r; asm volatile("v_cvt_pk_bf16_f32 %0, %1, %2" : "=v"(r) : "v"(lo), "v"(hi)); return r; }
; __global__ void __launch_bounds__(NTHREADS, 2) hybrid_fwd(Args a) {
;     ...
; #pragma unroll
;                     for (int j = 0; j < 8; ++j) { const f32x4 gg = *(const f32x4*)(lg + j * 256 + lane * 4), bb = *(const f32x4*)(lb + j * 256 + lane * 4);
;                         y[j] = y[j] * rstd * gg + bb;
;                         if (lastl) __builtin_nontemporal_store(y[j], (f32x4*)(a.out + (size_t)row * DM + j * 256 + lane * 4));
;                         else { u32x2 w; w.x = cvt_pk_bf16(y[j][0], y[j][1]); w.y = cvt_pk_bf16(y[j][2], y[j][3]); __builtin_nontemporal_store(w, (u32x2*)(XA16 + (size_t)row * DM + j * 256 + lane * 4)); }
;                         if (!lastl) __builtin_nontemporal_store(cvt4_fp8(y[j][0], y[j][1], y[j][2], y[j][3]), (unsigned*)(XB + (size_t)row * DM + j * 256 + lane * 4)); }
.LBB0_1350:
	s_nop 0
	v_mov_b32_e32 v64, v90
	v_mov_b32_e32 v65, v90
	v_pk_mul_f32 v[70:71], v[90:91], v[70:71]
	v_pk_mul_f32 v[64:65], v[64:65], v[76:77]
	s_and_b64 vcc, exec, s[2:3]
	s_mov_b64 s[22:23], -1
	v_pk_fma_f32 v[2:3], v[64:65], v[170:171], v[204:205]
	v_pk_fma_f32 v[0:1], v[70:71], v[168:169], v[202:203]
	s_cbranch_vccnz .LBB0_1405
	v_add_co_u32_e32 v70, vcc, 0x38000000, v40
	s_nop 1
	v_addc_co_u32_e32 v71, vcc, 0, v41, vcc
	v_cvt_pk_bf16_f32 v64, v0, v1
	v_cvt_pk_bf16_f32 v65, v2, v3
	flat_store_dwordx2 v[70:71], v[64:65] offset:1536 nt
	s_cbranch_execz .LBB0_1406

; __device__ __forceinline__ unsigned cvt_pk_bf16(float lo, float hi) { unsigned r; asm volatile("v_cvt_pk_bf16_f32 %0, %1, %2" : "=v"(r) : "v"(lo), "v"(hi)); return r; }
; __global__ void __launch_bounds__(NTHREADS, 2) hybrid_fwd(Args a) {
;     ...
; #pragma unroll
;                     for (int j = 0; j < 8; ++j) { const f32x4 gg = *(const f32x4*)(lg + j * 256 + lane * 4), bb = *(const f32x4*)(lb + j * 256 + lane * 4);
;                         y[j] = y[j] * rstd * gg + bb;
;                         if (lastl) __builtin_nontemporal_store(y[j], (f32x4*)(a.out + (size_t)row * DM + j * 256 + lane * 4));
;                         else { u32x2 w; w.x = cvt_pk_bf16(y[j][0], y[j][1]); w.y = cvt_pk_bf16(y[j][2], y[j][3]); __builtin_nontemporal_store(w, (u32x2*)(XA16 + (size_t)row * DM + j * 256 + lane * 4)); }
;                         if (!lastl) __builtin_nontemporal_store(cvt4_fp8(y[j][0], y[j][1], y[j][2], y[j][3]), (unsigned*)(XB + (size_t)row * DM + j * 256 + lane * 4)); }
.LBB0_1354:
	s_nop 0
	v_mov_b32_e32 v64, v90
	v_mov_b32_e32 v65, v90
	v_pk_mul_f32 v[68:69], v[90:91], v[68:69]
	v_pk_mul_f32 v[64:65], v[64:65], v[74:75]
	s_and_b64 vcc, exec, s[2:3]
	s_mov_b64 s[22:23], -1
	v_pk_fma_f32 v[2:3], v[64:65], v[174:175], v[218:219]
	v_pk_fma_f32 v[0:1], v[68:69], v[172:173], v[216:217]
	s_cbranch_vccnz .LBB0_1407
	v_add_co_u32_e32 v68, vcc, 0x38000000, v40
	s_nop 1
	v_addc_co_u32_e32 v69, vcc, 0, v41, vcc
	v_cvt_pk_bf16_f32 v64, v0, v1
	v_cvt_pk_bf16_f32 v65, v2, v3
	flat_store_dwordx2 v[68:69], v[64:65] offset:2048 nt
	s_cbranch_execz .LBB0_1408

; __device__ __forceinline__ unsigned cvt_pk_bf16(float lo, float hi) { unsigned r; asm volatile("v_cvt_pk_bf16_f32 %0, %1, %2" : "=v"(r) : "v"(lo), "v"(hi)); return r; }
; __global__ void __launch_bounds__(NTHREADS, 2) hybrid_fwd(Args a) {
;     ...
; #pragma unroll
;                     for (int j = 0; j < 8; ++j) { const f32x4 gg = *(const f32x4*)(lg + j * 256 + lane * 4), bb = *(const f32x4*)(lb + j * 256 + lane * 4);
;                         y[j] = y[j] * rstd * gg + bb;
;                         if (lastl) __builtin_nontemporal_store(y[j], (f32x4*)(a.out + (size_t)row * DM + j * 256 + lane * 4));
;                         else { u32x2 w; w.x = cvt_pk_bf16(y[j][0], y[j][1]); w.y = cvt_pk_bf16(y[j][2], y[j][3]); __builtin_nontemporal_store(w, (u32x2*)(XA16 + (size_t)row * DM + j * 256 + lane * 4)); }
;                         if (!lastl) __builtin_nontemporal_store(cvt4_fp8(y[j][0], y[j][1], y[j][2], y[j][3]), (unsigned*)(XB + (size_t)row * DM + j * 256 + lane * 4)); }
.LBB0_1358:
	s_nop 0
	v_mov_b32_e32 v64, v90
	v_mov_b32_e32 v65, v90
	v_pk_mul_f32 v[62:63], v[90:91], v[62:63]
	v_pk_mul_f32 v[64:65], v[64:65], v[66:67]
	s_and_b64 vcc, exec, s[2:3]
	s_mov_b64 s[22:23], -1
	v_pk_fma_f32 v[2:3], v[64:65], v[178:179], v[222:223]
	v_pk_fma_f32 v[0:1], v[62:63], v[176:177], v[220:221]
	s_cbranch_vccnz .LBB0_1409
	v_add_co_u32_e32 v64, vcc, 0x38000000, v40
	s_nop 1
	v_addc_co_u32_e32 v65, vcc, 0, v41, vcc
	v_cvt_pk_bf16_f32 v62, v0, v1
	v_cvt_pk_bf16_f32 v63, v2, v3
	flat_store_dwordx2 v[64:65], v[62:63] offset:2560 nt
	s_cbranch_execz .LBB0_1410

; __device__ __forceinline__ unsigned cvt_pk_bf16(float lo, float hi) { unsigned r; asm volatile("v_cvt_pk_bf16_f32 %0, %1, %2" : "=v"(r) : "v"(lo), "v"(hi)); return r; }
; __global__ void __launch_bounds__(NTHREADS, 2) hybrid_fwd(Args a) {
;     ...
; #pragma unroll
;                     for (int j = 0; j < 8; ++j) { const f32x4 gg = *(const f32x4*)(lg + j * 256 + lane * 4), bb = *(const f32x4*)(lb + j * 256 + lane * 4);
;                         y[j] = y[j] * rstd * gg + bb;
;                         if (lastl) __builtin_nontemporal_store(y[j], (f32x4*)(a.out + (size_t)row * DM + j * 256 + lane * 4));
;                         else { u32x2 w; w.x = cvt_pk_bf16(y[j][0], y[j][1]); w.y = cvt_pk_bf16(y[j][2], y[j][3]); __builtin_nontemporal_store(w, (u32x2*)(XA16 + (size_t)row * DM + j * 256 + lane * 4)); }
;                         if (!lastl) __builtin_nontemporal_store(cvt4_fp8(y[j][0], y[j][1], y[j][2], y[j][3]), (unsigned*)(XB + (size_t)row * DM + j * 256 + lane * 4)); }
.LBB0_1362:
	s_nop 0
	v_mov_b32_e32 v66, v90
	v_mov_b32_e32 v67, v90
	v_pk_mul_f32 v[58:59], v[90:91], v[58:59]
	v_pk_mul_f32 v[60:61], v[66:67], v[60:61]
	s_and_b64 vcc, exec, s[2:3]
	s_mov_b64 s[22:23], -1
	v_pk_fma_f32 v[2:3], v[60:61], v[182:183], v[226:227]
	v_pk_fma_f32 v[0:1], v[58:59], v[180:181], v[224:225]
	s_cbranch_vccnz .LBB0_1411
	v_add_co_u32_e32 v60, vcc, 0x38000000, v40
	s_nop 1
	v_addc_co_u32_e32 v61, vcc, 0, v41, vcc
	v_cvt_pk_bf16_f32 v58, v0, v1
	v_cvt_pk_bf16_f32 v59, v2, v3
	flat_store_dwordx2 v[60:61], v[58:59] offset:3072 nt
	s_cbranch_execz .LBB0_1412

; __device__ __forceinline__ unsigned cvt_pk_bf16(float lo, float hi) { unsigned r; asm volatile("v_cvt_pk_bf16_f32 %0, %1, %2" : "=v"(r) : "v"(lo), "v"(hi)); return r; }
; __global__ void __launch_bounds__(NTHREADS, 2) hybrid_fwd(Args a) {
;     ...
; #pragma unroll
;                     for (int j = 0; j < 8; ++j) { const f32x4 gg = *(const f32x4*)(lg + j * 256 + lane * 4), bb = *(const f32x4*)(lb + j * 256 + lane * 4);
;                         y[j] = y[j] * rstd * gg + bb;
;                         if (lastl) __builtin_nontemporal_store(y[j], (f32x4*)(a.out + (size_t)row * DM + j * 256 + lane * 4));
;                         else { u32x2 w; w.x = cvt_pk_bf16(y[j][0], y[j][1]); w.y = cvt_pk_bf16(y[j][2], y[j][3]); __builtin_nontemporal_store(w, (u32x2*)(XA16 + (size_t)row * DM + j * 256 + lane * 4)); }
;                         if (!lastl) __builtin_nontemporal_store(cvt4_fp8(y[j][0], y[j][1], y[j][2], y[j][3]), (unsigned*)(XB + (size_t)row * DM + j * 256 + lane * 4)); }
.LBB0_1366:
	s_nop 0
	v_mov_b32_e32 v62, v90
	v_mov_b32_e32 v63, v90
	v_pk_mul_f32 v[64:65], v[90:91], v[86:87]
	v_pk_mul_f32 v[62:63], v[62:63], v[88:89]
	s_and_b64 vcc, exec, s[2:3]
	s_mov_b64 s[22:23], -1
	v_pk_fma_f32 v[2:3], v[62:63], v[186:187], v[230:231]
	v_pk_fma_f32 v[0:1], v[64:65], v[184:185], v[228:229]
	s_cbranch_vccnz .LBB0_1413
	v_add_co_u32_e32 v40, vcc, 0x38000000, v40
	s_nop 1
	v_addc_co_u32_e32 v41, vcc, 0, v41, vcc
	v_cvt_pk_bf16_f32 v58, v0, v1
	v_cvt_pk_bf16_f32 v59, v2, v3
	flat_store_dwordx2 v[40:41], v[58:59] offset:3584 nt
	s_cbranch_execz .LBB0_1414

; __device__ __forceinline__ float bflo(unsigned w) { return __uint_as_float(w << 16); }
; __device__ __forceinline__ float bfhi(unsigned w) { return __uint_as_float(w & 0xffff0000u); }
; __global__ void __launch_bounds__(NTHREADS, 2) hybrid_fwd(Args a) {
;     ...
;                 for (int rr = 0; rr < 2; ++rr) { const int row = row0 + rr * NGW;
;                     f32x4 y[8]; float s = 0.f;
; #pragma unroll
;                     for (int j = 0; j < 8; ++j) { const u32x2 x = xw[rr][j]; const int p = (int)pw_[rr][j], q = (int)qw[rr][j];
;                         const f32x2 p0 = __builtin_amdgcn_cvt_pk_f32_fp8(p, false), p1 = __builtin_amdgcn_cvt_pk_f32_fp8(p, true), q0 = __builtin_amdgcn_cvt_pk_f32_fp8(q, false), q1 = __builtin_amdgcn_cvt_pk_f32_fp8(q, true);
;                         y[j][0] = bflo(x.x) * ALPHA + (p0.x + q0.x) * (1.f / Y2_SCALE); y[j][1] = bfhi(x.x) * ALPHA + (p0.y + q0.y) * (1.f / Y2_SCALE);
;                         y[j][2] = bflo(x.y) * ALPHA + (p1.x + q1.x) * (1.f / Y2_SCALE); y[j][3] = bfhi(x.y) * ALPHA + (p1.y + q1.y) * (1.f / Y2_SCALE);
;                         s += (y[j][0] + y[j][1]) + (y[j][2] + y[j][3]); }
.LBB0_1370:
	v_cvt_pk_f32_fp8_e32 v[0:1], v109
	v_cvt_pk_f32_fp8_e32 v[4:5], v108
	v_cvt_pk_f32_fp8_sdwa v[2:3], v109 src0_sel:WORD_1
	v_cvt_pk_f32_fp8_sdwa v[6:7], v108 src0_sel:WORD_1
	v_lshlrev_b32_e32 v40, 16, v56
	v_pk_add_f32 v[0:1], v[0:1], v[4:5]
	v_and_b32_e32 v41, 0xffff0000, v56
	v_pk_mul_f32 v[0:1], v[0:1], s[72:73] op_sel_hi:[1,0]
	v_pk_add_f32 v[2:3], v[2:3], v[6:7]
	v_pk_fma_f32 v[70:71], v[40:41], s[90:91], v[0:1] op_sel_hi:[1,0,1]
	v_lshlrev_b32_e32 v0, 16, v57
	v_and_b32_e32 v1, 0xffff0000, v57
	v_pk_mul_f32 v[2:3], v[2:3], s[72:73] op_sel_hi:[1,0]
	v_cvt_pk_f32_fp8_e32 v[4:5], v104
	v_pk_fma_f32 v[72:73], v[0:1], s[90:91], v[2:3] op_sel_hi:[1,0,1]
	v_add_f32_e32 v1, v70, v71
	v_add_f32_e32 v0, v73, v72
	v_add_f32_e32 v0, v1, v0
	v_add_f32_e32 v56, 0, v0
	v_cvt_pk_f32_fp8_e32 v[0:1], v106
	v_cvt_pk_f32_fp8_sdwa v[2:3], v106 src0_sel:WORD_1
	v_cvt_pk_f32_fp8_sdwa v[6:7], v104 src0_sel:WORD_1
	v_lshlrev_b32_e32 v40, 16, v52
	v_pk_add_f32 v[0:1], v[0:1], v[4:5]
	v_and_b32_e32 v41, 0xffff0000, v52
	v_pk_mul_f32 v[0:1], v[0:1], s[72:73] op_sel_hi:[1,0]
	v_pk_add_f32 v[2:3], v[2:3], v[6:7]
	v_pk_fma_f32 v[66:67], v[40:41], s[90:91], v[0:1] op_sel_hi:[1,0,1]
	v_lshlrev_b32_e32 v0, 16, v53
	v_and_b32_e32 v1, 0xffff0000, v53
	v_pk_mul_f32 v[2:3], v[2:3], s[72:73] op_sel_hi:[1,0]
	v_cvt_pk_f32_fp8_e32 v[4:5], v100
	v_pk_fma_f32 v[68:69], v[0:1], s[90:91], v[2:3] op_sel_hi:[1,0,1]
	v_add_f32_e32 v1, v66, v67
	v_add_f32_e32 v0, v69, v68
	v_add_f32_e32 v0, v1, v0
	v_add_f32_e32 v52, v56, v0
	v_cvt_pk_f32_fp8_e32 v[0:1], v101
	v_cvt_pk_f32_fp8_sdwa v[2:3], v101 src0_sel:WORD_1
	v_cvt_pk_f32_fp8_sdwa v[6:7], v100 src0_sel:WORD_1
	v_lshlrev_b32_e32 v40, 16, v48
	v_pk_add_f32 v[0:1], v[0:1], v[4:5]
	v_and_b32_e32 v41, 0xffff0000, v48
	v_pk_mul_f32 v[0:1], v[0:1], s[72:73] op_sel_hi:[1,0]
	v_pk_add_f32 v[2:3], v[2:3], v[6:7]
	v_pk_fma_f32 v[64:65], v[40:41], s[90:91], v[0:1] op_sel_hi:[1,0,1]
	v_lshlrev_b32_e32 v0, 16, v49
	v_and_b32_e32 v1, 0xffff0000, v49
	v_pk_mul_f32 v[2:3], v[2:3], s[72:73] op_sel_hi:[1,0]
	v_cvt_pk_f32_fp8_e32 v[4:5], v105
	v_pk_fma_f32 v[62:63], v[0:1], s[90:91], v[2:3] op_sel_hi:[1,0,1]
	v_add_f32_e32 v1, v64, v65
	v_add_f32_e32 v0, v63, v62
	v_add_f32_e32 v0, v1, v0
	v_add_f32_e32 v48, v52, v0
	v_cvt_pk_f32_fp8_e32 v[0:1], v107
	v_cvt_pk_f32_fp8_sdwa v[2:3], v107 src0_sel:WORD_1
	v_cvt_pk_f32_fp8_sdwa v[6:7], v105 src0_sel:WORD_1
	v_lshlrev_b32_e32 v40, 16, v54
	v_pk_add_f32 v[0:1], v[0:1], v[4:5]
	v_and_b32_e32 v41, 0xffff0000, v54
	v_pk_mul_f32 v[0:1], v[0:1], s[72:73] op_sel_hi:[1,0]
	v_pk_add_f32 v[2:3], v[2:3], v[6:7]
	v_pk_fma_f32 v[60:61], v[40:41], s[90:91], v[0:1] op_sel_hi:[1,0,1]
	v_lshlrev_b32_e32 v0, 16, v55
	v_and_b32_e32 v1, 0xffff0000, v55
	v_pk_mul_f32 v[2:3], v[2:3], s[72:73] op_sel_hi:[1,0]
	v_cvt_pk_f32_fp8_e32 v[4:5], v102
	v_pk_fma_f32 v[58:59], v[0:1], s[90:91], v[2:3] op_sel_hi:[1,0,1]
	v_add_f32_e32 v1, v60, v61
	v_add_f32_e32 v0, v59, v58
	v_add_f32_e32 v0, v1, v0
	v_add_f32_e32 v48, v48, v0
	v_cvt_pk_f32_fp8_e32 v[0:1], v103
	v_cvt_pk_f32_fp8_sdwa v[2:3], v103 src0_sel:WORD_1
	v_cvt_pk_f32_fp8_sdwa v[6:7], v102 src0_sel:WORD_1
	v_lshlrev_b32_e32 v40, 16, v50
	v_pk_add_f32 v[0:1], v[0:1], v[4:5]
	v_and_b32_e32 v41, 0xffff0000, v50
	v_pk_mul_f32 v[0:1], v[0:1], s[72:73] op_sel_hi:[1,0]
	v_pk_add_f32 v[2:3], v[2:3], v[6:7]
	v_pk_fma_f32 v[56:57], v[40:41], s[90:91], v[0:1] op_sel_hi:[1,0,1]
	v_lshlrev_b32_e32 v0, 16, v51
	v_and_b32_e32 v1, 0xffff0000, v51
	v_pk_mul_f32 v[2:3], v[2:3], s[72:73] op_sel_hi:[1,0]
	v_cvt_pk_f32_fp8_e32 v[4:5], v98
	v_pk_fma_f32 v[54:55], v[0:1], s[90:91], v[2:3] op_sel_hi:[1,0,1]
	v_add_f32_e32 v1, v56, v57
	v_add_f32_e32 v0, v55, v54
	v_add_f32_e32 v0, v1, v0
	v_add_f32_e32 v48, v48, v0
	v_cvt_pk_f32_fp8_e32 v[0:1], v99
	v_cvt_pk_f32_fp8_sdwa v[2:3], v99 src0_sel:WORD_1
	v_cvt_pk_f32_fp8_sdwa v[6:7], v98 src0_sel:WORD_1
	v_lshlrev_b32_e32 v40, 16, v46
	v_pk_add_f32 v[0:1], v[0:1], v[4:5]
	v_and_b32_e32 v41, 0xffff0000, v46
	v_pk_mul_f32 v[0:1], v[0:1], s[72:73] op_sel_hi:[1,0]
	v_pk_add_f32 v[2:3], v[2:3], v[6:7]
	v_pk_fma_f32 v[52:53], v[40:41], s[90:91], v[0:1] op_sel_hi:[1,0,1]
	v_lshlrev_b32_e32 v0, 16, v47
	v_and_b32_e32 v1, 0xffff0000, v47
	v_pk_mul_f32 v[2:3], v[2:3], s[72:73] op_sel_hi:[1,0]
	v_cvt_pk_f32_fp8_e32 v[4:5], v96
	v_pk_fma_f32 v[50:51], v[0:1], s[90:91], v[2:3] op_sel_hi:[1,0,1]
	v_add_f32_e32 v1, v52, v53
	v_add_f32_e32 v0, v51, v50
	v_add_f32_e32 v0, v1, v0
	v_add_f32_e32 v74, v48, v0
	v_cvt_pk_f32_fp8_e32 v[0:1], v97
	v_cvt_pk_f32_fp8_sdwa v[2:3], v97 src0_sel:WORD_1
	v_cvt_pk_f32_fp8_sdwa v[6:7], v96 src0_sel:WORD_1
	v_lshlrev_b32_e32 v40, 16, v44
	v_pk_add_f32 v[0:1], v[0:1], v[4:5]
	v_and_b32_e32 v41, 0xffff0000, v44
	v_pk_mul_f32 v[0:1], v[0:1], s[72:73] op_sel_hi:[1,0]
	v_pk_add_f32 v[2:3], v[2:3], v[6:7]
	v_pk_fma_f32 v[48:49], v[40:41], s[90:91], v[0:1] op_sel_hi:[1,0,1]
	v_lshlrev_b32_e32 v0, 16, v45
	v_and_b32_e32 v1, 0xffff0000, v45
	v_pk_mul_f32 v[2:3], v[2:3], s[72:73] op_sel_hi:[1,0]
	v_cvt_pk_f32_fp8_e32 v[4:5], v94
; __device__ __forceinline__ unsigned cvt_pk_bf16(float lo, float hi) { unsigned r; asm volatile("v_cvt_pk_bf16_f32 %0, %1, %2" : "=v"(r) : "v"(lo), "v"(hi)); return r; }
; __global__ void __launch_bounds__(NTHREADS, 2) hybrid_fwd(Args a) {
;     ...
;                     const float mean = wave_sum(s) * (1.f / DM); float s2 = 0.f;
; #pragma unroll
;                     for (int j = 0; j < 8; ++j) { y[j] = y[j] - mean; s2 += (y[j][0] * y[j][0] + y[j][1] * y[j][1]) + (y[j][2] * y[j][2] + y[j][3] * y[j][3]); }
;                     const float rstd = __builtin_amdgcn_rsqf(wave_sum(s2) * (1.f / DM) + LN_EPS);
; #pragma unroll
;                     for (int j = 0; j < 8; ++j) { const f32x4 gg = *(const f32x4*)(lg + j * 256 + lane * 4), bb = *(const f32x4*)(lb + j * 256 + lane * 4);
;                         y[j] = y[j] * rstd * gg + bb;
;                         if (lastl) __builtin_nontemporal_store(y[j], (f32x4*)(a.out + (size_t)row * DM + j * 256 + lane * 4));
;                         else { u32x2 w; w.x = cvt_pk_bf16(y[j][0], y[j][1]); w.y = cvt_pk_bf16(y[j][2], y[j][3]); __builtin_nontemporal_store(w, (u32x2*)(XA16 + (size_t)row * DM + j * 256 + lane * 4)); }
;                         if (!lastl) __builtin_nontemporal_store(cvt4_fp8(y[j][0], y[j][1], y[j][2], y[j][3]), (unsigned*)(XB + (size_t)row * DM + j * 256 + lane * 4)); }
	v_pk_fma_f32 v[46:47], v[0:1], s[90:91], v[2:3] op_sel_hi:[1,0,1]
	v_add_f32_e32 v1, v48, v49
	v_add_f32_e32 v0, v47, v46
	v_add_f32_e32 v0, v1, v0
	v_add_f32_e32 v74, v74, v0
	v_cvt_pk_f32_fp8_e32 v[0:1], v95
	v_cvt_pk_f32_fp8_sdwa v[2:3], v95 src0_sel:WORD_1
	v_cvt_pk_f32_fp8_sdwa v[6:7], v94 src0_sel:WORD_1
	v_lshlrev_b32_e32 v40, 16, v42
	v_pk_add_f32 v[0:1], v[0:1], v[4:5]
	v_and_b32_e32 v41, 0xffff0000, v42
	v_pk_mul_f32 v[0:1], v[0:1], s[72:73] op_sel_hi:[1,0]
	v_pk_add_f32 v[2:3], v[2:3], v[6:7]
	v_pk_fma_f32 v[44:45], v[40:41], s[90:91], v[0:1] op_sel_hi:[1,0,1]
	v_lshlrev_b32_e32 v0, 16, v43
	v_and_b32_e32 v1, 0xffff0000, v43
	v_pk_mul_f32 v[2:3], v[2:3], s[72:73] op_sel_hi:[1,0]
	s_mov_b64 s[22:23], -1
	v_pk_fma_f32 v[40:41], v[0:1], s[90:91], v[2:3] op_sel_hi:[1,0,1]
	v_add_f32_e32 v1, v44, v45
	v_add_f32_e32 v0, v41, v40
	v_add_f32_e32 v0, v1, v0
	v_add_f32_e32 v0, v74, v0
	s_and_b64 vcc, exec, s[2:3]
	s_nop 0
	v_add_f32_dpp v0, v0, v0 quad_perm:[1,0,3,2] row_mask:0xf bank_mask:0xf bound_ctrl:1
	s_nop 1
	v_add_f32_dpp v0, v0, v0 quad_perm:[2,3,0,1] row_mask:0xf bank_mask:0xf bound_ctrl:1
	s_nop 1
	v_add_f32_dpp v0, v0, v0 row_ror:4 row_mask:0xf bank_mask:0xf bound_ctrl:1
	s_nop 1
	v_add_f32_dpp v0, v0, v0 row_ror:8 row_mask:0xf bank_mask:0xf bound_ctrl:1
	v_mov_b32_e32 v1, v0
	s_nop 1
	v_permlane16_swap_b32_e32 v0, v1
	v_add_f32_e32 v0, v0, v1
	v_mov_b32_e32 v1, v0
	s_nop 1
	v_permlane32_swap_b32_e32 v0, v1
	v_add_f32_e32 v0, v0, v1
	v_fmac_f32_e32 v73, 0xba000000, v0
	v_fmac_f32_e32 v71, 0xba000000, v0
	v_fmamk_f32 v72, v0, 0xba000000, v72
	v_fmamk_f32 v70, v0, 0xba000000, v70
	v_mul_f32_e32 v1, v71, v71
	v_mul_f32_e32 v2, v73, v73
	v_fmac_f32_e32 v1, v70, v70
	v_fmac_f32_e32 v2, v72, v72
	v_fmamk_f32 v69, v0, 0xba000000, v69
	v_fmamk_f32 v67, v0, 0xba000000, v67
	v_add_f32_e32 v1, v1, v2
	v_fmac_f32_e32 v68, 0xba000000, v0
	v_fmac_f32_e32 v66, 0xba000000, v0
	v_mul_f32_e32 v2, v67, v67
	v_mul_f32_e32 v3, v69, v69
	v_fmac_f32_e32 v2, v66, v66
	v_fmac_f32_e32 v3, v68, v68
	v_add_f32_e32 v2, v2, v3
	v_fmamk_f32 v63, v0, 0xba000000, v63
	v_fmamk_f32 v65, v0, 0xba000000, v65
	v_add_f32_e32 v1, v1, v2
	v_fmac_f32_e32 v62, 0xba000000, v0
	v_fmac_f32_e32 v64, 0xba000000, v0
	v_mul_f32_e32 v2, v65, v65
	v_mul_f32_e32 v3, v63, v63
	v_fmac_f32_e32 v2, v64, v64
	v_fmac_f32_e32 v3, v62, v62
	v_add_f32_e32 v2, v2, v3
	v_fmamk_f32 v59, v0, 0xba000000, v59
	v_fmamk_f32 v61, v0, 0xba000000, v61
	v_add_f32_e32 v1, v1, v2
	v_fmac_f32_e32 v58, 0xba000000, v0
	v_fmac_f32_e32 v60, 0xba000000, v0
	v_mul_f32_e32 v2, v61, v61
	v_mul_f32_e32 v3, v59, v59
	v_fmac_f32_e32 v2, v60, v60
	v_fmac_f32_e32 v3, v58, v58
	v_add_f32_e32 v2, v2, v3
	v_fmamk_f32 v55, v0, 0xba000000, v55
	v_fmamk_f32 v57, v0, 0xba000000, v57
	v_add_f32_e32 v1, v1, v2
	v_fmac_f32_e32 v54, 0xba000000, v0
	v_fmac_f32_e32 v56, 0xba000000, v0
	v_mul_f32_e32 v2, v57, v57
	v_mul_f32_e32 v3, v55, v55
	v_fmac_f32_e32 v2, v56, v56
	v_fmac_f32_e32 v3, v54, v54
	v_add_f32_e32 v2, v2, v3
	v_fmamk_f32 v51, v0, 0xba000000, v51
	v_fmamk_f32 v53, v0, 0xba000000, v53
	v_add_f32_e32 v1, v1, v2
	v_fmac_f32_e32 v50, 0xba000000, v0
	v_fmac_f32_e32 v52, 0xba000000, v0
	v_mul_f32_e32 v2, v53, v53
	v_mul_f32_e32 v3, v51, v51
	v_fmac_f32_e32 v2, v52, v52
	v_fmac_f32_e32 v3, v50, v50
	v_add_f32_e32 v2, v2, v3
	v_fmamk_f32 v47, v0, 0xba000000, v47
	v_fmamk_f32 v49, v0, 0xba000000, v49
	v_add_f32_e32 v1, v1, v2
	v_fmac_f32_e32 v46, 0xba000000, v0
	v_fmac_f32_e32 v48, 0xba000000, v0
	v_mul_f32_e32 v2, v49, v49
	v_mul_f32_e32 v3, v47, v47
	v_fmac_f32_e32 v2, v48, v48
	v_fmac_f32_e32 v3, v46, v46
	v_add_f32_e32 v2, v2, v3
	v_fmamk_f32 v41, v0, 0xba000000, v41
	v_fmamk_f32 v45, v0, 0xba000000, v45
	v_add_f32_e32 v1, v1, v2
	v_fmac_f32_e32 v40, 0xba000000, v0
	v_fmac_f32_e32 v44, 0xba000000, v0
	v_mul_f32_e32 v0, v45, v45
	v_mul_f32_e32 v2, v41, v41
	v_fmac_f32_e32 v0, v44, v44
	v_fmac_f32_e32 v2, v40, v40
	v_add_f32_e32 v0, v0, v2
	v_add_f32_e32 v0, v1, v0
	s_nop 1
	v_add_f32_dpp v0, v0, v0 quad_perm:[1,0,3,2] row_mask:0xf bank_mask:0xf bound_ctrl:1
	s_nop 1
	v_add_f32_dpp v0, v0, v0 quad_perm:[2,3,0,1] row_mask:0xf bank_mask:0xf bound_ctrl:1
	s_nop 1
	v_add_f32_dpp v0, v0, v0 row_ror:4 row_mask:0xf bank_mask:0xf bound_ctrl:1
	s_nop 1
	v_add_f32_dpp v0, v0, v0 row_ror:8 row_mask:0xf bank_mask:0xf bound_ctrl:1
	v_mov_b32_e32 v1, v0
	s_nop 1
	v_permlane16_swap_b32_e32 v0, v1
	v_add_f32_e32 v0, v0, v1
	v_mov_b32_e32 v1, v0
	s_nop 1
	v_permlane32_swap_b32_e32 v0, v1
	v_add_f32_e32 v0, v0, v1
	v_fmamk_f32 v0, v0, 0x3a000000, v207
	v_rsq_f32_e32 v42, v0
	s_nop 0
	v_pk_mul_f32 v[70:71], v[42:43], v[70:71] op_sel_hi:[0,1]
	v_pk_mul_f32 v[72:73], v[42:43], v[72:73] op_sel_hi:[0,1]
	v_pk_fma_f32 v[2:3], v[72:73], v[154:155], v[190:191]
	v_pk_fma_f32 v[0:1], v[70:71], v[152:153], v[188:189]
	s_cbranch_vccnz .LBB0_1415
	v_add_co_u32_e32 v6, vcc, 0x38000000, v38
	s_nop 1
	v_addc_co_u32_e32 v7, vcc, 0, v39, vcc
	v_cvt_pk_bf16_f32 v4, v0, v1
	v_cvt_pk_bf16_f32 v5, v2, v3
	flat_store_dwordx2 v[6:7], v[4:5] nt
	v_lshl_add_u64 v[6:7], s[20:21], 0, v[192:193]
	s_cbranch_execz .LBB0_1416

; __device__ __forceinline__ unsigned cvt_pk_bf16(float lo, float hi) { unsigned r; asm volatile("v_cvt_pk_bf16_f32 %0, %1, %2" : "=v"(r) : "v"(lo), "v"(hi)); return r; }
; __global__ void __launch_bounds__(NTHREADS, 2) hybrid_fwd(Args a) {
;     ...
; #pragma unroll
;                     for (int j = 0; j < 8; ++j) { const f32x4 gg = *(const f32x4*)(lg + j * 256 + lane * 4), bb = *(const f32x4*)(lb + j * 256 + lane * 4);
;                         y[j] = y[j] * rstd * gg + bb;
;                         if (lastl) __builtin_nontemporal_store(y[j], (f32x4*)(a.out + (size_t)row * DM + j * 256 + lane * 4));
;                         else { u32x2 w; w.x = cvt_pk_bf16(y[j][0], y[j][1]); w.y = cvt_pk_bf16(y[j][2], y[j][3]); __builtin_nontemporal_store(w, (u32x2*)(XA16 + (size_t)row * DM + j * 256 + lane * 4)); }
;                         if (!lastl) __builtin_nontemporal_store(cvt4_fp8(y[j][0], y[j][1], y[j][2], y[j][3]), (unsigned*)(XB + (size_t)row * DM + j * 256 + lane * 4)); }
.LBB0_1374:
	s_nop 0
	v_mov_b32_e32 v43, v42
	v_mov_b32_e32 v74, v42
	v_mov_b32_e32 v75, v42
	v_pk_mul_f32 v[68:69], v[74:75], v[68:69]
	v_pk_mul_f32 v[66:67], v[42:43], v[66:67]
	s_and_b64 vcc, exec, s[2:3]
	s_mov_b64 s[22:23], -1
	v_pk_fma_f32 v[2:3], v[68:69], v[158:159], v[196:197]
	v_pk_fma_f32 v[0:1], v[66:67], v[156:157], v[194:195]
	s_cbranch_vccnz .LBB0_1417
	v_add_co_u32_e32 v68, vcc, 0x38000000, v38
	s_nop 1
	v_addc_co_u32_e32 v69, vcc, 0, v39, vcc
	v_cvt_pk_bf16_f32 v66, v0, v1
	v_cvt_pk_bf16_f32 v67, v2, v3
	flat_store_dwordx2 v[68:69], v[66:67] offset:512 nt
	s_cbranch_execz .LBB0_1418

; __device__ __forceinline__ unsigned cvt_pk_bf16(float lo, float hi) { unsigned r; asm volatile("v_cvt_pk_bf16_f32 %0, %1, %2" : "=v"(r) : "v"(lo), "v"(hi)); return r; }
; __global__ void __launch_bounds__(NTHREADS, 2) hybrid_fwd(Args a) {
;     ...
; #pragma unroll
;                     for (int j = 0; j < 8; ++j) { const f32x4 gg = *(const f32x4*)(lg + j * 256 + lane * 4), bb = *(const f32x4*)(lb + j * 256 + lane * 4);
;                         y[j] = y[j] * rstd * gg + bb;
;                         if (lastl) __builtin_nontemporal_store(y[j], (f32x4*)(a.out + (size_t)row * DM + j * 256 + lane * 4));
;                         else { u32x2 w; w.x = cvt_pk_bf16(y[j][0], y[j][1]); w.y = cvt_pk_bf16(y[j][2], y[j][3]); __builtin_nontemporal_store(w, (u32x2*)(XA16 + (size_t)row * DM + j * 256 + lane * 4)); }
;                         if (!lastl) __builtin_nontemporal_store(cvt4_fp8(y[j][0], y[j][1], y[j][2], y[j][3]), (unsigned*)(XB + (size_t)row * DM + j * 256 + lane * 4)); }
.LBB0_1378:
	s_nop 0
	v_mov_b32_e32 v70, v42
	v_mov_b32_e32 v71, v42
	v_pk_mul_f32 v[64:65], v[42:43], v[64:65]
	v_pk_mul_f32 v[62:63], v[70:71], v[62:63]
	s_and_b64 vcc, exec, s[2:3]
	s_mov_b64 s[22:23], -1
	v_pk_fma_f32 v[2:3], v[62:63], v[162:163], v[200:201]
	v_pk_fma_f32 v[0:1], v[64:65], v[160:161], v[198:199]
	s_cbranch_vccnz .LBB0_1419
	v_add_co_u32_e32 v64, vcc, 0x38000000, v38
	s_nop 1
	v_addc_co_u32_e32 v65, vcc, 0, v39, vcc
	v_cvt_pk_bf16_f32 v62, v0, v1
	v_cvt_pk_bf16_f32 v63, v2, v3
	flat_store_dwordx2 v[64:65], v[62:63] offset:1024 nt
	s_cbranch_execz .LBB0_1420

; __device__ __forceinline__ unsigned cvt_pk_bf16(float lo, float hi) { unsigned r; asm volatile("v_cvt_pk_bf16_f32 %0, %1, %2" : "=v"(r) : "v"(lo), "v"(hi)); return r; }
; __global__ void __launch_bounds__(NTHREADS, 2) hybrid_fwd(Args a) {
;     ...
; #pragma unroll
;                     for (int j = 0; j < 8; ++j) { const f32x4 gg = *(const f32x4*)(lg + j * 256 + lane * 4), bb = *(const f32x4*)(lb + j * 256 + lane * 4);
;                         y[j] = y[j] * rstd * gg + bb;
;                         if (lastl) __builtin_nontemporal_store(y[j], (f32x4*)(a.out + (size_t)row * DM + j * 256 + lane * 4));
;                         else { u32x2 w; w.x = cvt_pk_bf16(y[j][0], y[j][1]); w.y = cvt_pk_bf16(y[j][2], y[j][3]); __builtin_nontemporal_store(w, (u32x2*)(XA16 + (size_t)row * DM + j * 256 + lane * 4)); }
;                         if (!lastl) __builtin_nontemporal_store(cvt4_fp8(y[j][0], y[j][1], y[j][2], y[j][3]), (unsigned*)(XB + (size_t)row * DM + j * 256 + lane * 4)); }
.LBB0_1382:
	s_nop 0
	v_mov_b32_e32 v66, v42
	v_mov_b32_e32 v67, v42
	v_pk_mul_f32 v[60:61], v[42:43], v[60:61]
	v_pk_mul_f32 v[58:59], v[66:67], v[58:59]
	s_and_b64 vcc, exec, s[2:3]
	s_mov_b64 s[22:23], -1
	v_pk_fma_f32 v[2:3], v[58:59], v[170:171], v[204:205]
	v_pk_fma_f32 v[0:1], v[60:61], v[168:169], v[202:203]
	s_cbranch_vccnz .LBB0_1421
	v_add_co_u32_e32 v60, vcc, 0x38000000, v38
	s_nop 1
	v_addc_co_u32_e32 v61, vcc, 0, v39, vcc
	v_cvt_pk_bf16_f32 v58, v0, v1
	v_cvt_pk_bf16_f32 v59, v2, v3
	flat_store_dwordx2 v[60:61], v[58:59] offset:1536 nt
	s_cbranch_execz .LBB0_1422

; __device__ __forceinline__ unsigned cvt_pk_bf16(float lo, float hi) { unsigned r; asm volatile("v_cvt_pk_bf16_f32 %0, %1, %2" : "=v"(r) : "v"(lo), "v"(hi)); return r; }
; __global__ void __launch_bounds__(NTHREADS, 2) hybrid_fwd(Args a) {
;     ...
; #pragma unroll
;                     for (int j = 0; j < 8; ++j) { const f32x4 gg = *(const f32x4*)(lg + j * 256 + lane * 4), bb = *(const f32x4*)(lb + j * 256 + lane * 4);
;                         y[j] = y[j] * rstd * gg + bb;
;                         if (lastl) __builtin_nontemporal_store(y[j], (f32x4*)(a.out + (size_t)row * DM + j * 256 + lane * 4));
;                         else { u32x2 w; w.x = cvt_pk_bf16(y[j][0], y[j][1]); w.y = cvt_pk_bf16(y[j][2], y[j][3]); __builtin_nontemporal_store(w, (u32x2*)(XA16 + (size_t)row * DM + j * 256 + lane * 4)); }
;                         if (!lastl) __builtin_nontemporal_store(cvt4_fp8(y[j][0], y[j][1], y[j][2], y[j][3]), (unsigned*)(XB + (size_t)row * DM + j * 256 + lane * 4)); }
.LBB0_1386:
	s_nop 0
	v_mov_b32_e32 v62, v42
	v_mov_b32_e32 v63, v42
	v_pk_mul_f32 v[56:57], v[42:43], v[56:57]
	v_pk_mul_f32 v[54:55], v[62:63], v[54:55]
	s_and_b64 vcc, exec, s[2:3]
	s_mov_b64 s[22:23], -1
	v_pk_fma_f32 v[2:3], v[54:55], v[174:175], v[218:219]
	v_pk_fma_f32 v[0:1], v[56:57], v[172:173], v[216:217]
	s_cbranch_vccnz .LBB0_1423
	v_add_co_u32_e32 v56, vcc, 0x38000000, v38
	s_nop 1
	v_addc_co_u32_e32 v57, vcc, 0, v39, vcc
	v_cvt_pk_bf16_f32 v54, v0, v1
	v_cvt_pk_bf16_f32 v55, v2, v3
	flat_store_dwordx2 v[56:57], v[54:55] offset:2048 nt
	s_cbranch_execz .LBB0_1424

; __device__ __forceinline__ unsigned cvt_pk_bf16(float lo, float hi) { unsigned r; asm volatile("v_cvt_pk_bf16_f32 %0, %1, %2" : "=v"(r) : "v"(lo), "v"(hi)); return r; }
; __global__ void __launch_bounds__(NTHREADS, 2) hybrid_fwd(Args a) {
;     ...
; #pragma unroll
;                     for (int j = 0; j < 8; ++j) { const f32x4 gg = *(const f32x4*)(lg + j * 256 + lane * 4), bb = *(const f32x4*)(lb + j * 256 + lane * 4);
;                         y[j] = y[j] * rstd * gg + bb;
;                         if (lastl) __builtin_nontemporal_store(y[j], (f32x4*)(a.out + (size_t)row * DM + j * 256 + lane * 4));
;                         else { u32x2 w; w.x = cvt_pk_bf16(y[j][0], y[j][1]); w.y = cvt_pk_bf16(y[j][2], y[j][3]); __builtin_nontemporal_store(w, (u32x2*)(XA16 + (size_t)row * DM + j * 256 + lane * 4)); }
;                         if (!lastl) __builtin_nontemporal_store(cvt4_fp8(y[j][0], y[j][1], y[j][2], y[j][3]), (unsigned*)(XB + (size_t)row * DM + j * 256 + lane * 4)); }
.LBB0_1390:
	s_nop 0
	v_mov_b32_e32 v58, v42
	v_mov_b32_e32 v59, v42
	v_pk_mul_f32 v[52:53], v[42:43], v[52:53]
	v_pk_mul_f32 v[50:51], v[58:59], v[50:51]
	s_and_b64 vcc, exec, s[2:3]
	s_mov_b64 s[22:23], -1
	v_pk_fma_f32 v[2:3], v[50:51], v[178:179], v[222:223]
	v_pk_fma_f32 v[0:1], v[52:53], v[176:177], v[220:221]
	s_cbranch_vccnz .LBB0_1425
	v_add_co_u32_e32 v52, vcc, 0x38000000, v38
	s_nop 1
	v_addc_co_u32_e32 v53, vcc, 0, v39, vcc
	v_cvt_pk_bf16_f32 v50, v0, v1
	v_cvt_pk_bf16_f32 v51, v2, v3
	flat_store_dwordx2 v[52:53], v[50:51] offset:2560 nt
	s_cbranch_execz .LBB0_1426

; __device__ __forceinline__ unsigned cvt_pk_bf16(float lo, float hi) { unsigned r; asm volatile("v_cvt_pk_bf16_f32 %0, %1, %2" : "=v"(r) : "v"(lo), "v"(hi)); return r; }
; __global__ void __launch_bounds__(NTHREADS, 2) hybrid_fwd(Args a) {
;     ...
; #pragma unroll
;                     for (int j = 0; j < 8; ++j) { const f32x4 gg = *(const f32x4*)(lg + j * 256 + lane * 4), bb = *(const f32x4*)(lb + j * 256 + lane * 4);
;                         y[j] = y[j] * rstd * gg + bb;
;                         if (lastl) __builtin_nontemporal_store(y[j], (f32x4*)(a.out + (size_t)row * DM + j * 256 + lane * 4));
;                         else { u32x2 w; w.x = cvt_pk_bf16(y[j][0], y[j][1]); w.y = cvt_pk_bf16(y[j][2], y[j][3]); __builtin_nontemporal_store(w, (u32x2*)(XA16 + (size_t)row * DM + j * 256 + lane * 4)); }
;                         if (!lastl) __builtin_nontemporal_store(cvt4_fp8(y[j][0], y[j][1], y[j][2], y[j][3]), (unsigned*)(XB + (size_t)row * DM + j * 256 + lane * 4)); }
.LBB0_1394:
	s_nop 0
	v_mov_b32_e32 v54, v42
	v_mov_b32_e32 v55, v42
	v_pk_mul_f32 v[48:49], v[42:43], v[48:49]
	v_pk_mul_f32 v[46:47], v[54:55], v[46:47]
	s_and_b64 vcc, exec, s[2:3]
	s_mov_b64 s[22:23], -1
	v_pk_fma_f32 v[2:3], v[46:47], v[182:183], v[226:227]
	v_pk_fma_f32 v[0:1], v[48:49], v[180:181], v[224:225]
	s_cbranch_vccnz .LBB0_1427
	v_add_co_u32_e32 v48, vcc, 0x38000000, v38
	s_nop 1
	v_addc_co_u32_e32 v49, vcc, 0, v39, vcc
	v_cvt_pk_bf16_f32 v46, v0, v1
	v_cvt_pk_bf16_f32 v47, v2, v3
	flat_store_dwordx2 v[48:49], v[46:47] offset:3072 nt
	s_cbranch_execz .LBB0_1428

; __device__ __forceinline__ unsigned cvt_pk_bf16(float lo, float hi) { unsigned r; asm volatile("v_cvt_pk_bf16_f32 %0, %1, %2" : "=v"(r) : "v"(lo), "v"(hi)); return r; }
; __global__ void __launch_bounds__(NTHREADS, 2) hybrid_fwd(Args a) {
;     ...
; #pragma unroll
;                     for (int j = 0; j < 8; ++j) { const f32x4 gg = *(const f32x4*)(lg + j * 256 + lane * 4), bb = *(const f32x4*)(lb + j * 256 + lane * 4);
;                         y[j] = y[j] * rstd * gg + bb;
;                         if (lastl) __builtin_nontemporal_store(y[j], (f32x4*)(a.out + (size_t)row * DM + j * 256 + lane * 4));
;                         else { u32x2 w; w.x = cvt_pk_bf16(y[j][0], y[j][1]); w.y = cvt_pk_bf16(y[j][2], y[j][3]); __builtin_nontemporal_store(w, (u32x2*)(XA16 + (size_t)row * DM + j * 256 + lane * 4)); }
;                         if (!lastl) __builtin_nontemporal_store(cvt4_fp8(y[j][0], y[j][1], y[j][2], y[j][3]), (unsigned*)(XB + (size_t)row * DM + j * 256 + lane * 4)); }
.LBB0_1398:
	s_nop 0
	v_mov_b32_e32 v50, v42
	v_mov_b32_e32 v51, v42
	v_pk_mul_f32 v[42:43], v[42:43], v[44:45]
	v_pk_mul_f32 v[40:41], v[50:51], v[40:41]
	s_and_b64 vcc, exec, s[2:3]
	s_mov_b64 s[22:23], -1
	v_pk_fma_f32 v[2:3], v[40:41], v[186:187], v[230:231]
	v_pk_fma_f32 v[0:1], v[42:43], v[184:185], v[228:229]
	s_cbranch_vccnz .LBB0_1429
	v_add_co_u32_e32 v38, vcc, 0x38000000, v38
	s_nop 1
	v_addc_co_u32_e32 v39, vcc, 0, v39, vcc
	v_cvt_pk_bf16_f32 v40, v0, v1
	v_cvt_pk_bf16_f32 v41, v2, v3
	flat_store_dwordx2 v[38:39], v[40:41] offset:3584 nt
	s_cbranch_execz .LBB0_1430
